# v057 + packed f32 VALU ops outside attention replaced by plain f32 pairs (1416 sites)
# baseline (speedup 1.0000x reference)
; #define LAS __attribute__((address_space(3)))
; __global__ void __launch_bounds__(512, 2) hymba_fwd(Args args) {
;     ...
;             float a[8] = {0.f, 0.f, 0.f, 0.f, 0.f, 0.f, 0.f, 0.f}; const float* wp = argp->in[2] + (size_t)(kc * 128) * 6144 + ng * 64 + lane;
; #pragma unroll 8
;             for (int kk = 0; kk < 128; ++kk) { const float w = wp[(size_t)kk * 6144]; const LAS f32x4* sp = (const LAS f32x4*)(scr + kk * 8); const f32x4 s0 = sp[0], s1 = sp[1];
;                 a[0] += s0[0] * w; a[1] += s0[1] * w; a[2] += s0[2] * w; a[3] += s0[3] * w; a[4] += s1[0] * w; a[5] += s1[1] * w; a[6] += s1[2] * w; a[7] += s1[3] * w; }
; #pragma unroll
;             for (int b = 0; b < 8; ++b) MODP[((size_t)kc * 8 + b) * 6144 + ng * 64 + lane] = a[b];
.LBB0_14:
	v_lshl_add_u64 v[34:35], v[6:7], 0, s[8:9]
	v_add_co_u32_e32 v36, vcc, s17, v34
	global_load_dword v90, v[34:35], off
	s_nop 0
	v_addc_co_u32_e32 v37, vcc, 0, v35, vcc
	v_add_co_u32_e32 v38, vcc, s18, v34
	v_mov_b32_e32 v33, s26
	s_nop 0
	v_addc_co_u32_e32 v39, vcc, 0, v35, vcc
	v_add_co_u32_e32 v40, vcc, s19, v34
	s_addk_i32 s26, 0x100
	s_nop 0
	v_addc_co_u32_e32 v41, vcc, 0, v35, vcc
	v_add_co_u32_e32 v42, vcc, s20, v34
	s_add_u32 s8, s8, 0x30000
	s_nop 0
	v_addc_co_u32_e32 v43, vcc, 0, v35, vcc
	v_add_co_u32_e32 v44, vcc, s21, v34
	s_addc_u32 s9, s9, 0
	s_nop 0
	v_addc_co_u32_e32 v45, vcc, 0, v35, vcc
	v_add_co_u32_e32 v46, vcc, s22, v34
	s_cmp_eq_u32 s8, 0x300000
	s_nop 0
	v_addc_co_u32_e32 v47, vcc, 0, v35, vcc
	v_add_co_u32_e32 v34, vcc, s23, v34
	s_nop 1
	v_addc_co_u32_e32 v35, vcc, 0, v35, vcc
	global_load_dword v102, v[36:37], off
	global_load_dword v104, v[38:39], off
	global_load_dword v106, v[40:41], off
	global_load_dword v108, v[42:43], off
	global_load_dword v110, v[44:45], off
	global_load_dword v112, v[46:47], off
	global_load_dword v114, v[34:35], off
	ds_read_b128 v[34:37], v33
	ds_read_b128 v[38:41], v33 offset:16
	ds_read_b128 v[42:45], v33 offset:32
	ds_read_b128 v[46:49], v33 offset:48
	ds_read_b128 v[50:53], v33 offset:64
	ds_read_b128 v[54:57], v33 offset:80
	ds_read_b128 v[58:61], v33 offset:96
	ds_read_b128 v[62:65], v33 offset:112
	ds_read_b128 v[66:69], v33 offset:128
	ds_read_b128 v[70:73], v33 offset:144
	ds_read_b128 v[74:77], v33 offset:160
	ds_read_b128 v[78:81], v33 offset:176
	ds_read_b128 v[82:85], v33 offset:192
	ds_read_b128 v[86:89], v33 offset:208
	ds_read_b128 v[94:97], v33 offset:224
	ds_read_b128 v[98:101], v33 offset:240
	s_waitcnt vmcnt(7) lgkmcnt(14)
	v_fma_f32 v12, v90, v34, v12
	v_fma_f32 v13, v90, v35, v13
	v_fma_f32 v10, v90, v36, v10
	v_fma_f32 v11, v90, v37, v11
	v_fma_f32 v8, v90, v38, v8
	v_fma_f32 v9, v90, v39, v9
	v_fma_f32 v4, v90, v40, v4
	v_fma_f32 v5, v90, v41, v5
	s_waitcnt vmcnt(6) lgkmcnt(13)
	v_fma_f32 v12, v102, v42, v12
	v_fma_f32 v13, v102, v43, v13
	v_fma_f32 v10, v102, v44, v10
	v_fma_f32 v11, v102, v45, v11
	s_waitcnt lgkmcnt(12)
	v_fma_f32 v8, v102, v46, v8
	v_fma_f32 v9, v102, v47, v9
	v_fma_f32 v4, v102, v48, v4
	v_fma_f32 v5, v102, v49, v5
	s_waitcnt vmcnt(5) lgkmcnt(11)
	v_fma_f32 v12, v104, v50, v12
	v_fma_f32 v13, v104, v51, v13
	v_fma_f32 v10, v104, v52, v10
	v_fma_f32 v11, v104, v53, v11
	s_waitcnt lgkmcnt(10)
	v_fma_f32 v8, v104, v54, v8
	v_fma_f32 v9, v104, v55, v9
	v_fma_f32 v4, v104, v56, v4
	v_fma_f32 v5, v104, v57, v5
	s_waitcnt vmcnt(4) lgkmcnt(9)
	v_fma_f32 v12, v106, v58, v12
	v_fma_f32 v13, v106, v59, v13
	v_fma_f32 v10, v106, v60, v10
	v_fma_f32 v11, v106, v61, v11
	s_waitcnt lgkmcnt(8)
	v_fma_f32 v8, v106, v62, v8
	v_fma_f32 v9, v106, v63, v9
	v_fma_f32 v4, v106, v64, v4
	v_fma_f32 v5, v106, v65, v5
	s_waitcnt vmcnt(3) lgkmcnt(7)
	v_fma_f32 v12, v108, v66, v12
	v_fma_f32 v13, v108, v67, v13
	v_fma_f32 v10, v108, v68, v10
	v_fma_f32 v11, v108, v69, v11
	s_waitcnt lgkmcnt(6)
	v_fma_f32 v8, v108, v70, v8
	v_fma_f32 v9, v108, v71, v9
	v_fma_f32 v4, v108, v72, v4
	v_fma_f32 v5, v108, v73, v5
	s_waitcnt vmcnt(2) lgkmcnt(5)
	v_fma_f32 v12, v110, v74, v12
	v_fma_f32 v13, v110, v75, v13
	v_fma_f32 v10, v110, v76, v10
	v_fma_f32 v11, v110, v77, v11
	s_waitcnt lgkmcnt(4)
	v_fma_f32 v8, v110, v78, v8
	v_fma_f32 v9, v110, v79, v9
	v_fma_f32 v4, v110, v80, v4
	v_fma_f32 v5, v110, v81, v5
	s_waitcnt vmcnt(1) lgkmcnt(3)
	v_fma_f32 v12, v112, v82, v12
	v_fma_f32 v13, v112, v83, v13
	v_fma_f32 v10, v112, v84, v10
	v_fma_f32 v11, v112, v85, v11
	s_waitcnt lgkmcnt(2)
	v_fma_f32 v8, v112, v86, v8
	v_fma_f32 v9, v112, v87, v9
	v_fma_f32 v4, v112, v88, v4
	v_fma_f32 v5, v112, v89, v5
	s_waitcnt vmcnt(0) lgkmcnt(1)
	v_fma_f32 v12, v114, v94, v12
	v_fma_f32 v13, v114, v95, v13
	v_fma_f32 v10, v114, v96, v10
	v_fma_f32 v11, v114, v97, v11
	s_waitcnt lgkmcnt(0)
	v_fma_f32 v8, v114, v98, v8
	v_fma_f32 v9, v114, v99, v9
	v_fma_f32 v4, v114, v100, v4
	v_fma_f32 v5, v114, v101, v5
	s_cbranch_scc0 .LBB0_14
	v_lshl_add_u64 v[6:7], s[4:5], 2, v[2:3]
	v_mad_i64_i32 v[6:7], s[4:5], s25, v32, v[6:7]
	v_add_co_u32_e32 v34, vcc, 0x6000, v6
	global_store_dword v[6:7], v12, off
	s_nop 0
	v_addc_co_u32_e32 v35, vcc, 0, v7, vcc
	v_add_co_u32_e32 v12, vcc, 0xc000, v6
	global_store_dword v[34:35], v13, off
	s_nop 0
	v_addc_co_u32_e32 v13, vcc, 0, v7, vcc
	global_store_dword v[12:13], v10, off
	v_add_co_u32_e32 v12, vcc, 0x12000, v6
	s_add_i32 s24, s24, s0
	s_nop 0
	v_addc_co_u32_e32 v13, vcc, 0, v7, vcc
	v_add_co_u32_e32 v10, vcc, 0x18000, v6
	global_store_dword v[12:13], v11, off
	s_nop 0
	v_addc_co_u32_e32 v11, vcc, 0, v7, vcc
	global_store_dword v[10:11], v8, off
	v_add_co_u32_e32 v10, vcc, 0x1e000, v6
	s_cmpk_gt_i32 s24, 0x2ff
	s_nop 0
	v_addc_co_u32_e32 v11, vcc, 0, v7, vcc
	v_add_co_u32_e32 v8, vcc, 0x24000, v6
	global_store_dword v[10:11], v9, off
	s_nop 0
	v_addc_co_u32_e32 v9, vcc, 0, v7, vcc
	v_add_co_u32_e32 v6, vcc, 0x2a000, v6
	global_store_dword v[8:9], v4, off
	s_nop 0
	v_addc_co_u32_e32 v7, vcc, 0, v7, vcc
	global_store_dword v[6:7], v5, off
	s_waitcnt lgkmcnt(0)
	s_cbranch_scc0 .LBB0_13

; #define LAS __attribute__((address_space(3)))
; template <bool HASK = false>
; __device__ __forceinline__ void cvt_item(const float* W, int N, int scol, const float* kscale, int k0, bf16_t* WT, int K, int drow0, LAS float* scr, int lane) {
; #pragma unroll 16
;     for (int i = 0; i < 32; ++i) { const int kk = 2 * i + (lane >> 5); float v = 0.f, ks = 1.f;
;         if (scol >= 0) { v = W[(size_t)(k0 + kk) * N + scol]; if constexpr (HASK) ks = kscale[k0 + kk]; }
;         scr[kk * 33 + (lane & 31)] = v * ks; }
; __global__ void __launch_bounds__(512, 2) hymba_fwd(Args args) {
;     ...
;             if (r < I_KV) { const int nblk = 32, kb = r / nblk, nb = r % nblk;
;                 cvt_item<true>(argp->in[9], 1024, nb * 32 + l31, argp->in[8], kb * 64, WKV, 256, nb * 32, scr, lane); continue; }
.LBB0_24:
	s_andn2_b64 vcc, exec, s[4:5]
	s_cbranch_vccnz .LBB0_26
	s_lshl_b32 s10, s1, 1
	s_load_dwordx4 s[4:7], s[14:15], 0x40
	s_and_b32 s10, s10, 0xfc0
	s_addk_i32 s10, 0xf640
	v_or_b32_e32 v2, s29, v93
	v_add_u32_e32 v58, s10, v6
	v_add_u32_e32 v60, s10, v7
	v_lshlrev_b32_e32 v2, 2, v2
	v_ashrrev_i32_e32 v61, 31, v60
	v_ashrrev_i32_e32 v59, 31, v58
	s_waitcnt lgkmcnt(0)
	v_lshl_add_u64 v[54:55], s[6:7], 0, v[2:3]
	v_lshl_add_u64 v[56:57], v[58:59], 2, s[4:5]
	v_lshl_add_u64 v[62:63], v[60:61], 2, s[4:5]
	v_lshlrev_b64 v[58:59], 12, v[58:59]
	v_add_u32_e32 v66, s10, v14
	v_add_u32_e32 v68, s10, v15
	global_load_dword v56, v[56:57], off
	s_nop 0
	global_load_dword v57, v[62:63], off
	v_lshlrev_b64 v[60:61], 12, v[60:61]
	v_lshl_add_u64 v[62:63], v[54:55], 0, v[58:59]
	v_ashrrev_i32_e32 v69, 31, v68
	v_ashrrev_i32_e32 v67, 31, v66
	v_add_u32_e32 v70, s10, v16
	v_add_u32_e32 v72, s10, v17
	v_lshl_add_u64 v[60:61], v[54:55], 0, v[60:61]
	global_load_dword v58, v[62:63], off
	global_load_dword v59, v[60:61], off
	v_lshl_add_u64 v[62:63], v[66:67], 2, s[4:5]
	v_lshl_add_u64 v[64:65], v[68:69], 2, s[4:5]
	v_ashrrev_i32_e32 v73, 31, v72
	v_ashrrev_i32_e32 v71, 31, v70
	global_load_dword v60, v[62:63], off
	global_load_dword v61, v[64:65], off
	v_lshl_add_u64 v[64:65], v[70:71], 2, s[4:5]
	v_lshl_add_u64 v[74:75], v[72:73], 2, s[4:5]
	v_add_u32_e32 v76, s10, v18
	global_load_dword v62, v[64:65], off
	global_load_dword v63, v[74:75], off
	v_add_u32_e32 v74, s10, v19
	v_ashrrev_i32_e32 v77, 31, v76
	v_ashrrev_i32_e32 v75, 31, v74
	v_lshl_add_u64 v[78:79], v[76:77], 2, s[4:5]
	v_lshlrev_b64 v[68:69], 12, v[68:69]
	v_lshlrev_b64 v[66:67], 12, v[66:67]
	v_lshl_add_u64 v[80:81], v[74:75], 2, s[4:5]
	global_load_dword v64, v[78:79], off
	global_load_dword v65, v[80:81], off
	v_lshl_add_u64 v[78:79], v[54:55], 0, v[66:67]
	v_lshl_add_u64 v[68:69], v[54:55], 0, v[68:69]
	global_load_dword v66, v[78:79], off
	global_load_dword v67, v[68:69], off
	v_lshlrev_b64 v[68:69], 12, v[72:73]
	v_lshlrev_b64 v[70:71], 12, v[70:71]
	v_lshl_add_u64 v[70:71], v[54:55], 0, v[70:71]
	v_lshl_add_u64 v[72:73], v[54:55], 0, v[68:69]
	global_load_dword v68, v[70:71], off
	global_load_dword v69, v[72:73], off
	v_lshlrev_b64 v[70:71], 12, v[74:75]
	v_lshlrev_b64 v[72:73], 12, v[76:77]
	v_lshl_add_u64 v[72:73], v[54:55], 0, v[72:73]
	v_lshl_add_u64 v[74:75], v[54:55], 0, v[70:71]
	global_load_dword v70, v[72:73], off
	global_load_dword v71, v[74:75], off
	v_add_u32_e32 v74, s10, v20
	v_add_u32_e32 v76, s10, v21
	v_ashrrev_i32_e32 v75, 31, v74
	v_ashrrev_i32_e32 v77, 31, v76
	v_lshl_add_u64 v[78:79], v[74:75], 2, s[4:5]
	v_lshlrev_b64 v[74:75], 12, v[74:75]
	v_lshl_add_u64 v[80:81], v[76:77], 2, s[4:5]
	global_load_dword v72, v[78:79], off
	global_load_dword v73, v[80:81], off
	v_lshlrev_b64 v[76:77], 12, v[76:77]
	v_lshl_add_u64 v[78:79], v[54:55], 0, v[74:75]
	v_lshl_add_u64 v[76:77], v[54:55], 0, v[76:77]
	global_load_dword v74, v[78:79], off
	global_load_dword v75, v[76:77], off
	v_add_u32_e32 v78, s10, v22
	v_add_u32_e32 v80, s10, v23
	v_ashrrev_i32_e32 v79, 31, v78
	v_ashrrev_i32_e32 v81, 31, v80
	v_lshl_add_u64 v[82:83], v[78:79], 2, s[4:5]
	v_lshlrev_b64 v[78:79], 12, v[78:79]
	v_lshl_add_u64 v[84:85], v[80:81], 2, s[4:5]
	global_load_dword v76, v[82:83], off
	global_load_dword v77, v[84:85], off
	v_lshlrev_b64 v[80:81], 12, v[80:81]
	v_lshl_add_u64 v[82:83], v[54:55], 0, v[78:79]
	v_lshl_add_u64 v[80:81], v[54:55], 0, v[80:81]
	global_load_dword v78, v[82:83], off
	global_load_dword v79, v[80:81], off
	v_add_u32_e32 v82, s10, v25
	v_add_u32_e32 v84, s10, v24
	v_ashrrev_i32_e32 v83, 31, v82
	v_ashrrev_i32_e32 v85, 31, v84
	v_lshl_add_u64 v[80:81], v[84:85], 2, s[4:5]
	v_lshl_add_u64 v[86:87], v[82:83], 2, s[4:5]
	v_lshlrev_b64 v[82:83], 12, v[82:83]
	v_lshlrev_b64 v[84:85], 12, v[84:85]
	global_load_dword v80, v[80:81], off
	s_nop 0
	global_load_dword v81, v[86:87], off
	v_lshl_add_u64 v[84:85], v[54:55], 0, v[84:85]
	v_lshl_add_u64 v[86:87], v[54:55], 0, v[82:83]
	global_load_dword v82, v[84:85], off
	global_load_dword v83, v[86:87], off
	v_add_u32_e32 v86, s10, v26
	v_add_u32_e32 v88, s10, v27
	v_ashrrev_i32_e32 v89, 31, v88
	v_ashrrev_i32_e32 v87, 31, v86
	v_lshl_add_u64 v[84:85], v[86:87], 2, s[4:5]
	v_lshl_add_u64 v[90:91], v[88:89], 2, s[4:5]
	global_load_dword v84, v[84:85], off
	s_nop 0
	global_load_dword v85, v[90:91], off
	v_lshlrev_b64 v[88:89], 12, v[88:89]
	v_lshlrev_b64 v[86:87], 12, v[86:87]
	v_add_u32_e32 v90, s10, v28
	v_add_u32_e32 v134, s10, v29
	v_lshl_add_u64 v[86:87], v[54:55], 0, v[86:87]
	v_lshl_add_u64 v[88:89], v[54:55], 0, v[88:89]
	v_ashrrev_i32_e32 v135, 31, v134
	v_ashrrev_i32_e32 v91, 31, v90
	global_load_dword v86, v[86:87], off
	s_nop 0
	global_load_dword v87, v[88:89], off
	v_lshl_add_u64 v[88:89], v[90:91], 2, s[4:5]
	v_lshl_add_u64 v[136:137], v[134:135], 2, s[4:5]
	v_lshlrev_b64 v[134:135], 12, v[134:135]
	v_lshlrev_b64 v[90:91], 12, v[90:91]
	v_lshl_add_u64 v[90:91], v[54:55], 0, v[90:91]
	v_lshl_add_u64 v[134:135], v[54:55], 0, v[134:135]
	global_load_dword v88, v[88:89], off
	s_nop 0
	global_load_dword v89, v[136:137], off
	s_nop 0
	global_load_dword v90, v[90:91], off
	s_nop 0
	global_load_dword v91, v[134:135], off
	v_add_u32_e32 v134, s10, v33
	v_add_u32_e32 v136, s10, v32
	v_ashrrev_i32_e32 v135, 31, v134
	v_ashrrev_i32_e32 v137, 31, v136
	v_lshl_add_u64 v[138:139], v[136:137], 2, s[4:5]
	v_lshl_add_u64 v[140:141], v[134:135], 2, s[4:5]
	v_lshlrev_b64 v[134:135], 12, v[134:135]
	v_lshlrev_b64 v[136:137], 12, v[136:137]
	v_lshl_add_u64 v[136:137], v[54:55], 0, v[136:137]
	v_lshl_add_u64 v[134:135], v[54:55], 0, v[134:135]
; #define LAS __attribute__((address_space(3)))
; #define LDS_WAIT() asm volatile("s_waitcnt lgkmcnt(0)" ::: "memory")
; template <bool HASK = false>
; __device__ __forceinline__ void cvt_item(const float* W, int N, int scol, const float* kscale, int k0, bf16_t* WT, int K, int drow0, LAS float* scr, int lane) {
; #pragma unroll 16
;     for (int i = 0; i < 32; ++i) { const int kk = 2 * i + (lane >> 5); float v = 0.f, ks = 1.f;
;         if (scol >= 0) { v = W[(size_t)(k0 + kk) * N + scol]; if constexpr (HASK) ks = kscale[k0 + kk]; }
;         scr[kk * 33 + (lane & 31)] = v * ks; }
;     LDS_WAIT(); asm volatile("" ::: "memory");
	global_load_dword v138, v[138:139], off
	s_nop 0
	global_load_dword v139, v[140:141], off
	s_nop 0
	global_load_dword v136, v[136:137], off
	s_nop 0
	global_load_dword v137, v[134:135], off
	v_add_u32_e32 v134, s10, v34
	v_add_u32_e32 v140, s10, v35
	v_ashrrev_i32_e32 v141, 31, v140
	v_ashrrev_i32_e32 v135, 31, v134
	v_lshl_add_u64 v[142:143], v[134:135], 2, s[4:5]
	v_lshl_add_u64 v[144:145], v[140:141], 2, s[4:5]
	v_lshlrev_b64 v[140:141], 12, v[140:141]
	v_lshlrev_b64 v[134:135], 12, v[134:135]
	v_lshl_add_u64 v[134:135], v[54:55], 0, v[134:135]
	v_lshl_add_u64 v[140:141], v[54:55], 0, v[140:141]
	global_load_dword v142, v[142:143], off
	s_nop 0
	global_load_dword v143, v[144:145], off
	s_nop 0
	global_load_dword v134, v[134:135], off
	s_nop 0
	global_load_dword v135, v[140:141], off
	v_add_u32_e32 v140, s10, v36
	v_add_u32_e32 v144, s10, v37
	v_ashrrev_i32_e32 v145, 31, v144
	v_ashrrev_i32_e32 v141, 31, v140
	v_lshl_add_u64 v[146:147], v[140:141], 2, s[4:5]
	v_lshl_add_u64 v[148:149], v[144:145], 2, s[4:5]
	v_lshlrev_b64 v[144:145], 12, v[144:145]
	v_lshlrev_b64 v[140:141], 12, v[140:141]
	v_lshl_add_u64 v[140:141], v[54:55], 0, v[140:141]
	v_lshl_add_u64 v[144:145], v[54:55], 0, v[144:145]
	global_load_dword v146, v[146:147], off
	s_nop 0
	global_load_dword v147, v[148:149], off
	s_nop 0
	global_load_dword v140, v[140:141], off
	s_nop 0
	global_load_dword v141, v[144:145], off
	v_add_u32_e32 v144, s10, v39
	v_add_u32_e32 v148, s10, v38
	v_ashrrev_i32_e32 v145, 31, v144
	v_ashrrev_i32_e32 v149, 31, v148
	v_lshl_add_u64 v[150:151], v[148:149], 2, s[4:5]
	v_lshl_add_u64 v[152:153], v[144:145], 2, s[4:5]
	v_lshlrev_b64 v[144:145], 12, v[144:145]
	v_lshlrev_b64 v[148:149], 12, v[148:149]
	v_lshl_add_u64 v[148:149], v[54:55], 0, v[148:149]
	v_lshl_add_u64 v[144:145], v[54:55], 0, v[144:145]
	global_load_dword v150, v[150:151], off
	s_nop 0
	global_load_dword v151, v[152:153], off
	s_nop 0
	global_load_dword v148, v[148:149], off
	s_nop 0
	global_load_dword v149, v[144:145], off
	v_add_u32_e32 v144, s10, v40
	v_add_u32_e32 v152, s10, v41
	v_ashrrev_i32_e32 v153, 31, v152
	v_ashrrev_i32_e32 v145, 31, v144
	v_lshl_add_u64 v[154:155], v[144:145], 2, s[4:5]
	v_lshl_add_u64 v[156:157], v[152:153], 2, s[4:5]
	v_lshlrev_b64 v[152:153], 12, v[152:153]
	v_lshlrev_b64 v[144:145], 12, v[144:145]
	v_lshl_add_u64 v[144:145], v[54:55], 0, v[144:145]
	v_lshl_add_u64 v[152:153], v[54:55], 0, v[152:153]
	global_load_dword v154, v[154:155], off
	s_nop 0
	global_load_dword v155, v[156:157], off
	s_nop 0
	global_load_dword v144, v[144:145], off
	s_nop 0
	global_load_dword v145, v[152:153], off
	v_add_u32_e32 v152, s10, v42
	v_add_u32_e32 v156, s10, v43
	v_ashrrev_i32_e32 v157, 31, v156
	v_ashrrev_i32_e32 v153, 31, v152
	v_lshl_add_u64 v[158:159], v[152:153], 2, s[4:5]
	v_lshl_add_u64 v[160:161], v[156:157], 2, s[4:5]
	v_lshlrev_b64 v[156:157], 12, v[156:157]
	v_lshlrev_b64 v[152:153], 12, v[152:153]
	global_load_dword v158, v[158:159], off
	s_nop 0
	global_load_dword v159, v[160:161], off
	v_lshl_add_u64 v[152:153], v[54:55], 0, v[152:153]
	v_lshl_add_u64 v[156:157], v[54:55], 0, v[156:157]
	v_add_u32_e32 v160, s10, v44
	global_load_dword v152, v[152:153], off
	s_nop 0
	global_load_dword v153, v[156:157], off
	v_add_u32_e32 v156, s10, v45
	v_ashrrev_i32_e32 v161, 31, v160
	v_ashrrev_i32_e32 v157, 31, v156
	v_lshl_add_u64 v[162:163], v[160:161], 2, s[4:5]
	v_lshlrev_b64 v[160:161], 12, v[160:161]
	v_lshl_add_u64 v[164:165], v[156:157], 2, s[4:5]
	v_lshlrev_b64 v[156:157], 12, v[156:157]
	v_lshl_add_u64 v[160:161], v[54:55], 0, v[160:161]
	global_load_dword v162, v[162:163], off
	s_nop 0
	global_load_dword v163, v[164:165], off
	v_lshl_add_u64 v[54:55], v[54:55], 0, v[156:157]
	global_load_dword v156, v[160:161], off
	global_load_dword v157, v[54:55], off
	v_add_u32_e32 v2, v98, v100
	s_waitcnt vmcnt(60)
	v_mul_f32_e32 v54, v56, v58
	v_mul_f32_e32 v55, v57, v59
	v_add_u32_e32 v31, v98, v101
	ds_write_b32 v2, v54
	ds_write_b32 v31, v55
	s_waitcnt vmcnt(52)
	v_mul_f32_e32 v54, v60, v66
	v_mul_f32_e32 v55, v61, v67
	v_add_u32_e32 v2, v98, v102
	v_add_u32_e32 v31, v98, v103
	ds_write_b32 v2, v54
	v_add_u32_e32 v2, v98, v107
	s_waitcnt vmcnt(50)
	v_mul_f32_e32 v56, v62, v68
	v_mul_f32_e32 v57, v63, v69
	v_add_u32_e32 v60, v98, v104
	s_waitcnt vmcnt(48)
	v_mul_f32_e32 v58, v64, v70
	v_mul_f32_e32 v59, v65, v71
	v_add_u32_e32 v61, v98, v105
	v_add_u32_e32 v62, v98, v106
	ds_write_b32 v31, v55
	ds_write_b32 v60, v56
	ds_write_b32 v61, v57
	ds_write_b32 v62, v58
	ds_write_b32 v2, v59
	s_waitcnt vmcnt(44)
	v_mul_f32_e32 v54, v72, v74
	v_mul_f32_e32 v55, v73, v75
	v_add_u32_e32 v2, v98, v108
	ds_write_b32 v2, v54
	v_add_u32_e32 v2, v98, v109
	ds_write_b32 v2, v55
	s_waitcnt vmcnt(40)
	v_mul_f32_e32 v54, v76, v78
	v_mul_f32_e32 v55, v77, v79
	v_add_u32_e32 v2, v98, v110
	ds_write_b32 v2, v54
	v_add_u32_e32 v2, v98, v111
	ds_write_b32 v2, v55
	s_waitcnt vmcnt(36)
	v_mul_f32_e32 v54, v80, v82
	v_mul_f32_e32 v55, v81, v83
	v_add_u32_e32 v2, v98, v112
	ds_write_b32 v2, v54
	v_add_u32_e32 v2, v98, v113
	ds_write_b32 v2, v55
	s_waitcnt vmcnt(32)
	v_mul_f32_e32 v54, v84, v86
	v_mul_f32_e32 v55, v85, v87
	v_add_u32_e32 v2, v98, v114
	ds_write_b32 v2, v54
	v_add_u32_e32 v2, v98, v115
	ds_write_b32 v2, v55
	s_waitcnt vmcnt(28)
	v_mul_f32_e32 v54, v88, v90
	v_mul_f32_e32 v55, v89, v91
	v_add_u32_e32 v2, v98, v116
	ds_write_b32 v2, v54
	v_add_u32_e32 v2, v98, v117
	ds_write_b32 v2, v55
	s_waitcnt vmcnt(24)
	v_mul_f32_e32 v54, v138, v136
	v_mul_f32_e32 v55, v139, v137
	v_add_u32_e32 v2, v98, v118
	ds_write_b32 v2, v54
	v_add_u32_e32 v2, v98, v119
	ds_write_b32 v2, v55
	s_waitcnt vmcnt(20)
; #define GAS __attribute__((address_space(1)))
; #define LAS __attribute__((address_space(3)))
; #define LDS_WAIT() asm volatile("s_waitcnt lgkmcnt(0)" ::: "memory")
; __device__ __forceinline__ unsigned pk2(float lo, float hi) { return f2bf(lo) | (f2bf(hi) << 16); }
; template <bool HASK = false>
; __device__ __forceinline__ void cvt_item(const float* W, int N, int scol, const float* kscale, int k0, bf16_t* WT, int K, int drow0, LAS float* scr, int lane) {
;     ...
;     for (int i = 0; i < 32; ++i) { const int kk = 2 * i + (lane >> 5); float v = 0.f, ks = 1.f;
;         if (scol >= 0) { v = W[(size_t)(k0 + kk) * N + scol]; if constexpr (HASK) ks = kscale[k0 + kk]; }
;         scr[kk * 33 + (lane & 31)] = v * ks; }
;     LDS_WAIT(); asm volatile("" ::: "memory");
;     const int c = lane & 7;
; #pragma unroll
;     for (int j = 0; j < 4; ++j) { const int n = (lane >> 3) + 8 * j; const LAS float* s = scr + (8 * c) * 33 + n;
;         u32x4 o; o.x = pk2(s[0 * 33], s[1 * 33]); o.y = pk2(s[2 * 33], s[3 * 33]); o.z = pk2(s[4 * 33], s[5 * 33]); o.w = pk2(s[6 * 33], s[7 * 33]);
;         *(GAS u32x4*)(WT + (size_t)(drow0 + n) * K + k0 + 8 * c) = o; }
;     LDS_WAIT(); asm volatile("" ::: "memory");
	v_mul_f32_e32 v54, v142, v134
	v_mul_f32_e32 v55, v143, v135
	v_add_u32_e32 v2, v98, v120
	ds_write_b32 v2, v54
	v_add_u32_e32 v2, v98, v121
	ds_write_b32 v2, v55
	s_waitcnt vmcnt(16)
	v_mul_f32_e32 v54, v146, v140
	v_mul_f32_e32 v55, v147, v141
	v_add_u32_e32 v2, v98, v122
	ds_write_b32 v2, v54
	v_add_u32_e32 v2, v98, v123
	ds_write_b32 v2, v55
	s_waitcnt vmcnt(12)
	v_mul_f32_e32 v54, v150, v148
	v_mul_f32_e32 v55, v151, v149
	v_add_u32_e32 v2, v98, v124
	ds_write_b32 v2, v54
	v_add_u32_e32 v2, v98, v125
	ds_write_b32 v2, v55
	s_waitcnt vmcnt(8)
	v_mul_f32_e32 v54, v154, v144
	v_mul_f32_e32 v55, v155, v145
	v_add_u32_e32 v2, v98, v126
	ds_write_b32 v2, v54
	v_add_u32_e32 v2, v98, v127
	ds_write_b32 v2, v55
	v_add_u32_e32 v2, v98, v128
	v_lshlrev_b64 v[52:53], 9, v[52:53]
	v_lshl_add_u64 v[74:75], s[10:11], 1, v[8:9]
	s_waitcnt vmcnt(4)
	v_mul_f32_e32 v54, v158, v152
	v_mul_f32_e32 v55, v159, v153
	ds_write_b32 v2, v54
	v_add_u32_e32 v2, v98, v129
	ds_write_b32 v2, v55
	v_add_u32_e32 v2, v98, v131
	v_lshl_add_u64 v[52:53], v[74:75], 0, v[52:53]
	v_lshlrev_b64 v[50:51], 9, v[50:51]
	v_lshl_add_u64 v[50:51], v[74:75], 0, v[50:51]
	v_lshlrev_b64 v[48:49], 9, v[48:49]
	v_lshl_add_u64 v[48:49], v[74:75], 0, v[48:49]
	v_lshlrev_b64 v[46:47], 9, v[46:47]
	s_waitcnt vmcnt(0)
	v_mul_f32_e32 v54, v162, v156
	v_mul_f32_e32 v55, v163, v157
	ds_write_b32 v2, v54
	v_add_u32_e32 v2, v98, v133
	ds_write_b32 v2, v55
	s_waitcnt lgkmcnt(0)
	ds_read2_b32 v[58:59], v97 offset1:8
	ds_read2_b32 v[60:61], v97 offset0:33 offset1:41
	ds_read2_b32 v[62:63], v97 offset0:66 offset1:74
	ds_read2_b32 v[64:65], v97 offset0:99 offset1:107
	ds_read2_b32 v[66:67], v97 offset0:132 offset1:140
	ds_read2_b32 v[68:69], v97 offset0:165 offset1:173
	s_waitcnt lgkmcnt(5)
	v_bfe_u32 v2, v58, 16, 1
	s_waitcnt lgkmcnt(3)
	v_bfe_u32 v54, v62, 16, 1
	v_add3_u32 v2, v58, v2, s22
	v_bfe_u32 v31, v60, 16, 1
	v_add3_u32 v54, v62, v54, s22
	ds_read2_b32 v[70:71], v97 offset0:198 offset1:206
	v_lshrrev_b32_e32 v2, 16, v2
	v_add3_u32 v31, v60, v31, s22
	v_lshrrev_b32_e32 v55, 16, v54
	s_waitcnt lgkmcnt(3)
	v_bfe_u32 v54, v64, 16, 1
	ds_read2_b32 v[72:73], v97 offset0:231 offset1:239
	v_add3_u32 v56, v64, v54, s22
	v_and_or_b32 v54, v31, s23, v2
	s_waitcnt lgkmcnt(3)
	v_bfe_u32 v2, v66, 16, 1
	v_add3_u32 v2, v66, v2, s22
	s_waitcnt lgkmcnt(2)
	v_bfe_u32 v31, v68, 16, 1
	v_lshrrev_b32_e32 v2, 16, v2
	v_add3_u32 v31, v68, v31, s22
	v_and_or_b32 v55, v56, s23, v55
	v_and_or_b32 v56, v31, s23, v2
	s_waitcnt lgkmcnt(1)
	v_bfe_u32 v2, v70, 16, 1
	v_add3_u32 v2, v70, v2, s22
	s_waitcnt lgkmcnt(0)
	v_bfe_u32 v31, v72, 16, 1
	v_lshrrev_b32_e32 v2, 16, v2
	v_add3_u32 v31, v72, v31, s22
	v_and_or_b32 v57, v31, s23, v2
	v_bfe_u32 v2, v59, 16, 1
	global_store_dwordx4 v[52:53], v[54:57], off
	v_add3_u32 v2, v59, v2, s22
	v_bfe_u32 v31, v61, 16, 1
	v_bfe_u32 v52, v63, 16, 1
	v_add3_u32 v31, v61, v31, s22
	v_add3_u32 v52, v63, v52, s22
	v_lshrrev_b32_e32 v2, 16, v2
	v_lshrrev_b32_e32 v54, 16, v52
	v_and_or_b32 v52, v31, s23, v2
	v_bfe_u32 v2, v67, 16, 1
	v_bfe_u32 v53, v65, 16, 1
	v_add3_u32 v2, v67, v2, s22
	v_bfe_u32 v31, v69, 16, 1
	v_add3_u32 v53, v65, v53, s22
	v_lshrrev_b32_e32 v2, 16, v2
	v_add3_u32 v31, v69, v31, s22
	v_and_or_b32 v53, v53, s23, v54
	v_and_or_b32 v54, v31, s23, v2
	v_bfe_u32 v2, v71, 16, 1
	v_add3_u32 v2, v71, v2, s22
	v_bfe_u32 v31, v73, 16, 1
	v_lshrrev_b32_e32 v2, 16, v2
	v_add3_u32 v31, v73, v31, s22
	v_and_or_b32 v55, v31, s23, v2
	ds_read2_b32 v[56:57], v97 offset0:16 offset1:24
	global_store_dwordx4 v[50:51], v[52:55], off
	ds_read2_b32 v[54:55], v97 offset0:49 offset1:57
	ds_read2_b32 v[58:59], v97 offset0:82 offset1:90
	ds_read2_b32 v[60:61], v97 offset0:115 offset1:123
	s_waitcnt lgkmcnt(3)
	v_bfe_u32 v2, v56, 16, 1
	v_add3_u32 v2, v56, v2, s22
	s_waitcnt lgkmcnt(2)
	v_bfe_u32 v31, v54, 16, 1
	ds_read2_b32 v[62:63], v97 offset0:148 offset1:156
	v_lshrrev_b32_e32 v2, 16, v2
	v_add3_u32 v31, v54, v31, s22
	ds_read2_b32 v[64:65], v97 offset0:181 offset1:189
	v_and_or_b32 v50, v31, s23, v2
	s_waitcnt lgkmcnt(3)
	v_bfe_u32 v2, v58, 16, 1
	v_add3_u32 v2, v58, v2, s22
	s_waitcnt lgkmcnt(2)
	v_bfe_u32 v31, v60, 16, 1
	ds_read2_b32 v[66:67], v97 offset0:214 offset1:222
	v_lshrrev_b32_e32 v2, 16, v2
	v_add3_u32 v31, v60, v31, s22
	ds_read2_b32 v[68:69], v97 offset0:247 offset1:255
	v_and_or_b32 v51, v31, s23, v2
	s_waitcnt lgkmcnt(3)
	v_bfe_u32 v2, v62, 16, 1
	v_add3_u32 v2, v62, v2, s22
	s_waitcnt lgkmcnt(2)
	v_bfe_u32 v31, v64, 16, 1
	v_lshrrev_b32_e32 v2, 16, v2
	v_add3_u32 v31, v64, v31, s22
	v_and_or_b32 v52, v31, s23, v2
	s_waitcnt lgkmcnt(1)
	v_bfe_u32 v2, v66, 16, 1
	v_add3_u32 v2, v66, v2, s22
	s_waitcnt lgkmcnt(0)
	v_bfe_u32 v31, v68, 16, 1
	v_lshrrev_b32_e32 v2, 16, v2
	v_add3_u32 v31, v68, v31, s22
	v_and_or_b32 v53, v31, s23, v2
	v_bfe_u32 v2, v57, 16, 1
	v_add3_u32 v2, v57, v2, s22
	v_bfe_u32 v31, v55, 16, 1
	v_lshrrev_b32_e32 v2, 16, v2
	v_add3_u32 v31, v55, v31, s22
	global_store_dwordx4 v[48:49], v[50:53], off
	v_and_or_b32 v48, v31, s23, v2
	v_bfe_u32 v2, v59, 16, 1
	v_add3_u32 v2, v59, v2, s22
	v_bfe_u32 v31, v61, 16, 1
	v_lshrrev_b32_e32 v2, 16, v2
	v_add3_u32 v31, v61, v31, s22
	v_and_or_b32 v49, v31, s23, v2
	v_bfe_u32 v2, v63, 16, 1
	v_add3_u32 v2, v63, v2, s22
	v_bfe_u32 v31, v65, 16, 1
	v_lshrrev_b32_e32 v2, 16, v2
	v_add3_u32 v31, v65, v31, s22
	v_and_or_b32 v50, v31, s23, v2
	v_bfe_u32 v2, v67, 16, 1
	v_add3_u32 v2, v67, v2, s22
	v_bfe_u32 v31, v69, 16, 1
	v_lshrrev_b32_e32 v2, 16, v2
	v_add3_u32 v31, v69, v31, s22
	v_and_or_b32 v51, v31, s23, v2
	v_lshl_add_u64 v[46:47], v[74:75], 0, v[46:47]
	global_store_dwordx4 v[46:47], v[48:51], off
	s_waitcnt lgkmcnt(0)

; #define LAS __attribute__((address_space(3)))
; __device__ __forceinline__ int il64(int w) { return (w >> 1) + 32 * (w & 1); }
; template <bool HASK = false>
; __device__ __forceinline__ void cvt_item(const float* W, int N, int scol, const float* kscale, int k0, bf16_t* WT, int K, int drow0, LAS float* scr, int lane) {
; #pragma unroll 16
;     for (int i = 0; i < 32; ++i) { const int kk = 2 * i + (lane >> 5); float v = 0.f, ks = 1.f;
;         if (scol >= 0) { v = W[(size_t)(k0 + kk) * N + scol]; if constexpr (HASK) ks = kscale[k0 + kk]; }
;         scr[kk * 33 + (lane & 31)] = v * ks; }
; __global__ void __launch_bounds__(512, 2) hymba_fwd(Args args) {
;     ...
;             if (r < I_Q) { const int nblk = 24, kb = r / nblk, nb = r % nblk, n = nb * 32 + l31; const int hd = n / 192, w = n % 192; const int sc = (w < 128) ? n : hd * 192 + 128 + il64(w - 128);
;                 cvt_item<true>(argp->in[7], 768, sc, argp->in[6], kb * 64, WQ, 256, nb * 32, scr, lane); continue; }
.LBB0_27:
	s_andn2_b64 vcc, exec, s[4:5]
	s_cbranch_vccnz .LBB0_31
	s_xor_b32 s4, s1, 0xff80
	s_and_b32 s5, s4, 0xff
	s_mulk_i32 s5, 0xab
	s_bfe_u32 s10, s5, 0x4000c
	s_mul_i32 s5, s10, 24
	s_sub_i32 s4, s4, s5
	s_and_b32 s6, s4, 0xff
	s_lshl_b32 s29, s6, 5
	v_or_b32_e32 v2, s29, v93
	v_mul_u32_u24_e32 v31, 0xaab, v2
	v_lshrrev_b32_e32 v31, 19, v31
	v_mul_lo_u16_e32 v31, 0xc0, v31
	v_sub_u16_e32 v31, v2, v31
	v_cmp_lt_u16_e32 vcc, s24, v31
	s_and_saveexec_b64 s[4:5], vcc
	s_mulk_i32 s6, 0xab
	v_add_u32_e32 v2, 0xffffff80, v31
	s_bfe_u32 s6, s6, 0x6000a
	v_lshlrev_b32_e32 v31, 5, v2
	v_lshrrev_b32_e32 v2, 1, v2
	s_mulk_i32 s6, 0xc0
	v_and_or_b32 v2, v31, 32, v2
	s_addk_i32 s6, 0x80
	v_add_u32_e32 v2, s6, v2
	s_or_b64 exec, exec, s[4:5]
	s_load_dwordx4 s[4:7], s[14:15], 0x30
	s_and_b32 s10, 0xffff, s10
	s_lshl_b32 s30, s10, 6
	v_add_u32_e32 v50, s30, v6
	v_add_u32_e32 v52, s30, v7
	v_ashrrev_i32_e32 v53, 31, v52
	v_ashrrev_i32_e32 v51, 31, v50
	s_waitcnt lgkmcnt(0)
	v_lshl_add_u64 v[48:49], v[50:51], 2, s[4:5]
	v_lshl_add_u64 v[54:55], v[52:53], 2, s[4:5]
	v_mov_b32_e32 v46, s6
	v_mov_b32_e32 v47, s7
	global_load_dword v48, v[48:49], off
	s_nop 0
	global_load_dword v49, v[54:55], off
	v_add_u32_e32 v54, s30, v14
	v_add_u32_e32 v56, s30, v15
	v_lshl_add_u64 v[46:47], v[2:3], 2, v[46:47]
	v_ashrrev_i32_e32 v57, 31, v56
	v_ashrrev_i32_e32 v55, 31, v54
	v_mad_i64_i32 v[50:51], s[6:7], v50, s25, v[46:47]
	v_mad_i64_i32 v[52:53], s[6:7], v52, s25, v[46:47]
	v_lshl_add_u64 v[58:59], v[54:55], 2, s[4:5]
	v_lshl_add_u64 v[60:61], v[56:57], 2, s[4:5]
	global_load_dword v50, v[50:51], off
	s_nop 0
	global_load_dword v51, v[52:53], off
	s_nop 0
	global_load_dword v52, v[58:59], off
	global_load_dword v53, v[60:61], off
	v_add_u32_e32 v58, s30, v16
	v_add_u32_e32 v60, s30, v17
	v_ashrrev_i32_e32 v61, 31, v60
	v_ashrrev_i32_e32 v59, 31, v58
	v_mad_i64_i32 v[54:55], s[6:7], v54, s25, v[46:47]
	v_mad_i64_i32 v[56:57], s[6:7], v56, s25, v[46:47]
	v_lshl_add_u64 v[62:63], v[58:59], 2, s[4:5]
	v_lshl_add_u64 v[64:65], v[60:61], 2, s[4:5]
	global_load_dword v54, v[54:55], off
	s_nop 0
	global_load_dword v55, v[56:57], off
	s_nop 0
	global_load_dword v56, v[62:63], off
	global_load_dword v57, v[64:65], off
	v_add_u32_e32 v62, s30, v18
	v_add_u32_e32 v64, s30, v19
	v_ashrrev_i32_e32 v65, 31, v64
	v_ashrrev_i32_e32 v63, 31, v62
	v_mad_i64_i32 v[58:59], s[6:7], v58, s25, v[46:47]
	v_mad_i64_i32 v[60:61], s[6:7], v60, s25, v[46:47]
	v_lshl_add_u64 v[66:67], v[62:63], 2, s[4:5]
	v_lshl_add_u64 v[68:69], v[64:65], 2, s[4:5]
	global_load_dword v58, v[58:59], off
	s_nop 0
	global_load_dword v59, v[60:61], off
	s_nop 0
	global_load_dword v60, v[66:67], off
	global_load_dword v61, v[68:69], off
	v_add_u32_e32 v66, s30, v20
	v_add_u32_e32 v68, s30, v21
	v_ashrrev_i32_e32 v69, 31, v68
	v_ashrrev_i32_e32 v67, 31, v66
	v_mad_i64_i32 v[62:63], s[6:7], v62, s25, v[46:47]
	v_mad_i64_i32 v[64:65], s[6:7], v64, s25, v[46:47]
	v_lshl_add_u64 v[70:71], v[66:67], 2, s[4:5]
	v_lshl_add_u64 v[72:73], v[68:69], 2, s[4:5]
	global_load_dword v62, v[62:63], off
	s_nop 0
	global_load_dword v63, v[64:65], off
	s_nop 0
	global_load_dword v64, v[70:71], off
	global_load_dword v65, v[72:73], off
	v_add_u32_e32 v70, s30, v22
	v_add_u32_e32 v72, s30, v23
	v_ashrrev_i32_e32 v73, 31, v72
	v_ashrrev_i32_e32 v71, 31, v70
	v_mad_i64_i32 v[66:67], s[6:7], v66, s25, v[46:47]
	v_mad_i64_i32 v[68:69], s[6:7], v68, s25, v[46:47]
	v_lshl_add_u64 v[74:75], v[70:71], 2, s[4:5]
	v_lshl_add_u64 v[76:77], v[72:73], 2, s[4:5]
	global_load_dword v66, v[66:67], off
	s_nop 0
	global_load_dword v67, v[68:69], off
	s_nop 0
	global_load_dword v68, v[74:75], off
	global_load_dword v69, v[76:77], off
	v_add_u32_e32 v74, s30, v24
	v_add_u32_e32 v76, s30, v25
	v_ashrrev_i32_e32 v77, 31, v76
	v_ashrrev_i32_e32 v75, 31, v74
	v_mad_i64_i32 v[70:71], s[6:7], v70, s25, v[46:47]
	v_mad_i64_i32 v[72:73], s[6:7], v72, s25, v[46:47]
	v_lshl_add_u64 v[78:79], v[74:75], 2, s[4:5]
	v_lshl_add_u64 v[80:81], v[76:77], 2, s[4:5]
	global_load_dword v70, v[70:71], off
	s_nop 0
	global_load_dword v71, v[72:73], off
	s_nop 0
	global_load_dword v72, v[78:79], off
	global_load_dword v73, v[80:81], off
	v_add_u32_e32 v78, s30, v26
	v_add_u32_e32 v80, s30, v27
	v_ashrrev_i32_e32 v81, 31, v80
	v_ashrrev_i32_e32 v79, 31, v78
	v_mad_i64_i32 v[74:75], s[6:7], v74, s25, v[46:47]
	v_mad_i64_i32 v[76:77], s[6:7], v76, s25, v[46:47]
	v_lshl_add_u64 v[82:83], v[78:79], 2, s[4:5]
	v_lshl_add_u64 v[84:85], v[80:81], 2, s[4:5]
	v_mad_i64_i32 v[78:79], s[6:7], v78, s25, v[46:47]
	v_mad_i64_i32 v[80:81], s[6:7], v80, s25, v[46:47]
	global_load_dword v74, v[74:75], off
	s_nop 0
	global_load_dword v75, v[76:77], off
	s_nop 0
	global_load_dword v76, v[82:83], off
	global_load_dword v77, v[84:85], off
	s_nop 0
	global_load_dword v78, v[78:79], off
	s_nop 0
	global_load_dword v79, v[80:81], off
	v_add_u32_e32 v80, s30, v28
	v_add_u32_e32 v82, s30, v29
	v_ashrrev_i32_e32 v83, 31, v82
	v_ashrrev_i32_e32 v81, 31, v80
	v_lshl_add_u64 v[84:85], v[80:81], 2, s[4:5]
	v_lshl_add_u64 v[86:87], v[82:83], 2, s[4:5]
	v_mad_i64_i32 v[80:81], s[6:7], v80, s25, v[46:47]
	v_mad_i64_i32 v[82:83], s[6:7], v82, s25, v[46:47]
	global_load_dword v88, v[84:85], off
	global_load_dword v89, v[86:87], off
	s_nop 0
	global_load_dword v80, v[80:81], off
	s_nop 0
	global_load_dword v81, v[82:83], off
	v_add_u32_e32 v82, s30, v32
	v_add_u32_e32 v84, s30, v33
	v_ashrrev_i32_e32 v85, 31, v84
	v_ashrrev_i32_e32 v83, 31, v82
	v_lshl_add_u64 v[86:87], v[82:83], 2, s[4:5]
	v_lshl_add_u64 v[90:91], v[84:85], 2, s[4:5]
	v_mad_i64_i32 v[82:83], s[6:7], v82, s25, v[46:47]
; #define LAS __attribute__((address_space(3)))
; template <bool HASK = false>
; __device__ __forceinline__ void cvt_item(const float* W, int N, int scol, const float* kscale, int k0, bf16_t* WT, int K, int drow0, LAS float* scr, int lane) {
; #pragma unroll 16
;     for (int i = 0; i < 32; ++i) { const int kk = 2 * i + (lane >> 5); float v = 0.f, ks = 1.f;
;         if (scol >= 0) { v = W[(size_t)(k0 + kk) * N + scol]; if constexpr (HASK) ks = kscale[k0 + kk]; }
;         scr[kk * 33 + (lane & 31)] = v * ks; }
	v_mad_i64_i32 v[84:85], s[6:7], v84, s25, v[46:47]
	global_load_dword v86, v[86:87], off
	s_nop 0
	global_load_dword v87, v[90:91], off
	s_nop 0
	global_load_dword v82, v[82:83], off
	s_nop 0
	global_load_dword v83, v[84:85], off
	v_add_u32_e32 v84, s30, v34
	v_add_u32_e32 v90, s30, v35
	v_ashrrev_i32_e32 v91, 31, v90
	v_ashrrev_i32_e32 v85, 31, v84
	v_lshl_add_u64 v[134:135], v[84:85], 2, s[4:5]
	v_lshl_add_u64 v[136:137], v[90:91], 2, s[4:5]
	v_mad_i64_i32 v[84:85], s[6:7], v84, s25, v[46:47]
	v_mad_i64_i32 v[90:91], s[6:7], v90, s25, v[46:47]
	global_load_dword v134, v[134:135], off
	s_nop 0
	global_load_dword v135, v[136:137], off
	s_nop 0
	global_load_dword v84, v[84:85], off
	s_nop 0
	global_load_dword v85, v[90:91], off
	v_add_u32_e32 v90, s30, v36
	v_add_u32_e32 v136, s30, v37
	v_ashrrev_i32_e32 v137, 31, v136
	v_ashrrev_i32_e32 v91, 31, v90
	v_lshl_add_u64 v[138:139], v[90:91], 2, s[4:5]
	v_lshl_add_u64 v[140:141], v[136:137], 2, s[4:5]
	v_mad_i64_i32 v[90:91], s[6:7], v90, s25, v[46:47]
	v_mad_i64_i32 v[136:137], s[6:7], v136, s25, v[46:47]
	global_load_dword v138, v[138:139], off
	s_nop 0
	global_load_dword v139, v[140:141], off
	s_nop 0
	global_load_dword v90, v[90:91], off
	s_nop 0
	global_load_dword v91, v[136:137], off
	v_add_u32_e32 v136, s30, v38
	v_add_u32_e32 v140, s30, v39
	v_ashrrev_i32_e32 v141, 31, v140
	v_ashrrev_i32_e32 v137, 31, v136
	v_lshl_add_u64 v[142:143], v[136:137], 2, s[4:5]
	v_lshl_add_u64 v[144:145], v[140:141], 2, s[4:5]
	v_mad_i64_i32 v[136:137], s[6:7], v136, s25, v[46:47]
	v_mad_i64_i32 v[140:141], s[6:7], v140, s25, v[46:47]
	global_load_dword v142, v[142:143], off
	s_nop 0
	global_load_dword v143, v[144:145], off
	s_nop 0
	global_load_dword v136, v[136:137], off
	s_nop 0
	global_load_dword v137, v[140:141], off
	v_add_u32_e32 v140, s30, v40
	v_add_u32_e32 v144, s30, v41
	v_ashrrev_i32_e32 v145, 31, v144
	v_ashrrev_i32_e32 v141, 31, v140
	v_lshl_add_u64 v[146:147], v[140:141], 2, s[4:5]
	v_lshl_add_u64 v[148:149], v[144:145], 2, s[4:5]
	v_mad_i64_i32 v[140:141], s[6:7], v140, s25, v[46:47]
	v_mad_i64_i32 v[144:145], s[6:7], v144, s25, v[46:47]
	global_load_dword v146, v[146:147], off
	s_nop 0
	global_load_dword v147, v[148:149], off
	s_nop 0
	global_load_dword v140, v[140:141], off
	s_nop 0
	global_load_dword v141, v[144:145], off
	v_add_u32_e32 v144, s30, v42
	v_add_u32_e32 v148, s30, v43
	v_ashrrev_i32_e32 v149, 31, v148
	v_ashrrev_i32_e32 v145, 31, v144
	v_lshl_add_u64 v[150:151], v[144:145], 2, s[4:5]
	v_lshl_add_u64 v[152:153], v[148:149], 2, s[4:5]
	v_mad_i64_i32 v[144:145], s[6:7], v144, s25, v[46:47]
	v_mad_i64_i32 v[148:149], s[6:7], v148, s25, v[46:47]
	global_load_dword v150, v[150:151], off
	s_nop 0
	global_load_dword v151, v[152:153], off
	s_nop 0
	global_load_dword v144, v[144:145], off
	s_nop 0
	global_load_dword v145, v[148:149], off
	v_add_u32_e32 v148, s30, v44
	v_add_u32_e32 v152, s30, v45
	v_ashrrev_i32_e32 v153, 31, v152
	v_ashrrev_i32_e32 v149, 31, v148
	v_lshl_add_u64 v[154:155], v[148:149], 2, s[4:5]
	v_lshl_add_u64 v[156:157], v[152:153], 2, s[4:5]
	v_mad_i64_i32 v[148:149], s[4:5], v148, s25, v[46:47]
	global_load_dword v154, v[154:155], off
	s_nop 0
	global_load_dword v155, v[156:157], off
	v_mad_i64_i32 v[46:47], s[4:5], v152, s25, v[46:47]
	global_load_dword v148, v[148:149], off
	s_nop 0
	global_load_dword v149, v[46:47], off
	s_waitcnt vmcnt(60)
	v_mul_f32_e32 v46, v48, v50
	v_mul_f32_e32 v47, v49, v51
	v_add_u32_e32 v2, v98, v100
	v_add_u32_e32 v31, v98, v101
	ds_write_b32 v2, v46
	v_add_u32_e32 v2, v98, v102
	ds_write_b32 v31, v47
	s_waitcnt vmcnt(56)
	v_mul_f32_e32 v46, v52, v54
	v_mul_f32_e32 v47, v53, v55
	v_add_u32_e32 v31, v98, v103
	ds_write_b32 v2, v46
	ds_write_b32 v31, v47
	v_add_u32_e32 v2, v98, v104
	s_waitcnt vmcnt(52)
	v_mul_f32_e32 v46, v56, v58
	v_mul_f32_e32 v47, v57, v59
	v_add_u32_e32 v31, v98, v105
	v_add_u32_e32 v50, v98, v106
	v_add_u32_e32 v51, v98, v107
	s_waitcnt vmcnt(48)
	v_mul_f32_e32 v48, v60, v62
	v_mul_f32_e32 v49, v61, v63
	ds_write_b32 v2, v46
	ds_write_b32 v31, v47
	ds_write_b32 v50, v48
	ds_write_b32 v51, v49
	s_waitcnt vmcnt(44)
	v_mul_f32_e32 v46, v64, v66
	v_mul_f32_e32 v47, v65, v67
	v_add_u32_e32 v2, v98, v108
	ds_write_b32 v2, v46
	v_add_u32_e32 v2, v98, v109
	ds_write_b32 v2, v47
	s_waitcnt vmcnt(40)
	v_mul_f32_e32 v46, v68, v70
	v_mul_f32_e32 v47, v69, v71
	v_add_u32_e32 v2, v98, v110
	ds_write_b32 v2, v46
	v_add_u32_e32 v2, v98, v111
	ds_write_b32 v2, v47
	s_waitcnt vmcnt(36)
	v_mul_f32_e32 v46, v72, v74
	v_mul_f32_e32 v47, v73, v75
	v_add_u32_e32 v2, v98, v112
	ds_write_b32 v2, v46
	v_add_u32_e32 v2, v98, v113
	ds_write_b32 v2, v47
	s_waitcnt vmcnt(32)
	v_mul_f32_e32 v46, v76, v78
	v_mul_f32_e32 v47, v77, v79
	v_add_u32_e32 v2, v98, v114
	ds_write_b32 v2, v46
	v_add_u32_e32 v2, v98, v115
	ds_write_b32 v2, v47
	s_waitcnt vmcnt(28)
	v_mul_f32_e32 v46, v88, v80
	v_mul_f32_e32 v47, v89, v81
	v_add_u32_e32 v2, v98, v116
	ds_write_b32 v2, v46
	v_add_u32_e32 v2, v98, v117
	ds_write_b32 v2, v47
	s_waitcnt vmcnt(24)
	v_mul_f32_e32 v46, v86, v82
	v_mul_f32_e32 v47, v87, v83
	v_add_u32_e32 v2, v98, v118
	ds_write_b32 v2, v46
	v_add_u32_e32 v2, v98, v119
	ds_write_b32 v2, v47
	s_waitcnt vmcnt(20)
	v_mul_f32_e32 v46, v134, v84
	v_mul_f32_e32 v47, v135, v85
	v_add_u32_e32 v2, v98, v120
	ds_write_b32 v2, v46
	v_add_u32_e32 v2, v98, v121
	ds_write_b32 v2, v47
	s_waitcnt vmcnt(16)
	v_mul_f32_e32 v46, v138, v90
	v_mul_f32_e32 v47, v139, v91
	v_add_u32_e32 v2, v98, v122
	ds_write_b32 v2, v46
	v_add_u32_e32 v2, v98, v123
	ds_write_b32 v2, v47
	s_waitcnt vmcnt(12)
; #define GAS __attribute__((address_space(1)))
; #define LAS __attribute__((address_space(3)))
; #define LDS_WAIT() asm volatile("s_waitcnt lgkmcnt(0)" ::: "memory")
; __device__ __forceinline__ unsigned pk2(float lo, float hi) { return f2bf(lo) | (f2bf(hi) << 16); }
; template <bool HASK = false>
; __device__ __forceinline__ void cvt_item(const float* W, int N, int scol, const float* kscale, int k0, bf16_t* WT, int K, int drow0, LAS float* scr, int lane) {
;     ...
;         scr[kk * 33 + (lane & 31)] = v * ks; }
;     LDS_WAIT(); asm volatile("" ::: "memory");
;     const int c = lane & 7;
; #pragma unroll
;     for (int j = 0; j < 4; ++j) { const int n = (lane >> 3) + 8 * j; const LAS float* s = scr + (8 * c) * 33 + n;
;         u32x4 o; o.x = pk2(s[0 * 33], s[1 * 33]); o.y = pk2(s[2 * 33], s[3 * 33]); o.z = pk2(s[4 * 33], s[5 * 33]); o.w = pk2(s[6 * 33], s[7 * 33]);
;         *(GAS u32x4*)(WT + (size_t)(drow0 + n) * K + k0 + 8 * c) = o; }
;     LDS_WAIT(); asm volatile("" ::: "memory");
	v_mul_f32_e32 v46, v142, v136
	v_mul_f32_e32 v47, v143, v137
	v_add_u32_e32 v2, v98, v124
	ds_write_b32 v2, v46
	v_add_u32_e32 v2, v98, v125
	ds_write_b32 v2, v47
	s_waitcnt vmcnt(8)
	v_mul_f32_e32 v46, v146, v140
	v_mul_f32_e32 v47, v147, v141
	v_add_u32_e32 v2, v98, v126
	ds_write_b32 v2, v46
	v_add_u32_e32 v2, v98, v127
	ds_write_b32 v2, v47
	v_add_u32_e32 v2, v98, v128
	s_waitcnt vmcnt(4)
	v_mul_f32_e32 v46, v150, v144
	v_mul_f32_e32 v47, v151, v145
	ds_write_b32 v2, v46
	v_add_u32_e32 v2, v98, v129
	ds_write_b32 v2, v47
	v_add_u32_e32 v2, v98, v131
	v_add_u32_e32 v66, s29, v92
	s_lshl_b32 s10, s10, 7
	v_ashrrev_i32_e32 v67, 31, v66
	v_lshlrev_b64 v[66:67], 9, v[66:67]
	v_lshl_add_u64 v[68:69], v[10:11], 0, s[10:11]
	v_lshl_add_u64 v[66:67], v[68:69], 0, v[66:67]
	s_waitcnt vmcnt(0)
	v_mul_f32_e32 v46, v154, v148
	v_mul_f32_e32 v47, v155, v149
	ds_write_b32 v2, v46
	v_add_u32_e32 v2, v98, v133
	ds_write_b32 v2, v47
	s_waitcnt lgkmcnt(0)
	ds_read2_b32 v[50:51], v97 offset1:8
	ds_read2_b32 v[52:53], v97 offset0:33 offset1:41
	ds_read2_b32 v[54:55], v97 offset0:66 offset1:74
	ds_read2_b32 v[56:57], v97 offset0:99 offset1:107
	ds_read2_b32 v[58:59], v97 offset0:132 offset1:140
	s_waitcnt lgkmcnt(4)
	v_bfe_u32 v2, v50, 16, 1
	v_add3_u32 v2, v50, v2, s22
	s_waitcnt lgkmcnt(3)
	v_bfe_u32 v31, v52, 16, 1
	v_lshrrev_b32_e32 v2, 16, v2
	v_add3_u32 v31, v52, v31, s22
	ds_read2_b32 v[60:61], v97 offset0:165 offset1:173
	v_and_or_b32 v46, v31, s23, v2
	s_waitcnt lgkmcnt(3)
	v_bfe_u32 v2, v54, 16, 1
	v_add3_u32 v2, v54, v2, s22
	s_waitcnt lgkmcnt(2)
	v_bfe_u32 v31, v56, 16, 1
	ds_read2_b32 v[62:63], v97 offset0:198 offset1:206
	v_lshrrev_b32_e32 v2, 16, v2
	v_add3_u32 v31, v56, v31, s22
	ds_read2_b32 v[64:65], v97 offset0:231 offset1:239
	v_and_or_b32 v47, v31, s23, v2
	s_waitcnt lgkmcnt(3)
	v_bfe_u32 v2, v58, 16, 1
	v_add3_u32 v2, v58, v2, s22
	s_waitcnt lgkmcnt(2)
	v_bfe_u32 v31, v60, 16, 1
	v_lshrrev_b32_e32 v2, 16, v2
	v_add3_u32 v31, v60, v31, s22
	v_and_or_b32 v48, v31, s23, v2
	s_waitcnt lgkmcnt(1)
	v_bfe_u32 v2, v62, 16, 1
	v_add3_u32 v2, v62, v2, s22
	s_waitcnt lgkmcnt(0)
	v_bfe_u32 v31, v64, 16, 1
	v_lshrrev_b32_e32 v2, 16, v2
	v_add3_u32 v31, v64, v31, s22
	v_and_or_b32 v49, v31, s23, v2
	v_bfe_u32 v2, v51, 16, 1
	v_add3_u32 v2, v51, v2, s22
	v_bfe_u32 v31, v53, 16, 1
	global_store_dwordx4 v[66:67], v[46:49], off
	v_lshrrev_b32_e32 v2, 16, v2
	v_add3_u32 v31, v53, v31, s22
	v_bfe_u32 v46, v55, 16, 1
	v_add3_u32 v47, v55, v46, s22
	v_and_or_b32 v46, v31, s23, v2
	v_bfe_u32 v31, v57, 16, 1
	v_lshrrev_b32_e32 v2, 16, v47
	v_add3_u32 v31, v57, v31, s22
	v_and_or_b32 v47, v31, s23, v2
	v_bfe_u32 v2, v59, 16, 1
	v_add3_u32 v2, v59, v2, s22
	v_bfe_u32 v31, v61, 16, 1
	v_lshrrev_b32_e32 v2, 16, v2
	v_add3_u32 v31, v61, v31, s22
	v_and_or_b32 v48, v31, s23, v2
	v_bfe_u32 v2, v63, 16, 1
	v_add_u32_e32 v50, s29, v94
	v_add3_u32 v2, v63, v2, s22
	v_bfe_u32 v31, v65, 16, 1
	v_ashrrev_i32_e32 v51, 31, v50
	v_lshrrev_b32_e32 v2, 16, v2
	v_add3_u32 v31, v65, v31, s22
	v_lshlrev_b64 v[50:51], 9, v[50:51]
	v_and_or_b32 v49, v31, s23, v2
	ds_read2_b32 v[52:53], v97 offset0:16 offset1:24
	v_lshl_add_u64 v[50:51], v[68:69], 0, v[50:51]
	global_store_dwordx4 v[50:51], v[46:49], off
	ds_read2_b32 v[50:51], v97 offset0:49 offset1:57
	ds_read2_b32 v[54:55], v97 offset0:82 offset1:90
	ds_read2_b32 v[56:57], v97 offset0:115 offset1:123
	s_waitcnt lgkmcnt(3)
	v_bfe_u32 v2, v52, 16, 1
	v_add3_u32 v2, v52, v2, s22
	s_waitcnt lgkmcnt(2)
	v_bfe_u32 v31, v50, 16, 1
	ds_read2_b32 v[58:59], v97 offset0:148 offset1:156
	v_lshrrev_b32_e32 v2, 16, v2
	v_add3_u32 v31, v50, v31, s22
	ds_read2_b32 v[60:61], v97 offset0:181 offset1:189
	v_and_or_b32 v46, v31, s23, v2
	s_waitcnt lgkmcnt(3)
	v_bfe_u32 v2, v54, 16, 1
	v_add3_u32 v2, v54, v2, s22
	s_waitcnt lgkmcnt(2)
	v_bfe_u32 v31, v56, 16, 1
	ds_read2_b32 v[62:63], v97 offset0:214 offset1:222
	v_lshrrev_b32_e32 v2, 16, v2
	v_add3_u32 v31, v56, v31, s22
	ds_read2_b32 v[64:65], v97 offset0:247 offset1:255
	v_and_or_b32 v47, v31, s23, v2
	s_waitcnt lgkmcnt(3)
	v_bfe_u32 v2, v58, 16, 1
	v_add3_u32 v2, v58, v2, s22
	s_waitcnt lgkmcnt(2)
	v_bfe_u32 v31, v60, 16, 1
	v_lshrrev_b32_e32 v2, 16, v2
	v_add3_u32 v31, v60, v31, s22
	v_and_or_b32 v48, v31, s23, v2
	s_waitcnt lgkmcnt(1)
	v_bfe_u32 v2, v62, 16, 1
	v_add3_u32 v2, v62, v2, s22
	s_waitcnt lgkmcnt(0)
	v_bfe_u32 v31, v64, 16, 1
	v_add_u32_e32 v66, s29, v95
	v_lshrrev_b32_e32 v2, 16, v2
	v_add3_u32 v31, v64, v31, s22
	v_ashrrev_i32_e32 v67, 31, v66
	v_and_or_b32 v49, v31, s23, v2
	v_lshlrev_b64 v[66:67], 9, v[66:67]
	v_bfe_u32 v2, v53, 16, 1
	v_lshl_add_u64 v[66:67], v[68:69], 0, v[66:67]
	v_add3_u32 v2, v53, v2, s22
	v_bfe_u32 v31, v51, 16, 1
	global_store_dwordx4 v[66:67], v[46:49], off
	v_lshrrev_b32_e32 v2, 16, v2
	v_add3_u32 v31, v51, v31, s22
	v_bfe_u32 v46, v55, 16, 1
	v_add3_u32 v47, v55, v46, s22
	v_and_or_b32 v46, v31, s23, v2
	v_bfe_u32 v31, v57, 16, 1
	v_lshrrev_b32_e32 v2, 16, v47
	v_add3_u32 v31, v57, v31, s22
	v_and_or_b32 v47, v31, s23, v2
	v_bfe_u32 v2, v59, 16, 1
	v_add3_u32 v2, v59, v2, s22
	v_bfe_u32 v31, v61, 16, 1
	v_lshrrev_b32_e32 v2, 16, v2
	v_add3_u32 v31, v61, v31, s22
	v_and_or_b32 v48, v31, s23, v2
	v_bfe_u32 v2, v63, 16, 1
	v_add_u32_e32 v50, s29, v96
	v_add3_u32 v2, v63, v2, s22
	v_bfe_u32 v31, v65, 16, 1
	v_ashrrev_i32_e32 v51, 31, v50
	v_lshrrev_b32_e32 v2, 16, v2
	v_add3_u32 v31, v65, v31, s22
	v_lshlrev_b64 v[50:51], 9, v[50:51]
	v_and_or_b32 v49, v31, s23, v2
	v_lshl_add_u64 v[50:51], v[68:69], 0, v[50:51]
	global_store_dwordx4 v[50:51], v[46:49], off
	s_waitcnt lgkmcnt(0)

; __global__ void __launch_bounds__(512, 2) hymba_fwd(Args args) {
;     ...
;         for (int p = vcu; p < NPANEL; p += G) { const int b = p >> 5;
;             f32x4 av[4], sv[4];
; #pragma unroll
;             for (int j = 0; j < 4; ++j) { const int c0 = 4 * lane + 256 * j;
; #pragma unroll
;                 for (int q = 0; q < 4; ++q) { float sh = argp->in[3][c0 + q], scl = argp->in[3][1024 + c0 + q];
; #pragma unroll
;                     for (int kc = 0; kc < 8; ++kc) { sh += MODP[((size_t)kc * 8 + b) * 6144 + c0 + q]; scl += MODP[((size_t)kc * 8 + b) * 6144 + 1024 + c0 + q]; }
;                     av[j][q] = argp->in[4][c0 + q] * (1.0f + scl); sv[j][q] = sh; } }
.LBB0_157:
	s_ashr_i32 s4, s76, 5
	s_mul_hi_i32 s5, s4, 0x6000
	s_mulk_i32 s4, 0x6000
	s_add_u32 s4, s15, s4
	s_addc_u32 s5, s52, s5
	v_lshl_add_u64 v[116:117], v[98:99], 2, s[4:5]
	v_add_co_u32_e32 v8, vcc, s51, v116
	global_load_dwordx4 v[0:3], v[100:101], off
	global_load_dwordx4 v[4:7], v[116:117], off
	v_addc_co_u32_e32 v9, vcc, 0, v117, vcc
	v_add_co_u32_e32 v10, vcc, s61, v116
	global_load_dwordx4 v[28:31], v[102:103], off
	s_nop 0
	v_addc_co_u32_e32 v11, vcc, 0, v117, vcc
	v_add_co_u32_e32 v56, vcc, s63, v116
	v_lshl_add_u64 v[164:165], v[116:117], 0, s[26:27]
	s_nop 0
	v_addc_co_u32_e32 v57, vcc, 0, v117, vcc
	v_add_co_u32_e32 v12, vcc, s49, v116
	v_lshl_add_u64 v[118:119], v[116:117], 0, s[12:13]
	s_nop 0
	v_addc_co_u32_e32 v13, vcc, 0, v117, vcc
	global_load_dwordx4 v[32:35], v[12:13], off
	v_add_co_u32_e32 v58, vcc, s80, v116
	global_load_dwordx4 v[36:39], v[8:9], off
	global_load_dwordx4 v[40:43], v[10:11], off
	global_load_dwordx4 v[48:51], v[56:57], off
	v_addc_co_u32_e32 v59, vcc, 0, v117, vcc
	v_add_co_u32_e32 v60, vcc, s81, v116
	v_lshl_add_u64 v[166:167], v[116:117], 0, s[30:31]
	s_nop 0
	v_addc_co_u32_e32 v61, vcc, 0, v117, vcc
	v_add_co_u32_e32 v62, vcc, s82, v116
	global_load_dwordx4 v[44:47], v[58:59], off
	global_load_dwordx4 v[52:55], v[60:61], off
	v_addc_co_u32_e32 v63, vcc, 0, v117, vcc
	global_load_dwordx4 v[24:27], v[62:63], off
	v_add_co_u32_e32 v92, vcc, s83, v116
	v_lshl_add_u64 v[176:177], v[116:117], 0, s[36:37]
	s_nop 0
	v_addc_co_u32_e32 v93, vcc, 0, v117, vcc
	global_load_dwordx4 v[20:23], v[92:93], off
	global_load_dwordx4 v[16:19], v[104:105], off
	global_load_dwordx4 v[12:15], v[8:9], off offset:-4096
	s_nop 0
	global_load_dwordx4 v[8:11], v[10:11], off offset:-4096
	s_nop 0
	global_load_dwordx4 v[68:71], v[106:107], off
	global_load_dwordx4 v[88:91], v[118:119], off offset:1024
	global_load_dwordx4 v[80:83], v[56:57], off offset:-4096
	global_load_dwordx4 v[76:79], v[100:101], off offset:1024
	global_load_dwordx4 v[84:87], v[116:117], off offset:1024
	global_load_dwordx4 v[72:75], v[58:59], off offset:-4096
	global_load_dwordx4 v[64:67], v[60:61], off offset:-4096
	s_nop 0
	global_load_dwordx4 v[60:63], v[62:63], off offset:-4096
	s_nop 0
	global_load_dwordx4 v[56:59], v[92:93], off offset:-4096
	global_load_dwordx4 v[124:127], v[164:165], off offset:1024
	global_load_dwordx4 v[128:131], v[166:167], off offset:1024
	global_load_dwordx4 v[132:135], v[176:177], off offset:1024
	v_lshl_add_u64 v[184:185], v[116:117], 0, s[40:41]
	global_load_dwordx4 v[136:139], v[184:185], off offset:1024
	v_lshl_add_u64 v[188:189], v[116:117], 0, s[44:45]
	global_load_dwordx4 v[140:143], v[188:189], off offset:1024
	v_lshl_add_u64 v[192:193], v[116:117], 0, s[58:59]
	global_load_dwordx4 v[144:147], v[192:193], off offset:1024
	v_lshl_add_u64 v[168:169], v[116:117], 0, s[68:69]
	global_load_dwordx4 v[148:151], v[168:169], off offset:1024
	global_load_dwordx4 v[152:155], v[104:105], off offset:1024
	v_lshl_add_u64 v[196:197], v[116:117], 0, s[24:25]
	v_lshl_add_u64 v[212:213], v[116:117], 0, s[28:29]
	global_load_dwordx4 v[92:95], v[168:169], off offset:3072
	global_load_dwordx4 v[156:159], v[196:197], off offset:1024
	global_load_dwordx4 v[160:163], v[212:213], off offset:1024
	v_lshl_add_u64 v[224:225], v[116:117], 0, s[42:43]
	v_lshl_add_u64 v[228:229], v[116:117], 0, s[46:47]
	s_ashr_i32 s77, s76, 31
	s_lshl_b64 s[4:5], s[76:77], 8
	s_add_u32 s78, s4, s57
	s_addc_u32 s79, s5, 0
	s_lshl_b64 s[4:5], s[78:79], 12
	s_add_u32 s4, s10, s4
	s_addc_u32 s5, s11, s5
	s_mov_b32 s77, -3
	s_waitcnt vmcnt(32)
	v_add_f32_e32 v170, v0, v4
	v_add_f32_e32 v171, v1, v5
	v_add_f32_e32 v172, v2, v6
	v_add_f32_e32 v173, v3, v7
	s_waitcnt vmcnt(30)
	v_add_f32_e32 v0, v28, v32
	v_add_f32_e32 v1, v29, v33
	v_add_f32_e32 v2, v30, v34
	v_add_f32_e32 v3, v31, v35
	s_waitcnt vmcnt(29)
	v_add_f32_e32 v0, v0, v36
	v_add_f32_e32 v1, v1, v37
	v_add_f32_e32 v2, v2, v38
	v_add_f32_e32 v3, v3, v39
	s_waitcnt vmcnt(28)
	v_add_f32_e32 v0, v0, v40
	v_add_f32_e32 v1, v1, v41
	v_add_f32_e32 v2, v2, v42
	v_add_f32_e32 v3, v3, v43
	s_waitcnt vmcnt(27)
	v_add_f32_e32 v0, v0, v48
	v_add_f32_e32 v1, v1, v49
	v_add_f32_e32 v4, v2, v50
	v_add_f32_e32 v5, v3, v51
	v_lshl_add_u64 v[28:29], v[116:117], 0, s[34:35]
	s_waitcnt vmcnt(26)
	v_add_f32_e32 v6, v0, v44
	v_add_f32_e32 v7, v1, v45
	global_load_dwordx4 v[0:3], v[28:29], off offset:1024
	v_add_f32_e32 v4, v4, v46
	v_add_f32_e32 v5, v5, v47
	s_waitcnt vmcnt(26)
	v_add_f32_e32 v6, v6, v52
	v_add_f32_e32 v7, v7, v53
	v_lshl_add_u64 v[46:47], v[116:117], 0, s[38:39]
	v_add_f32_e32 v30, v4, v54
	v_add_f32_e32 v31, v5, v55
	s_waitcnt vmcnt(25)
	v_add_f32_e32 v32, v6, v24
	v_add_f32_e32 v33, v7, v25
	global_load_dwordx4 v[4:7], v[46:47], off offset:1024
	v_add_f32_e32 v34, v30, v26
	v_add_f32_e32 v35, v31, v27
	global_load_dwordx4 v[24:27], v[224:225], off offset:1024
	s_waitcnt vmcnt(26)
	v_add_f32_e32 v20, v32, v20
	v_add_f32_e32 v21, v33, v21
	global_load_dwordx4 v[30:33], v[228:229], off offset:1024
	s_waitcnt vmcnt(25)
	v_add_f32_e32 v12, v170, v12
	v_add_f32_e32 v13, v171, v13
	v_add_f32_e32 v14, v172, v14
	v_add_f32_e32 v15, v173, v15
	s_waitcnt vmcnt(24)
	v_add_f32_e32 v8, v12, v8
	v_add_f32_e32 v9, v13, v9
	v_add_f32_e32 v10, v14, v10
	v_add_f32_e32 v11, v15, v11
	s_waitcnt vmcnt(21)
	v_add_f32_e32 v8, v8, v80
	v_add_f32_e32 v9, v9, v81
	v_add_f32_e32 v12, v68, v88
	v_add_f32_e32 v13, v69, v89
	s_waitcnt vmcnt(18)
	v_add_f32_e32 v8, v8, v72
	v_add_f32_e32 v9, v9, v73
	v_add_f32_e32 v10, v10, v82
	v_add_f32_e32 v11, v11, v83
	s_waitcnt vmcnt(17)
; #define P1_LD(bi, r) do { const GAS f32x4* xr_ = (const GAS f32x4*)(XIN + ((size_t)p * 256 + wave * 32 + (r)) * DM) + lane; _Pragma("unroll") for (int j = 0; j < 4; ++j) xq[bi][j] = xr_[64 * j]; } while (0)
; __global__ void __launch_bounds__(512, 2) hymba_fwd(Args args) {
;     ...
;             for (int j = 0; j < 4; ++j) { const int c0 = 4 * lane + 256 * j;
; #pragma unroll
;                 for (int q = 0; q < 4; ++q) { float sh = argp->in[3][c0 + q], scl = argp->in[3][1024 + c0 + q];
; #pragma unroll
;                     for (int kc = 0; kc < 8; ++kc) { sh += MODP[((size_t)kc * 8 + b) * 6144 + c0 + q]; scl += MODP[((size_t)kc * 8 + b) * 6144 + 1024 + c0 + q]; }
;                     av[j][q] = argp->in[4][c0 + q] * (1.0f + scl); sv[j][q] = sh; } }
;             f32x4 xq[3][4];
;     ...
;             P1_LD(0, 0); P1_LD(1, 1); asm volatile("" ::: "memory");
	v_add_f32_e32 v8, v8, v64
	v_add_f32_e32 v9, v9, v65
	v_add_f32_e32 v22, v34, v22
	v_add_f32_e32 v23, v35, v23
	s_waitcnt vmcnt(16)
	v_add_f32_e32 v8, v8, v60
	v_add_f32_e32 v9, v9, v61
	global_load_dwordx4 v[34:37], v[108:109], off
	global_load_dwordx4 v[38:41], v[118:119], off offset:2048
	s_waitcnt vmcnt(17)
	v_add_f32_e32 v52, v8, v56
	v_add_f32_e32 v53, v9, v57
	s_waitcnt vmcnt(16)
	v_add_f32_e32 v8, v12, v124
	v_add_f32_e32 v9, v13, v125
	v_lshl_add_u64 v[12:13], v[116:117], 0, s[66:67]
	v_add_f32_e32 v10, v10, v74
	v_add_f32_e32 v11, v11, v75
	global_load_dwordx4 v[72:75], v[12:13], off offset:1024
	v_add_f32_e32 v10, v10, v66
	v_add_f32_e32 v11, v11, v67
	global_load_dwordx4 v[42:45], v[164:165], off offset:2048
	v_add_f32_e32 v10, v10, v62
	v_add_f32_e32 v11, v11, v63
	global_load_dwordx4 v[62:65], v[166:167], off offset:2048
	v_add_f32_e32 v22, 1.0, v22
	v_add_f32_e32 v23, 1.0, v23
	v_add_f32_e32 v20, 1.0, v20
	v_add_f32_e32 v21, 1.0, v21
	v_add_f32_e32 v14, v70, v90
	v_add_f32_e32 v15, v71, v91
	global_load_dwordx4 v[68:71], v[176:177], off offset:2048
	global_load_dwordx4 v[88:91], v[168:169], off offset:2048
	v_mul_f32_e32 v50, v22, v18
	v_mul_f32_e32 v51, v23, v19
	v_mul_f32_e32 v48, v20, v16
	v_mul_f32_e32 v49, v21, v17
	v_add_f32_e32 v16, v76, v84
	v_add_f32_e32 v17, v77, v85
	v_add_f32_e32 v18, v78, v86
	v_add_f32_e32 v19, v79, v87
	v_add_f32_e32 v54, v10, v58
	v_add_f32_e32 v55, v11, v59
	v_add_f32_e32 v10, v14, v126
	v_add_f32_e32 v11, v15, v127
	global_load_dwordx4 v[76:79], v[184:185], off offset:2048
	global_load_dwordx4 v[80:83], v[188:189], off offset:2048
	s_waitcnt vmcnt(22)
	v_add_f32_e32 v8, v8, v128
	v_add_f32_e32 v9, v9, v129
	v_add_f32_e32 v10, v10, v130
	v_add_f32_e32 v11, v11, v131
	s_waitcnt vmcnt(21)
	v_add_f32_e32 v8, v8, v132
	v_add_f32_e32 v9, v9, v133
	v_add_f32_e32 v10, v10, v134
	v_add_f32_e32 v11, v11, v135
	global_load_dwordx4 v[84:87], v[192:193], off offset:2048
	s_waitcnt vmcnt(21)
	v_add_f32_e32 v8, v8, v136
	v_add_f32_e32 v9, v9, v137
	v_add_f32_e32 v10, v10, v138
	v_add_f32_e32 v11, v11, v139
	s_waitcnt vmcnt(20)
	v_add_f32_e32 v8, v8, v140
	v_add_f32_e32 v9, v9, v141
	v_add_f32_e32 v10, v10, v142
	v_add_f32_e32 v11, v11, v143
	s_waitcnt vmcnt(19)
	v_add_f32_e32 v8, v8, v144
	v_add_f32_e32 v9, v9, v145
	v_add_f32_e32 v10, v10, v146
	v_add_f32_e32 v11, v11, v147
	global_load_dwordx4 v[124:127], v[118:119], off offset:3072
	global_load_dwordx4 v[128:131], v[104:105], off offset:2048
	global_load_dwordx4 v[132:135], v[100:101], off offset:2048
	global_load_dwordx4 v[136:139], v[116:117], off offset:2048
	s_waitcnt vmcnt(22)
	v_add_f32_e32 v8, v8, v148
	v_add_f32_e32 v9, v9, v149
	v_add_f32_e32 v10, v10, v150
	v_add_f32_e32 v11, v11, v151
	v_add_f32_e32 v8, 1.0, v8
	v_add_f32_e32 v9, 1.0, v9
	v_add_f32_e32 v10, 1.0, v10
	v_add_f32_e32 v11, 1.0, v11
	global_load_dwordx4 v[140:143], v[196:197], off offset:2048
	global_load_dwordx4 v[144:147], v[164:165], off offset:3072
	global_load_dwordx4 v[148:151], v[212:213], off offset:2048
	s_waitcnt vmcnt(24)
	v_mul_f32_e32 v58, v10, v154
	v_mul_f32_e32 v59, v11, v155
	v_mul_f32_e32 v56, v8, v152
	v_mul_f32_e32 v57, v9, v153
	global_load_dwordx4 v[152:155], v[28:29], off offset:2048
	s_waitcnt vmcnt(23)
	v_add_f32_e32 v8, v16, v156
	v_add_f32_e32 v9, v17, v157
	v_add_f32_e32 v10, v18, v158
	v_add_f32_e32 v11, v19, v159
	s_waitcnt vmcnt(22)
	v_add_f32_e32 v8, v8, v160
	v_add_f32_e32 v9, v9, v161
	v_add_f32_e32 v10, v10, v162
	v_add_f32_e32 v11, v11, v163
	global_load_dwordx4 v[156:159], v[46:47], off offset:2048
	global_load_dwordx4 v[160:163], v[166:167], off offset:3072
	s_nop 0
	global_load_dwordx4 v[164:167], v[224:225], off offset:2048
	global_load_dwordx4 v[168:171], v[228:229], off offset:2048
	global_load_dwordx4 v[172:175], v[12:13], off offset:2048
	s_nop 0
	global_load_dwordx4 v[176:179], v[176:177], off offset:3072
	s_nop 0
	global_load_dwordx4 v[180:183], v[110:111], off
	s_waitcnt vmcnt(28)
	v_add_f32_e32 v0, v8, v0
	v_add_f32_e32 v1, v9, v1
	global_load_dwordx4 v[184:187], v[184:185], off offset:3072
	v_add_f32_e32 v2, v10, v2
	v_add_f32_e32 v3, v11, v3
	global_load_dwordx4 v[188:191], v[188:189], off offset:3072
	s_nop 0
	global_load_dwordx4 v[192:195], v[192:193], off offset:3072
	s_nop 0
	global_load_dwordx4 v[200:203], v[104:105], off offset:3072
	global_load_dwordx4 v[204:207], v[100:101], off offset:3072
	s_nop 0
	global_load_dwordx4 v[116:119], v[116:117], off offset:3072
	s_nop 0
	global_load_dwordx4 v[208:211], v[196:197], off offset:3072
	s_nop 0
	global_load_dwordx4 v[212:215], v[212:213], off offset:3072
	s_nop 0
	global_load_dwordx4 v[216:219], v[28:29], off offset:3072
	global_load_dwordx4 v[220:223], v[46:47], off offset:3072
	s_nop 0
	global_load_dwordx4 v[224:227], v[224:225], off offset:3072
	s_nop 0
	global_load_dwordx4 v[228:231], v[228:229], off offset:3072
	s_nop 0
	global_load_dwordx4 v[232:235], v[12:13], off offset:3072
	s_waitcnt vmcnt(40)
	v_add_f32_e32 v0, v0, v4
	v_add_f32_e32 v1, v1, v5
	v_add_f32_e32 v2, v2, v6
	v_add_f32_e32 v3, v3, v7
	s_waitcnt vmcnt(39)
	v_add_f32_e32 v0, v0, v24
	v_add_f32_e32 v1, v1, v25
	v_add_f32_e32 v60, v2, v26
	v_add_f32_e32 v61, v3, v27
	s_waitcnt vmcnt(38)
	v_add_f32_e32 v66, v0, v30
	v_add_f32_e32 v67, v1, v31
	v_lshl_add_u64 v[0:1], v[96:97], 4, s[4:5]
	global_load_dwordx4 v[28:31], v[0:1], off
	global_load_dwordx4 v[24:27], v[0:1], off offset:1024
	global_load_dwordx4 v[20:23], v[0:1], off offset:2048
	global_load_dwordx4 v[16:19], v[0:1], off offset:3072
	v_lshl_add_u64 v[2:3], v[0:1], 0, s[12:13]
	v_add_co_u32_e32 v0, vcc, 0x1000, v0
	v_add_f32_e32 v32, v60, v32
	v_add_f32_e32 v33, v61, v33
	s_nop 0
	v_addc_co_u32_e32 v1, vcc, 0, v1, vcc
	global_load_dwordx4 v[8:11], v[2:3], off offset:1024
	global_load_dwordx4 v[4:7], v[2:3], off offset:2048
	global_load_dwordx4 v[12:15], v[0:1], off
	s_nop 0
	global_load_dwordx4 v[0:3], v[2:3], off offset:3072
	s_waitcnt vmcnt(43)
; __global__ void __launch_bounds__(512, 2) hymba_fwd(Args args) {
;     ...
;                 for (int q = 0; q < 4; ++q) { float sh = argp->in[3][c0 + q], scl = argp->in[3][1024 + c0 + q];
; #pragma unroll
;                     for (int kc = 0; kc < 8; ++kc) { sh += MODP[((size_t)kc * 8 + b) * 6144 + c0 + q]; scl += MODP[((size_t)kc * 8 + b) * 6144 + 1024 + c0 + q]; }
;                     av[j][q] = argp->in[4][c0 + q] * (1.0f + scl); sv[j][q] = sh; } }
	v_add_f32_e32 v60, v66, v72
	v_add_f32_e32 v61, v67, v73
	v_add_f32_e32 v66, v32, v74
	v_add_f32_e32 v67, v33, v75
	v_add_f32_e32 v32, v34, v38
	v_add_f32_e32 v33, v35, v39
	v_add_f32_e32 v34, v36, v40
	v_add_f32_e32 v35, v37, v41
	s_waitcnt vmcnt(42)
	v_add_f32_e32 v32, v32, v42
	v_add_f32_e32 v33, v33, v43
	v_add_f32_e32 v34, v34, v44
	v_add_f32_e32 v35, v35, v45
	s_waitcnt vmcnt(41)
	v_add_f32_e32 v32, v32, v62
	v_add_f32_e32 v33, v33, v63
	v_add_f32_e32 v34, v34, v64
	v_add_f32_e32 v35, v35, v65
	s_waitcnt vmcnt(40)
	v_add_f32_e32 v32, v32, v68
	v_add_f32_e32 v33, v33, v69
	v_add_f32_e32 v34, v34, v70
	v_add_f32_e32 v35, v35, v71
	s_waitcnt vmcnt(38)
	v_add_f32_e32 v32, v32, v76
	v_add_f32_e32 v33, v33, v77
	v_add_f32_e32 v34, v34, v78
	v_add_f32_e32 v35, v35, v79
	s_waitcnt vmcnt(37)
	v_add_f32_e32 v32, v32, v80
	v_add_f32_e32 v33, v33, v81
	v_add_f32_e32 v34, v34, v82
	v_add_f32_e32 v35, v35, v83
	v_mov_b64_e32 v[80:81], v[114:115]
	v_mov_b64_e32 v[82:83], v[112:113]
	s_waitcnt vmcnt(36)
	v_add_f32_e32 v32, v32, v84
	v_add_f32_e32 v33, v33, v85
	v_add_f32_e32 v34, v34, v86
	v_add_f32_e32 v35, v35, v87
	v_add_f32_e32 v32, v32, v88
	v_add_f32_e32 v33, v33, v89
	v_add_f32_e32 v34, v34, v90
	v_add_f32_e32 v35, v35, v91
	v_add_f32_e32 v32, 1.0, v32
	v_add_f32_e32 v33, 1.0, v33
	v_add_f32_e32 v34, 1.0, v34
	v_add_f32_e32 v35, 1.0, v35
	s_waitcnt vmcnt(34)
	v_mul_f32_e32 v62, v32, v128
	v_mul_f32_e32 v63, v33, v129
	v_mul_f32_e32 v64, v34, v130
	v_mul_f32_e32 v65, v35, v131
	s_waitcnt vmcnt(32)
	v_add_f32_e32 v32, v132, v136
	v_add_f32_e32 v33, v133, v137
	v_add_f32_e32 v34, v134, v138
	v_add_f32_e32 v35, v135, v139
	s_waitcnt vmcnt(31)
	v_add_f32_e32 v32, v32, v140
	v_add_f32_e32 v33, v33, v141
	v_add_f32_e32 v34, v34, v142
	v_add_f32_e32 v35, v35, v143
	s_waitcnt vmcnt(29)
	v_add_f32_e32 v32, v32, v148
	v_add_f32_e32 v33, v33, v149
	v_add_f32_e32 v34, v34, v150
	v_add_f32_e32 v35, v35, v151
	s_waitcnt vmcnt(28)
	v_add_f32_e32 v32, v32, v152
	v_add_f32_e32 v33, v33, v153
	v_add_f32_e32 v34, v34, v154
	v_add_f32_e32 v35, v35, v155
	s_waitcnt vmcnt(27)
	v_add_f32_e32 v32, v32, v156
	v_add_f32_e32 v33, v33, v157
	v_add_f32_e32 v34, v34, v158
	v_add_f32_e32 v35, v35, v159
	s_waitcnt vmcnt(25)
	v_add_f32_e32 v32, v32, v164
	v_add_f32_e32 v33, v33, v165
	v_add_f32_e32 v34, v34, v166
	v_add_f32_e32 v35, v35, v167
	s_waitcnt vmcnt(24)
	v_add_f32_e32 v32, v32, v168
	v_add_f32_e32 v33, v33, v169
	v_add_f32_e32 v34, v34, v170
	v_add_f32_e32 v35, v35, v171
	s_waitcnt vmcnt(23)
	v_add_f32_e32 v70, v32, v172
	v_add_f32_e32 v71, v33, v173
	v_add_f32_e32 v74, v34, v174
	v_add_f32_e32 v75, v35, v175
	s_waitcnt vmcnt(21)
	v_add_f32_e32 v32, v180, v124
	v_add_f32_e32 v33, v181, v125
	v_add_f32_e32 v34, v182, v126
	v_add_f32_e32 v35, v183, v127
	v_add_f32_e32 v32, v32, v144
	v_add_f32_e32 v33, v33, v145
	v_add_f32_e32 v34, v34, v146
	v_add_f32_e32 v35, v35, v147
	v_add_f32_e32 v32, v32, v160
	v_add_f32_e32 v33, v33, v161
	v_add_f32_e32 v34, v34, v162
	v_add_f32_e32 v35, v35, v163
	v_add_f32_e32 v32, v32, v176
	v_add_f32_e32 v33, v33, v177
	v_add_f32_e32 v34, v34, v178
	v_add_f32_e32 v35, v35, v179
	s_waitcnt vmcnt(20)
	v_add_f32_e32 v32, v32, v184
	v_add_f32_e32 v33, v33, v185
	v_add_f32_e32 v34, v34, v186
	v_add_f32_e32 v35, v35, v187
	s_waitcnt vmcnt(19)
	v_add_f32_e32 v32, v32, v188
	v_add_f32_e32 v33, v33, v189
	v_add_f32_e32 v34, v34, v190
	v_add_f32_e32 v35, v35, v191
	s_waitcnt vmcnt(18)
	v_add_f32_e32 v32, v32, v192
	v_add_f32_e32 v33, v33, v193
	v_add_f32_e32 v34, v34, v194
	v_add_f32_e32 v35, v35, v195
	v_add_f32_e32 v32, v32, v92
	v_add_f32_e32 v33, v33, v93
	v_add_f32_e32 v34, v34, v94
	v_add_f32_e32 v35, v35, v95
	v_add_f32_e32 v32, 1.0, v32
	v_add_f32_e32 v33, 1.0, v33
	v_add_f32_e32 v34, 1.0, v34
	v_add_f32_e32 v35, 1.0, v35
	s_waitcnt vmcnt(17)
	v_mul_f32_e32 v68, v32, v200
	v_mul_f32_e32 v69, v33, v201
	v_mul_f32_e32 v72, v34, v202
	v_mul_f32_e32 v73, v35, v203
	s_waitcnt vmcnt(15)
	v_add_f32_e32 v32, v204, v116
	v_add_f32_e32 v33, v205, v117
	v_add_f32_e32 v34, v206, v118
	v_add_f32_e32 v35, v207, v119
	s_waitcnt vmcnt(14)
	v_add_f32_e32 v32, v32, v208
	v_add_f32_e32 v33, v33, v209
	v_add_f32_e32 v34, v34, v210
	v_add_f32_e32 v35, v35, v211
	s_waitcnt vmcnt(13)
	v_add_f32_e32 v32, v32, v212
	v_add_f32_e32 v33, v33, v213
	v_add_f32_e32 v34, v34, v214
	v_add_f32_e32 v35, v35, v215
	s_waitcnt vmcnt(12)
	v_add_f32_e32 v32, v32, v216
	v_add_f32_e32 v33, v33, v217
	v_add_f32_e32 v34, v34, v218
	v_add_f32_e32 v35, v35, v219
	s_waitcnt vmcnt(11)
	v_add_f32_e32 v32, v32, v220
	v_add_f32_e32 v33, v33, v221
	v_add_f32_e32 v34, v34, v222
	v_add_f32_e32 v35, v35, v223
	s_waitcnt vmcnt(10)
	v_add_f32_e32 v32, v32, v224
	v_add_f32_e32 v33, v33, v225
	v_add_f32_e32 v34, v34, v226
	v_add_f32_e32 v35, v35, v227
	s_waitcnt vmcnt(9)
	v_add_f32_e32 v32, v32, v228
	v_add_f32_e32 v33, v33, v229
	v_add_f32_e32 v34, v34, v230
	v_add_f32_e32 v35, v35, v231
	s_waitcnt vmcnt(8)
	v_add_f32_e32 v76, v32, v232
	v_add_f32_e32 v77, v33, v233
	v_add_f32_e32 v78, v34, v234
	v_add_f32_e32 v79, v35, v235
; #define P1_LD(bi, r) do { const GAS f32x4* xr_ = (const GAS f32x4*)(XIN + ((size_t)p * 256 + wave * 32 + (r)) * DM) + lane; _Pragma("unroll") for (int j = 0; j < 4; ++j) xq[bi][j] = xr_[64 * j]; } while (0)
; __global__ void __launch_bounds__(512, 2) hymba_fwd(Args args) {
;     ...
;             P1_LD(0, 0); P1_LD(1, 1); asm volatile("" ::: "memory");
; #pragma nounroll
;             for (int rr = 0; rr < 30; rr += 3) {
;                 P1_LD(2, rr + 2); asm volatile("" ::: "memory"); P1_ST(0, rr); asm volatile("" ::: "memory");
;                 P1_LD(0, rr + 3); asm volatile("" ::: "memory"); P1_ST(1, rr + 1); asm volatile("" ::: "memory");
;                 P1_LD(1, rr + 4); asm volatile("" ::: "memory"); P1_ST(2, rr + 2); asm volatile("" ::: "memory"); }
.LBB0_158:
	v_add_co_u32_e32 v32, vcc, 0xffffe000, v82
	v_and_b32_e32 v39, 64, v122
	v_xor_b32_e32 v124, 1, v122
	v_addc_co_u32_e32 v33, vcc, -1, v83, vcc
	v_add_u32_e32 v150, 64, v39
	s_waitcnt vmcnt(4)
	v_mul_f32_e32 v117, v16, v16
	v_mul_f32_e32 v38, v21, v21
	v_xor_b32_e32 v125, 2, v122
	s_waitcnt vmcnt(2)
	v_mul_f32_e32 v116, v7, v7
	v_cmp_lt_i32_e32 vcc, v124, v150
	v_mul_f32_e32 v119, v18, v18
	v_mul_f32_e32 v40, v23, v23
	v_xor_b32_e32 v126, 4, v122
	v_fma_f32 v134, v20, v20, v38
	v_fma_f32 v135, v21, v21, v38
	v_fma_f32 v144, v6, v6, v116
	v_fma_f32 v145, v7, v7, v116
	v_cndmask_b32_e32 v116, v122, v124, vcc
	v_cmp_lt_i32_e32 vcc, v125, v150
	v_mul_f32_e32 v36, v26, v26
	v_mul_f32_e32 v37, v27, v27
	v_mul_f32_e32 v90, v24, v24
	v_mul_f32_e32 v91, v25, v25
	v_mul_f32_e32 v123, v19, v19
	v_xor_b32_e32 v127, 8, v122
	v_fma_f32 v136, v22, v22, v40
	v_fma_f32 v137, v23, v23, v40
	v_mov_b32_e32 v135, v119
	v_cndmask_b32_e32 v119, v122, v125, vcc
	v_cmp_lt_i32_e32 vcc, v126, v150
	v_mul_f32_e32 v34, v30, v30
	v_mul_f32_e32 v35, v31, v31
	v_mul_f32_e32 v88, v28, v28
	v_mul_f32_e32 v89, v29, v29
	v_xor_b32_e32 v128, 16, v122
	v_pk_mov_b32 v[132:133], v[90:91], v[36:37] op_sel:[1,0]
	v_mov_b32_e32 v91, v37
	v_mov_b32_e32 v137, v123
	v_cndmask_b32_e32 v123, v122, v126, vcc
	v_cmp_lt_i32_e32 vcc, v127, v150
	v_xor_b32_e32 v129, 32, v122
	s_waitcnt vmcnt(1)
	v_mul_f32_e32 v42, v14, v14
	v_mul_f32_e32 v43, v15, v15
	v_mul_f32_e32 v92, v12, v12
	v_mul_f32_e32 v93, v13, v13
	v_mul_f32_e32 v44, v10, v10
	v_mul_f32_e32 v45, v11, v11
	v_mul_f32_e32 v94, v8, v8
	v_mul_f32_e32 v95, v9, v9
	v_pk_mov_b32 v[130:131], v[88:89], v[34:35] op_sel:[1,0]
	v_mov_b32_e32 v89, v35
	v_add_f32_e32 v90, v132, v90
	v_add_f32_e32 v91, v133, v91
	v_cndmask_b32_e32 v132, v122, v127, vcc
	v_cmp_lt_i32_e32 vcc, v128, v150
	v_pk_mov_b32 v[138:139], v[92:93], v[42:43] op_sel:[1,0]
	v_mov_b32_e32 v93, v43
	v_pk_mov_b32 v[140:141], v[94:95], v[44:45] op_sel:[1,0]
	v_mov_b32_e32 v95, v45
	v_add_f32_e32 v88, v130, v88
	v_add_f32_e32 v89, v131, v89
	v_cndmask_b32_e32 v133, v122, v128, vcc
	v_cmp_lt_i32_e32 vcc, v129, v150
	v_mul_f32_e32 v118, v17, v17
	v_mul_f32_e32 v46, v5, v5
	v_cndmask_b32_e32 v150, v122, v129, vcc
	v_add_f32_e32 v124, v138, v92
	v_add_f32_e32 v125, v139, v93
	v_add_f32_e32 v94, v140, v94
	v_add_f32_e32 v95, v141, v95
	v_add_f32_e32 v126, v88, v89
	v_add_f32_e32 v127, v89, v88
	v_add_f32_e32 v128, v90, v91
	v_add_f32_e32 v129, v91, v90
	s_waitcnt vmcnt(0)
	v_mul_f32_e32 v146, v0, v0
	v_mul_f32_e32 v147, v1, v1
	v_mul_f32_e32 v148, v2, v2
	v_mul_f32_e32 v149, v3, v3
	v_fma_f32 v142, v4, v4, v46
	v_fma_f32 v143, v5, v5, v46
	global_load_dwordx4 v[44:47], v[32:33], off offset:-3072
	global_load_dwordx4 v[40:43], v[32:33], off offset:-2048
	global_load_dwordx4 v[36:39], v[32:33], off offset:-1024
	s_nop 0
	global_load_dwordx4 v[32:35], v[32:33], off
	v_pk_add_f32 v[124:125], v[124:125], v[124:125] op_sel:[0,1] op_sel_hi:[1,0]
	v_pk_add_f32 v[94:95], v[94:95], v[94:95] op_sel:[0,1] op_sel_hi:[1,0]
	v_mov_b32_e32 v127, v117
	v_mov_b32_e32 v129, v118
	v_mov_b32_e32 v143, v148
	v_mov_b32_e32 v145, v149
	v_add_f32_e32 v130, v134, v136
	v_add_f32_e32 v131, v135, v137
	v_lshlrev_b32_e32 v93, 2, v116
	v_mov_b32_e32 v125, v146
	v_mov_b32_e32 v95, v147
	v_add_f32_e32 v116, v126, v128
	v_add_f32_e32 v117, v127, v129
	v_lshlrev_b32_e32 v90, 2, v132
	v_lshlrev_b32_e32 v89, 2, v133
	v_add_f32_e32 v132, v142, v144
	v_add_f32_e32 v133, v143, v145
	v_add_f32_e32 v94, v124, v94
	v_add_f32_e32 v95, v125, v95
	v_add_f32_e32 v116, v116, v130
	v_add_f32_e32 v117, v117, v131
	v_add_f32_e32 v94, v94, v132
	v_add_f32_e32 v95, v95, v133
	v_add_f32_e32 v116, v116, v117
	v_add_f32_e32 v94, v94, v95
	ds_bpermute_b32 v95, v93, v116
	ds_bpermute_b32 v117, v93, v94
	v_lshlrev_b32_e32 v92, 2, v119
	v_lshlrev_b32_e32 v91, 2, v123
	v_lshlrev_b32_e32 v88, 2, v150
	s_waitcnt lgkmcnt(1)
	v_add_f32_e32 v95, v116, v95
	s_waitcnt lgkmcnt(0)
	v_add_f32_e32 v94, v94, v117
	ds_bpermute_b32 v116, v92, v95
	ds_bpermute_b32 v117, v92, v94
	v_add_co_u32_e64 v84, s[4:5], s87, v80
	s_waitcnt lgkmcnt(1)
	v_add_f32_e32 v95, v95, v116
	s_waitcnt lgkmcnt(0)
	v_add_f32_e32 v94, v94, v117
	ds_bpermute_b32 v116, v91, v95
	ds_bpermute_b32 v117, v91, v94
	v_addc_co_u32_e64 v85, s[4:5], -1, v81, s[4:5]
	v_add_co_u32_e64 v86, s[4:5], s87, v82
	s_waitcnt lgkmcnt(1)
	v_add_f32_e32 v95, v95, v116
	s_waitcnt lgkmcnt(0)
	v_add_f32_e32 v94, v94, v117
	ds_bpermute_b32 v116, v90, v95
	ds_bpermute_b32 v117, v90, v94
	v_addc_co_u32_e64 v87, s[4:5], -1, v83, s[4:5]
	s_add_i32 s77, s77, 3
	s_waitcnt lgkmcnt(1)
	v_add_f32_e32 v95, v95, v116
	s_waitcnt lgkmcnt(0)
	v_add_f32_e32 v94, v94, v117
	ds_bpermute_b32 v116, v89, v95
	ds_bpermute_b32 v117, v89, v94
	s_cmp_lt_u32 s77, 27
	s_waitcnt lgkmcnt(1)
	v_add_f32_e32 v95, v95, v116
	s_waitcnt lgkmcnt(0)
	v_add_f32_e32 v94, v94, v117
	ds_bpermute_b32 v116, v88, v95
	ds_bpermute_b32 v117, v88, v94
	s_waitcnt lgkmcnt(1)
	v_add_f32_e32 v95, v95, v116
	s_waitcnt lgkmcnt(0)
	v_add_f32_e32 v94, v94, v117
	v_fmamk_f32 v95, v95, 0x3a800000, v120
	v_fmamk_f32 v94, v94, 0x3a800000, v120
	v_mul_f32_e32 v116, 0x4f800000, v95
	v_cmp_gt_f32_e64 s[4:5], s84, v95
	v_mul_f32_e32 v117, 0x4f800000, v94
	v_cmp_gt_f32_e32 vcc, s84, v94
	v_cndmask_b32_e64 v95, v95, v116, s[4:5]
	v_sqrt_f32_e32 v116, v95
	v_cndmask_b32_e32 v94, v94, v117, vcc
	v_sqrt_f32_e32 v117, v94
	v_add_u32_e32 v118, -1, v116
	v_add_u32_e32 v119, 1, v116
	v_add_u32_e32 v123, -1, v117
	v_fma_f32 v125, -v118, v116, v95
	v_add_u32_e32 v124, 1, v117
	v_fma_f32 v126, -v119, v116, v95
	v_fma_f32 v127, -v123, v117, v94
	v_cmp_ge_f32_e64 s[6:7], 0, v125
	v_fma_f32 v128, -v124, v117, v94
	v_cmp_lt_f32_e64 s[8:9], 0, v126
	v_cndmask_b32_e64 v116, v116, v118, s[6:7]
	v_cmp_ge_f32_e64 s[6:7], 0, v127
	v_cndmask_b32_e64 v116, v116, v119, s[8:9]
	v_mul_f32_e32 v118, 0x37800000, v116
	v_cndmask_b32_e64 v117, v117, v123, s[6:7]
	v_cmp_lt_f32_e64 s[6:7], 0, v128
	v_cndmask_b32_e64 v116, v116, v118, s[4:5]
	v_cmp_class_f32_e64 s[4:5], v95, v121
	v_cndmask_b32_e64 v117, v117, v124, s[6:7]
	v_mul_f32_e32 v119, 0x37800000, v117
	v_cndmask_b32_e32 v117, v117, v119, vcc
	v_cmp_class_f32_e32 vcc, v94, v121
	v_cndmask_b32_e64 v95, v116, v95, s[4:5]
	s_nop 0
	v_cndmask_b32_e32 v116, v117, v94, vcc
	v_div_scale_f32 v94, s[4:5], v95, v95, 1.0
	v_div_scale_f32 v118, s[4:5], v116, v116, 1.0
	v_rcp_f32_e32 v123, v94
	v_rcp_f32_e32 v124, v118
	v_div_scale_f32 v117, vcc, 1.0, v95, 1.0
	v_fma_f32 v125, -v94, v123, 1.0
	v_fma_f32 v126, -v118, v124, 1.0
	v_fmac_f32_e32 v123, v125, v123
	v_div_scale_f32 v119, s[4:5], 1.0, v116, 1.0
	v_fmac_f32_e32 v124, v126, v124
	v_mul_f32_e32 v125, v117, v123
	v_mul_f32_e32 v126, v119, v124
	v_fma_f32 v127, -v94, v125, v117
	v_fma_f32 v128, -v118, v126, v119
	v_fmac_f32_e32 v125, v127, v123
	v_fmac_f32_e32 v126, v128, v124
	v_fma_f32 v94, -v94, v125, v117
	v_fma_f32 v117, -v118, v126, v119
	v_div_fmas_f32 v94, v94, v123, v125
	s_mov_b64 vcc, s[4:5]
	v_div_fixup_f32 v94, v94, v95, 1.0
	v_div_fmas_f32 v95, v117, v124, v126
	v_mul_f32_e32 v28, v94, v28
	v_mul_f32_e32 v29, v94, v29
	v_mul_f32_e32 v30, v94, v30
	v_mul_f32_e32 v31, v94, v31
	v_mul_f32_e32 v24, v94, v24
	v_mul_f32_e32 v25, v94, v25
	v_mul_f32_e32 v26, v94, v26
	v_mul_f32_e32 v27, v94, v27
	v_mul_f32_e32 v20, v94, v20
	v_mul_f32_e32 v21, v94, v21
	v_mul_f32_e32 v22, v94, v22
	v_mul_f32_e32 v23, v94, v23
	v_mul_f32_e32 v16, v94, v16
	v_mul_f32_e32 v17, v94, v17
	v_mul_f32_e32 v18, v94, v18
	v_mul_f32_e32 v19, v94, v19
	v_div_fixup_f32 v94, v95, v116, 1.0
	v_fma_f32 v30, v30, v50, v54
	v_fma_f32 v31, v31, v51, v55
	v_fma_f32 v28, v28, v48, v52
	v_fma_f32 v29, v29, v49, v53
	v_fma_f32 v26, v26, v58, v66
	v_fma_f32 v27, v27, v59, v67
	v_fma_f32 v24, v24, v56, v60
	v_fma_f32 v25, v25, v57, v61
	v_fma_f32 v22, v22, v64, v74
	v_fma_f32 v23, v23, v65, v75
	v_fma_f32 v20, v20, v62, v70
	v_fma_f32 v21, v21, v63, v71
	v_fma_f32 v18, v18, v72, v78
	v_fma_f32 v19, v19, v73, v79
	v_fma_f32 v16, v16, v68, v76
	v_fma_f32 v17, v17, v69, v77
	v_mul_f32_e32 v12, v94, v12
	v_mul_f32_e32 v13, v94, v13
	v_mul_f32_e32 v14, v94, v14
	v_mul_f32_e32 v15, v94, v15
	v_mul_f32_e32 v8, v94, v8
	v_mul_f32_e32 v9, v94, v9
	v_mul_f32_e32 v10, v94, v10
	v_mul_f32_e32 v11, v94, v11
	v_mul_f32_e32 v4, v94, v4
	v_mul_f32_e32 v5, v94, v5
	v_mul_f32_e32 v6, v94, v6
	v_mul_f32_e32 v7, v94, v7
	v_mul_f32_e32 v0, v94, v0
	v_mul_f32_e32 v1, v94, v1
	v_mul_f32_e32 v2, v94, v2
	v_mul_f32_e32 v3, v94, v3
	v_bfe_u32 v94, v28, 16, 1
	v_bfe_u32 v116, v30, 16, 1
	v_bfe_u32 v95, v29, 16, 1
	v_bfe_u32 v117, v31, 16, 1
	v_bfe_u32 v118, v24, 16, 1
	v_bfe_u32 v119, v25, 16, 1
	v_bfe_u32 v123, v26, 16, 1
	v_bfe_u32 v125, v20, 16, 1
	v_bfe_u32 v127, v22, 16, 1
	v_bfe_u32 v129, v16, 16, 1
	v_bfe_u32 v130, v17, 16, 1
	v_bfe_u32 v131, v18, 16, 1
	v_fma_f32 v14, v14, v50, v54
	v_fma_f32 v15, v15, v51, v55
	v_fma_f32 v12, v12, v48, v52
	v_fma_f32 v13, v13, v49, v53
	v_fma_f32 v8, v8, v56, v60
	v_fma_f32 v9, v9, v57, v61
	v_fma_f32 v0, v0, v68, v76
	v_fma_f32 v1, v1, v69, v77
	v_add3_u32 v28, v28, v94, s85
	v_add3_u32 v30, v30, v116, s85
	v_bfe_u32 v124, v27, 16, 1
	v_bfe_u32 v126, v21, 16, 1
	v_bfe_u32 v128, v23, 16, 1
	v_bfe_u32 v132, v19, 16, 1
	v_fma_f32 v10, v10, v58, v66
	v_fma_f32 v11, v11, v59, v67
	v_fma_f32 v6, v6, v64, v74
	v_fma_f32 v7, v7, v65, v75
	v_fma_f32 v4, v4, v62, v70
	v_fma_f32 v5, v5, v63, v71
	v_fma_f32 v2, v2, v72, v78
	v_fma_f32 v3, v3, v73, v79
	v_add3_u32 v29, v29, v95, s85
	v_add3_u32 v31, v31, v117, s85
	v_add3_u32 v24, v24, v118, s85
	v_add3_u32 v25, v25, v119, s85
	v_add3_u32 v26, v26, v123, s85
	v_add3_u32 v20, v20, v125, s85
	v_add3_u32 v22, v22, v127, s85
	v_add3_u32 v16, v16, v129, s85
	v_add3_u32 v17, v17, v130, s85
	v_add3_u32 v18, v18, v131, s85
	v_bfe_u32 v94, v12, 16, 1
	v_bfe_u32 v116, v14, 16, 1
	v_bfe_u32 v118, v8, 16, 1
	v_bfe_u32 v119, v9, 16, 1
	v_bfe_u32 v129, v0, 16, 1
	v_bfe_u32 v130, v1, 16, 1
	v_lshrrev_b32_e32 v28, 16, v28
	v_lshrrev_b32_e32 v30, 16, v30
	v_add3_u32 v27, v27, v124, s85
	v_add3_u32 v21, v21, v126, s85
	v_add3_u32 v23, v23, v128, s85
	v_add3_u32 v19, v19, v132, s85
	v_bfe_u32 v95, v13, 16, 1
	v_bfe_u32 v117, v15, 16, 1
	v_bfe_u32 v123, v10, 16, 1
	v_bfe_u32 v124, v11, 16, 1
	v_bfe_u32 v125, v4, 16, 1
	v_bfe_u32 v126, v5, 16, 1
	v_bfe_u32 v127, v6, 16, 1
	v_bfe_u32 v128, v7, 16, 1
	v_bfe_u32 v131, v2, 16, 1
	v_bfe_u32 v132, v3, 16, 1
	v_lshrrev_b32_e32 v24, 16, v24
	v_lshrrev_b32_e32 v26, 16, v26
	v_lshrrev_b32_e32 v20, 16, v20
	v_lshrrev_b32_e32 v22, 16, v22
	v_lshrrev_b32_e32 v16, 16, v16
	v_lshrrev_b32_e32 v18, 16, v18
	v_add3_u32 v12, v12, v94, s85
	v_add3_u32 v14, v14, v116, s85
; #define P1_LD(bi, r) do { const GAS f32x4* xr_ = (const GAS f32x4*)(XIN + ((size_t)p * 256 + wave * 32 + (r)) * DM) + lane; _Pragma("unroll") for (int j = 0; j < 4; ++j) xq[bi][j] = xr_[64 * j]; } while (0)
; __global__ void __launch_bounds__(512, 2) hymba_fwd(Args args) {
;     ...
;             P1_LD(0, 0); P1_LD(1, 1); asm volatile("" ::: "memory");
; #pragma nounroll
;             for (int rr = 0; rr < 30; rr += 3) {
;                 P1_LD(2, rr + 2); asm volatile("" ::: "memory"); P1_ST(0, rr); asm volatile("" ::: "memory");
;                 P1_LD(0, rr + 3); asm volatile("" ::: "memory"); P1_ST(1, rr + 1); asm volatile("" ::: "memory");
;                 P1_LD(1, rr + 4); asm volatile("" ::: "memory"); P1_ST(2, rr + 2); asm volatile("" ::: "memory"); }
	v_add3_u32 v8, v8, v118, s85
	v_add3_u32 v9, v9, v119, s85
	v_add3_u32 v118, v0, v129, s85
	v_add3_u32 v119, v1, v130, s85
	v_and_or_b32 v0, v29, s86, v28
	v_and_or_b32 v1, v31, s86, v30
	v_add3_u32 v13, v13, v95, s85
	v_add3_u32 v15, v15, v117, s85
	v_add3_u32 v10, v10, v123, s85
	v_add3_u32 v11, v11, v124, s85
	v_add3_u32 v94, v4, v125, s85
	v_add3_u32 v95, v5, v126, s85
	v_add3_u32 v116, v6, v127, s85
	v_add3_u32 v117, v7, v128, s85
	v_add3_u32 v123, v2, v131, s85
	v_add3_u32 v124, v3, v132, s85
	v_and_or_b32 v2, v25, s86, v24
	v_and_or_b32 v3, v27, s86, v26
	v_and_or_b32 v4, v21, s86, v20
	v_and_or_b32 v5, v23, s86, v22
	v_and_or_b32 v6, v17, s86, v16
	v_and_or_b32 v7, v19, s86, v18
	v_lshrrev_b32_e32 v12, 16, v12
	v_lshrrev_b32_e32 v14, 16, v14
	global_store_dwordx2 v[84:85], v[0:1], off offset:-1536
	global_store_dwordx2 v[84:85], v[2:3], off offset:-1024
	global_store_dwordx2 v[84:85], v[4:5], off offset:-512
	global_store_dwordx2 v[80:81], v[6:7], off offset:-4096
	v_lshrrev_b32_e32 v8, 16, v8
	v_lshrrev_b32_e32 v10, 16, v10
	v_lshrrev_b32_e32 v16, 16, v94
	v_lshrrev_b32_e32 v17, 16, v116
	v_lshrrev_b32_e32 v18, 16, v118
	v_lshrrev_b32_e32 v19, 16, v123
	v_and_or_b32 v0, v13, s86, v12
	v_and_or_b32 v1, v15, s86, v14
	v_and_or_b32 v2, v9, s86, v8
	v_and_or_b32 v3, v11, s86, v10
	v_and_or_b32 v4, v95, s86, v16
	v_and_or_b32 v5, v117, s86, v17
	v_and_or_b32 v6, v119, s86, v18
	v_and_or_b32 v7, v124, s86, v19
	global_load_dwordx4 v[28:31], v[86:87], off offset:-3072
	global_load_dwordx4 v[24:27], v[86:87], off offset:-2048
	global_load_dwordx4 v[20:23], v[86:87], off offset:-1024
	global_load_dwordx4 v[16:19], v[82:83], off offset:-4096
	global_store_dwordx2 v[80:81], v[0:1], off offset:-3584
	global_store_dwordx2 v[80:81], v[2:3], off offset:-3072
	global_store_dwordx2 v[80:81], v[4:5], off offset:-2560
	global_store_dwordx2 v[80:81], v[6:7], off offset:-2048
	global_load_dwordx4 v[12:15], v[82:83], off offset:-3072
	global_load_dwordx4 v[8:11], v[82:83], off offset:-2048
	global_load_dwordx4 v[4:7], v[82:83], off offset:-1024
	global_load_dwordx4 v[0:3], v[82:83], off
	s_waitcnt vmcnt(19)
	v_mul_f32_e32 v84, v46, v46
	v_mul_f32_e32 v85, v47, v47
	v_mul_f32_e32 v86, v44, v44
	v_mul_f32_e32 v87, v45, v45
	s_waitcnt vmcnt(18)
	v_mul_f32_e32 v94, v42, v42
	v_mul_f32_e32 v95, v43, v43
	v_mul_f32_e32 v116, v40, v40
	v_mul_f32_e32 v117, v41, v41
	v_pk_mov_b32 v[126:127], v[86:87], v[84:85] op_sel:[1,0]
	v_mov_b32_e32 v87, v85
	v_pk_mov_b32 v[84:85], v[116:117], v[94:95] op_sel:[1,0]
	v_mov_b32_e32 v117, v95
	s_waitcnt vmcnt(16)
	v_mul_f32_e32 v125, v33, v33
	v_mul_f32_e32 v118, v37, v37
	v_mul_f32_e32 v124, v39, v39
	v_add_f32_e32 v86, v126, v86
	v_add_f32_e32 v87, v127, v87
	v_add_f32_e32 v84, v84, v116
	v_add_f32_e32 v85, v85, v117
	v_mul_f32_e32 v123, v32, v32
	v_mul_f32_e32 v128, v34, v34
	v_mul_f32_e32 v129, v35, v35
	v_fma_f32 v94, v36, v36, v118
	v_fma_f32 v95, v37, v37, v118
	v_fma_f32 v118, v38, v38, v124
	v_fma_f32 v119, v39, v39, v124
	v_pk_add_f32 v[86:87], v[86:87], v[86:87] op_sel:[0,1] op_sel_hi:[1,0]
	v_pk_add_f32 v[84:85], v[84:85], v[84:85] op_sel:[0,1] op_sel_hi:[1,0]
	v_mov_b32_e32 v95, v128
	v_mov_b32_e32 v119, v129
	v_mov_b32_e32 v87, v123
	v_mov_b32_e32 v85, v125
	v_add_f32_e32 v94, v94, v118
	v_add_f32_e32 v95, v95, v119
	v_add_f32_e32 v84, v86, v84
	v_add_f32_e32 v85, v87, v85
	v_lshl_add_u64 v[82:83], v[82:83], 0, s[70:71]
	v_add_f32_e32 v84, v84, v94
	v_add_f32_e32 v85, v85, v95
	s_nop 0
	v_add_f32_e32 v84, v84, v85
	ds_bpermute_b32 v85, v93, v84
	s_waitcnt lgkmcnt(0)
	v_add_f32_e32 v84, v84, v85
	ds_bpermute_b32 v85, v92, v84
	s_waitcnt lgkmcnt(0)
	v_add_f32_e32 v84, v84, v85
	ds_bpermute_b32 v85, v91, v84
	s_waitcnt lgkmcnt(0)
	v_add_f32_e32 v84, v84, v85
	ds_bpermute_b32 v85, v90, v84
	s_waitcnt lgkmcnt(0)
	v_add_f32_e32 v84, v84, v85
	ds_bpermute_b32 v85, v89, v84
	s_waitcnt lgkmcnt(0)
	v_add_f32_e32 v84, v84, v85
	ds_bpermute_b32 v85, v88, v84
	s_waitcnt lgkmcnt(0)
	v_add_f32_e32 v84, v84, v85
	v_fmamk_f32 v84, v84, 0x3a800000, v120
	v_mul_f32_e32 v85, 0x4f800000, v84
	v_cmp_gt_f32_e32 vcc, s84, v84
	s_nop 1
	v_cndmask_b32_e32 v84, v84, v85, vcc
	v_sqrt_f32_e32 v85, v84
	s_nop 0
	v_add_u32_e32 v86, -1, v85
	v_add_u32_e32 v87, 1, v85
	v_fma_f32 v94, -v86, v85, v84
	v_fma_f32 v95, -v87, v85, v84
	v_cmp_ge_f32_e64 s[4:5], 0, v94
	s_nop 1
	v_cndmask_b32_e64 v85, v85, v86, s[4:5]
	v_cmp_lt_f32_e64 s[4:5], 0, v95
	s_nop 1
	v_cndmask_b32_e64 v85, v85, v87, s[4:5]
	v_mul_f32_e32 v86, 0x37800000, v85
	v_cndmask_b32_e32 v85, v85, v86, vcc
	v_cmp_class_f32_e32 vcc, v84, v121
	s_nop 1
	v_cndmask_b32_e32 v84, v85, v84, vcc
	v_div_scale_f32 v85, s[4:5], v84, v84, 1.0
	v_rcp_f32_e32 v87, v85
	v_div_scale_f32 v86, vcc, 1.0, v84, 1.0
	v_fma_f32 v94, -v85, v87, 1.0
	v_fmac_f32_e32 v87, v94, v87
	v_mul_f32_e32 v94, v86, v87
	v_fma_f32 v95, -v85, v94, v86
	v_fmac_f32_e32 v94, v95, v87
	v_fma_f32 v85, -v85, v94, v86
	v_div_fmas_f32 v85, v85, v87, v94
	v_div_fixup_f32 v84, v85, v84, 1.0
	v_mul_f32_e32 v44, v84, v44
	v_mul_f32_e32 v45, v84, v45
	v_mul_f32_e32 v46, v84, v46
	v_mul_f32_e32 v47, v84, v47
	v_mul_f32_e32 v40, v84, v40
	v_mul_f32_e32 v41, v84, v41
	v_mul_f32_e32 v42, v84, v42
	v_mul_f32_e32 v43, v84, v43
	v_mul_f32_e32 v36, v84, v36
	v_mul_f32_e32 v37, v84, v37
	v_mul_f32_e32 v38, v84, v38
	v_mul_f32_e32 v39, v84, v39
	v_mul_f32_e32 v32, v84, v32
	v_mul_f32_e32 v33, v84, v33
	v_mul_f32_e32 v34, v84, v34
	v_mul_f32_e32 v35, v84, v35
	v_fma_f32 v46, v46, v50, v54
	v_fma_f32 v47, v47, v51, v55
	v_fma_f32 v44, v44, v48, v52
	v_fma_f32 v45, v45, v49, v53
	v_fma_f32 v42, v42, v58, v66
	v_fma_f32 v43, v43, v59, v67
; #define P1_LD(bi, r) do { const GAS f32x4* xr_ = (const GAS f32x4*)(XIN + ((size_t)p * 256 + wave * 32 + (r)) * DM) + lane; _Pragma("unroll") for (int j = 0; j < 4; ++j) xq[bi][j] = xr_[64 * j]; } while (0)
; __global__ void __launch_bounds__(512, 2) hymba_fwd(Args args) {
;     ...
;             P1_LD(0, 0); P1_LD(1, 1); asm volatile("" ::: "memory");
; #pragma nounroll
;             for (int rr = 0; rr < 30; rr += 3) {
;                 P1_LD(2, rr + 2); asm volatile("" ::: "memory"); P1_ST(0, rr); asm volatile("" ::: "memory");
;                 P1_LD(0, rr + 3); asm volatile("" ::: "memory"); P1_ST(1, rr + 1); asm volatile("" ::: "memory");
;                 P1_LD(1, rr + 4); asm volatile("" ::: "memory"); P1_ST(2, rr + 2); asm volatile("" ::: "memory"); }
;             P1_ST(0, 30); asm volatile("" ::: "memory"); P1_ST(1, 31);
	v_fma_f32 v40, v40, v56, v60
	v_fma_f32 v41, v41, v57, v61
	v_fma_f32 v38, v38, v64, v74
	v_fma_f32 v39, v39, v65, v75
	v_fma_f32 v36, v36, v62, v70
	v_fma_f32 v37, v37, v63, v71
	v_fma_f32 v34, v34, v72, v78
	v_fma_f32 v35, v35, v73, v79
	v_fma_f32 v32, v32, v68, v76
	v_fma_f32 v33, v33, v69, v77
	v_bfe_u32 v84, v44, 16, 1
	v_bfe_u32 v86, v46, 16, 1
	v_bfe_u32 v85, v45, 16, 1
	v_bfe_u32 v87, v47, 16, 1
	v_bfe_u32 v94, v40, 16, 1
	v_bfe_u32 v116, v42, 16, 1
	v_bfe_u32 v118, v36, 16, 1
	v_bfe_u32 v123, v38, 16, 1
	v_bfe_u32 v125, v32, 16, 1
	v_bfe_u32 v126, v33, 16, 1
	v_bfe_u32 v127, v34, 16, 1
	v_bfe_u32 v128, v35, 16, 1
	v_add3_u32 v44, v44, v84, s85
	v_add3_u32 v46, v46, v86, s85
	v_bfe_u32 v95, v41, 16, 1
	v_bfe_u32 v117, v43, 16, 1
	v_bfe_u32 v119, v37, 16, 1
	v_bfe_u32 v124, v39, 16, 1
	v_add3_u32 v45, v45, v85, s85
	v_add3_u32 v47, v47, v87, s85
	v_add3_u32 v40, v40, v94, s85
	v_add3_u32 v42, v42, v116, s85
	v_add3_u32 v36, v36, v118, s85
	v_add3_u32 v38, v38, v123, s85
	v_add3_u32 v32, v32, v125, s85
	v_add3_u32 v84, v33, v126, s85
	v_add3_u32 v33, v34, v127, s85
	v_add3_u32 v85, v35, v128, s85
	v_lshrrev_b32_e32 v34, 16, v44
	v_lshrrev_b32_e32 v35, 16, v46
	v_add3_u32 v41, v41, v95, s85
	v_add3_u32 v43, v43, v117, s85
	v_add3_u32 v37, v37, v119, s85
	v_add3_u32 v39, v39, v124, s85
	v_lshrrev_b32_e32 v40, 16, v40
	v_lshrrev_b32_e32 v42, 16, v42
	v_lshrrev_b32_e32 v36, 16, v36
	v_lshrrev_b32_e32 v38, 16, v38
	v_lshrrev_b32_e32 v44, 16, v32
	v_lshrrev_b32_e32 v46, 16, v33
	v_and_or_b32 v32, v45, s86, v34
	v_and_or_b32 v33, v47, s86, v35
	v_and_or_b32 v34, v41, s86, v40
	v_and_or_b32 v35, v43, s86, v42
	v_and_or_b32 v36, v37, s86, v36
	v_and_or_b32 v37, v39, s86, v38
	v_and_or_b32 v38, v84, s86, v44
	v_and_or_b32 v39, v85, s86, v46
	global_store_dwordx2 v[80:81], v[32:33], off offset:-1536
	global_store_dwordx2 v[80:81], v[34:35], off offset:-1024
	global_store_dwordx2 v[80:81], v[36:37], off offset:-512
	global_store_dwordx2 v[80:81], v[38:39], off
	v_lshl_add_u64 v[80:81], v[80:81], 0, s[18:19]
	s_cbranch_scc1 .LBB0_158
	s_waitcnt vmcnt(15)
	v_mul_f32_e32 v32, v30, v30
	v_mul_f32_e32 v33, v31, v31
	v_mul_f32_e32 v34, v28, v28
	v_mul_f32_e32 v35, v29, v29
	v_lshl_add_u64 v[112:113], v[112:113], 0, s[20:21]
	v_pk_mov_b32 v[36:37], v[34:35], v[32:33] op_sel:[1,0]
	v_mov_b32_e32 v35, v33
	v_add_f32_e32 v32, v36, v34
	v_add_f32_e32 v33, v37, v35
	s_waitcnt vmcnt(14)
	v_mul_f32_e32 v34, v26, v26
	v_mul_f32_e32 v35, v27, v27
	v_mul_f32_e32 v36, v24, v24
	v_mul_f32_e32 v37, v25, v25
	v_pk_add_f32 v[32:33], v[32:33], v[32:33] op_sel:[0,1] op_sel_hi:[1,0]
	v_pk_mov_b32 v[38:39], v[36:37], v[34:35] op_sel:[1,0]
	v_mov_b32_e32 v37, v35
	v_add_f32_e32 v34, v38, v36
	v_add_f32_e32 v35, v39, v37
	s_waitcnt vmcnt(12)
	v_mul_f32_e32 v36, v16, v16
	v_mul_f32_e32 v37, v17, v17
	v_pk_add_f32 v[34:35], v[34:35], v[34:35] op_sel:[0,1] op_sel_hi:[1,0]
	v_mov_b32_e32 v33, v36
	v_mov_b32_e32 v35, v37
	v_add_f32_e32 v32, v32, v34
	v_add_f32_e32 v33, v33, v35
	v_mul_f32_e32 v34, v21, v21
	v_mul_f32_e32 v36, v23, v23
	v_mul_f32_e32 v38, v18, v18
	v_mul_f32_e32 v39, v19, v19
	v_fma_f32 v35, v21, v21, v34
	v_fma_f32 v34, v20, v20, v34
	v_fma_f32 v37, v23, v23, v36
	v_fma_f32 v36, v22, v22, v36
	v_mov_b32_e32 v35, v38
	v_mov_b32_e32 v37, v39
	v_add_f32_e32 v34, v34, v36
	v_add_f32_e32 v35, v35, v37
	v_lshl_add_u64 v[114:115], v[114:115], 0, s[22:23]
	v_add_f32_e32 v32, v32, v34
	v_add_f32_e32 v33, v33, v35
	s_nop 0
	v_add_f32_e32 v32, v32, v33
	ds_bpermute_b32 v33, v93, v32
	s_waitcnt lgkmcnt(0)
	v_add_f32_e32 v32, v32, v33
	ds_bpermute_b32 v33, v92, v32
	s_waitcnt lgkmcnt(0)
	v_add_f32_e32 v32, v32, v33
	ds_bpermute_b32 v33, v91, v32
	s_waitcnt lgkmcnt(0)
	v_add_f32_e32 v32, v32, v33
	ds_bpermute_b32 v33, v90, v32
	s_waitcnt lgkmcnt(0)
	v_add_f32_e32 v32, v32, v33
	ds_bpermute_b32 v33, v89, v32
	s_waitcnt lgkmcnt(0)
	v_add_f32_e32 v32, v32, v33
	ds_bpermute_b32 v33, v88, v32
	s_waitcnt lgkmcnt(0)
	v_add_f32_e32 v32, v32, v33
	v_fmamk_f32 v32, v32, 0x3a800000, v120
	v_mul_f32_e32 v33, 0x4f800000, v32
	v_cmp_gt_f32_e32 vcc, s84, v32
	s_nop 1
	v_cndmask_b32_e32 v32, v32, v33, vcc
	v_sqrt_f32_e32 v33, v32
	s_nop 0
	v_add_u32_e32 v34, -1, v33
	v_add_u32_e32 v35, 1, v33
	v_fma_f32 v36, -v34, v33, v32
	v_fma_f32 v37, -v35, v33, v32
	v_cmp_ge_f32_e64 s[4:5], 0, v36
	s_nop 1
	v_cndmask_b32_e64 v33, v33, v34, s[4:5]
	v_cmp_lt_f32_e64 s[4:5], 0, v37
	s_nop 1
	v_cndmask_b32_e64 v33, v33, v35, s[4:5]
	v_mul_f32_e32 v34, 0x37800000, v33
	v_cndmask_b32_e32 v33, v33, v34, vcc
	v_cmp_class_f32_e32 vcc, v32, v121
	s_nop 1
	v_cndmask_b32_e32 v32, v33, v32, vcc
	v_div_scale_f32 v33, s[4:5], v32, v32, 1.0
	v_rcp_f32_e32 v34, v33
	v_div_scale_f32 v35, vcc, 1.0, v32, 1.0
	s_lshl_b64 s[4:5], s[78:79], 11
	v_fma_f32 v36, -v33, v34, 1.0
	v_fmac_f32_e32 v34, v36, v34
	v_mul_f32_e32 v36, v35, v34
	v_fma_f32 v37, -v33, v36, v35
	v_fmac_f32_e32 v36, v37, v34
	v_fma_f32 v33, -v33, v36, v35
	v_div_fmas_f32 v33, v33, v34, v36
	v_div_fixup_f32 v32, v33, v32, 1.0
	v_mul_f32_e32 v28, v32, v28
	v_mul_f32_e32 v29, v32, v29
	v_fma_f32 v28, v28, v48, v52
	v_fma_f32 v29, v29, v49, v53
	v_mul_f32_e32 v30, v32, v30
	v_mul_f32_e32 v31, v32, v31
	v_bfe_u32 v33, v28, 16, 1
	v_add3_u32 v28, v28, v33, s85
	v_bfe_u32 v33, v29, 16, 1
	v_fma_f32 v30, v30, v50, v54
	v_fma_f32 v31, v31, v51, v55
	v_lshrrev_b32_e32 v28, 16, v28
	v_add3_u32 v29, v29, v33, s85
	s_add_u32 s4, s53, s4
	v_and_or_b32 v28, v29, s86, v28
	v_bfe_u32 v29, v30, 16, 1
	s_addc_u32 s5, s60, s5
	v_add3_u32 v29, v30, v29, s85
	v_bfe_u32 v30, v31, 16, 1
	v_lshl_add_u64 v[34:35], v[96:97], 3, s[4:5]
	v_lshrrev_b32_e32 v29, 16, v29
	v_add3_u32 v30, v31, v30, s85
	v_and_or_b32 v29, v30, s86, v29
	v_add_co_u32_e32 v30, vcc, s88, v34
	v_mul_f32_e32 v24, v32, v24
	v_mul_f32_e32 v25, v32, v25
	s_nop 0
	v_addc_co_u32_e32 v31, vcc, 0, v35, vcc
	v_fma_f32 v24, v24, v56, v60
	v_fma_f32 v25, v25, v57, v61
	global_store_dwordx2 v[30:31], v[28:29], off
	v_bfe_u32 v28, v24, 16, 1
	v_mul_f32_e32 v26, v32, v26
	v_mul_f32_e32 v27, v32, v27
	v_add3_u32 v24, v24, v28, s85
	v_bfe_u32 v28, v25, 16, 1
	v_fma_f32 v26, v26, v58, v66
	v_fma_f32 v27, v27, v59, v67
	v_lshrrev_b32_e32 v24, 16, v24
	v_add3_u32 v25, v25, v28, s85
	v_and_or_b32 v24, v25, s86, v24
	v_bfe_u32 v25, v26, 16, 1
	v_add3_u32 v25, v26, v25, s85
	v_bfe_u32 v26, v27, 16, 1
	v_lshrrev_b32_e32 v25, 16, v25
	v_add3_u32 v26, v27, v26, s85
	v_lshl_add_u64 v[36:37], v[34:35], 0, s[72:73]
	v_and_or_b32 v25, v26, s86, v25
	global_store_dwordx2 v[36:37], v[24:25], off offset:512
	s_waitcnt vmcnt(9)
; #define P1_LD(bi, r) do { const GAS f32x4* xr_ = (const GAS f32x4*)(XIN + ((size_t)p * 256 + wave * 32 + (r)) * DM) + lane; _Pragma("unroll") for (int j = 0; j < 4; ++j) xq[bi][j] = xr_[64 * j]; } while (0)
; __global__ void __launch_bounds__(512, 2) hymba_fwd(Args args) {
;     ...
;             P1_LD(0, 0); P1_LD(1, 1); asm volatile("" ::: "memory");
; #pragma nounroll
;             for (int rr = 0; rr < 30; rr += 3) {
;                 P1_LD(2, rr + 2); asm volatile("" ::: "memory"); P1_ST(0, rr); asm volatile("" ::: "memory");
;                 P1_LD(0, rr + 3); asm volatile("" ::: "memory"); P1_ST(1, rr + 1); asm volatile("" ::: "memory");
;                 P1_LD(1, rr + 4); asm volatile("" ::: "memory"); P1_ST(2, rr + 2); asm volatile("" ::: "memory"); }
;             P1_ST(0, 30); asm volatile("" ::: "memory"); P1_ST(1, 31);
	v_mul_f32_e32 v24, v14, v14
	v_mul_f32_e32 v25, v15, v15
	v_mul_f32_e32 v26, v12, v12
	v_mul_f32_e32 v27, v13, v13
	v_mul_f32_e32 v20, v32, v20
	v_mul_f32_e32 v21, v32, v21
	v_pk_mov_b32 v[28:29], v[26:27], v[24:25] op_sel:[1,0]
	v_mov_b32_e32 v27, v25
	v_add_f32_e32 v24, v28, v26
	v_add_f32_e32 v25, v29, v27
	s_waitcnt vmcnt(8)
	v_mul_f32_e32 v26, v10, v10
	v_mul_f32_e32 v27, v11, v11
	v_mul_f32_e32 v28, v8, v8
	v_mul_f32_e32 v29, v9, v9
	v_pk_add_f32 v[24:25], v[24:25], v[24:25] op_sel:[0,1] op_sel_hi:[1,0]
	v_pk_mov_b32 v[38:39], v[28:29], v[26:27] op_sel:[1,0]
	v_mov_b32_e32 v29, v27
	v_add_f32_e32 v26, v38, v28
	v_add_f32_e32 v27, v39, v29
	s_waitcnt vmcnt(6)
	v_mul_f32_e32 v28, v0, v0
	v_mul_f32_e32 v29, v1, v1
	v_pk_add_f32 v[26:27], v[26:27], v[26:27] op_sel:[0,1] op_sel_hi:[1,0]
	v_mov_b32_e32 v25, v28
	v_mov_b32_e32 v27, v29
	v_add_f32_e32 v24, v24, v26
	v_add_f32_e32 v25, v25, v27
	v_mul_f32_e32 v26, v5, v5
	v_mul_f32_e32 v28, v7, v7
	v_mul_f32_e32 v38, v2, v2
	v_mul_f32_e32 v39, v3, v3
	v_fma_f32 v27, v5, v5, v26
	v_fma_f32 v26, v4, v4, v26
	v_fma_f32 v29, v7, v7, v28
	v_fma_f32 v28, v6, v6, v28
	v_mov_b32_e32 v27, v38
	v_mov_b32_e32 v29, v39
	v_add_f32_e32 v26, v26, v28
	v_add_f32_e32 v27, v27, v29
	v_fma_f32 v20, v20, v62, v70
	v_fma_f32 v21, v21, v63, v71
	v_add_f32_e32 v24, v24, v26
	v_add_f32_e32 v25, v25, v27
	v_mul_f32_e32 v22, v32, v22
	v_mul_f32_e32 v23, v32, v23
	v_add_f32_e32 v24, v24, v25
	ds_bpermute_b32 v25, v93, v24
	v_bfe_u32 v33, v20, 16, 1
	v_add3_u32 v20, v20, v33, s85
	v_bfe_u32 v26, v21, 16, 1
	v_fma_f32 v22, v22, v64, v74
	v_fma_f32 v23, v23, v65, v75
	s_waitcnt lgkmcnt(0)
	v_add_f32_e32 v24, v24, v25
	ds_bpermute_b32 v25, v92, v24
	v_lshrrev_b32_e32 v20, 16, v20
	v_add3_u32 v21, v21, v26, s85
	v_and_or_b32 v20, v21, s86, v20
	v_bfe_u32 v21, v22, 16, 1
	v_add3_u32 v21, v22, v21, s85
	s_waitcnt lgkmcnt(0)
	v_add_f32_e32 v22, v24, v25
	ds_bpermute_b32 v24, v91, v22
	v_bfe_u32 v25, v23, 16, 1
	v_lshrrev_b32_e32 v21, 16, v21
	v_add3_u32 v23, v23, v25, s85
	v_and_or_b32 v21, v23, s86, v21
	global_store_dwordx2 v[36:37], v[20:21], off offset:1024
	s_waitcnt lgkmcnt(0)
	v_add_f32_e32 v20, v22, v24
	ds_bpermute_b32 v21, v90, v20
	v_mul_f32_e32 v16, v32, v16
	v_mul_f32_e32 v17, v32, v17
	v_fma_f32 v16, v16, v68, v76
	v_fma_f32 v17, v17, v69, v77
	v_mul_f32_e32 v18, v32, v18
	v_mul_f32_e32 v19, v32, v19
	v_bfe_u32 v22, v16, 16, 1
	s_waitcnt lgkmcnt(0)
	v_add_f32_e32 v20, v20, v21
	ds_bpermute_b32 v21, v89, v20
	v_add3_u32 v16, v16, v22, s85
	v_bfe_u32 v22, v17, 16, 1
	v_fma_f32 v18, v18, v72, v78
	v_fma_f32 v19, v19, v73, v79
	v_lshrrev_b32_e32 v16, 16, v16
	s_waitcnt lgkmcnt(0)
	v_add_f32_e32 v20, v20, v21
	ds_bpermute_b32 v21, v88, v20
	v_add3_u32 v17, v17, v22, s85
	v_and_or_b32 v16, v17, s86, v16
	v_bfe_u32 v17, v18, 16, 1
	v_add3_u32 v17, v18, v17, s85
	s_waitcnt lgkmcnt(0)
	v_add_f32_e32 v18, v20, v21
	v_fmamk_f32 v18, v18, 0x3a800000, v120
	v_mul_f32_e32 v20, 0x4f800000, v18
	v_cmp_gt_f32_e32 vcc, s84, v18
	v_bfe_u32 v21, v19, 16, 1
	v_add3_u32 v19, v19, v21, s85
	v_cndmask_b32_e32 v18, v18, v20, vcc
	v_sqrt_f32_e32 v20, v18
	v_lshrrev_b32_e32 v17, 16, v17
	v_and_or_b32 v17, v19, s86, v17
	global_store_dwordx2 v[36:37], v[16:17], off offset:1536
	v_add_u32_e32 v21, -1, v20
	v_fma_f32 v22, -v21, v20, v18
	v_cmp_ge_f32_e64 s[4:5], 0, v22
	v_add_u32_e32 v22, 1, v20
	s_add_i32 s76, s76, s48
	v_cndmask_b32_e64 v21, v20, v21, s[4:5]
	v_fma_f32 v20, -v22, v20, v18
	v_cmp_lt_f32_e64 s[4:5], 0, v20
	s_cmpk_gt_i32 s76, 0xff
	s_nop 0
	v_cndmask_b32_e64 v20, v21, v22, s[4:5]
	v_mul_f32_e32 v21, 0x37800000, v20
	v_cndmask_b32_e32 v20, v20, v21, vcc
	v_cmp_class_f32_e32 vcc, v18, v121
	s_nop 1
	v_cndmask_b32_e32 v18, v20, v18, vcc
	v_div_scale_f32 v20, s[4:5], v18, v18, 1.0
	v_rcp_f32_e32 v21, v20
	s_nop 0
	v_fma_f32 v16, -v20, v21, 1.0
	v_fmac_f32_e32 v21, v16, v21
	v_div_scale_f32 v16, vcc, 1.0, v18, 1.0
	v_mul_f32_e32 v17, v16, v21
	v_fma_f32 v19, -v20, v17, v16
	v_fmac_f32_e32 v17, v19, v21
	v_fma_f32 v16, -v20, v17, v16
	v_div_fmas_f32 v16, v16, v21, v17
	v_div_fixup_f32 v16, v16, v18, 1.0
	v_mul_f32_e32 v12, v16, v12
	v_mul_f32_e32 v13, v16, v13
	v_fma_f32 v12, v12, v48, v52
	v_fma_f32 v13, v13, v49, v53
	v_mul_f32_e32 v14, v16, v14
	v_mul_f32_e32 v15, v16, v15
	v_bfe_u32 v17, v12, 16, 1
	v_add3_u32 v12, v12, v17, s85
	v_bfe_u32 v17, v13, 16, 1
	v_fma_f32 v14, v14, v50, v54
	v_fma_f32 v15, v15, v51, v55
	v_lshrrev_b32_e32 v12, 16, v12
	v_add3_u32 v13, v13, v17, s85
	v_and_or_b32 v12, v13, s86, v12
	v_bfe_u32 v13, v14, 16, 1
	v_add3_u32 v13, v14, v13, s85
	v_bfe_u32 v14, v15, 16, 1
	v_lshrrev_b32_e32 v13, 16, v13
	v_add3_u32 v14, v15, v14, s85
	v_mul_f32_e32 v8, v16, v8
	v_mul_f32_e32 v9, v16, v9
	v_and_or_b32 v13, v14, s86, v13
	v_fma_f32 v8, v8, v56, v60
	v_fma_f32 v9, v9, v57, v61
	global_store_dwordx2 v[30:31], v[12:13], off offset:2048
	v_bfe_u32 v12, v8, 16, 1
	v_mul_f32_e32 v10, v16, v10
	v_mul_f32_e32 v11, v16, v11
	v_add3_u32 v8, v8, v12, s85
	v_bfe_u32 v12, v9, 16, 1
	v_fma_f32 v10, v10, v58, v66
	v_fma_f32 v11, v11, v59, v67
	v_lshrrev_b32_e32 v8, 16, v8
	v_add3_u32 v9, v9, v12, s85
	v_and_or_b32 v8, v9, s86, v8
	v_bfe_u32 v9, v10, 16, 1
	v_add3_u32 v9, v10, v9, s85
	v_bfe_u32 v10, v11, 16, 1
	v_lshrrev_b32_e32 v9, 16, v9
	v_add3_u32 v10, v11, v10, s85
	v_mul_f32_e32 v4, v16, v4
	v_mul_f32_e32 v5, v16, v5
	v_lshl_add_u64 v[18:19], v[34:35], 0, s[74:75]
	v_and_or_b32 v9, v10, s86, v9
	v_fma_f32 v4, v4, v62, v70
	v_fma_f32 v5, v5, v63, v71
	global_store_dwordx2 v[18:19], v[8:9], off offset:512
	v_bfe_u32 v8, v4, 16, 1
	v_mul_f32_e32 v6, v16, v6
	v_mul_f32_e32 v7, v16, v7
	v_add3_u32 v4, v4, v8, s85
	v_bfe_u32 v8, v5, 16, 1
	v_fma_f32 v6, v6, v64, v74
	v_fma_f32 v7, v7, v65, v75
	v_lshrrev_b32_e32 v4, 16, v4
	v_add3_u32 v5, v5, v8, s85
	v_and_or_b32 v4, v5, s86, v4
	v_bfe_u32 v5, v6, 16, 1
	v_add3_u32 v5, v6, v5, s85
	v_bfe_u32 v6, v7, 16, 1
	v_lshrrev_b32_e32 v5, 16, v5
	v_add3_u32 v6, v7, v6, s85
	v_mul_f32_e32 v0, v16, v0
	v_mul_f32_e32 v1, v16, v1
	v_and_or_b32 v5, v6, s86, v5
	v_fma_f32 v0, v0, v68, v76
	v_fma_f32 v1, v1, v69, v77
	global_store_dwordx2 v[18:19], v[4:5], off offset:1024
	v_bfe_u32 v4, v0, 16, 1
	v_mul_f32_e32 v2, v16, v2
	v_mul_f32_e32 v3, v16, v3
	v_add3_u32 v0, v0, v4, s85
	v_bfe_u32 v4, v1, 16, 1
	v_fma_f32 v2, v2, v72, v78
	v_fma_f32 v3, v3, v73, v79
	v_lshrrev_b32_e32 v0, 16, v0
	v_add3_u32 v1, v1, v4, s85
	v_and_or_b32 v0, v1, s86, v0
	v_bfe_u32 v1, v2, 16, 1
	v_add3_u32 v1, v2, v1, s85
	v_bfe_u32 v2, v3, 16, 1
	v_lshrrev_b32_e32 v1, 16, v1
	v_add3_u32 v2, v3, v2, s85
	v_and_or_b32 v1, v2, s86, v1
	global_store_dwordx2 v[18:19], v[0:1], off offset:1536
	s_cbranch_scc0 .LBB0_157

; __device__ __forceinline__ u32x4 pack8(f32x4 v0, f32x4 v1) { u32x4 w; w.x = cvt_pk_bf16(v0[0], v0[1]); w.y = cvt_pk_bf16(v0[2], v0[3]); w.z = cvt_pk_bf16(v1[0], v1[1]); w.w = cvt_pk_bf16(v1[2], v1[3]); return w; }
; #define EPI_PIN8(a) asm volatile("" : "+v"(a[0][0]), "+v"(a[0][1]), "+v"(a[0][2]), "+v"(a[0][3]), "+v"(a[1][0]), "+v"(a[1][1]), "+v"(a[1][2]), "+v"(a[1][3]) :: "memory")
; __device__ __forceinline__ void rope8h(f32x4& v0, f32x4& v1, u32x4 t) {
;     float c[4], s[4];
; #pragma unroll
;     for (int k = 0; k < 4; ++k) { const h16x2 h = __builtin_bit_cast(h16x2, (unsigned)t[k]); c[k] = (float)h[0]; s[k] = (float)h[1]; }
;     f32x4 a, b;
;     a[0] = v0[0] * c[0] - v0[1] * s[0]; a[1] = v0[1] * c[0] + v0[0] * s[0]; a[2] = v0[2] * c[1] - v0[3] * s[1]; a[3] = v0[3] * c[1] + v0[2] * s[1];
;     b[0] = v1[0] * c[2] - v1[1] * s[2]; b[1] = v1[1] * c[2] + v1[0] * s[2]; b[2] = v1[2] * c[3] - v1[3] * s[3]; b[3] = v1[3] * c[3] + v1[2] * s[3];
;     v0 = a; v1 = b;
; }
;     __device__ __forceinline__ int operator()(AccT acc, const Unit& u, int wr, int wc, int, int) const {
;     ...
;             if (wc < 2) { const int p0 = 16 * wc + 4 * fq;
;                 u32x4 th[2][4];
; #pragma unroll
;                 for (int ai = 0; ai < 2; ++ai)
; #pragma unroll
;                     for (int m = 0; m < 4; ++m) { const int pos = (row0 + ai * HALF + m * 16) & (SEQ - 1); th[ai][m] = *(const u32x4*)(rope + (size_t)pos * 32 + p0); }
;                 EPI_PIN8(th);
; #pragma unroll
;                 for (int ai = 0; ai < 2; ++ai)
; #pragma unroll
;                     for (int m = 0; m < 4; ++m) { const int r = row0 + ai * HALF + m * 16;
;                         f32x4 v0 = acc[ai][0][m][0], v1 = acc[ai][0][m][1]; rope8h(v0, v1, th[ai][m]); const u32x4 w = pack8(v0, v1);
; #pragma unroll
;                         for (int h = 0; h < 4; ++h) *(u32x4*)(KA + (size_t)r * 768 + h * 192 + 128 + cw) = w; } }
.LBB0_271:
	s_lshl_b32 s10, s10, 8
	v_mbcnt_lo_u32_b32 v181, -1, 0
	v_mbcnt_hi_u32_b32 v181, -1, v181
	s_add_i32 s10, s10, s1
	v_ashrrev_i32_e32 v170, 4, v181
	v_and_or_b32 v166, v181, 15, s10
	v_lshl_add_u32 v168, v170, 3, s77
	s_cmp_gt_i32 s14, 1
	s_mov_b64 s[10:11], -1
	s_cbranch_scc0 .LBB0_283
	s_cmp_gt_u32 s14, 5
	s_cbranch_scc0 .LBB0_280
	s_cmp_gt_u32 s14, 7
	s_cbranch_scc0 .LBB0_277
	s_andn2_b64 vcc, exec, s[28:29]
	s_cbranch_vccnz .LBB0_276
	v_lshl_add_u32 v128, v170, 2, s78
	v_ashrrev_i32_e32 v129, 31, v128
	v_lshlrev_b32_e32 v130, 7, v166
	v_lshl_add_u64 v[128:129], v[128:129], 2, s[26:27]
	v_and_b32_e32 v160, 0xfe780, v130
	v_lshl_add_u64 v[130:131], v[128:129], 0, v[160:161]
	global_load_dwordx4 v[182:185], v[130:131], off
	global_load_dwordx4 v[186:189], v[130:131], off offset:2048
	v_add_co_u32_e32 v130, vcc, 0x1000, v130
	v_ashrrev_i32_e32 v169, 31, v168
	s_nop 0
	v_addc_co_u32_e32 v131, vcc, 0, v131, vcc
	global_load_dwordx4 v[190:193], v[130:131], off
	global_load_dwordx4 v[144:147], v[130:131], off offset:2048
	v_lshl_add_u32 v130, v166, 5, v178
	v_and_b32_e32 v130, 0x3f9e0, v130
	v_lshlrev_b32_e32 v160, 2, v130
	v_lshl_add_u64 v[128:129], v[128:129], 0, v[160:161]
	global_load_dwordx4 v[140:143], v[128:129], off
	global_load_dwordx4 v[136:139], v[128:129], off offset:2048
	v_add_co_u32_e32 v128, vcc, s89, v128
	v_mov_b64_e32 v[148:149], s[24:25]
	s_nop 0
	v_addc_co_u32_e32 v129, vcc, 0, v129, vcc
	global_load_dwordx4 v[132:135], v[128:129], off
	s_nop 0
	global_load_dwordx4 v[128:131], v[128:129], off offset:2048
	v_or_b32_e32 v160, 16, v166
	v_mad_i64_i32 v[172:173], s[10:11], v166, s90, v[148:149]
	v_lshlrev_b64 v[150:151], 1, v[168:169]
	v_mad_i64_i32 v[194:195], s[10:11], v160, s90, v[148:149]
	v_lshl_add_u64 v[172:173], v[172:173], 0, v[150:151]
	v_lshl_add_u64 v[194:195], v[194:195], 0, v[150:151]
	s_waitcnt vmcnt(0)
	s_nop 0
	v_cvt_f32_f16_e32 v200, v184
	v_cvt_f32_f16_sdwa v201, v184 dst_sel:DWORD dst_unused:UNUSED_PAD src0_sel:WORD_1
	v_cvt_f32_f16_e32 v184, v185
	v_cvt_f32_f16_sdwa v185, v185 dst_sel:DWORD dst_unused:UNUSED_PAD src0_sel:WORD_1
	v_cvt_f32_f16_e32 v196, v182
	v_cvt_f32_f16_sdwa v197, v182 dst_sel:DWORD dst_unused:UNUSED_PAD src0_sel:WORD_1
	v_cvt_f32_f16_e32 v182, v183
	v_cvt_f32_f16_sdwa v183, v183 dst_sel:DWORD dst_unused:UNUSED_PAD src0_sel:WORD_1
	v_cvt_f32_f16_e32 v202, v186
	v_cvt_f32_f16_sdwa v203, v186 dst_sel:DWORD dst_unused:UNUSED_PAD src0_sel:WORD_1
	v_cvt_f32_f16_e32 v186, v187
	v_cvt_f32_f16_sdwa v187, v187 dst_sel:DWORD dst_unused:UNUSED_PAD src0_sel:WORD_1
	v_cvt_f32_f16_e32 v204, v188
	v_cvt_f32_f16_sdwa v205, v188 dst_sel:DWORD dst_unused:UNUSED_PAD src0_sel:WORD_1
	v_cvt_f32_f16_e32 v188, v189
	v_cvt_f32_f16_sdwa v189, v189 dst_sel:DWORD dst_unused:UNUSED_PAD src0_sel:WORD_1
	v_mul_f32_e32 v212, v122, v184
	v_mul_f32_e32 v213, v123, v185
	v_mul_f32_e32 v184, v123, v184
	v_mul_f32_e32 v185, v122, v185
	v_mul_f32_e32 v206, v124, v196
	v_mul_f32_e32 v207, v125, v197
	v_mul_f32_e32 v196, v125, v196
	v_mul_f32_e32 v197, v124, v197
	v_mul_f32_e32 v208, v126, v182
	v_mul_f32_e32 v209, v127, v183
	v_mul_f32_e32 v182, v127, v182
	v_mul_f32_e32 v183, v126, v183
	v_mul_f32_e32 v210, v120, v200
	v_mul_f32_e32 v211, v121, v201
	v_mul_f32_e32 v200, v121, v200
	v_mul_f32_e32 v201, v120, v201
	v_add_f32_e32 v185, v184, v185
	v_sub_f32_e32 v160, v206, v207
	v_add_f32_e32 v167, v196, v197
	v_sub_f32_e32 v169, v208, v209
	v_add_f32_e32 v171, v182, v183
	v_sub_f32_e32 v196, v210, v211
	v_add_f32_e32 v197, v200, v201
	v_sub_f32_e32 v198, v212, v213
	v_cvt_pk_bf16_f32 v182, v160, v167
	v_cvt_pk_bf16_f32 v183, v169, v171
	v_cvt_pk_bf16_f32 v184, v196, v197
	v_cvt_pk_bf16_f32 v185, v198, v185
	v_mul_f32_e32 v214, v108, v202
	v_mul_f32_e32 v215, v109, v203
	v_mul_f32_e32 v202, v109, v202
	v_mul_f32_e32 v203, v108, v203
	v_mul_f32_e32 v216, v110, v186
	v_mul_f32_e32 v217, v111, v187
	v_mul_f32_e32 v186, v111, v186
	v_mul_f32_e32 v187, v110, v187
	v_mul_f32_e32 v218, v104, v204
	v_mul_f32_e32 v219, v105, v205
	v_mul_f32_e32 v204, v105, v204
	v_mul_f32_e32 v205, v104, v205
	v_mul_f32_e32 v220, v106, v188
	v_mul_f32_e32 v221, v107, v189
	v_mul_f32_e32 v188, v107, v188
	v_mul_f32_e32 v189, v106, v189
	global_store_dwordx4 v[172:173], v[182:185], off offset:256
	global_store_dwordx4 v[172:173], v[182:185], off offset:640
	global_store_dwordx4 v[172:173], v[182:185], off offset:1024
	global_store_dwordx4 v[172:173], v[182:185], off offset:1408
	v_cvt_f32_f16_e32 v172, v190
	v_cvt_f32_f16_sdwa v173, v190 dst_sel:DWORD dst_unused:UNUSED_PAD src0_sel:WORD_1
	v_sub_f32_e32 v200, v214, v215
	v_add_f32_e32 v201, v202, v203
	v_sub_f32_e32 v202, v216, v217
	v_add_f32_e32 v186, v186, v187
	v_sub_f32_e32 v187, v218, v219
	v_add_f32_e32 v203, v204, v205
	v_sub_f32_e32 v204, v220, v221
	v_add_f32_e32 v188, v188, v189
	v_cvt_pk_bf16_f32 v182, v200, v201
	v_cvt_pk_bf16_f32 v183, v202, v186
	v_cvt_pk_bf16_f32 v184, v187, v203
	v_cvt_pk_bf16_f32 v185, v204, v188
	global_store_dwordx4 v[194:195], v[182:185], off offset:256
	global_store_dwordx4 v[194:195], v[182:185], off offset:640
	global_store_dwordx4 v[194:195], v[182:185], off offset:1024
	global_store_dwordx4 v[194:195], v[182:185], off offset:1408
	v_or_b32_e32 v160, 32, v166
	s_nop 0
	v_cvt_f32_f16_e32 v184, v191
	v_cvt_f32_f16_sdwa v185, v191 dst_sel:DWORD dst_unused:UNUSED_PAD src0_sel:WORD_1
	v_mul_f32_e32 v182, v92, v172
	v_mul_f32_e32 v183, v93, v173
	v_mul_f32_e32 v172, v93, v172
	v_mul_f32_e32 v173, v92, v173
	v_sub_f32_e32 v167, v182, v183
	v_cvt_f32_f16_e32 v182, v192
	v_cvt_f32_f16_sdwa v183, v192 dst_sel:DWORD dst_unused:UNUSED_PAD src0_sel:WORD_1
; __device__ __forceinline__ u32x4 pack8(f32x4 v0, f32x4 v1) { u32x4 w; w.x = cvt_pk_bf16(v0[0], v0[1]); w.y = cvt_pk_bf16(v0[2], v0[3]); w.z = cvt_pk_bf16(v1[0], v1[1]); w.w = cvt_pk_bf16(v1[2], v1[3]); return w; }
; __device__ __forceinline__ void rope8h(f32x4& v0, f32x4& v1, u32x4 t) {
;     float c[4], s[4];
; #pragma unroll
;     for (int k = 0; k < 4; ++k) { const h16x2 h = __builtin_bit_cast(h16x2, (unsigned)t[k]); c[k] = (float)h[0]; s[k] = (float)h[1]; }
;     f32x4 a, b;
;     a[0] = v0[0] * c[0] - v0[1] * s[0]; a[1] = v0[1] * c[0] + v0[0] * s[0]; a[2] = v0[2] * c[1] - v0[3] * s[1]; a[3] = v0[3] * c[1] + v0[2] * s[1];
;     b[0] = v1[0] * c[2] - v1[1] * s[2]; b[1] = v1[1] * c[2] + v1[0] * s[2]; b[2] = v1[2] * c[3] - v1[3] * s[3]; b[3] = v1[3] * c[3] + v1[2] * s[3];
;     v0 = a; v1 = b;
; }
;     __device__ __forceinline__ int operator()(AccT acc, const Unit& u, int wr, int wc, int, int) const {
;     ...
;                 for (int ai = 0; ai < 2; ++ai)
; #pragma unroll
;                     for (int m = 0; m < 4; ++m) { const int r = row0 + ai * HALF + m * 16;
;                         f32x4 v0 = acc[ai][0][m][0], v1 = acc[ai][0][m][1]; rope8h(v0, v1, th[ai][m]); const u32x4 w = pack8(v0, v1);
; #pragma unroll
;                         for (int h = 0; h < 4; ++h) *(u32x4*)(KA + (size_t)r * 768 + h * 192 + 128 + cw) = w; } }
	v_add_f32_e32 v169, v172, v173
	v_mul_f32_e32 v172, v94, v184
	v_mul_f32_e32 v173, v95, v185
	s_nop 0
	v_sub_f32_e32 v171, v172, v173
	v_mul_f32_e32 v172, v95, v184
	v_mul_f32_e32 v173, v94, v185
	v_cvt_f32_f16_e32 v184, v193
	v_cvt_f32_f16_sdwa v185, v193 dst_sel:DWORD dst_unused:UNUSED_PAD src0_sel:WORD_1
	v_add_f32_e32 v186, v172, v173
	v_mul_f32_e32 v172, v88, v182
	v_mul_f32_e32 v173, v89, v183
	s_nop 0
	v_sub_f32_e32 v187, v172, v173
	v_mul_f32_e32 v172, v89, v182
	v_mul_f32_e32 v173, v88, v183
	v_add_f32_e32 v188, v172, v173
	v_mul_f32_e32 v172, v90, v184
	v_mul_f32_e32 v173, v91, v185
	v_cvt_pk_bf16_f32 v182, v167, v169
	v_cvt_pk_bf16_f32 v183, v171, v186
	v_cvt_f32_f16_e32 v186, v144
	v_sub_f32_e32 v189, v172, v173
	v_mul_f32_e32 v172, v91, v184
	v_mul_f32_e32 v173, v90, v185
	v_add_f32_e32 v172, v172, v173
	v_cvt_pk_bf16_f32 v184, v187, v188
	v_cvt_f32_f16_sdwa v187, v144 dst_sel:DWORD dst_unused:UNUSED_PAD src0_sel:WORD_1
	v_cvt_pk_bf16_f32 v185, v189, v172
	v_mad_i64_i32 v[172:173], s[10:11], v160, s90, v[148:149]
	v_lshl_add_u64 v[172:173], v[172:173], 0, v[150:151]
	v_cvt_f32_f16_e32 v144, v145
	v_cvt_f32_f16_sdwa v145, v145 dst_sel:DWORD dst_unused:UNUSED_PAD src0_sel:WORD_1
	global_store_dwordx4 v[172:173], v[182:185], off offset:256
	global_store_dwordx4 v[172:173], v[182:185], off offset:640
	global_store_dwordx4 v[172:173], v[182:185], off offset:1024
	global_store_dwordx4 v[172:173], v[182:185], off offset:1408
	v_mul_f32_e32 v172, v76, v186
	v_mul_f32_e32 v173, v77, v187
	v_or_b32_e32 v160, 48, v166
	v_cvt_f32_f16_e32 v182, v146
	v_cvt_f32_f16_sdwa v183, v146 dst_sel:DWORD dst_unused:UNUSED_PAD src0_sel:WORD_1
	v_sub_f32_e32 v167, v172, v173
	v_mul_f32_e32 v172, v77, v186
	v_mul_f32_e32 v173, v76, v187
	v_cvt_f32_f16_e32 v146, v147
	v_cvt_f32_f16_sdwa v147, v147 dst_sel:DWORD dst_unused:UNUSED_PAD src0_sel:WORD_1
	v_add_f32_e32 v169, v172, v173
	v_mul_f32_e32 v172, v78, v144
	v_mul_f32_e32 v173, v79, v145
	v_mul_f32_e32 v144, v79, v144
	v_mul_f32_e32 v145, v78, v145
	v_sub_f32_e32 v171, v172, v173
	v_add_f32_e32 v172, v144, v145
	v_mul_f32_e32 v144, v72, v182
	v_mul_f32_e32 v145, v73, v183
	s_nop 0
	v_sub_f32_e32 v173, v144, v145
	v_mul_f32_e32 v144, v73, v182
	v_mul_f32_e32 v145, v72, v183
	v_add_f32_e32 v182, v144, v145
	v_mul_f32_e32 v144, v74, v146
	v_mul_f32_e32 v145, v75, v147
	s_nop 0
	v_sub_f32_e32 v183, v144, v145
	v_mul_f32_e32 v144, v75, v146
	v_mul_f32_e32 v145, v74, v147
	v_add_f32_e32 v147, v144, v145
	v_cvt_pk_bf16_f32 v144, v167, v169
	v_cvt_pk_bf16_f32 v145, v171, v172
	v_cvt_pk_bf16_f32 v146, v173, v182
	v_cvt_pk_bf16_f32 v147, v183, v147
	v_cvt_f32_f16_e32 v182, v140
	v_cvt_f32_f16_sdwa v183, v140 dst_sel:DWORD dst_unused:UNUSED_PAD src0_sel:WORD_1
	v_mad_i64_i32 v[172:173], s[10:11], v160, s90, v[148:149]
	v_lshl_add_u64 v[172:173], v[172:173], 0, v[150:151]
	v_cvt_f32_f16_e32 v140, v141
	v_cvt_f32_f16_sdwa v141, v141 dst_sel:DWORD dst_unused:UNUSED_PAD src0_sel:WORD_1
	global_store_dwordx4 v[172:173], v[144:147], off offset:256
	global_store_dwordx4 v[172:173], v[144:147], off offset:640
	global_store_dwordx4 v[172:173], v[144:147], off offset:1024
	global_store_dwordx4 v[172:173], v[144:147], off offset:1408
	v_add_u32_e32 v160, 0x80, v166
	s_nop 0
	v_cvt_f32_f16_e32 v146, v142
	v_cvt_f32_f16_sdwa v147, v142 dst_sel:DWORD dst_unused:UNUSED_PAD src0_sel:WORD_1
	v_mul_f32_e32 v144, v60, v182
	v_mul_f32_e32 v145, v61, v183
	v_cvt_f32_f16_e32 v142, v143
	v_sub_f32_e32 v167, v144, v145
	v_mul_f32_e32 v144, v61, v182
	v_mul_f32_e32 v145, v60, v183
	v_cvt_f32_f16_sdwa v143, v143 dst_sel:DWORD dst_unused:UNUSED_PAD src0_sel:WORD_1
	v_add_f32_e32 v169, v144, v145
	v_mul_f32_e32 v144, v62, v140
	v_mul_f32_e32 v145, v63, v141
	v_mul_f32_e32 v140, v63, v140
	v_mul_f32_e32 v141, v62, v141
	v_sub_f32_e32 v144, v144, v145
	v_add_f32_e32 v145, v140, v141
	v_mul_f32_e32 v140, v56, v146
	v_mul_f32_e32 v141, v57, v147
	s_nop 0
	v_sub_f32_e32 v171, v140, v141
	v_mul_f32_e32 v140, v57, v146
	v_mul_f32_e32 v141, v56, v147
	v_add_f32_e32 v146, v140, v141
	v_mul_f32_e32 v140, v58, v142
	v_mul_f32_e32 v141, v59, v143
	s_nop 0
	v_sub_f32_e32 v147, v140, v141
	v_mul_f32_e32 v140, v59, v142
	v_mul_f32_e32 v141, v58, v143
	v_add_f32_e32 v143, v140, v141
	v_cvt_pk_bf16_f32 v140, v167, v169
	v_cvt_pk_bf16_f32 v141, v144, v145
	v_cvt_pk_bf16_f32 v142, v171, v146
	v_cvt_pk_bf16_f32 v143, v147, v143
	v_cvt_f32_f16_e32 v146, v136
	v_cvt_f32_f16_sdwa v147, v136 dst_sel:DWORD dst_unused:UNUSED_PAD src0_sel:WORD_1
	v_mad_i64_i32 v[144:145], s[10:11], v160, s90, v[148:149]
	v_lshl_add_u64 v[144:145], v[144:145], 0, v[150:151]
	v_cvt_f32_f16_e32 v136, v137
	v_cvt_f32_f16_sdwa v137, v137 dst_sel:DWORD dst_unused:UNUSED_PAD src0_sel:WORD_1
	global_store_dwordx4 v[144:145], v[140:143], off offset:256
	global_store_dwordx4 v[144:145], v[140:143], off offset:640
	global_store_dwordx4 v[144:145], v[140:143], off offset:1024
	global_store_dwordx4 v[144:145], v[140:143], off offset:1408
	v_add_u32_e32 v144, 0x90, v166
	s_nop 0
; __device__ __forceinline__ u32x4 pack8(f32x4 v0, f32x4 v1) { u32x4 w; w.x = cvt_pk_bf16(v0[0], v0[1]); w.y = cvt_pk_bf16(v0[2], v0[3]); w.z = cvt_pk_bf16(v1[0], v1[1]); w.w = cvt_pk_bf16(v1[2], v1[3]); return w; }
; __device__ __forceinline__ void rope8h(f32x4& v0, f32x4& v1, u32x4 t) {
;     float c[4], s[4];
; #pragma unroll
;     for (int k = 0; k < 4; ++k) { const h16x2 h = __builtin_bit_cast(h16x2, (unsigned)t[k]); c[k] = (float)h[0]; s[k] = (float)h[1]; }
;     f32x4 a, b;
;     a[0] = v0[0] * c[0] - v0[1] * s[0]; a[1] = v0[1] * c[0] + v0[0] * s[0]; a[2] = v0[2] * c[1] - v0[3] * s[1]; a[3] = v0[3] * c[1] + v0[2] * s[1];
;     b[0] = v1[0] * c[2] - v1[1] * s[2]; b[1] = v1[1] * c[2] + v1[0] * s[2]; b[2] = v1[2] * c[3] - v1[3] * s[3]; b[3] = v1[3] * c[3] + v1[2] * s[3];
;     v0 = a; v1 = b;
; }
;     __device__ __forceinline__ int operator()(AccT acc, const Unit& u, int wr, int wc, int, int) const {
;     ...
;                 for (int ai = 0; ai < 2; ++ai)
; #pragma unroll
;                     for (int m = 0; m < 4; ++m) { const int r = row0 + ai * HALF + m * 16;
;                         f32x4 v0 = acc[ai][0][m][0], v1 = acc[ai][0][m][1]; rope8h(v0, v1, th[ai][m]); const u32x4 w = pack8(v0, v1);
; #pragma unroll
;                         for (int h = 0; h < 4; ++h) *(u32x4*)(KA + (size_t)r * 768 + h * 192 + 128 + cw) = w; } }
	v_cvt_f32_f16_e32 v142, v138
	v_cvt_f32_f16_sdwa v143, v138 dst_sel:DWORD dst_unused:UNUSED_PAD src0_sel:WORD_1
	v_mul_f32_e32 v140, v44, v146
	v_mul_f32_e32 v141, v45, v147
	v_cvt_f32_f16_e32 v138, v139
	v_sub_f32_e32 v145, v140, v141
	v_mul_f32_e32 v140, v45, v146
	v_mul_f32_e32 v141, v44, v147
	v_cvt_f32_f16_sdwa v139, v139 dst_sel:DWORD dst_unused:UNUSED_PAD src0_sel:WORD_1
	v_add_f32_e32 v146, v140, v141
	v_mul_f32_e32 v140, v46, v136
	v_mul_f32_e32 v141, v47, v137
	v_mul_f32_e32 v136, v47, v136
	v_mul_f32_e32 v137, v46, v137
	v_sub_f32_e32 v140, v140, v141
	v_add_f32_e32 v141, v136, v137
	v_mul_f32_e32 v136, v40, v142
	v_mul_f32_e32 v137, v41, v143
	s_nop 0
	v_sub_f32_e32 v147, v136, v137
	v_mul_f32_e32 v136, v41, v142
	v_mul_f32_e32 v137, v40, v143
	v_add_f32_e32 v142, v136, v137
	v_mul_f32_e32 v136, v42, v138
	v_mul_f32_e32 v137, v43, v139
	s_nop 0
	v_sub_f32_e32 v143, v136, v137
	v_mul_f32_e32 v136, v43, v138
	v_mul_f32_e32 v137, v42, v139
	v_add_f32_e32 v139, v136, v137
	v_cvt_pk_bf16_f32 v136, v145, v146
	v_cvt_pk_bf16_f32 v137, v140, v141
	v_cvt_pk_bf16_f32 v138, v147, v142
	v_cvt_pk_bf16_f32 v139, v143, v139
	v_cvt_f32_f16_e32 v142, v132
	v_cvt_f32_f16_sdwa v143, v132 dst_sel:DWORD dst_unused:UNUSED_PAD src0_sel:WORD_1
	v_mad_i64_i32 v[140:141], s[10:11], v144, s90, v[148:149]
	v_lshl_add_u64 v[140:141], v[140:141], 0, v[150:151]
	v_cvt_f32_f16_e32 v132, v133
	v_cvt_f32_f16_sdwa v133, v133 dst_sel:DWORD dst_unused:UNUSED_PAD src0_sel:WORD_1
	global_store_dwordx4 v[140:141], v[136:139], off offset:256
	global_store_dwordx4 v[140:141], v[136:139], off offset:640
	global_store_dwordx4 v[140:141], v[136:139], off offset:1024
	global_store_dwordx4 v[140:141], v[136:139], off offset:1408
	v_add_u32_e32 v140, 0xa0, v166
	s_nop 0
	v_cvt_f32_f16_e32 v138, v134
	v_cvt_f32_f16_sdwa v139, v134 dst_sel:DWORD dst_unused:UNUSED_PAD src0_sel:WORD_1
	v_mul_f32_e32 v136, v28, v142
	v_mul_f32_e32 v137, v29, v143
	v_cvt_f32_f16_e32 v134, v135
	v_sub_f32_e32 v141, v136, v137
	v_mul_f32_e32 v136, v29, v142
	v_mul_f32_e32 v137, v28, v143
	v_cvt_f32_f16_sdwa v135, v135 dst_sel:DWORD dst_unused:UNUSED_PAD src0_sel:WORD_1
	v_add_f32_e32 v142, v136, v137
	v_mul_f32_e32 v136, v30, v132
	v_mul_f32_e32 v137, v31, v133
	v_mul_f32_e32 v132, v31, v132
	v_mul_f32_e32 v133, v30, v133
	v_sub_f32_e32 v136, v136, v137
	v_add_f32_e32 v137, v132, v133
	v_mul_f32_e32 v132, v24, v138
	v_mul_f32_e32 v133, v25, v139
	s_nop 0
	v_sub_f32_e32 v143, v132, v133
	v_mul_f32_e32 v132, v25, v138
	v_mul_f32_e32 v133, v24, v139
	v_add_f32_e32 v138, v132, v133
	v_mul_f32_e32 v132, v26, v134
	v_mul_f32_e32 v133, v27, v135
	s_nop 0
	v_sub_f32_e32 v139, v132, v133
	v_mul_f32_e32 v132, v27, v134
	v_mul_f32_e32 v133, v26, v135
	v_add_f32_e32 v135, v132, v133
	v_cvt_pk_bf16_f32 v132, v141, v142
	v_cvt_pk_bf16_f32 v133, v136, v137
	v_cvt_pk_bf16_f32 v134, v143, v138
	v_cvt_pk_bf16_f32 v135, v139, v135
	v_cvt_f32_f16_e32 v138, v128
	v_cvt_f32_f16_sdwa v139, v128 dst_sel:DWORD dst_unused:UNUSED_PAD src0_sel:WORD_1
	v_mad_i64_i32 v[136:137], s[10:11], v140, s90, v[148:149]
	v_lshl_add_u64 v[136:137], v[136:137], 0, v[150:151]
	v_cvt_f32_f16_e32 v128, v129
	v_cvt_f32_f16_sdwa v129, v129 dst_sel:DWORD dst_unused:UNUSED_PAD src0_sel:WORD_1
	global_store_dwordx4 v[136:137], v[132:135], off offset:256
	global_store_dwordx4 v[136:137], v[132:135], off offset:640
	global_store_dwordx4 v[136:137], v[132:135], off offset:1024
	global_store_dwordx4 v[136:137], v[132:135], off offset:1408
	v_add_u32_e32 v136, 0xb0, v166
	s_nop 0
	v_cvt_f32_f16_e32 v134, v130
	v_cvt_f32_f16_sdwa v135, v130 dst_sel:DWORD dst_unused:UNUSED_PAD src0_sel:WORD_1
	v_mul_f32_e32 v132, v12, v138
	v_mul_f32_e32 v133, v13, v139
	v_cvt_f32_f16_e32 v130, v131
	v_sub_f32_e32 v137, v132, v133
	v_mul_f32_e32 v132, v13, v138
	v_mul_f32_e32 v133, v12, v139
	v_cvt_f32_f16_sdwa v131, v131 dst_sel:DWORD dst_unused:UNUSED_PAD src0_sel:WORD_1
	v_add_f32_e32 v138, v132, v133
	v_mul_f32_e32 v132, v14, v128
	v_mul_f32_e32 v133, v15, v129
	v_mul_f32_e32 v128, v15, v128
	v_mul_f32_e32 v129, v14, v129
	v_sub_f32_e32 v132, v132, v133
	v_add_f32_e32 v133, v128, v129
	v_mul_f32_e32 v128, v8, v134
	v_mul_f32_e32 v129, v9, v135
	s_nop 0
	v_sub_f32_e32 v139, v128, v129
	v_mul_f32_e32 v128, v9, v134
	v_mul_f32_e32 v129, v8, v135
	v_add_f32_e32 v134, v128, v129
	v_mul_f32_e32 v128, v10, v130
	v_mul_f32_e32 v129, v11, v131
	s_nop 0
	v_sub_f32_e32 v135, v128, v129
	v_mul_f32_e32 v128, v11, v130
	v_mul_f32_e32 v129, v10, v131
	v_add_f32_e32 v131, v128, v129
	v_cvt_pk_bf16_f32 v128, v137, v138
	v_cvt_pk_bf16_f32 v129, v132, v133
	v_mad_i64_i32 v[132:133], s[10:11], v136, s90, v[148:149]
	v_cvt_pk_bf16_f32 v130, v139, v134
	v_cvt_pk_bf16_f32 v131, v135, v131
	v_lshl_add_u64 v[132:133], v[132:133], 0, v[150:151]
	global_store_dwordx4 v[132:133], v[128:131], off offset:256
	global_store_dwordx4 v[132:133], v[128:131], off offset:640
	global_store_dwordx4 v[132:133], v[128:131], off offset:1024
	global_store_dwordx4 v[132:133], v[128:131], off offset:1408

; __device__ __forceinline__ u32x4 pack8(f32x4 v0, f32x4 v1) { u32x4 w; w.x = cvt_pk_bf16(v0[0], v0[1]); w.y = cvt_pk_bf16(v0[2], v0[3]); w.z = cvt_pk_bf16(v1[0], v1[1]); w.w = cvt_pk_bf16(v1[2], v1[3]); return w; }
; #define EPI_PIN8(a) asm volatile("" : "+v"(a[0][0]), "+v"(a[0][1]), "+v"(a[0][2]), "+v"(a[0][3]), "+v"(a[1][0]), "+v"(a[1][1]), "+v"(a[1][2]), "+v"(a[1][3]) :: "memory")
; __device__ __forceinline__ void rope8h(f32x4& v0, f32x4& v1, u32x4 t) {
;     float c[4], s[4];
; #pragma unroll
;     for (int k = 0; k < 4; ++k) { const h16x2 h = __builtin_bit_cast(h16x2, (unsigned)t[k]); c[k] = (float)h[0]; s[k] = (float)h[1]; }
;     f32x4 a, b;
;     a[0] = v0[0] * c[0] - v0[1] * s[0]; a[1] = v0[1] * c[0] + v0[0] * s[0]; a[2] = v0[2] * c[1] - v0[3] * s[1]; a[3] = v0[3] * c[1] + v0[2] * s[1];
;     b[0] = v1[0] * c[2] - v1[1] * s[2]; b[1] = v1[1] * c[2] + v1[0] * s[2]; b[2] = v1[2] * c[3] - v1[3] * s[3]; b[3] = v1[3] * c[3] + v1[2] * s[3];
;     v0 = a; v1 = b;
; }
;     __device__ __forceinline__ int operator()(AccT acc, const Unit& u, int wr, int wc, int, int) const {
;     ...
;         } else if (pn <= 5) {
;             bf16_t* dst = (pn <= 3) ? DQ : DK; const int cbase = ((pn - 2) & 1) * 256; const int p0 = 16 * (wc & 1) + 4 * fq; const float qs = (pn <= 3) ? QSC_DIFF : 1.0f;
;             u32x4 th[2][4];
; #pragma unroll
;             for (int ai = 0; ai < 2; ++ai)
; #pragma unroll
;                 for (int m = 0; m < 4; ++m) { const int pos = (row0 + ai * HALF + m * 16) & (SEQ - 1); th[ai][m] = *(const u32x4*)(rope + (size_t)pos * 32 + p0); }
;             EPI_PIN8(th);
; #pragma unroll
;             for (int ai = 0; ai < 2; ++ai)
; #pragma unroll
;                 for (int m = 0; m < 4; ++m) { const int r = row0 + ai * HALF + m * 16;
; #pragma unroll
;                     for (int bj = 0; bj < 2; ++bj) { f32x4 v0 = acc[ai][bj][m][0] * qs, v1 = acc[ai][bj][m][1] * qs; rope8h(v0, v1, th[ai][m]);
;                         *(u32x4*)(dst + (size_t)r * 512 + cbase + bj * HALF + cw) = pack8(v0, v1); } }
.LBB0_280:
	s_andn2_b64 vcc, exec, s[10:11]
	s_cbranch_vccnz .LBB0_282
	v_lshl_add_u32 v128, v170, 2, s79
	v_ashrrev_i32_e32 v129, 31, v128
	v_lshlrev_b32_e32 v130, 7, v166
	v_lshl_add_u64 v[128:129], v[128:129], 2, s[26:27]
	v_and_b32_e32 v160, 0xfe780, v130
	v_lshl_add_u64 v[130:131], v[128:129], 0, v[160:161]
	global_load_dwordx4 v[182:185], v[130:131], off
	global_load_dwordx4 v[186:189], v[130:131], off offset:2048
	v_add_co_u32_e32 v130, vcc, s89, v130
	s_cmp_lt_u32 s14, 4
	s_nop 0
	v_addc_co_u32_e32 v131, vcc, 0, v131, vcc
	global_load_dwordx4 v[148:151], v[130:131], off
	global_load_dwordx4 v[144:147], v[130:131], off offset:2048
	v_lshl_add_u32 v130, v166, 5, v178
	v_and_b32_e32 v130, 0x3f9e0, v130
	v_lshlrev_b32_e32 v160, 2, v130
	v_lshl_add_u64 v[128:129], v[128:129], 0, v[160:161]
	global_load_dwordx4 v[140:143], v[128:129], off
	global_load_dwordx4 v[136:139], v[128:129], off offset:2048
	v_add_co_u32_e32 v128, vcc, s89, v128
	s_brev_b32 s20, 36
	s_nop 0
	v_addc_co_u32_e32 v129, vcc, 0, v129, vcc
	global_load_dwordx4 v[132:135], v[128:129], off
	s_nop 0
	global_load_dwordx4 v[128:131], v[128:129], off offset:2048
	s_cselect_b64 vcc, -1, 0
	s_and_b64 s[10:11], vcc, exec
	s_cselect_b32 s10, s20, 0x28000000
	s_add_u32 s10, s12, s10
	s_addc_u32 s11, s13, 0
	s_lshl_b32 s20, s14, 9
	v_cndmask_b32_e32 v160, 1.0, v179, vcc
	s_and_b32 s20, s20, 0x200
	v_mul_f32_e32 v190, v160, v126
	v_mul_f32_e32 v191, v160, v127
	v_mul_f32_e32 v192, v160, v124
	v_mul_f32_e32 v193, v160, v125
	v_mul_f32_e32 v196, v160, v120
	v_mul_f32_e32 v197, v160, v121
	s_add_u32 s10, s10, s20
	v_ashrrev_i32_e32 v169, 31, v168
	v_mul_f32_e32 v194, v160, v122
	v_mul_f32_e32 v195, v160, v123
	v_mul_f32_e32 v200, v160, v118
	v_mul_f32_e32 v201, v160, v119
	v_mul_f32_e32 v202, v160, v116
	v_mul_f32_e32 v203, v160, v117
	v_mul_f32_e32 v204, v160, v114
	v_mul_f32_e32 v205, v160, v115
	v_mul_f32_e32 v206, v160, v112
	v_mul_f32_e32 v207, v160, v113
	s_addc_u32 s11, s11, 0
	v_ashrrev_i32_e32 v167, 31, v166
	v_lshl_add_u64 v[172:173], v[168:169], 1, s[10:11]
	v_lshlrev_b64 v[170:171], 10, v[166:167]
	v_lshl_add_u64 v[170:171], v[172:173], 0, v[170:171]
	s_mov_b32 s10, 0x20000
	s_waitcnt vmcnt(0)
	s_nop 0
	v_cvt_f32_f16_e32 v208, v182
	v_cvt_f32_f16_sdwa v209, v182 dst_sel:DWORD dst_unused:UNUSED_PAD src0_sel:WORD_1
	v_cvt_f32_f16_e32 v182, v183
	v_cvt_f32_f16_sdwa v183, v183 dst_sel:DWORD dst_unused:UNUSED_PAD src0_sel:WORD_1
	v_cvt_f32_f16_e32 v210, v184
	v_cvt_f32_f16_sdwa v211, v184 dst_sel:DWORD dst_unused:UNUSED_PAD src0_sel:WORD_1
	v_cvt_f32_f16_e32 v184, v185
	v_cvt_f32_f16_sdwa v185, v185 dst_sel:DWORD dst_unused:UNUSED_PAD src0_sel:WORD_1
	v_mul_f32_e32 v212, v192, v208
	v_mul_f32_e32 v213, v193, v209
	v_pk_mul_f32 v[192:193], v[192:193], v[208:209] op_sel:[1,0] op_sel_hi:[0,1]
	v_mul_f32_e32 v214, v190, v182
	v_mul_f32_e32 v215, v191, v183
	v_mul_f32_e32 v216, v196, v210
	v_mul_f32_e32 v217, v197, v211
	v_pk_mul_f32 v[196:197], v[196:197], v[210:211] op_sel:[1,0] op_sel_hi:[0,1]
	v_pk_mul_f32 v[190:191], v[190:191], v[182:183] op_sel:[1,0] op_sel_hi:[0,1]
	v_mul_f32_e32 v218, v194, v184
	v_mul_f32_e32 v219, v195, v185
	v_pk_mul_f32 v[194:195], v[194:195], v[184:185] op_sel:[1,0] op_sel_hi:[0,1]
	v_mul_f32_e32 v220, v202, v208
	v_mul_f32_e32 v221, v203, v209
	v_pk_mul_f32 v[202:203], v[202:203], v[208:209] op_sel:[1,0] op_sel_hi:[0,1]
	v_mul_f32_e32 v208, v200, v182
	v_mul_f32_e32 v209, v201, v183
	v_mul_f32_e32 v182, v201, v182
	v_mul_f32_e32 v183, v200, v183
	v_mul_f32_e32 v200, v206, v210
	v_mul_f32_e32 v201, v207, v211
	v_pk_mul_f32 v[206:207], v[206:207], v[210:211] op_sel:[1,0] op_sel_hi:[0,1]
	v_mul_f32_e32 v210, v204, v184
	v_mul_f32_e32 v211, v205, v185
	v_mul_f32_e32 v184, v205, v184
	v_mul_f32_e32 v185, v204, v185
	v_add_f32_e32 v169, v192, v193
	v_sub_f32_e32 v192, v214, v215
	v_add_f32_e32 v193, v196, v197
	v_sub_f32_e32 v167, v212, v213
	v_add_f32_e32 v190, v190, v191
	v_sub_f32_e32 v191, v216, v217
	v_add_f32_e32 v197, v202, v203
	v_add_f32_e32 v202, v182, v183
	v_add_f32_e32 v204, v184, v185
	v_cvt_pk_bf16_f32 v182, v167, v169
	v_cvt_pk_bf16_f32 v183, v192, v190
	v_cvt_pk_bf16_f32 v184, v191, v193
	v_cvt_f32_f16_e32 v192, v186
	v_cvt_f32_f16_sdwa v193, v186 dst_sel:DWORD dst_unused:UNUSED_PAD src0_sel:WORD_1
	v_sub_f32_e32 v196, v218, v219
	v_add_f32_e32 v194, v194, v195
	v_cvt_pk_bf16_f32 v185, v196, v194
	v_sub_f32_e32 v195, v220, v221
	v_sub_f32_e32 v198, v208, v209
	v_sub_f32_e32 v200, v200, v201
	v_add_f32_e32 v201, v206, v207
	v_sub_f32_e32 v203, v210, v211
	global_store_dwordx4 v[170:171], v[182:185], off
	v_cvt_f32_f16_e32 v186, v187
	v_cvt_f32_f16_sdwa v187, v187 dst_sel:DWORD dst_unused:UNUSED_PAD src0_sel:WORD_1
	v_cvt_pk_bf16_f32 v182, v195, v197
	v_cvt_pk_bf16_f32 v183, v198, v202
	v_cvt_pk_bf16_f32 v184, v200, v201
	v_cvt_pk_bf16_f32 v185, v203, v204
	global_store_dwordx4 v[170:171], v[182:185], off offset:256
	v_mul_f32_e32 v196, v160, v104
	v_mul_f32_e32 v197, v160, v105
	v_mul_f32_e32 v194, v160, v106
	v_mul_f32_e32 v195, v160, v107
	v_mul_f32_e32 v184, v160, v108
	v_mul_f32_e32 v185, v160, v109
	v_or_b32_e32 v182, 16, v166
	v_mul_f32_e32 v200, v184, v192
	v_mul_f32_e32 v201, v185, v193
	v_ashrrev_i32_e32 v183, 31, v182
	v_sub_f32_e32 v167, v200, v201
	v_cvt_f32_f16_e32 v200, v188
	v_cvt_f32_f16_sdwa v201, v188 dst_sel:DWORD dst_unused:UNUSED_PAD src0_sel:WORD_1
	v_lshlrev_b64 v[182:183], 10, v[182:183]
	v_lshl_add_u64 v[190:191], v[172:173], 0, v[182:183]
	v_mul_f32_e32 v182, v160, v110
	v_mul_f32_e32 v183, v160, v111
	v_pk_mul_f32 v[184:185], v[184:185], v[192:193] op_sel:[1,0] op_sel_hi:[0,1]
	v_cvt_f32_f16_e32 v188, v189
; __device__ __forceinline__ u32x4 pack8(f32x4 v0, f32x4 v1) { u32x4 w; w.x = cvt_pk_bf16(v0[0], v0[1]); w.y = cvt_pk_bf16(v0[2], v0[3]); w.z = cvt_pk_bf16(v1[0], v1[1]); w.w = cvt_pk_bf16(v1[2], v1[3]); return w; }
; __device__ __forceinline__ void rope8h(f32x4& v0, f32x4& v1, u32x4 t) {
;     float c[4], s[4];
; #pragma unroll
;     for (int k = 0; k < 4; ++k) { const h16x2 h = __builtin_bit_cast(h16x2, (unsigned)t[k]); c[k] = (float)h[0]; s[k] = (float)h[1]; }
;     f32x4 a, b;
;     a[0] = v0[0] * c[0] - v0[1] * s[0]; a[1] = v0[1] * c[0] + v0[0] * s[0]; a[2] = v0[2] * c[1] - v0[3] * s[1]; a[3] = v0[3] * c[1] + v0[2] * s[1];
;     b[0] = v1[0] * c[2] - v1[1] * s[2]; b[1] = v1[1] * c[2] + v1[0] * s[2]; b[2] = v1[2] * c[3] - v1[3] * s[3]; b[3] = v1[3] * c[3] + v1[2] * s[3];
;     v0 = a; v1 = b;
; }
;     __device__ __forceinline__ int operator()(AccT acc, const Unit& u, int wr, int wc, int, int) const {
;     ...
;             for (int ai = 0; ai < 2; ++ai)
; #pragma unroll
;                 for (int m = 0; m < 4; ++m) { const int r = row0 + ai * HALF + m * 16;
; #pragma unroll
;                     for (int bj = 0; bj < 2; ++bj) { f32x4 v0 = acc[ai][bj][m][0] * qs, v1 = acc[ai][bj][m][1] * qs; rope8h(v0, v1, th[ai][m]);
;                         *(u32x4*)(dst + (size_t)r * 512 + cbase + bj * HALF + cw) = pack8(v0, v1); } }
	v_cvt_f32_f16_sdwa v189, v189 dst_sel:DWORD dst_unused:UNUSED_PAD src0_sel:WORD_1
	v_add_f32_e32 v169, v184, v185
	v_mul_f32_e32 v184, v182, v186
	v_mul_f32_e32 v185, v183, v187
	v_pk_mul_f32 v[182:183], v[182:183], v[186:187] op_sel:[1,0] op_sel_hi:[0,1]
	v_sub_f32_e32 v184, v184, v185
	v_add_f32_e32 v185, v182, v183
	v_mul_f32_e32 v182, v196, v200
	v_mul_f32_e32 v183, v197, v201
	s_nop 0
	v_sub_f32_e32 v198, v182, v183
	v_mul_f32_e32 v182, v197, v200
	v_mul_f32_e32 v183, v196, v201
	v_add_f32_e32 v196, v182, v183
	v_mul_f32_e32 v182, v194, v188
	v_mul_f32_e32 v183, v195, v189
	s_nop 0
	v_sub_f32_e32 v197, v182, v183
	v_mul_f32_e32 v182, v195, v188
	v_mul_f32_e32 v183, v194, v189
	v_add_f32_e32 v194, v182, v183
	v_cvt_pk_bf16_f32 v182, v167, v169
	v_cvt_pk_bf16_f32 v183, v184, v185
	v_cvt_pk_bf16_f32 v184, v198, v196
	v_cvt_pk_bf16_f32 v185, v197, v194
	global_store_dwordx4 v[190:191], v[182:185], off
	v_mul_f32_e32 v196, v160, v96
	v_mul_f32_e32 v197, v160, v97
	v_mul_f32_e32 v194, v160, v98
	v_mul_f32_e32 v195, v160, v99
	v_mul_f32_e32 v184, v160, v100
	v_mul_f32_e32 v185, v160, v101
	v_mul_f32_e32 v182, v160, v102
	v_mul_f32_e32 v183, v160, v103
	v_mul_f32_e32 v202, v184, v192
	v_mul_f32_e32 v203, v185, v193
	v_pk_mul_f32 v[184:185], v[184:185], v[192:193] op_sel:[1,0] op_sel_hi:[0,1]
	v_add_f32_e32 v169, v184, v185
	v_mul_f32_e32 v184, v182, v186
	v_mul_f32_e32 v185, v183, v187
	v_pk_mul_f32 v[182:183], v[182:183], v[186:187] op_sel:[1,0] op_sel_hi:[0,1]
	v_sub_f32_e32 v184, v184, v185
	v_add_f32_e32 v185, v182, v183
	v_mul_f32_e32 v182, v196, v200
	v_mul_f32_e32 v183, v197, v201
	v_sub_f32_e32 v167, v202, v203
	v_sub_f32_e32 v186, v182, v183
	v_mul_f32_e32 v182, v197, v200
	v_mul_f32_e32 v183, v196, v201
	v_add_f32_e32 v187, v182, v183
	v_mul_f32_e32 v182, v194, v188
	v_mul_f32_e32 v183, v195, v189
	v_cvt_f32_f16_e32 v196, v149
	v_sub_f32_e32 v192, v182, v183
	v_mul_f32_e32 v182, v195, v188
	v_mul_f32_e32 v183, v194, v189
	v_add_f32_e32 v188, v182, v183
	v_cvt_pk_bf16_f32 v182, v167, v169
	v_cvt_pk_bf16_f32 v183, v184, v185
	v_cvt_pk_bf16_f32 v184, v186, v187
	v_cvt_f32_f16_e32 v186, v148
	v_cvt_f32_f16_sdwa v187, v148 dst_sel:DWORD dst_unused:UNUSED_PAD src0_sel:WORD_1
	v_cvt_f32_f16_sdwa v197, v149 dst_sel:DWORD dst_unused:UNUSED_PAD src0_sel:WORD_1
	v_cvt_pk_bf16_f32 v185, v192, v188
	v_mul_f32_e32 v188, v160, v92
	v_mul_f32_e32 v189, v160, v93
	global_store_dwordx4 v[190:191], v[182:185], off offset:256
	v_mul_f32_e32 v194, v188, v186
	v_mul_f32_e32 v195, v189, v187
	v_mul_f32_e32 v148, v189, v186
	v_mul_f32_e32 v149, v188, v187
	v_mul_f32_e32 v184, v160, v94
	v_mul_f32_e32 v185, v160, v95
	v_cvt_f32_f16_e32 v188, v150
	v_cvt_f32_f16_sdwa v189, v150 dst_sel:DWORD dst_unused:UNUSED_PAD src0_sel:WORD_1
	v_add_f32_e32 v169, v148, v149
	v_mul_f32_e32 v148, v184, v196
	v_mul_f32_e32 v149, v185, v197
	v_mul_f32_e32 v192, v160, v88
	v_mul_f32_e32 v193, v160, v89
	v_sub_f32_e32 v150, v148, v149
	v_mul_f32_e32 v148, v185, v196
	v_mul_f32_e32 v149, v184, v197
	v_cvt_f32_f16_e32 v184, v151
	v_cvt_f32_f16_sdwa v185, v151 dst_sel:DWORD dst_unused:UNUSED_PAD src0_sel:WORD_1
	v_sub_f32_e32 v167, v194, v195
	v_add_f32_e32 v194, v148, v149
	v_mul_f32_e32 v148, v192, v188
	v_mul_f32_e32 v149, v193, v189
	v_or_b32_e32 v182, 32, v166
	v_mul_f32_e32 v190, v160, v90
	v_mul_f32_e32 v191, v160, v91
	v_sub_f32_e32 v151, v148, v149
	v_mul_f32_e32 v148, v193, v188
	v_mul_f32_e32 v149, v192, v189
	v_ashrrev_i32_e32 v183, 31, v182
	v_add_f32_e32 v192, v148, v149
	v_mul_f32_e32 v148, v190, v184
	v_mul_f32_e32 v149, v191, v185
	v_lshlrev_b64 v[182:183], 10, v[182:183]
	v_sub_f32_e32 v193, v148, v149
	v_mul_f32_e32 v148, v191, v184
	v_mul_f32_e32 v149, v190, v185
	v_lshl_add_u64 v[182:183], v[172:173], 0, v[182:183]
	v_add_f32_e32 v190, v148, v149
	v_cvt_pk_bf16_f32 v148, v167, v169
	v_cvt_pk_bf16_f32 v149, v150, v194
	v_cvt_pk_bf16_f32 v150, v151, v192
	v_cvt_pk_bf16_f32 v151, v193, v190
	global_store_dwordx4 v[182:183], v[148:151], off
	v_mul_f32_e32 v192, v160, v80
	v_mul_f32_e32 v193, v160, v81
	v_mul_f32_e32 v190, v160, v82
	v_mul_f32_e32 v191, v160, v83
	v_mul_f32_e32 v150, v160, v84
	v_mul_f32_e32 v151, v160, v85
	v_mul_f32_e32 v148, v160, v86
	v_mul_f32_e32 v149, v160, v87
	v_mul_f32_e32 v194, v150, v186
	v_mul_f32_e32 v195, v151, v187
	v_pk_mul_f32 v[150:151], v[150:151], v[186:187] op_sel:[1,0] op_sel_hi:[0,1]
	v_add_f32_e32 v169, v150, v151
	v_mul_f32_e32 v150, v148, v196
	v_mul_f32_e32 v151, v149, v197
	v_pk_mul_f32 v[148:149], v[148:149], v[196:197] op_sel:[1,0] op_sel_hi:[0,1]
	v_sub_f32_e32 v150, v150, v151
	v_add_f32_e32 v151, v148, v149
	v_mul_f32_e32 v148, v192, v188
	v_mul_f32_e32 v149, v193, v189
	v_sub_f32_e32 v167, v194, v195
	v_sub_f32_e32 v186, v148, v149
	v_mul_f32_e32 v148, v193, v188
	v_mul_f32_e32 v149, v192, v189
	v_add_f32_e32 v187, v148, v149
	v_mul_f32_e32 v148, v190, v184
	v_mul_f32_e32 v149, v191, v185
	s_nop 0
	v_sub_f32_e32 v188, v148, v149
	v_mul_f32_e32 v148, v191, v184
	v_mul_f32_e32 v149, v190, v185
	v_add_f32_e32 v184, v148, v149
	v_cvt_pk_bf16_f32 v148, v167, v169
	v_cvt_pk_bf16_f32 v149, v150, v151
	v_cvt_pk_bf16_f32 v150, v186, v187
	v_cvt_pk_bf16_f32 v151, v188, v184
	global_store_dwordx4 v[182:183], v[148:151], off offset:256
	v_cvt_f32_f16_e32 v190, v145
	v_cvt_f32_f16_sdwa v191, v145 dst_sel:DWORD dst_unused:UNUSED_PAD src0_sel:WORD_1
	v_or_b32_e32 v148, 48, v166
	v_ashrrev_i32_e32 v149, 31, v148
	v_lshlrev_b64 v[148:149], 10, v[148:149]
	v_lshl_add_u64 v[148:149], v[172:173], 0, v[148:149]
	v_cvt_f32_f16_e32 v172, v144
	v_cvt_f32_f16_sdwa v173, v144 dst_sel:DWORD dst_unused:UNUSED_PAD src0_sel:WORD_1
; __device__ __forceinline__ u32x4 pack8(f32x4 v0, f32x4 v1) { u32x4 w; w.x = cvt_pk_bf16(v0[0], v0[1]); w.y = cvt_pk_bf16(v0[2], v0[3]); w.z = cvt_pk_bf16(v1[0], v1[1]); w.w = cvt_pk_bf16(v1[2], v1[3]); return w; }
; __device__ __forceinline__ void rope8h(f32x4& v0, f32x4& v1, u32x4 t) {
;     float c[4], s[4];
; #pragma unroll
;     for (int k = 0; k < 4; ++k) { const h16x2 h = __builtin_bit_cast(h16x2, (unsigned)t[k]); c[k] = (float)h[0]; s[k] = (float)h[1]; }
;     f32x4 a, b;
;     a[0] = v0[0] * c[0] - v0[1] * s[0]; a[1] = v0[1] * c[0] + v0[0] * s[0]; a[2] = v0[2] * c[1] - v0[3] * s[1]; a[3] = v0[3] * c[1] + v0[2] * s[1];
;     b[0] = v1[0] * c[2] - v1[1] * s[2]; b[1] = v1[1] * c[2] + v1[0] * s[2]; b[2] = v1[2] * c[3] - v1[3] * s[3]; b[3] = v1[3] * c[3] + v1[2] * s[3];
;     v0 = a; v1 = b;
; }
;     __device__ __forceinline__ int operator()(AccT acc, const Unit& u, int wr, int wc, int, int) const {
;     ...
;             for (int ai = 0; ai < 2; ++ai)
; #pragma unroll
;                 for (int m = 0; m < 4; ++m) { const int r = row0 + ai * HALF + m * 16;
; #pragma unroll
;                     for (int bj = 0; bj < 2; ++bj) { f32x4 v0 = acc[ai][bj][m][0] * qs, v1 = acc[ai][bj][m][1] * qs; rope8h(v0, v1, th[ai][m]);
;                         *(u32x4*)(dst + (size_t)r * 512 + cbase + bj * HALF + cw) = pack8(v0, v1); } }
	v_mul_f32_e32 v182, v160, v76
	v_mul_f32_e32 v183, v160, v77
	v_mul_f32_e32 v150, v160, v78
	v_mul_f32_e32 v151, v160, v79
	v_mul_f32_e32 v186, v160, v72
	v_mul_f32_e32 v187, v160, v73
	v_mul_f32_e32 v188, v182, v172
	v_mul_f32_e32 v189, v183, v173
	v_mul_f32_e32 v144, v183, v172
	v_mul_f32_e32 v145, v182, v173
	v_cvt_f32_f16_e32 v182, v146
	v_cvt_f32_f16_sdwa v183, v146 dst_sel:DWORD dst_unused:UNUSED_PAD src0_sel:WORD_1
	v_add_f32_e32 v169, v144, v145
	v_mul_f32_e32 v144, v150, v190
	v_mul_f32_e32 v145, v151, v191
	v_sub_f32_e32 v167, v188, v189
	v_sub_f32_e32 v146, v144, v145
	v_mul_f32_e32 v144, v151, v190
	v_mul_f32_e32 v145, v150, v191
	v_cvt_f32_f16_e32 v150, v147
	v_cvt_f32_f16_sdwa v151, v147 dst_sel:DWORD dst_unused:UNUSED_PAD src0_sel:WORD_1
	v_add_f32_e32 v188, v144, v145
	v_mul_f32_e32 v144, v186, v182
	v_mul_f32_e32 v145, v187, v183
	v_mul_f32_e32 v184, v160, v74
	v_mul_f32_e32 v185, v160, v75
	v_sub_f32_e32 v147, v144, v145
	v_mul_f32_e32 v144, v187, v182
	v_mul_f32_e32 v145, v186, v183
	v_add_f32_e32 v186, v144, v145
	v_mul_f32_e32 v144, v184, v150
	v_mul_f32_e32 v145, v185, v151
	s_nop 0
	v_sub_f32_e32 v187, v144, v145
	v_mul_f32_e32 v144, v185, v150
	v_mul_f32_e32 v145, v184, v151
	v_add_f32_e32 v184, v144, v145
	v_cvt_pk_bf16_f32 v144, v167, v169
	v_cvt_pk_bf16_f32 v145, v146, v188
	v_cvt_pk_bf16_f32 v146, v147, v186
	v_cvt_pk_bf16_f32 v147, v187, v184
	global_store_dwordx4 v[148:149], v[144:147], off
	v_mul_f32_e32 v186, v160, v64
	v_mul_f32_e32 v187, v160, v65
	v_mul_f32_e32 v184, v160, v66
	v_mul_f32_e32 v185, v160, v67
	v_mul_f32_e32 v146, v160, v68
	v_mul_f32_e32 v147, v160, v69
	v_mul_f32_e32 v144, v160, v70
	v_mul_f32_e32 v145, v160, v71
	v_mul_f32_e32 v188, v146, v172
	v_mul_f32_e32 v189, v147, v173
	v_pk_mul_f32 v[146:147], v[146:147], v[172:173] op_sel:[1,0] op_sel_hi:[0,1]
	v_add_f32_e32 v169, v146, v147
	v_mul_f32_e32 v146, v144, v190
	v_mul_f32_e32 v147, v145, v191
	v_pk_mul_f32 v[144:145], v[144:145], v[190:191] op_sel:[1,0] op_sel_hi:[0,1]
	v_sub_f32_e32 v146, v146, v147
	v_add_f32_e32 v147, v144, v145
	v_mul_f32_e32 v144, v186, v182
	v_mul_f32_e32 v145, v187, v183
	v_sub_f32_e32 v167, v188, v189
	v_sub_f32_e32 v172, v144, v145
	v_mul_f32_e32 v144, v187, v182
	v_mul_f32_e32 v145, v186, v183
	v_add_f32_e32 v173, v144, v145
	v_mul_f32_e32 v144, v184, v150
	v_mul_f32_e32 v145, v185, v151
	v_cvt_f32_f16_e32 v186, v141
	v_sub_f32_e32 v182, v144, v145
	v_mul_f32_e32 v144, v185, v150
	v_mul_f32_e32 v145, v184, v151
	v_add_f32_e32 v150, v144, v145
	v_cvt_pk_bf16_f32 v144, v167, v169
	v_cvt_pk_bf16_f32 v145, v146, v147
	v_cvt_pk_bf16_f32 v146, v172, v173
	v_cvt_pk_bf16_f32 v147, v182, v150
	global_store_dwordx4 v[148:149], v[144:147], off offset:256
	v_cvt_f32_f16_e32 v148, v140
	v_cvt_f32_f16_sdwa v149, v140 dst_sel:DWORD dst_unused:UNUSED_PAD src0_sel:WORD_1
	v_cvt_f32_f16_sdwa v187, v141 dst_sel:DWORD dst_unused:UNUSED_PAD src0_sel:WORD_1
	v_mul_f32_e32 v150, v160, v60
	v_mul_f32_e32 v151, v160, v61
	v_mul_f32_e32 v146, v160, v62
	v_mul_f32_e32 v147, v160, v63
	v_mul_f32_e32 v184, v150, v148
	v_mul_f32_e32 v185, v151, v149
	v_mul_f32_e32 v140, v151, v148
	v_mul_f32_e32 v141, v150, v149
	v_cvt_f32_f16_e32 v150, v142
	v_cvt_f32_f16_sdwa v151, v142 dst_sel:DWORD dst_unused:UNUSED_PAD src0_sel:WORD_1
	v_add_f32_e32 v169, v140, v141
	v_mul_f32_e32 v140, v146, v186
	v_mul_f32_e32 v141, v147, v187
	v_mul_f32_e32 v182, v160, v56
	v_mul_f32_e32 v183, v160, v57
	v_sub_f32_e32 v142, v140, v141
	v_mul_f32_e32 v140, v147, v186
	v_mul_f32_e32 v141, v146, v187
	v_cvt_f32_f16_e32 v146, v143
	v_cvt_f32_f16_sdwa v147, v143 dst_sel:DWORD dst_unused:UNUSED_PAD src0_sel:WORD_1
	v_sub_f32_e32 v167, v184, v185
	v_add_f32_e32 v184, v140, v141
	v_mul_f32_e32 v140, v182, v150
	v_mul_f32_e32 v141, v183, v151
	v_mul_f32_e32 v172, v160, v58
	v_mul_f32_e32 v173, v160, v59
	v_sub_f32_e32 v143, v140, v141
	v_mul_f32_e32 v140, v183, v150
	v_mul_f32_e32 v141, v182, v151
	v_add_f32_e32 v182, v140, v141
	v_mul_f32_e32 v140, v172, v146
	v_mul_f32_e32 v141, v173, v147
	v_lshl_add_u64 v[144:145], v[170:171], 0, s[34:35]
	v_sub_f32_e32 v183, v140, v141
	v_mul_f32_e32 v140, v173, v146
	v_mul_f32_e32 v141, v172, v147
	v_add_f32_e32 v172, v140, v141
	v_cvt_pk_bf16_f32 v140, v167, v169
	v_cvt_pk_bf16_f32 v141, v142, v184
	v_cvt_pk_bf16_f32 v142, v143, v182
	v_cvt_pk_bf16_f32 v143, v183, v172
	v_add_co_u32_e32 v172, vcc, s10, v170
	v_mul_f32_e32 v182, v160, v48
	v_mul_f32_e32 v183, v160, v49
	s_nop 0
	v_addc_co_u32_e32 v173, vcc, 0, v171, vcc
	global_store_dwordx4 v[172:173], v[140:143], off
	v_mul_f32_e32 v172, v160, v50
	v_mul_f32_e32 v173, v160, v51
	s_mov_b32 s10, 0x24000
	v_mul_f32_e32 v142, v160, v52
	v_mul_f32_e32 v143, v160, v53
	v_mul_f32_e32 v140, v160, v54
	v_mul_f32_e32 v141, v160, v55
	v_mul_f32_e32 v184, v142, v148
	v_mul_f32_e32 v185, v143, v149
	v_pk_mul_f32 v[142:143], v[142:143], v[148:149] op_sel:[1,0] op_sel_hi:[0,1]
	v_add_f32_e32 v148, v142, v143
	v_mul_f32_e32 v142, v140, v186
	v_mul_f32_e32 v143, v141, v187
	v_pk_mul_f32 v[140:141], v[140:141], v[186:187] op_sel:[1,0] op_sel_hi:[0,1]
	v_sub_f32_e32 v142, v142, v143
	v_add_f32_e32 v143, v140, v141
	v_mul_f32_e32 v140, v182, v150
	v_mul_f32_e32 v141, v183, v151
	v_sub_f32_e32 v167, v184, v185
	v_sub_f32_e32 v149, v140, v141
	v_mul_f32_e32 v140, v183, v150
	v_mul_f32_e32 v141, v182, v151
	v_add_f32_e32 v150, v140, v141
	v_mul_f32_e32 v140, v172, v146
	v_mul_f32_e32 v141, v173, v147
	v_cvt_f32_f16_e32 v182, v137
	v_sub_f32_e32 v151, v140, v141
	v_mul_f32_e32 v140, v173, v146
	v_mul_f32_e32 v141, v172, v147
	v_add_f32_e32 v146, v140, v141
	v_cvt_pk_bf16_f32 v140, v167, v148
; __device__ __forceinline__ u32x4 pack8(f32x4 v0, f32x4 v1) { u32x4 w; w.x = cvt_pk_bf16(v0[0], v0[1]); w.y = cvt_pk_bf16(v0[2], v0[3]); w.z = cvt_pk_bf16(v1[0], v1[1]); w.w = cvt_pk_bf16(v1[2], v1[3]); return w; }
; __device__ __forceinline__ void rope8h(f32x4& v0, f32x4& v1, u32x4 t) {
;     float c[4], s[4];
; #pragma unroll
;     for (int k = 0; k < 4; ++k) { const h16x2 h = __builtin_bit_cast(h16x2, (unsigned)t[k]); c[k] = (float)h[0]; s[k] = (float)h[1]; }
;     f32x4 a, b;
;     a[0] = v0[0] * c[0] - v0[1] * s[0]; a[1] = v0[1] * c[0] + v0[0] * s[0]; a[2] = v0[2] * c[1] - v0[3] * s[1]; a[3] = v0[3] * c[1] + v0[2] * s[1];
;     b[0] = v1[0] * c[2] - v1[1] * s[2]; b[1] = v1[1] * c[2] + v1[0] * s[2]; b[2] = v1[2] * c[3] - v1[3] * s[3]; b[3] = v1[3] * c[3] + v1[2] * s[3];
;     v0 = a; v1 = b;
; }
;     __device__ __forceinline__ int operator()(AccT acc, const Unit& u, int wr, int wc, int, int) const {
;     ...
;             for (int ai = 0; ai < 2; ++ai)
; #pragma unroll
;                 for (int m = 0; m < 4; ++m) { const int r = row0 + ai * HALF + m * 16;
; #pragma unroll
;                     for (int bj = 0; bj < 2; ++bj) { f32x4 v0 = acc[ai][bj][m][0] * qs, v1 = acc[ai][bj][m][1] * qs; rope8h(v0, v1, th[ai][m]);
;                         *(u32x4*)(dst + (size_t)r * 512 + cbase + bj * HALF + cw) = pack8(v0, v1); } }
	v_cvt_pk_bf16_f32 v141, v142, v143
	v_cvt_pk_bf16_f32 v142, v149, v150
	v_cvt_pk_bf16_f32 v143, v151, v146
	global_store_dwordx4 v[144:145], v[140:143], off offset:256
	v_cvt_f32_f16_e32 v144, v136
	v_cvt_f32_f16_sdwa v145, v136 dst_sel:DWORD dst_unused:UNUSED_PAD src0_sel:WORD_1
	v_cvt_f32_f16_sdwa v183, v137 dst_sel:DWORD dst_unused:UNUSED_PAD src0_sel:WORD_1
	v_mul_f32_e32 v146, v160, v44
	v_mul_f32_e32 v147, v160, v45
	v_mul_f32_e32 v142, v160, v46
	v_mul_f32_e32 v143, v160, v47
	v_mul_f32_e32 v172, v146, v144
	v_mul_f32_e32 v173, v147, v145
	v_mul_f32_e32 v136, v147, v144
	v_mul_f32_e32 v137, v146, v145
	v_cvt_f32_f16_e32 v146, v138
	v_cvt_f32_f16_sdwa v147, v138 dst_sel:DWORD dst_unused:UNUSED_PAD src0_sel:WORD_1
	v_add_f32_e32 v169, v136, v137
	v_mul_f32_e32 v136, v142, v182
	v_mul_f32_e32 v137, v143, v183
	v_mul_f32_e32 v150, v160, v40
	v_mul_f32_e32 v151, v160, v41
	v_sub_f32_e32 v138, v136, v137
	v_mul_f32_e32 v136, v143, v182
	v_mul_f32_e32 v137, v142, v183
	v_cvt_f32_f16_e32 v142, v139
	v_cvt_f32_f16_sdwa v143, v139 dst_sel:DWORD dst_unused:UNUSED_PAD src0_sel:WORD_1
	v_sub_f32_e32 v167, v172, v173
	v_add_f32_e32 v172, v136, v137
	v_mul_f32_e32 v136, v150, v146
	v_mul_f32_e32 v137, v151, v147
	v_mul_f32_e32 v148, v160, v42
	v_mul_f32_e32 v149, v160, v43
	v_sub_f32_e32 v139, v136, v137
	v_mul_f32_e32 v136, v151, v146
	v_mul_f32_e32 v137, v150, v147
	v_add_f32_e32 v150, v136, v137
	v_mul_f32_e32 v136, v148, v142
	v_mul_f32_e32 v137, v149, v143
	v_lshl_add_u64 v[140:141], v[170:171], 0, s[36:37]
	v_sub_f32_e32 v151, v136, v137
	v_mul_f32_e32 v136, v149, v142
	v_mul_f32_e32 v137, v148, v143
	v_add_f32_e32 v148, v136, v137
	v_cvt_pk_bf16_f32 v136, v167, v169
	v_cvt_pk_bf16_f32 v137, v138, v172
	v_cvt_pk_bf16_f32 v138, v139, v150
	v_cvt_pk_bf16_f32 v139, v151, v148
	v_add_co_u32_e32 v148, vcc, s10, v170
	v_mul_f32_e32 v150, v160, v32
	v_mul_f32_e32 v151, v160, v33
	s_nop 0
	v_addc_co_u32_e32 v149, vcc, 0, v171, vcc
	global_store_dwordx4 v[148:149], v[136:139], off
	v_mul_f32_e32 v148, v160, v34
	v_mul_f32_e32 v149, v160, v35
	s_mov_b32 s10, 0x28000
	v_mul_f32_e32 v138, v160, v36
	v_mul_f32_e32 v139, v160, v37
	v_mul_f32_e32 v136, v160, v38
	v_mul_f32_e32 v137, v160, v39
	v_mul_f32_e32 v172, v138, v144
	v_mul_f32_e32 v173, v139, v145
	v_pk_mul_f32 v[138:139], v[138:139], v[144:145] op_sel:[1,0] op_sel_hi:[0,1]
	v_add_f32_e32 v144, v138, v139
	v_mul_f32_e32 v138, v136, v182
	v_mul_f32_e32 v139, v137, v183
	v_pk_mul_f32 v[136:137], v[136:137], v[182:183] op_sel:[1,0] op_sel_hi:[0,1]
	v_sub_f32_e32 v138, v138, v139
	v_add_f32_e32 v139, v136, v137
	v_mul_f32_e32 v136, v150, v146
	v_mul_f32_e32 v137, v151, v147
	v_sub_f32_e32 v167, v172, v173
	v_sub_f32_e32 v145, v136, v137
	v_mul_f32_e32 v136, v151, v146
	v_mul_f32_e32 v137, v150, v147
	v_add_f32_e32 v146, v136, v137
	v_mul_f32_e32 v136, v148, v142
	v_mul_f32_e32 v137, v149, v143
	v_cvt_f32_f16_e32 v150, v133
	v_sub_f32_e32 v147, v136, v137
	v_mul_f32_e32 v136, v149, v142
	v_mul_f32_e32 v137, v148, v143
	v_add_f32_e32 v142, v136, v137
	v_cvt_pk_bf16_f32 v136, v167, v144
	v_cvt_pk_bf16_f32 v137, v138, v139
	v_cvt_pk_bf16_f32 v138, v145, v146
	v_cvt_pk_bf16_f32 v139, v147, v142
	global_store_dwordx4 v[140:141], v[136:139], off offset:256
	v_cvt_f32_f16_e32 v140, v132
	v_cvt_f32_f16_sdwa v141, v132 dst_sel:DWORD dst_unused:UNUSED_PAD src0_sel:WORD_1
	v_cvt_f32_f16_sdwa v151, v133 dst_sel:DWORD dst_unused:UNUSED_PAD src0_sel:WORD_1
	v_mul_f32_e32 v142, v160, v28
	v_mul_f32_e32 v143, v160, v29
	v_mul_f32_e32 v138, v160, v30
	v_mul_f32_e32 v139, v160, v31
	v_mul_f32_e32 v148, v142, v140
	v_mul_f32_e32 v149, v143, v141
	v_mul_f32_e32 v132, v143, v140
	v_mul_f32_e32 v133, v142, v141
	v_cvt_f32_f16_e32 v142, v134
	v_cvt_f32_f16_sdwa v143, v134 dst_sel:DWORD dst_unused:UNUSED_PAD src0_sel:WORD_1
	v_sub_f32_e32 v148, v148, v149
	v_add_f32_e32 v149, v132, v133
	v_mul_f32_e32 v132, v138, v150
	v_mul_f32_e32 v133, v139, v151
	v_mul_f32_e32 v146, v160, v24
	v_mul_f32_e32 v147, v160, v25
	v_sub_f32_e32 v134, v132, v133
	v_mul_f32_e32 v132, v139, v150
	v_mul_f32_e32 v133, v138, v151
	v_cvt_f32_f16_e32 v138, v135
	v_cvt_f32_f16_sdwa v139, v135 dst_sel:DWORD dst_unused:UNUSED_PAD src0_sel:WORD_1
	v_add_f32_e32 v167, v132, v133
	v_mul_f32_e32 v132, v146, v142
	v_mul_f32_e32 v133, v147, v143
	v_mul_f32_e32 v144, v160, v26
	v_mul_f32_e32 v145, v160, v27
	v_sub_f32_e32 v135, v132, v133
	v_mul_f32_e32 v132, v147, v142
	v_mul_f32_e32 v133, v146, v143
	v_add_f32_e32 v146, v132, v133
	v_mul_f32_e32 v132, v144, v138
	v_mul_f32_e32 v133, v145, v139
	v_lshl_add_u64 v[136:137], v[170:171], 0, s[38:39]
	v_sub_f32_e32 v147, v132, v133
	v_mul_f32_e32 v132, v145, v138
; __device__ __forceinline__ u32x4 pack8(f32x4 v0, f32x4 v1) { u32x4 w; w.x = cvt_pk_bf16(v0[0], v0[1]); w.y = cvt_pk_bf16(v0[2], v0[3]); w.z = cvt_pk_bf16(v1[0], v1[1]); w.w = cvt_pk_bf16(v1[2], v1[3]); return w; }
; #define EPI_PIN8(a) asm volatile("" : "+v"(a[0][0]), "+v"(a[0][1]), "+v"(a[0][2]), "+v"(a[0][3]), "+v"(a[1][0]), "+v"(a[1][1]), "+v"(a[1][2]), "+v"(a[1][3]) :: "memory")
; __device__ __forceinline__ void rope8h(f32x4& v0, f32x4& v1, u32x4 t) {
;     float c[4], s[4];
; #pragma unroll
;     for (int k = 0; k < 4; ++k) { const h16x2 h = __builtin_bit_cast(h16x2, (unsigned)t[k]); c[k] = (float)h[0]; s[k] = (float)h[1]; }
;     f32x4 a, b;
;     a[0] = v0[0] * c[0] - v0[1] * s[0]; a[1] = v0[1] * c[0] + v0[0] * s[0]; a[2] = v0[2] * c[1] - v0[3] * s[1]; a[3] = v0[3] * c[1] + v0[2] * s[1];
;     b[0] = v1[0] * c[2] - v1[1] * s[2]; b[1] = v1[1] * c[2] + v1[0] * s[2]; b[2] = v1[2] * c[3] - v1[3] * s[3]; b[3] = v1[3] * c[3] + v1[2] * s[3];
;     v0 = a; v1 = b;
;     __device__ __forceinline__ int operator()(AccT acc, const Unit& u, int wr, int wc, int, int) const {
;     ...
;             bf16_t* dst = (pn <= 3) ? DQ : DK; const int cbase = ((pn - 2) & 1) * 256; const int p0 = 16 * (wc & 1) + 4 * fq; const float qs = (pn <= 3) ? QSC_DIFF : 1.0f;
;             u32x4 th[2][4];
; #pragma unroll
;             for (int ai = 0; ai < 2; ++ai)
; #pragma unroll
;                 for (int m = 0; m < 4; ++m) { const int pos = (row0 + ai * HALF + m * 16) & (SEQ - 1); th[ai][m] = *(const u32x4*)(rope + (size_t)pos * 32 + p0); }
;             EPI_PIN8(th);
; #pragma unroll
;             for (int ai = 0; ai < 2; ++ai)
; #pragma unroll
;                 for (int m = 0; m < 4; ++m) { const int r = row0 + ai * HALF + m * 16;
; #pragma unroll
;                     for (int bj = 0; bj < 2; ++bj) { f32x4 v0 = acc[ai][bj][m][0] * qs, v1 = acc[ai][bj][m][1] * qs; rope8h(v0, v1, th[ai][m]);
;                         *(u32x4*)(dst + (size_t)r * 512 + cbase + bj * HALF + cw) = pack8(v0, v1); } }
	v_mul_f32_e32 v133, v144, v139
	v_add_f32_e32 v144, v132, v133
	v_cvt_pk_bf16_f32 v132, v148, v149
	v_cvt_pk_bf16_f32 v133, v134, v167
	v_cvt_pk_bf16_f32 v134, v135, v146
	v_cvt_pk_bf16_f32 v135, v147, v144
	v_add_co_u32_e32 v144, vcc, s10, v170
	v_mul_f32_e32 v146, v160, v16
	v_mul_f32_e32 v147, v160, v17
	s_nop 0
	v_addc_co_u32_e32 v145, vcc, 0, v171, vcc
	global_store_dwordx4 v[144:145], v[132:135], off
	v_mul_f32_e32 v144, v160, v18
	v_mul_f32_e32 v145, v160, v19
	s_mov_b32 s10, 0x2c000
	v_mul_f32_e32 v134, v160, v20
	v_mul_f32_e32 v135, v160, v21
	v_mul_f32_e32 v132, v160, v22
	v_mul_f32_e32 v133, v160, v23
	v_mul_f32_e32 v148, v134, v140
	v_mul_f32_e32 v149, v135, v141
	v_pk_mul_f32 v[134:135], v[134:135], v[140:141] op_sel:[1,0] op_sel_hi:[0,1]
	v_add_f32_e32 v140, v134, v135
	v_mul_f32_e32 v134, v132, v150
	v_mul_f32_e32 v135, v133, v151
	v_pk_mul_f32 v[132:133], v[132:133], v[150:151] op_sel:[1,0] op_sel_hi:[0,1]
	v_sub_f32_e32 v134, v134, v135
	v_add_f32_e32 v135, v132, v133
	v_mul_f32_e32 v132, v146, v142
	v_mul_f32_e32 v133, v147, v143
	v_sub_f32_e32 v148, v148, v149
	v_sub_f32_e32 v141, v132, v133
	v_mul_f32_e32 v132, v147, v142
	v_mul_f32_e32 v133, v146, v143
	v_add_f32_e32 v142, v132, v133
	v_mul_f32_e32 v132, v144, v138
	v_mul_f32_e32 v133, v145, v139
	v_cvt_f32_f16_e32 v146, v129
	v_sub_f32_e32 v143, v132, v133
	v_mul_f32_e32 v132, v145, v138
	v_mul_f32_e32 v133, v144, v139
	v_add_f32_e32 v138, v132, v133
	v_cvt_pk_bf16_f32 v132, v148, v140
	v_cvt_pk_bf16_f32 v133, v134, v135
	v_cvt_pk_bf16_f32 v134, v141, v142
	v_cvt_pk_bf16_f32 v135, v143, v138
	global_store_dwordx4 v[136:137], v[132:135], off offset:256
	v_cvt_f32_f16_e32 v136, v128
	v_cvt_f32_f16_sdwa v137, v128 dst_sel:DWORD dst_unused:UNUSED_PAD src0_sel:WORD_1
	v_cvt_f32_f16_sdwa v147, v129 dst_sel:DWORD dst_unused:UNUSED_PAD src0_sel:WORD_1
	v_mul_f32_e32 v138, v160, v12
	v_mul_f32_e32 v139, v160, v13
	v_mul_f32_e32 v134, v160, v14
	v_mul_f32_e32 v135, v160, v15
	v_mul_f32_e32 v144, v138, v136
	v_mul_f32_e32 v145, v139, v137
	v_mul_f32_e32 v128, v139, v136
	v_mul_f32_e32 v129, v138, v137
	v_cvt_f32_f16_e32 v138, v130
	v_cvt_f32_f16_sdwa v139, v130 dst_sel:DWORD dst_unused:UNUSED_PAD src0_sel:WORD_1
	v_sub_f32_e32 v144, v144, v145
	v_add_f32_e32 v145, v128, v129
	v_mul_f32_e32 v128, v134, v146
	v_mul_f32_e32 v129, v135, v147
	v_mul_f32_e32 v142, v160, v8
	v_mul_f32_e32 v143, v160, v9
	v_sub_f32_e32 v130, v128, v129
	v_mul_f32_e32 v128, v135, v146
	v_mul_f32_e32 v129, v134, v147
	v_cvt_f32_f16_e32 v134, v131
	v_cvt_f32_f16_sdwa v135, v131 dst_sel:DWORD dst_unused:UNUSED_PAD src0_sel:WORD_1
	v_add_f32_e32 v148, v128, v129
	v_mul_f32_e32 v128, v142, v138
	v_mul_f32_e32 v129, v143, v139
	v_mul_f32_e32 v140, v160, v10
	v_mul_f32_e32 v141, v160, v11
	v_sub_f32_e32 v131, v128, v129
	v_mul_f32_e32 v128, v143, v138
	v_mul_f32_e32 v129, v142, v139
	v_add_f32_e32 v142, v128, v129
	v_mul_f32_e32 v128, v140, v134
	v_mul_f32_e32 v129, v141, v135
	v_lshl_add_u64 v[132:133], v[170:171], 0, s[42:43]
	v_sub_f32_e32 v143, v128, v129
	v_mul_f32_e32 v128, v141, v134
	v_mul_f32_e32 v129, v140, v135
	v_add_f32_e32 v140, v128, v129
	v_cvt_pk_bf16_f32 v128, v144, v145
	v_cvt_pk_bf16_f32 v129, v130, v148
	v_cvt_pk_bf16_f32 v130, v131, v142
	v_cvt_pk_bf16_f32 v131, v143, v140
	v_add_co_u32_e32 v140, vcc, s10, v170
	v_mul_f32_e32 v142, v160, v0
	v_mul_f32_e32 v143, v160, v1
	s_nop 0
	v_addc_co_u32_e32 v141, vcc, 0, v171, vcc
	global_store_dwordx4 v[140:141], v[128:131], off
	v_mul_f32_e32 v140, v160, v2
	v_mul_f32_e32 v141, v160, v3
	s_nop 0
	v_mul_f32_e32 v130, v160, v4
	v_mul_f32_e32 v131, v160, v5
	v_mul_f32_e32 v128, v160, v6
	v_mul_f32_e32 v129, v160, v7
	v_mul_f32_e32 v144, v130, v136
	v_mul_f32_e32 v145, v131, v137
	v_pk_mul_f32 v[130:131], v[130:131], v[136:137] op_sel:[1,0] op_sel_hi:[0,1]
	v_add_f32_e32 v136, v130, v131
	v_mul_f32_e32 v130, v128, v146
	v_mul_f32_e32 v131, v129, v147
	v_pk_mul_f32 v[128:129], v[128:129], v[146:147] op_sel:[1,0] op_sel_hi:[0,1]
	v_sub_f32_e32 v130, v130, v131
	v_add_f32_e32 v131, v128, v129
	v_mul_f32_e32 v128, v142, v138
	v_mul_f32_e32 v129, v143, v139
	v_sub_f32_e32 v144, v144, v145
	v_sub_f32_e32 v137, v128, v129
	v_mul_f32_e32 v128, v143, v138
	v_mul_f32_e32 v129, v142, v139
	v_add_f32_e32 v138, v128, v129
	v_mul_f32_e32 v128, v140, v134
	v_mul_f32_e32 v129, v141, v135
	s_nop 0
	v_sub_f32_e32 v139, v128, v129
	v_mul_f32_e32 v128, v141, v134
	v_mul_f32_e32 v129, v140, v135
	v_add_f32_e32 v134, v128, v129
	v_cvt_pk_bf16_f32 v128, v144, v136
	v_cvt_pk_bf16_f32 v129, v130, v131
	v_cvt_pk_bf16_f32 v130, v137, v138
	v_cvt_pk_bf16_f32 v131, v139, v134
	global_store_dwordx4 v[132:133], v[128:131], off offset:256

; #define LAS __attribute__((address_space(3)))
;     __device__ __forceinline__ bool next(int i, Unit& u) const {
;         const long L = (long)i * G + c; if (L >= nwg) return false;
;         int wgid = (int)L; { const int q = nwg / NXCD, r = nwg % NXCD, xcd = wgid % NXCD, off = wgid / NXCD; wgid = (xcd < r ? xcd * (q + 1) : r * (q + 1) + (xcd - r) * q) + off; }
;         const int nig = WGM * nN, gid = wgid / nig, fm = gid * WGM, gsz = (nM - fm) < WGM ? (nM - fm) : WGM;
;         u.pm = fm + ((wgid % nig) % gsz); u.pn = (wgid % nig) / gsz; u.e = 0; u.t = u.pm; u.cnt = 0x7fffffff; u.i = i; return true;
;     }
;     __device__ __forceinline__ void fill_rstd(LAS float* tab, const float* ssq, float inv_ncol, float scale, int tid) const {
;         Unit u; float v[8];
; #pragma unroll
;         for (int i = 0; i < 8; ++i) { v[i] = 0.f; if (next(i, u)) { const f32x4 ss = *(const f32x4*)(ssq + ((size_t)u.pm * BM + (tid & 255)) * 4); v[i] = __builtin_amdgcn_rsqf(((ss[0] + ss[1]) + (ss[2] + ss[3])) * inv_ncol + EPS) * scale; } }
.LBB0_386:
	v_readlane_b32 s4, v248, 2
	v_readlane_b32 s5, v248, 3
	s_waitcnt vmcnt(63) expcnt(7) lgkmcnt(15)
	v_mbcnt_lo_u32_b32 v0, -1, 0
	v_mbcnt_hi_u32_b32 v0, -1, v0
	s_load_dwordx2 s[20:21], s[4:5], 0xd0
	v_add_u32_e32 v6, s56, v0
	v_lshlrev_b32_e32 v0, 2, v6
	v_and_b32_e32 v0, 0x3fc, v0
	v_mov_b32_e32 v1, 0
	v_lshlrev_b32_e32 v0, 2, v0
	s_cmpk_lt_i32 s2, 0x300
	s_waitcnt lgkmcnt(0)
	v_lshl_add_u64 v[2:3], s[20:21], 0, v[0:1]
	s_mov_b64 s[8:9], 0x600000
	s_cselect_b64 s[10:11], -1, 0
	s_cmpk_gt_i32 s2, 0x2ff
	s_movk_i32 s5, 0x100
	v_lshl_add_u64 v[2:3], v[2:3], 0, s[8:9]
	v_mov_b32_e32 v7, 0
	s_cbranch_scc1 .LBB0_388
	s_movk_i32 s4, 0x61
	s_and_b64 s[8:9], s[18:19], exec
	s_cselect_b32 s4, s4, 0x60
	s_mul_i32 s4, s0, s4
	s_add_i32 s4, s4, s51
	s_mul_hi_i32 s8, s4, 0x2aaaaaab
	s_lshr_b32 s9, s8, 31
	s_ashr_i32 s8, s8, 2
	s_add_i32 s8, s8, s9
	s_mul_i32 s9, s8, 24
	s_sub_i32 s4, s4, s9
	s_bfe_i32 s9, s4, 0x80000
	s_bfe_u32 s9, s9, 0x3000c
	s_add_i32 s9, s4, s9
	s_and_b32 s9, s9, 0xf8
	s_sub_i32 s4, s4, s9
	s_lshl_b32 s8, s8, 3
	s_sext_i32_i8 s4, s4
	s_add_i32 s8, s8, s4
	s_ashr_i32 s9, s8, 31
	s_lshl_b64 s[8:9], s[8:9], 12
	v_lshl_add_u64 v[4:5], v[2:3], 0, s[8:9]
	global_load_dwordx4 v[8:11], v[4:5], off
	s_waitcnt vmcnt(0)
	v_mov_b32_e32 v4, v9
	v_mov_b32_e32 v5, v10
	v_mov_b32_e32 v9, v11
	v_add_f32_e32 v4, v4, v8
	v_add_f32_e32 v5, v5, v9
	s_nop 0
	v_add_f32_e32 v4, v4, v5
	v_mov_b32_e32 v5, 0x358637bd
	v_fmac_f32_e32 v5, 0x3b800000, v4
	v_rsq_f32_e32 v4, v5
	s_nop 0
	v_mul_f32_e32 v7, 0x3dd53b94, v4
.LBB0_388:
	s_add_u32 s12, s48, s2
	s_addc_u32 s13, s49, s3
	s_ashr_i32 s4, s12, 31
	s_lshr_b32 s4, s4, 29
	s_add_i32 s8, s12, s4
	s_ashr_i32 s4, s8, 3
	s_and_b32 s8, s8, -8
	v_mov_b64_e32 v[4:5], 0x2ff
	s_sub_i32 s52, s12, s8
	v_cmp_gt_i64_e32 vcc, s[12:13], v[4:5]
	s_cmp_lt_i32 s52, 0
	s_cselect_b64 s[14:15], -1, 0
	s_cbranch_vccnz .LBB0_390
	s_movk_i32 s22, 0x61
	s_and_b64 s[8:9], s[14:15], exec
	s_cselect_b32 s8, s22, 0x60
	s_mul_i32 s8, s52, s8
	s_add_i32 s8, s8, s4
	s_mul_hi_i32 s9, s8, 0x2aaaaaab
	s_lshr_b32 s22, s9, 31
	s_ashr_i32 s9, s9, 2
	s_add_i32 s9, s9, s22
	s_lshl_b32 s22, s9, 3
	s_sub_i32 s23, 0x100, s22
	s_min_i32 s23, s23, 8
	s_abs_i32 s23, s23
	v_cvt_f32_u32_e32 v1, s23
	s_sub_i32 s24, 0, s23
	s_mul_i32 s9, s9, 24
	s_sub_i32 s8, s8, s9
	v_rcp_iflag_f32_e32 v1, v1
	s_ashr_i32 s9, s8, 31
	s_abs_i32 s8, s8
	v_mul_f32_e32 v1, 0x4f7ffffe, v1
	v_cvt_u32_f32_e32 v1, v1
	s_nop 0
	v_readfirstlane_b32 s25, v1
	s_mul_i32 s24, s24, s25
	s_mul_hi_u32 s24, s25, s24
	s_add_i32 s25, s25, s24
	s_mul_hi_u32 s24, s8, s25
	s_mul_i32 s24, s24, s23
	s_sub_i32 s8, s8, s24
	s_sub_i32 s24, s8, s23
	s_cmp_ge_u32 s8, s23
	s_cselect_b32 s8, s24, s8
	s_sub_i32 s24, s8, s23
	s_cmp_ge_u32 s8, s23
	s_cselect_b32 s8, s24, s8
	s_xor_b32 s8, s8, s9
	s_sub_i32 s8, s8, s9
	s_add_i32 s8, s22, s8
	s_ashr_i32 s9, s8, 31
	s_lshl_b64 s[8:9], s[8:9], 12
	v_lshl_add_u64 v[8:9], v[2:3], 0, s[8:9]
	global_load_dwordx4 v[8:11], v[8:9], off
	s_waitcnt vmcnt(0)
	v_mov_b32_e32 v12, v9
	v_mov_b32_e32 v13, v10
	v_mov_b32_e32 v9, v11
	v_add_f32_e32 v8, v12, v8
	v_add_f32_e32 v9, v13, v9
	s_nop 0
	v_add_f32_e32 v1, v8, v9
	v_mov_b32_e32 v8, 0x358637bd
	v_fmac_f32_e32 v8, 0x3b800000, v1
	v_rsq_f32_e32 v1, v8
	s_nop 0
	v_mul_f32_e32 v1, 0x3dd53b94, v1
.LBB0_390:
	s_add_u32 s24, s12, s48
	s_addc_u32 s25, s13, s49
	s_ashr_i32 s8, s24, 31
	s_lshr_b32 s8, s8, 29
	s_add_i32 s8, s24, s8
	s_ashr_i32 s53, s8, 3
	s_and_b32 s8, s8, -8
	s_sub_i32 s63, s24, s8
	v_cmp_gt_i64_e32 vcc, s[24:25], v[4:5]
	s_cmp_lt_i32 s63, 0
	v_mov_b32_e32 v8, 0
	s_cselect_b64 s[26:27], -1, 0
	v_mov_b32_e32 v9, 0
	s_cbranch_vccnz .LBB0_392
	s_movk_i32 s22, 0x61
	s_and_b64 s[8:9], s[26:27], exec
	s_cselect_b32 s8, s22, 0x60
	s_mul_i32 s8, s63, s8
	s_add_i32 s8, s8, s53
	s_mul_hi_i32 s9, s8, 0x2aaaaaab
	s_lshr_b32 s22, s9, 31
	s_ashr_i32 s9, s9, 2
	s_add_i32 s9, s9, s22
	s_lshl_b32 s22, s9, 3
	s_sub_i32 s23, 0x100, s22
	s_min_i32 s23, s23, 8
	s_abs_i32 s23, s23
	v_cvt_f32_u32_e32 v4, s23
	s_sub_i32 s28, 0, s23
	s_mul_i32 s9, s9, 24
	s_sub_i32 s8, s8, s9
	v_rcp_iflag_f32_e32 v4, v4
	s_ashr_i32 s9, s8, 31
	s_abs_i32 s8, s8
	v_mul_f32_e32 v4, 0x4f7ffffe, v4
	v_cvt_u32_f32_e32 v4, v4
	s_nop 0
	v_readfirstlane_b32 s29, v4
	s_mul_i32 s28, s28, s29
	s_mul_hi_u32 s28, s29, s28
	s_add_i32 s29, s29, s28
	s_mul_hi_u32 s28, s8, s29
	s_mul_i32 s28, s28, s23
	s_sub_i32 s8, s8, s28
	s_sub_i32 s28, s8, s23
	s_cmp_ge_u32 s8, s23
	s_cselect_b32 s8, s28, s8
	s_sub_i32 s28, s8, s23
	s_cmp_ge_u32 s8, s23
	s_cselect_b32 s8, s28, s8
	s_xor_b32 s8, s8, s9
	s_sub_i32 s8, s8, s9
	s_add_i32 s8, s22, s8
	s_ashr_i32 s9, s8, 31
	s_lshl_b64 s[8:9], s[8:9], 12
	v_lshl_add_u64 v[4:5], v[2:3], 0, s[8:9]
	global_load_dwordx4 v[10:13], v[4:5], off
	s_waitcnt vmcnt(0)
	v_mov_b32_e32 v4, v11
	v_mov_b32_e32 v5, v12
	v_mov_b32_e32 v11, v13
	v_add_f32_e32 v4, v4, v10
	v_add_f32_e32 v5, v5, v11
	s_nop 0
	v_add_f32_e32 v4, v4, v5
	v_mov_b32_e32 v5, 0x358637bd
	v_fmac_f32_e32 v5, 0x3b800000, v4
	v_rsq_f32_e32 v4, v5
	s_nop 0
	v_mul_f32_e32 v9, 0x3dd53b94, v4
; #define LAS __attribute__((address_space(3)))
;     __device__ __forceinline__ bool next(int i, Unit& u) const {
;         const long L = (long)i * G + c; if (L >= nwg) return false;
;         int wgid = (int)L; { const int q = nwg / NXCD, r = nwg % NXCD, xcd = wgid % NXCD, off = wgid / NXCD; wgid = (xcd < r ? xcd * (q + 1) : r * (q + 1) + (xcd - r) * q) + off; }
;         const int nig = WGM * nN, gid = wgid / nig, fm = gid * WGM, gsz = (nM - fm) < WGM ? (nM - fm) : WGM;
;         u.pm = fm + ((wgid % nig) % gsz); u.pn = (wgid % nig) / gsz; u.e = 0; u.t = u.pm; u.cnt = 0x7fffffff; u.i = i; return true;
;     }
;     __device__ __forceinline__ void fill_rstd(LAS float* tab, const float* ssq, float inv_ncol, float scale, int tid) const {
;         Unit u; float v[8];
; #pragma unroll
;         for (int i = 0; i < 8; ++i) { v[i] = 0.f; if (next(i, u)) { const f32x4 ss = *(const f32x4*)(ssq + ((size_t)u.pm * BM + (tid & 255)) * 4); v[i] = __builtin_amdgcn_rsqf(((ss[0] + ss[1]) + (ss[2] + ss[3])) * inv_ncol + EPS) * scale; } }
.LBB0_392:
	s_add_u32 s28, s24, s48
	s_addc_u32 s29, s25, s49
	s_ashr_i32 s8, s28, 31
	s_lshr_b32 s8, s8, 29
	s_add_i32 s8, s28, s8
	s_ashr_i32 s64, s8, 3
	s_and_b32 s8, s8, -8
	v_mov_b64_e32 v[4:5], 0x2ff
	s_sub_i32 s65, s28, s8
	v_cmp_gt_i64_e32 vcc, s[28:29], v[4:5]
	s_cmp_lt_i32 s65, 0
	s_cselect_b64 s[30:31], -1, 0
	s_cbranch_vccnz .LBB0_394
	s_movk_i32 s22, 0x61
	s_and_b64 s[8:9], s[30:31], exec
	s_cselect_b32 s8, s22, 0x60
	s_mul_i32 s8, s65, s8
	s_add_i32 s8, s8, s64
	s_mul_hi_i32 s9, s8, 0x2aaaaaab
	s_lshr_b32 s22, s9, 31
	s_ashr_i32 s9, s9, 2
	s_add_i32 s9, s9, s22
	s_lshl_b32 s22, s9, 3
	s_sub_i32 s23, 0x100, s22
	s_min_i32 s23, s23, 8
	s_abs_i32 s23, s23
	v_cvt_f32_u32_e32 v8, s23
	s_sub_i32 s34, 0, s23
	s_mul_i32 s9, s9, 24
	s_sub_i32 s8, s8, s9
	v_rcp_iflag_f32_e32 v8, v8
	s_ashr_i32 s9, s8, 31
	s_abs_i32 s8, s8
	v_mul_f32_e32 v8, 0x4f7ffffe, v8
	v_cvt_u32_f32_e32 v8, v8
	s_nop 0
	v_readfirstlane_b32 s35, v8
	s_mul_i32 s34, s34, s35
	s_mul_hi_u32 s34, s35, s34
	s_add_i32 s35, s35, s34
	s_mul_hi_u32 s34, s8, s35
	s_mul_i32 s34, s34, s23
	s_sub_i32 s8, s8, s34
	s_sub_i32 s34, s8, s23
	s_cmp_ge_u32 s8, s23
	s_cselect_b32 s8, s34, s8
	s_sub_i32 s34, s8, s23
	s_cmp_ge_u32 s8, s23
	s_cselect_b32 s8, s34, s8
	s_xor_b32 s8, s8, s9
	s_sub_i32 s8, s8, s9
	s_add_i32 s8, s22, s8
	s_ashr_i32 s9, s8, 31
	s_lshl_b64 s[8:9], s[8:9], 12
	v_lshl_add_u64 v[10:11], v[2:3], 0, s[8:9]
	global_load_dwordx4 v[10:13], v[10:11], off
	s_waitcnt vmcnt(0)
	v_mov_b32_e32 v14, v11
	v_mov_b32_e32 v15, v12
	v_mov_b32_e32 v11, v13
	v_add_f32_e32 v10, v14, v10
	v_add_f32_e32 v11, v15, v11
	s_nop 0
	v_add_f32_e32 v8, v10, v11
	v_mov_b32_e32 v10, 0x358637bd
	v_fmac_f32_e32 v10, 0x3b800000, v8
	v_rsq_f32_e32 v8, v10
	s_nop 0
	v_mul_f32_e32 v8, 0x3dd53b94, v8
.LBB0_394:
	s_add_u32 s34, s28, s48
	s_addc_u32 s35, s29, s49
	s_ashr_i32 s8, s34, 31
	s_lshr_b32 s8, s8, 29
	s_add_i32 s8, s34, s8
	s_ashr_i32 s66, s8, 3
	s_and_b32 s8, s8, -8
	s_sub_i32 s67, s34, s8
	v_cmp_gt_i64_e32 vcc, s[34:35], v[4:5]
	s_cmp_lt_i32 s67, 0
	v_mov_b32_e32 v10, 0
	s_cselect_b64 s[36:37], -1, 0
	v_mov_b32_e32 v11, 0
	s_cbranch_vccnz .LBB0_396
	s_movk_i32 s22, 0x61
	s_and_b64 s[8:9], s[36:37], exec
	s_cselect_b32 s8, s22, 0x60
	s_mul_i32 s8, s67, s8
	s_add_i32 s8, s8, s66
	s_mul_hi_i32 s9, s8, 0x2aaaaaab
	s_lshr_b32 s22, s9, 31
	s_ashr_i32 s9, s9, 2
	s_add_i32 s9, s9, s22
	s_lshl_b32 s22, s9, 3
	s_sub_i32 s23, 0x100, s22
	s_min_i32 s23, s23, 8
	s_abs_i32 s23, s23
	v_cvt_f32_u32_e32 v4, s23
	s_sub_i32 s38, 0, s23
	s_mul_i32 s9, s9, 24
	s_sub_i32 s8, s8, s9
	v_rcp_iflag_f32_e32 v4, v4
	s_ashr_i32 s9, s8, 31
	s_abs_i32 s8, s8
	v_mul_f32_e32 v4, 0x4f7ffffe, v4
	v_cvt_u32_f32_e32 v4, v4
	s_nop 0
	v_readfirstlane_b32 s39, v4
	s_mul_i32 s38, s38, s39
	s_mul_hi_u32 s38, s39, s38
	s_add_i32 s39, s39, s38
	s_mul_hi_u32 s38, s8, s39
	s_mul_i32 s38, s38, s23
	s_sub_i32 s8, s8, s38
	s_sub_i32 s38, s8, s23
	s_cmp_ge_u32 s8, s23
	s_cselect_b32 s8, s38, s8
	s_sub_i32 s38, s8, s23
	s_cmp_ge_u32 s8, s23
	s_cselect_b32 s8, s38, s8
	s_xor_b32 s8, s8, s9
	s_sub_i32 s8, s8, s9
	s_add_i32 s8, s22, s8
	s_ashr_i32 s9, s8, 31
	s_lshl_b64 s[8:9], s[8:9], 12
	v_lshl_add_u64 v[4:5], v[2:3], 0, s[8:9]
	global_load_dwordx4 v[12:15], v[4:5], off
	s_waitcnt vmcnt(0)
	v_mov_b32_e32 v4, v13
	v_mov_b32_e32 v5, v14
	v_mov_b32_e32 v13, v15
	v_add_f32_e32 v4, v4, v12
	v_add_f32_e32 v5, v5, v13
	s_nop 0
	v_add_f32_e32 v4, v4, v5
	v_mov_b32_e32 v5, 0x358637bd
	v_fmac_f32_e32 v5, 0x3b800000, v4
	v_rsq_f32_e32 v4, v5
	s_nop 0
	v_mul_f32_e32 v11, 0x3dd53b94, v4
; #define LAS __attribute__((address_space(3)))
;     __device__ __forceinline__ bool next(int i, Unit& u) const {
;         const long L = (long)i * G + c; if (L >= nwg) return false;
;         int wgid = (int)L; { const int q = nwg / NXCD, r = nwg % NXCD, xcd = wgid % NXCD, off = wgid / NXCD; wgid = (xcd < r ? xcd * (q + 1) : r * (q + 1) + (xcd - r) * q) + off; }
;         const int nig = WGM * nN, gid = wgid / nig, fm = gid * WGM, gsz = (nM - fm) < WGM ? (nM - fm) : WGM;
;         u.pm = fm + ((wgid % nig) % gsz); u.pn = (wgid % nig) / gsz; u.e = 0; u.t = u.pm; u.cnt = 0x7fffffff; u.i = i; return true;
;     }
;     __device__ __forceinline__ void fill_rstd(LAS float* tab, const float* ssq, float inv_ncol, float scale, int tid) const {
;         Unit u; float v[8];
; #pragma unroll
;         for (int i = 0; i < 8; ++i) { v[i] = 0.f; if (next(i, u)) { const f32x4 ss = *(const f32x4*)(ssq + ((size_t)u.pm * BM + (tid & 255)) * 4); v[i] = __builtin_amdgcn_rsqf(((ss[0] + ss[1]) + (ss[2] + ss[3])) * inv_ncol + EPS) * scale; } }
.LBB0_396:
	s_add_u32 s38, s34, s48
	s_addc_u32 s39, s35, s49
	s_ashr_i32 s8, s38, 31
	s_lshr_b32 s8, s8, 29
	s_add_i32 s8, s38, s8
	s_ashr_i32 s68, s8, 3
	s_and_b32 s8, s8, -8
	v_mov_b64_e32 v[4:5], 0x2ff
	s_sub_i32 s69, s38, s8
	v_cmp_gt_i64_e32 vcc, s[38:39], v[4:5]
	s_cmp_lt_i32 s69, 0
	s_cselect_b64 s[42:43], -1, 0
	s_cbranch_vccnz .LBB0_398
	s_movk_i32 s22, 0x61
	s_and_b64 s[8:9], s[42:43], exec
	s_cselect_b32 s8, s22, 0x60
	s_mul_i32 s8, s69, s8
	s_add_i32 s8, s8, s68
	s_mul_hi_i32 s9, s8, 0x2aaaaaab
	s_lshr_b32 s22, s9, 31
	s_ashr_i32 s9, s9, 2
	s_add_i32 s9, s9, s22
	s_lshl_b32 s22, s9, 3
	s_sub_i32 s23, 0x100, s22
	s_min_i32 s23, s23, 8
	s_abs_i32 s23, s23
	v_cvt_f32_u32_e32 v10, s23
	s_sub_i32 s44, 0, s23
	s_mul_i32 s9, s9, 24
	s_sub_i32 s8, s8, s9
	v_rcp_iflag_f32_e32 v10, v10
	s_ashr_i32 s9, s8, 31
	s_abs_i32 s8, s8
	v_mul_f32_e32 v10, 0x4f7ffffe, v10
	v_cvt_u32_f32_e32 v10, v10
	s_nop 0
	v_readfirstlane_b32 s45, v10
	s_mul_i32 s44, s44, s45
	s_mul_hi_u32 s44, s45, s44
	s_add_i32 s45, s45, s44
	s_mul_hi_u32 s44, s8, s45
	s_mul_i32 s44, s44, s23
	s_sub_i32 s8, s8, s44
	s_sub_i32 s44, s8, s23
	s_cmp_ge_u32 s8, s23
	s_cselect_b32 s8, s44, s8
	s_sub_i32 s44, s8, s23
	s_cmp_ge_u32 s8, s23
	s_cselect_b32 s8, s44, s8
	s_xor_b32 s8, s8, s9
	s_sub_i32 s8, s8, s9
	s_add_i32 s8, s22, s8
	s_ashr_i32 s9, s8, 31
	s_lshl_b64 s[8:9], s[8:9], 12
	v_lshl_add_u64 v[12:13], v[2:3], 0, s[8:9]
	global_load_dwordx4 v[12:15], v[12:13], off
	s_waitcnt vmcnt(0)
	v_mov_b32_e32 v16, v13
	v_mov_b32_e32 v17, v14
	v_mov_b32_e32 v13, v15
	v_add_f32_e32 v12, v16, v12
	v_add_f32_e32 v13, v17, v13
	s_nop 0
	v_add_f32_e32 v10, v12, v13
	v_mov_b32_e32 v12, 0x358637bd
	v_fmac_f32_e32 v12, 0x3b800000, v10
	v_rsq_f32_e32 v10, v12
	s_nop 0
	v_mul_f32_e32 v10, 0x3dd53b94, v10
.LBB0_398:
	s_add_u32 s44, s38, s48
	s_addc_u32 s45, s39, s49
	s_ashr_i32 s8, s44, 31
	s_lshr_b32 s8, s8, 29
	s_add_i32 s8, s44, s8
	s_ashr_i32 s73, s8, 3
	s_and_b32 s8, s8, -8
	s_sub_i32 s74, s44, s8
	v_cmp_gt_i64_e32 vcc, s[44:45], v[4:5]
	s_cmp_lt_i32 s74, 0
	v_mov_b32_e32 v4, 0
	s_cselect_b64 s[46:47], -1, 0
	v_mov_b32_e32 v5, 0
	s_cbranch_vccnz .LBB0_400
	s_movk_i32 s22, 0x61
	s_and_b64 s[8:9], s[46:47], exec
	s_cselect_b32 s8, s22, 0x60
	s_mul_i32 s8, s74, s8
	s_add_i32 s8, s8, s73
	s_mul_hi_i32 s9, s8, 0x2aaaaaab
	s_lshr_b32 s22, s9, 31
	s_ashr_i32 s9, s9, 2
	s_add_i32 s9, s9, s22
	s_lshl_b32 s22, s9, 3
	s_sub_i32 s23, 0x100, s22
	s_min_i32 s23, s23, 8
	s_abs_i32 s23, s23
	v_cvt_f32_u32_e32 v5, s23
	s_sub_i32 s58, 0, s23
	s_mul_i32 s9, s9, 24
	s_sub_i32 s8, s8, s9
	v_rcp_iflag_f32_e32 v5, v5
	s_ashr_i32 s9, s8, 31
	s_abs_i32 s8, s8
	v_mul_f32_e32 v5, 0x4f7ffffe, v5
	v_cvt_u32_f32_e32 v5, v5
	s_nop 0
	v_readfirstlane_b32 s59, v5
	s_mul_i32 s58, s58, s59
	s_mul_hi_u32 s58, s59, s58
	s_add_i32 s59, s59, s58
	s_mul_hi_u32 s58, s8, s59
	s_mul_i32 s58, s58, s23
	s_sub_i32 s8, s8, s58
	s_sub_i32 s58, s8, s23
	s_cmp_ge_u32 s8, s23
	s_cselect_b32 s8, s58, s8
	s_sub_i32 s58, s8, s23
	s_cmp_ge_u32 s8, s23
	s_cselect_b32 s8, s58, s8
	s_xor_b32 s8, s8, s9
	s_sub_i32 s8, s8, s9
	s_add_i32 s8, s22, s8
	s_ashr_i32 s9, s8, 31
	s_lshl_b64 s[8:9], s[8:9], 12
	v_lshl_add_u64 v[12:13], v[2:3], 0, s[8:9]
	global_load_dwordx4 v[12:15], v[12:13], off
	s_waitcnt vmcnt(0)
	v_mov_b32_e32 v16, v13
	v_mov_b32_e32 v17, v14
	v_mov_b32_e32 v13, v15
	v_add_f32_e32 v12, v16, v12
	v_add_f32_e32 v13, v17, v13
	s_nop 0
	v_add_f32_e32 v5, v12, v13
	v_mov_b32_e32 v12, 0x358637bd
	v_fmac_f32_e32 v12, 0x3b800000, v5
	v_rsq_f32_e32 v5, v12
	s_nop 0
	v_mul_f32_e32 v5, 0x3dd53b94, v5
.LBB0_400:
	s_add_u32 s58, s44, s48
	s_addc_u32 s59, s45, s49
	s_ashr_i32 s8, s58, 31
	s_lshr_b32 s8, s8, 29
	s_add_i32 s8, s58, s8
	s_ashr_i32 s75, s8, 3
	s_and_b32 s8, s8, -8
	v_mov_b64_e32 v[12:13], 0x2ff
	s_sub_i32 s76, s58, s8
	v_cmp_gt_i64_e32 vcc, s[58:59], v[12:13]
	s_cmp_lt_i32 s76, 0
	s_cselect_b64 s[60:61], -1, 0
	s_cbranch_vccnz .LBB0_402
	s_movk_i32 s22, 0x61
	s_and_b64 s[8:9], s[60:61], exec
	s_cselect_b32 s8, s22, 0x60
	s_mul_i32 s8, s76, s8
	s_add_i32 s8, s8, s75
	s_mul_hi_i32 s9, s8, 0x2aaaaaab
	s_lshr_b32 s22, s9, 31
	s_ashr_i32 s9, s9, 2
	s_add_i32 s9, s9, s22
	s_lshl_b32 s22, s9, 3
	s_sub_i32 s23, 0x100, s22
	s_min_i32 s23, s23, 8
	s_abs_i32 s23, s23
	v_cvt_f32_u32_e32 v4, s23
	s_sub_i32 s70, 0, s23
	s_mul_i32 s9, s9, 24
	s_sub_i32 s8, s8, s9
	v_rcp_iflag_f32_e32 v4, v4
	s_ashr_i32 s9, s8, 31
	s_abs_i32 s8, s8
	v_mul_f32_e32 v4, 0x4f7ffffe, v4
	v_cvt_u32_f32_e32 v4, v4
	s_nop 0
	v_readfirstlane_b32 s71, v4
	s_mul_i32 s70, s70, s71
	s_mul_hi_u32 s70, s71, s70
	s_add_i32 s71, s71, s70
	s_mul_hi_u32 s70, s8, s71
	s_mul_i32 s70, s70, s23
	s_sub_i32 s8, s8, s70
	s_sub_i32 s70, s8, s23
	s_cmp_ge_u32 s8, s23
	s_cselect_b32 s8, s70, s8
	s_sub_i32 s70, s8, s23
	s_cmp_ge_u32 s8, s23
	s_cselect_b32 s8, s70, s8
	s_xor_b32 s8, s8, s9
	s_sub_i32 s8, s8, s9
	s_add_i32 s8, s22, s8
	s_ashr_i32 s9, s8, 31
	s_lshl_b64 s[8:9], s[8:9], 12
	v_lshl_add_u64 v[2:3], v[2:3], 0, s[8:9]
	global_load_dwordx4 v[12:15], v[2:3], off
	s_waitcnt vmcnt(0)
	v_mov_b32_e32 v2, v13
	v_mov_b32_e32 v3, v14
	v_mov_b32_e32 v13, v15
	v_add_f32_e32 v2, v2, v12
	v_add_f32_e32 v3, v3, v13
	s_nop 0
	v_add_f32_e32 v2, v2, v3
	v_mov_b32_e32 v3, 0x358637bd
	v_fmac_f32_e32 v3, 0x3b800000, v2
	v_rsq_f32_e32 v2, v3
	s_nop 0
	v_mul_f32_e32 v4, 0x3dd53b94, v2

; #define LAS __attribute__((address_space(3)))
;     __device__ __forceinline__ bool next(int i, Unit& u) const {
;         const long L = (long)i * G + c; if (L >= nwg) return false;
;         int wgid = (int)L; { const int q = nwg / NXCD, r = nwg % NXCD, xcd = wgid % NXCD, off = wgid / NXCD; wgid = (xcd < r ? xcd * (q + 1) : r * (q + 1) + (xcd - r) * q) + off; }
;         const int nig = WGM * nN, gid = wgid / nig, fm = gid * WGM, gsz = (nM - fm) < WGM ? (nM - fm) : WGM;
;         u.pm = fm + ((wgid % nig) % gsz); u.pn = (wgid % nig) / gsz; u.e = 0; u.t = u.pm; u.cnt = 0x7fffffff; u.i = i; return true;
;     }
;     __device__ __forceinline__ void fill_rstd(LAS float* tab, const float* ssq, float inv_ncol, float scale, int tid) const {
;         Unit u; float v[8];
; #pragma unroll
;         for (int i = 0; i < 8; ++i) { v[i] = 0.f; if (next(i, u)) { const f32x4 ss = *(const f32x4*)(ssq + ((size_t)u.pm * BM + (tid & 255)) * 4); v[i] = __builtin_amdgcn_rsqf(((ss[0] + ss[1]) + (ss[2] + ss[3])) * inv_ncol + EPS) * scale; } }
; __global__ void __launch_bounds__(512, 2) hymba_fwd(Args args) {
;     ...
;         { pg8::StaticOrder S; S.init(T_TOK, 1024, G, bx); S.fill_rstd(rtk, SSQKV, 1.0f / 256.0f, 1.0f, tid); }
.LBB0_404:
	s_or_b64 exec, exec, s[22:23]
	s_cmpk_lt_i32 s2, 0x400
	v_mov_b32_e32 v1, 0
	s_cselect_b64 s[22:23], -1, 0
	s_lshl_b32 s70, s0, 7
	v_lshl_add_u64 v[2:3], s[20:21], 0, v[0:1]
	s_mov_b64 s[78:79], 0x700000
	s_cmpk_gt_i32 s2, 0x3ff
	s_mul_i32 s71, s0, 0x81
	v_lshl_add_u64 v[2:3], v[2:3], 0, s[78:79]
	v_mov_b32_e32 v0, 0
	s_cbranch_scc1 .LBB0_406
	s_and_b64 s[78:79], s[18:19], exec
	s_cselect_b32 s77, s71, s70
	s_add_i32 s77, s77, s51
	s_ashr_i32 s78, s77, 31
	s_lshr_b32 s78, s78, 27
	s_add_i32 s78, s77, s78
	s_ashr_i32 s79, s78, 5
	s_and_b32 s78, s78, 0xffe0
	s_sub_i32 s77, s77, s78
	s_lshl_b32 s78, s79, 3
	s_bfe_i32 s79, s77, 0x80000
	s_bfe_u32 s79, s79, 0x3000c
	s_add_i32 s79, s77, s79
	s_and_b32 s79, s79, 0xf8
	s_sub_i32 s77, s77, s79
	s_sext_i32_i8 s77, s77
	s_add_i32 s78, s78, s77
	s_ashr_i32 s79, s78, 31
	s_lshl_b64 s[78:79], s[78:79], 12
	v_lshl_add_u64 v[4:5], v[2:3], 0, s[78:79]
	global_load_dwordx4 v[8:11], v[4:5], off
	s_waitcnt vmcnt(0)
	v_mov_b32_e32 v4, v9
	v_mov_b32_e32 v5, v10
	v_mov_b32_e32 v9, v11
	v_add_f32_e32 v4, v4, v8
	v_add_f32_e32 v5, v5, v9
	s_nop 0
	v_add_f32_e32 v0, v4, v5
	v_mov_b32_e32 v4, 0x358637bd
	v_fmac_f32_e32 v4, 0x3b800000, v0
	v_rsq_f32_e32 v0, v4
.LBB0_406:
	v_mov_b64_e32 v[4:5], 0x3ff
	v_cmp_gt_i64_e32 vcc, s[12:13], v[4:5]
	s_cbranch_vccnz .LBB0_408
	s_lshl_b32 s77, s52, 7
	s_mulk_i32 s52, 0x81
	s_and_b64 s[12:13], s[14:15], exec
	s_cselect_b32 s12, s52, s77
	s_add_i32 s4, s12, s4
	s_ashr_i32 s12, s4, 31
	s_lshr_b32 s12, s12, 27
	s_add_i32 s12, s4, s12
	s_ashr_i32 s13, s12, 5
	s_lshl_b32 s13, s13, 3
	s_sub_i32 s14, 0x100, s13
	s_min_i32 s14, s14, 8
	s_abs_i32 s14, s14
	v_cvt_f32_u32_e32 v1, s14
	s_sub_i32 s15, 0, s14
	s_andn2_b32 s12, s12, 31
	s_sub_i32 s4, s4, s12
	v_rcp_iflag_f32_e32 v1, v1
	s_ashr_i32 s12, s4, 31
	s_abs_i32 s4, s4
	v_mov_b32_e32 v7, 0x358637bd
	v_mul_f32_e32 v1, 0x4f7ffffe, v1
	v_cvt_u32_f32_e32 v1, v1
	s_nop 0
	v_readfirstlane_b32 s52, v1
	s_mul_i32 s15, s15, s52
	s_mul_hi_u32 s15, s52, s15
	s_add_i32 s52, s52, s15
	s_mul_hi_u32 s15, s4, s52
	s_mul_i32 s15, s15, s14
	s_sub_i32 s4, s4, s15
	s_sub_i32 s15, s4, s14
	s_cmp_ge_u32 s4, s14
	s_cselect_b32 s4, s15, s4
	s_sub_i32 s15, s4, s14
	s_cmp_ge_u32 s4, s14
	s_cselect_b32 s4, s15, s4
	s_xor_b32 s4, s4, s12
	s_sub_i32 s4, s4, s12
	s_add_i32 s12, s13, s4
	s_ashr_i32 s13, s12, 31
	s_lshl_b64 s[12:13], s[12:13], 12
	v_lshl_add_u64 v[8:9], v[2:3], 0, s[12:13]
	global_load_dwordx4 v[8:11], v[8:9], off
	s_waitcnt vmcnt(0)
	v_mov_b32_e32 v12, v9
	v_mov_b32_e32 v13, v10
	v_mov_b32_e32 v9, v11
	v_add_f32_e32 v8, v12, v8
	v_add_f32_e32 v9, v13, v9
	s_nop 0
	v_add_f32_e32 v1, v8, v9
	v_fmac_f32_e32 v7, 0x3b800000, v1
	v_rsq_f32_e32 v1, v7
.LBB0_408:
	v_cmp_gt_i64_e32 vcc, s[24:25], v[4:5]
	v_mov_b32_e32 v7, 0
	v_mov_b32_e32 v8, 0
	s_cbranch_vccnz .LBB0_410
	s_lshl_b32 s4, s63, 7
	s_mulk_i32 s63, 0x81
	s_and_b64 s[12:13], s[26:27], exec
	s_cselect_b32 s4, s63, s4
	s_add_i32 s4, s4, s53
	s_ashr_i32 s12, s4, 31
	s_lshr_b32 s12, s12, 27
	s_add_i32 s12, s4, s12
	s_ashr_i32 s13, s12, 5
	s_lshl_b32 s13, s13, 3
	s_sub_i32 s14, 0x100, s13
	s_min_i32 s14, s14, 8
	s_abs_i32 s14, s14
	v_cvt_f32_u32_e32 v4, s14
	s_sub_i32 s15, 0, s14
	s_andn2_b32 s12, s12, 31
	s_sub_i32 s4, s4, s12
	v_rcp_iflag_f32_e32 v4, v4
	s_ashr_i32 s12, s4, 31
	s_abs_i32 s4, s4
	v_mul_f32_e32 v4, 0x4f7ffffe, v4
	v_cvt_u32_f32_e32 v4, v4
	s_nop 0
	v_readfirstlane_b32 s24, v4
	s_mul_i32 s15, s15, s24
	s_mul_hi_u32 s15, s24, s15
	s_add_i32 s24, s24, s15
	s_mul_hi_u32 s15, s4, s24
	s_mul_i32 s15, s15, s14
	s_sub_i32 s4, s4, s15
	s_sub_i32 s15, s4, s14
	s_cmp_ge_u32 s4, s14
	s_cselect_b32 s4, s15, s4
	s_sub_i32 s15, s4, s14
	s_cmp_ge_u32 s4, s14
	s_cselect_b32 s4, s15, s4
	s_xor_b32 s4, s4, s12
	s_sub_i32 s4, s4, s12
	s_add_i32 s12, s13, s4
	s_ashr_i32 s13, s12, 31
	s_lshl_b64 s[12:13], s[12:13], 12
	v_lshl_add_u64 v[4:5], v[2:3], 0, s[12:13]
	global_load_dwordx4 v[8:11], v[4:5], off
	s_waitcnt vmcnt(0)
	v_mov_b32_e32 v4, v9
	v_mov_b32_e32 v5, v10
	v_mov_b32_e32 v9, v11
	v_add_f32_e32 v4, v4, v8
	v_add_f32_e32 v5, v5, v9
	s_nop 0
	v_add_f32_e32 v4, v4, v5
	v_mov_b32_e32 v5, 0x358637bd
	v_fmac_f32_e32 v5, 0x3b800000, v4
	v_rsq_f32_e32 v8, v5
.LBB0_410:
	v_mov_b64_e32 v[4:5], 0x3ff
	v_cmp_gt_i64_e32 vcc, s[28:29], v[4:5]
	s_cbranch_vccnz .LBB0_412
	s_lshl_b32 s4, s65, 7
	s_mulk_i32 s65, 0x81
	s_and_b64 s[12:13], s[30:31], exec
	s_cselect_b32 s4, s65, s4
	s_add_i32 s4, s4, s64
	s_ashr_i32 s12, s4, 31
	s_lshr_b32 s12, s12, 27
	s_add_i32 s12, s4, s12
	s_ashr_i32 s13, s12, 5
	s_lshl_b32 s13, s13, 3
	s_sub_i32 s14, 0x100, s13
	s_min_i32 s14, s14, 8
	s_abs_i32 s14, s14
	v_cvt_f32_u32_e32 v7, s14
	s_sub_i32 s15, 0, s14
	s_andn2_b32 s12, s12, 31
	s_sub_i32 s4, s4, s12
	v_rcp_iflag_f32_e32 v7, v7
	s_ashr_i32 s12, s4, 31
	s_abs_i32 s4, s4
	v_mov_b32_e32 v9, 0x358637bd
	v_mul_f32_e32 v7, 0x4f7ffffe, v7
	v_cvt_u32_f32_e32 v7, v7
	s_nop 0
	v_readfirstlane_b32 s24, v7
	s_mul_i32 s15, s15, s24
	s_mul_hi_u32 s15, s24, s15
	s_add_i32 s24, s24, s15
	s_mul_hi_u32 s15, s4, s24
	s_mul_i32 s15, s15, s14
	s_sub_i32 s4, s4, s15
	s_sub_i32 s15, s4, s14
	s_cmp_ge_u32 s4, s14
	s_cselect_b32 s4, s15, s4
	s_sub_i32 s15, s4, s14
	s_cmp_ge_u32 s4, s14
	s_cselect_b32 s4, s15, s4
	s_xor_b32 s4, s4, s12
	s_sub_i32 s4, s4, s12
	s_add_i32 s12, s13, s4
	s_ashr_i32 s13, s12, 31
	s_lshl_b64 s[12:13], s[12:13], 12
	v_lshl_add_u64 v[10:11], v[2:3], 0, s[12:13]
	global_load_dwordx4 v[10:13], v[10:11], off
	s_waitcnt vmcnt(0)
	v_mov_b32_e32 v14, v11
	v_mov_b32_e32 v15, v12
	v_mov_b32_e32 v11, v13
	v_add_f32_e32 v10, v14, v10
	v_add_f32_e32 v11, v15, v11
	s_nop 0
	v_add_f32_e32 v7, v10, v11
	v_fmac_f32_e32 v9, 0x3b800000, v7
	v_rsq_f32_e32 v7, v9
; #define LAS __attribute__((address_space(3)))
;     __device__ __forceinline__ bool next(int i, Unit& u) const {
;         const long L = (long)i * G + c; if (L >= nwg) return false;
;         int wgid = (int)L; { const int q = nwg / NXCD, r = nwg % NXCD, xcd = wgid % NXCD, off = wgid / NXCD; wgid = (xcd < r ? xcd * (q + 1) : r * (q + 1) + (xcd - r) * q) + off; }
;         const int nig = WGM * nN, gid = wgid / nig, fm = gid * WGM, gsz = (nM - fm) < WGM ? (nM - fm) : WGM;
;         u.pm = fm + ((wgid % nig) % gsz); u.pn = (wgid % nig) / gsz; u.e = 0; u.t = u.pm; u.cnt = 0x7fffffff; u.i = i; return true;
;     }
;     __device__ __forceinline__ void fill_rstd(LAS float* tab, const float* ssq, float inv_ncol, float scale, int tid) const {
;         Unit u; float v[8];
; #pragma unroll
;         for (int i = 0; i < 8; ++i) { v[i] = 0.f; if (next(i, u)) { const f32x4 ss = *(const f32x4*)(ssq + ((size_t)u.pm * BM + (tid & 255)) * 4); v[i] = __builtin_amdgcn_rsqf(((ss[0] + ss[1]) + (ss[2] + ss[3])) * inv_ncol + EPS) * scale; } }
.LBB0_412:
	v_cmp_gt_i64_e32 vcc, s[34:35], v[4:5]
	v_mov_b32_e32 v9, 0
	v_mov_b32_e32 v10, 0
	s_cbranch_vccnz .LBB0_414
	s_lshl_b32 s4, s67, 7
	s_mulk_i32 s67, 0x81
	s_and_b64 s[12:13], s[36:37], exec
	s_cselect_b32 s4, s67, s4
	s_add_i32 s4, s4, s66
	s_ashr_i32 s12, s4, 31
	s_lshr_b32 s12, s12, 27
	s_add_i32 s12, s4, s12
	s_ashr_i32 s13, s12, 5
	s_lshl_b32 s13, s13, 3
	s_sub_i32 s14, 0x100, s13
	s_min_i32 s14, s14, 8
	s_abs_i32 s14, s14
	v_cvt_f32_u32_e32 v4, s14
	s_sub_i32 s15, 0, s14
	s_andn2_b32 s12, s12, 31
	s_sub_i32 s4, s4, s12
	v_rcp_iflag_f32_e32 v4, v4
	s_ashr_i32 s12, s4, 31
	s_abs_i32 s4, s4
	v_mul_f32_e32 v4, 0x4f7ffffe, v4
	v_cvt_u32_f32_e32 v4, v4
	s_nop 0
	v_readfirstlane_b32 s24, v4
	s_mul_i32 s15, s15, s24
	s_mul_hi_u32 s15, s24, s15
	s_add_i32 s24, s24, s15
	s_mul_hi_u32 s15, s4, s24
	s_mul_i32 s15, s15, s14
	s_sub_i32 s4, s4, s15
	s_sub_i32 s15, s4, s14
	s_cmp_ge_u32 s4, s14
	s_cselect_b32 s4, s15, s4
	s_sub_i32 s15, s4, s14
	s_cmp_ge_u32 s4, s14
	s_cselect_b32 s4, s15, s4
	s_xor_b32 s4, s4, s12
	s_sub_i32 s4, s4, s12
	s_add_i32 s12, s13, s4
	s_ashr_i32 s13, s12, 31
	s_lshl_b64 s[12:13], s[12:13], 12
	v_lshl_add_u64 v[4:5], v[2:3], 0, s[12:13]
	global_load_dwordx4 v[10:13], v[4:5], off
	s_waitcnt vmcnt(0)
	v_mov_b32_e32 v4, v11
	v_mov_b32_e32 v5, v12
	v_mov_b32_e32 v11, v13
	v_add_f32_e32 v4, v4, v10
	v_add_f32_e32 v5, v5, v11
	s_nop 0
	v_add_f32_e32 v4, v4, v5
	v_mov_b32_e32 v5, 0x358637bd
	v_fmac_f32_e32 v5, 0x3b800000, v4
	v_rsq_f32_e32 v10, v5
.LBB0_414:
	v_mov_b64_e32 v[4:5], 0x3ff
	v_cmp_gt_i64_e32 vcc, s[38:39], v[4:5]
	s_cbranch_vccnz .LBB0_416
	s_lshl_b32 s4, s69, 7
	s_mulk_i32 s69, 0x81
	s_and_b64 s[12:13], s[42:43], exec
	s_cselect_b32 s4, s69, s4
	s_add_i32 s4, s4, s68
	s_ashr_i32 s12, s4, 31
	s_lshr_b32 s12, s12, 27
	s_add_i32 s12, s4, s12
	s_ashr_i32 s13, s12, 5
	s_lshl_b32 s13, s13, 3
	s_sub_i32 s14, 0x100, s13
	s_min_i32 s14, s14, 8
	s_abs_i32 s14, s14
	v_cvt_f32_u32_e32 v9, s14
	s_sub_i32 s15, 0, s14
	s_andn2_b32 s12, s12, 31
	s_sub_i32 s4, s4, s12
	v_rcp_iflag_f32_e32 v9, v9
	s_ashr_i32 s12, s4, 31
	s_abs_i32 s4, s4
	v_mov_b32_e32 v11, 0x358637bd
	v_mul_f32_e32 v9, 0x4f7ffffe, v9
	v_cvt_u32_f32_e32 v9, v9
	s_nop 0
	v_readfirstlane_b32 s24, v9
	s_mul_i32 s15, s15, s24
	s_mul_hi_u32 s15, s24, s15
	s_add_i32 s24, s24, s15
	s_mul_hi_u32 s15, s4, s24
	s_mul_i32 s15, s15, s14
	s_sub_i32 s4, s4, s15
	s_sub_i32 s15, s4, s14
	s_cmp_ge_u32 s4, s14
	s_cselect_b32 s4, s15, s4
	s_sub_i32 s15, s4, s14
	s_cmp_ge_u32 s4, s14
	s_cselect_b32 s4, s15, s4
	s_xor_b32 s4, s4, s12
	s_sub_i32 s4, s4, s12
	s_add_i32 s12, s13, s4
	s_ashr_i32 s13, s12, 31
	s_lshl_b64 s[12:13], s[12:13], 12
	v_lshl_add_u64 v[12:13], v[2:3], 0, s[12:13]
	global_load_dwordx4 v[12:15], v[12:13], off
	s_waitcnt vmcnt(0)
	v_mov_b32_e32 v16, v13
	v_mov_b32_e32 v17, v14
	v_mov_b32_e32 v13, v15
	v_add_f32_e32 v12, v16, v12
	v_add_f32_e32 v13, v17, v13
	s_nop 0
	v_add_f32_e32 v9, v12, v13
	v_fmac_f32_e32 v11, 0x3b800000, v9
	v_rsq_f32_e32 v9, v11
.LBB0_416:
	v_cmp_gt_i64_e32 vcc, s[44:45], v[4:5]
	v_mov_b32_e32 v4, 0
	v_mov_b32_e32 v5, 0
	s_cbranch_vccnz .LBB0_486
	s_lshl_b32 s4, s74, 7
	s_mulk_i32 s74, 0x81
	s_and_b64 s[12:13], s[46:47], exec
	s_cselect_b32 s4, s74, s4
	s_add_i32 s4, s4, s73
	s_ashr_i32 s12, s4, 31
	s_lshr_b32 s12, s12, 27
	s_add_i32 s12, s4, s12
	s_ashr_i32 s13, s12, 5
	s_lshl_b32 s13, s13, 3
	s_sub_i32 s14, 0x100, s13
	s_min_i32 s14, s14, 8
	s_abs_i32 s14, s14
	v_cvt_f32_u32_e32 v5, s14
	s_sub_i32 s15, 0, s14
	s_andn2_b32 s12, s12, 31
	s_sub_i32 s4, s4, s12
	v_rcp_iflag_f32_e32 v5, v5
	s_ashr_i32 s12, s4, 31
	s_abs_i32 s4, s4
	v_mov_b32_e32 v11, 0x358637bd
	v_mul_f32_e32 v5, 0x4f7ffffe, v5
	v_cvt_u32_f32_e32 v5, v5
	s_nop 0
	v_readfirstlane_b32 s24, v5
	s_mul_i32 s15, s15, s24
	s_mul_hi_u32 s15, s24, s15
	s_add_i32 s24, s24, s15
	s_mul_hi_u32 s15, s4, s24
	s_mul_i32 s15, s15, s14
	s_sub_i32 s4, s4, s15
	s_sub_i32 s15, s4, s14
	s_cmp_ge_u32 s4, s14
	s_cselect_b32 s4, s15, s4
	s_sub_i32 s15, s4, s14
	s_cmp_ge_u32 s4, s14
	s_cselect_b32 s4, s15, s4
	s_xor_b32 s4, s4, s12
	s_sub_i32 s4, s4, s12
	s_add_i32 s12, s13, s4
	s_ashr_i32 s13, s12, 31
	s_lshl_b64 s[12:13], s[12:13], 12
	v_lshl_add_u64 v[12:13], v[2:3], 0, s[12:13]
	global_load_dwordx4 v[12:15], v[12:13], off
	s_waitcnt vmcnt(0)
	v_mov_b32_e32 v16, v13
	v_mov_b32_e32 v17, v14
	v_mov_b32_e32 v13, v15
	v_add_f32_e32 v12, v16, v12
	v_add_f32_e32 v13, v17, v13
	s_nop 0
	v_add_f32_e32 v5, v12, v13
	v_fmac_f32_e32 v11, 0x3b800000, v5
	v_rsq_f32_e32 v5, v11
	v_mov_b64_e32 v[12:13], 0x3ff
	v_cmp_gt_i64_e32 vcc, s[58:59], v[12:13]
	s_cbranch_vccz .LBB0_487

; __device__ __forceinline__ u32x4 pack8(f32x4 v0, f32x4 v1) { u32x4 w; w.x = cvt_pk_bf16(v0[0], v0[1]); w.y = cvt_pk_bf16(v0[2], v0[3]); w.z = cvt_pk_bf16(v1[0], v1[1]); w.w = cvt_pk_bf16(v1[2], v1[3]); return w; }
; #define EPI_PIN8(a) asm volatile("" : "+v"(a[0][0]), "+v"(a[0][1]), "+v"(a[0][2]), "+v"(a[0][3]), "+v"(a[1][0]), "+v"(a[1][1]), "+v"(a[1][2]), "+v"(a[1][3]) :: "memory")
; __device__ __forceinline__ void rope8h(f32x4& v0, f32x4& v1, u32x4 t) {
;     float c[4], s[4];
; #pragma unroll
;     for (int k = 0; k < 4; ++k) { const h16x2 h = __builtin_bit_cast(h16x2, (unsigned)t[k]); c[k] = (float)h[0]; s[k] = (float)h[1]; }
;     f32x4 a, b;
;     a[0] = v0[0] * c[0] - v0[1] * s[0]; a[1] = v0[1] * c[0] + v0[0] * s[0]; a[2] = v0[2] * c[1] - v0[3] * s[1]; a[3] = v0[3] * c[1] + v0[2] * s[1];
;     b[0] = v1[0] * c[2] - v1[1] * s[2]; b[1] = v1[1] * c[2] + v1[0] * s[2]; b[2] = v1[2] * c[3] - v1[3] * s[3]; b[3] = v1[3] * c[3] + v1[2] * s[3];
;     v0 = a; v1 = b;
;     __device__ __forceinline__ int operator()(AccT acc, const Unit& u, int wr, int wc, int, int) const {
;     ...
;             for (int m = 0; m < 4; ++m) { const int r = row0 + ai * HALF + m * 16; const int pos = r & (SEQ - 1);
;                 rs[ai][m] = rtab[u.i * 256 + wr * 64 + fr + ai * HALF + m * 16];
;                 th[ai][m] = (u32x4){0u, 0u, 0u, 0u}; if (rb >= 0) th[ai][m] = *(const u32x4*)(rope + (size_t)pos * 32 + p0); }
;         EPI_PIN8(rs); EPI_PIN8(th);
; #pragma unroll
;         for (int ai = 0; ai < 2; ++ai)
; #pragma unroll
;             for (int m = 0; m < 4; ++m) { const int r = row0 + ai * HALF + m * 16;
; #pragma unroll
;                 for (int bj = 0; bj < 2; ++bj) { const int col = u.pn * BM + bj * HALF + wc * 32 + 8 * fq;
;                     f32x4 v0 = acc[ai][bj][m][0] * rs[ai][m], v1 = acc[ai][bj][m][1] * rs[ai][m];
;                     if (bj == rb) rope8h(v0, v1, th[ai][m]);
;                     *(u32x4*)(QA + (size_t)r * 768 + col) = pack8(v0, v1); } }
.LBB0_451:
	s_waitcnt lgkmcnt(0)
	s_waitcnt vmcnt(0)
	s_andn2_b64 vcc, exec, s[14:15]
	v_mul_f32_e32 v196, v134, v188
	v_mul_f32_e32 v197, v135, v188
	v_mul_f32_e32 v192, v132, v188
	v_mul_f32_e32 v193, v133, v188
	v_mul_f32_e32 v194, v130, v188
	v_mul_f32_e32 v195, v131, v188
	v_cvt_f32_f16_e32 v168, v156
	v_cvt_f32_f16_sdwa v156, v156 dst_sel:DWORD dst_unused:UNUSED_PAD src0_sel:WORD_1
	v_cvt_f32_f16_e32 v132, v158
	v_cvt_f32_f16_sdwa v134, v158 dst_sel:DWORD dst_unused:UNUSED_PAD src0_sel:WORD_1
	v_cvt_f32_f16_sdwa v191, v157 dst_sel:DWORD dst_unused:UNUSED_PAD src0_sel:WORD_1
	v_cvt_f32_f16_e32 v190, v157
	v_cvt_f32_f16_sdwa v131, v159 dst_sel:DWORD dst_unused:UNUSED_PAD src0_sel:WORD_1
	v_cvt_f32_f16_e32 v130, v159
	v_cndmask_b32_e64 v133, 0, 1, s[14:15]
	v_cmp_ne_u32_e64 s[12:13], 1, v133
	v_mul_f32_e32 v158, v128, v188
	v_mul_f32_e32 v159, v129, v188
	s_cbranch_vccnz .LBB0_453
	v_mul_f32_e32 v204, v193, v156
	v_mul_f32_e32 v205, v192, v156
	v_mul_f32_e32 v128, v192, v168
	v_mul_f32_e32 v129, v193, v168
	v_fma_f32 v192, v192, v168, v204
	v_fma_f32 v193, v193, v168, v205
	v_mul_f32_e32 v210, v159, v134
	v_mul_f32_e32 v211, v158, v134
	v_mul_f32_e32 v192, v197, v191
	v_fma_f32 v206, v196, v190, -v192
	v_fma_f32 v207, v197, v191, -v192
	v_mul_f32_e32 v192, v196, v191
	v_fma_f32 v208, v197, v190, v192
	v_fma_f32 v209, v196, v191, v192
	v_mul_f32_e32 v196, v158, v132
	v_mul_f32_e32 v197, v159, v132
	v_fma_f32 v158, v158, v132, v210
	v_fma_f32 v159, v159, v132, v211
	v_sub_f32_e32 v192, v128, v204
	v_mul_f32_e32 v158, v195, v131
	v_fma_f32 v212, v194, v130, -v158
	v_fma_f32 v213, v195, v131, -v158
	v_mul_f32_e32 v158, v194, v131
	v_fma_f32 v214, v195, v130, v158
	v_fma_f32 v215, v194, v131, v158
	v_sub_f32_e32 v158, v196, v210
	v_mov_b32_e32 v194, v212
	v_mov_b32_e32 v195, v214
	v_mov_b32_e32 v196, v206
	v_mov_b32_e32 v197, v208
.LBB0_453:
	v_add_u32_e32 v128, s0, v177
	v_add_u32_e32 v128, s31, v128
	v_cvt_pk_bf16_f32 v204, v192, v193
	v_cvt_pk_bf16_f32 v205, v196, v197
	v_cvt_pk_bf16_f32 v206, v158, v159
	v_mov_b64_e32 v[158:159], s[24:25]
	v_mad_i64_i32 v[158:159], s[14:15], v203, s76, v[158:159]
	v_ashrrev_i32_e32 v129, 31, v128
	v_mov_b32_e32 v189, v188
	s_cmp_lt_i32 s35, 64
	v_cvt_pk_bf16_f32 v207, v194, v195
	v_lshl_add_u64 v[192:193], v[128:129], 1, v[158:159]
	v_mov_b32_e32 v194, v188
	v_mov_b32_e32 v195, v188
	s_cselect_b64 s[42:43], -1, 0
	s_cmp_gt_i32 s35, 63
	global_store_dwordx4 v[192:193], v[204:207], off
	v_mul_f32_e32 v192, v122, v194
	v_mul_f32_e32 v193, v123, v195
	v_mul_f32_e32 v120, v120, v188
	v_mul_f32_e32 v121, v121, v189
	v_mul_f32_e32 v122, v118, v194
	v_mul_f32_e32 v123, v119, v195
	v_mul_f32_e32 v118, v116, v188
	v_mul_f32_e32 v119, v117, v189
	s_cbranch_scc1 .LBB0_455
	v_mul_f32_e32 v157, v120, v156
	v_mul_f32_e32 v156, v121, v156
	v_mul_f32_e32 v116, v120, v168
	v_mul_f32_e32 v117, v121, v168
	v_fma_f32 v120, v120, v168, v156
	v_fma_f32 v121, v121, v168, v157
	v_mul_f32_e32 v135, v118, v134
	v_mul_f32_e32 v134, v119, v134
	v_mul_f32_e32 v120, v193, v191
	v_fma_f32 v188, v192, v190, -v120
	v_fma_f32 v189, v193, v191, -v120
	v_mul_f32_e32 v120, v192, v191
	v_fma_f32 v190, v193, v190, v120
	v_fma_f32 v191, v192, v191, v120
	v_mul_f32_e32 v192, v118, v132
	v_mul_f32_e32 v193, v119, v132
	v_fma_f32 v118, v118, v132, v134
	v_fma_f32 v119, v119, v132, v135
	v_sub_f32_e32 v120, v116, v156
	v_mul_f32_e32 v118, v123, v131
	v_fma_f32 v132, v122, v130, -v118
	v_fma_f32 v133, v123, v131, -v118
	v_mul_f32_e32 v118, v122, v131
	v_fma_f32 v130, v123, v130, v118
	v_fma_f32 v131, v122, v131, v118
	v_sub_f32_e32 v118, v192, v134
	v_mov_b32_e32 v122, v132
	v_mov_b32_e32 v123, v130
	v_mov_b32_e32 v192, v188
	v_mov_b32_e32 v193, v190
.LBB0_455:
	v_add_u32_e32 v116, 0x80, v128
	v_ashrrev_i32_e32 v117, 31, v116
	v_cvt_pk_bf16_f32 v130, v120, v121
	v_cvt_pk_bf16_f32 v131, v192, v193
	v_cvt_pk_bf16_f32 v132, v118, v119
	v_cvt_pk_bf16_f32 v133, v122, v123
	v_lshl_add_u64 v[118:119], v[116:117], 1, v[158:159]
	global_store_dwordx4 v[118:119], v[130:133], off
	v_mul_f32_e32 v134, v114, v186
	v_mul_f32_e32 v135, v115, v186
	v_cvt_f32_f16_e32 v122, v152
	v_mul_f32_e32 v132, v112, v186
	v_mul_f32_e32 v133, v113, v186
	v_cvt_f32_f16_sdwa v130, v152 dst_sel:DWORD dst_unused:UNUSED_PAD src0_sel:WORD_1
	v_cvt_f32_f16_e32 v114, v154
	v_cvt_f32_f16_sdwa v118, v154 dst_sel:DWORD dst_unused:UNUSED_PAD src0_sel:WORD_1
	v_cvt_f32_f16_sdwa v121, v153 dst_sel:DWORD dst_unused:UNUSED_PAD src0_sel:WORD_1
	v_cvt_f32_f16_e32 v120, v153
	v_cvt_f32_f16_sdwa v113, v155 dst_sel:DWORD dst_unused:UNUSED_PAD src0_sel:WORD_1
	v_cvt_f32_f16_e32 v112, v155
	v_mul_f32_e32 v110, v110, v186
	v_mul_f32_e32 v111, v111, v186
	s_and_b64 vcc, exec, s[12:13]
	v_mul_f32_e32 v108, v108, v186
	v_mul_f32_e32 v109, v109, v186
	s_cbranch_vccnz .LBB0_457
	v_mul_f32_e32 v154, v133, v130
	v_mul_f32_e32 v155, v132, v130
	v_mul_f32_e32 v152, v132, v122
	v_mul_f32_e32 v153, v133, v122
	v_fma_f32 v132, v132, v122, v154
	v_fma_f32 v133, v133, v122, v155
	v_mul_f32_e32 v188, v109, v118
	v_mul_f32_e32 v189, v108, v118
	v_mul_f32_e32 v132, v135, v121
	v_fma_f32 v156, v134, v120, -v132
	v_fma_f32 v157, v135, v121, -v132
	v_mul_f32_e32 v132, v134, v121
	v_fma_f32 v158, v135, v120, v132
	v_fma_f32 v159, v134, v121, v132
	v_mul_f32_e32 v134, v108, v114
	v_mul_f32_e32 v135, v109, v114
	v_fma_f32 v108, v108, v114, v188
	v_fma_f32 v109, v109, v114, v189
	v_sub_f32_e32 v132, v152, v154
	v_mul_f32_e32 v108, v111, v113
	v_fma_f32 v190, v110, v112, -v108
	v_fma_f32 v191, v111, v113, -v108
	v_mul_f32_e32 v108, v110, v113
	v_fma_f32 v192, v111, v112, v108
	v_fma_f32 v193, v110, v113, v108
	v_sub_f32_e32 v108, v134, v188
	v_mov_b32_e32 v110, v190
	v_mov_b32_e32 v111, v192
	v_mov_b32_e32 v134, v156
	v_mov_b32_e32 v135, v158
; __device__ __forceinline__ u32x4 pack8(f32x4 v0, f32x4 v1) { u32x4 w; w.x = cvt_pk_bf16(v0[0], v0[1]); w.y = cvt_pk_bf16(v0[2], v0[3]); w.z = cvt_pk_bf16(v1[0], v1[1]); w.w = cvt_pk_bf16(v1[2], v1[3]); return w; }
; #define EPI_PIN8(a) asm volatile("" : "+v"(a[0][0]), "+v"(a[0][1]), "+v"(a[0][2]), "+v"(a[0][3]), "+v"(a[1][0]), "+v"(a[1][1]), "+v"(a[1][2]), "+v"(a[1][3]) :: "memory")
; __device__ __forceinline__ void rope8h(f32x4& v0, f32x4& v1, u32x4 t) {
;     float c[4], s[4];
; #pragma unroll
;     for (int k = 0; k < 4; ++k) { const h16x2 h = __builtin_bit_cast(h16x2, (unsigned)t[k]); c[k] = (float)h[0]; s[k] = (float)h[1]; }
;     f32x4 a, b;
;     a[0] = v0[0] * c[0] - v0[1] * s[0]; a[1] = v0[1] * c[0] + v0[0] * s[0]; a[2] = v0[2] * c[1] - v0[3] * s[1]; a[3] = v0[3] * c[1] + v0[2] * s[1];
;     b[0] = v1[0] * c[2] - v1[1] * s[2]; b[1] = v1[1] * c[2] + v1[0] * s[2]; b[2] = v1[2] * c[3] - v1[3] * s[3]; b[3] = v1[3] * c[3] + v1[2] * s[3];
;     v0 = a; v1 = b;
;     __device__ __forceinline__ int operator()(AccT acc, const Unit& u, int wr, int wc, int, int) const {
;     ...
;             for (int m = 0; m < 4; ++m) { const int r = row0 + ai * HALF + m * 16; const int pos = r & (SEQ - 1);
;                 rs[ai][m] = rtab[u.i * 256 + wr * 64 + fr + ai * HALF + m * 16];
;                 th[ai][m] = (u32x4){0u, 0u, 0u, 0u}; if (rb >= 0) th[ai][m] = *(const u32x4*)(rope + (size_t)pos * 32 + p0); }
;         EPI_PIN8(rs); EPI_PIN8(th);
; #pragma unroll
;         for (int ai = 0; ai < 2; ++ai)
; #pragma unroll
;             for (int m = 0; m < 4; ++m) { const int r = row0 + ai * HALF + m * 16;
; #pragma unroll
;                 for (int bj = 0; bj < 2; ++bj) { const int col = u.pn * BM + bj * HALF + wc * 32 + 8 * fq;
;                     f32x4 v0 = acc[ai][bj][m][0] * rs[ai][m], v1 = acc[ai][bj][m][1] * rs[ai][m];
;                     if (bj == rb) rope8h(v0, v1, th[ai][m]);
;                     *(u32x4*)(QA + (size_t)r * 768 + col) = pack8(v0, v1); } }
.LBB0_457:
	v_or_b32_e32 v115, 16, v203
	v_cvt_pk_bf16_f32 v132, v132, v133
	v_cvt_pk_bf16_f32 v133, v134, v135
	v_cvt_pk_bf16_f32 v134, v108, v109
	v_mov_b64_e32 v[108:109], s[24:25]
	v_mad_i64_i32 v[108:109], s[14:15], v115, s76, v[108:109]
	v_cvt_pk_bf16_f32 v135, v110, v111
	v_lshl_add_u64 v[110:111], v[128:129], 1, v[108:109]
	global_store_dwordx4 v[110:111], v[132:135], off
	v_mov_b32_e32 v110, v186
	v_mov_b32_e32 v111, v186
	v_mov_b32_e32 v187, v186
	v_mul_f32_e32 v102, v102, v110
	v_mul_f32_e32 v103, v103, v111
	v_mul_f32_e32 v98, v98, v110
	v_mul_f32_e32 v99, v99, v111
	v_cndmask_b32_e64 v110, 0, 1, s[42:43]
	v_mul_f32_e32 v100, v100, v186
	v_mul_f32_e32 v101, v101, v187
	v_cmp_ne_u32_e64 s[14:15], 1, v110
	s_andn2_b64 vcc, exec, s[42:43]
	v_mul_f32_e32 v96, v96, v186
	v_mul_f32_e32 v97, v97, v187
	s_cbranch_vccnz .LBB0_459
	v_mul_f32_e32 v131, v100, v130
	v_mul_f32_e32 v130, v101, v130
	v_mul_f32_e32 v110, v100, v122
	v_mul_f32_e32 v111, v101, v122
	v_fma_f32 v100, v100, v122, v130
	v_fma_f32 v101, v101, v122, v131
	v_mul_f32_e32 v119, v96, v118
	v_mul_f32_e32 v118, v97, v118
	v_mul_f32_e32 v100, v103, v121
	v_fma_f32 v122, v102, v120, -v100
	v_fma_f32 v123, v103, v121, -v100
	v_mul_f32_e32 v100, v102, v121
	v_fma_f32 v120, v103, v120, v100
	v_fma_f32 v121, v102, v121, v100
	v_mul_f32_e32 v102, v96, v114
	v_mul_f32_e32 v103, v97, v114
	v_fma_f32 v96, v96, v114, v118
	v_fma_f32 v97, v97, v114, v119
	v_sub_f32_e32 v100, v110, v130
	v_mul_f32_e32 v96, v99, v113
	v_fma_f32 v114, v98, v112, -v96
	v_fma_f32 v115, v99, v113, -v96
	v_mul_f32_e32 v96, v98, v113
	v_fma_f32 v112, v99, v112, v96
	v_fma_f32 v113, v98, v113, v96
	v_sub_f32_e32 v96, v102, v118
	v_mov_b32_e32 v98, v114
	v_mov_b32_e32 v99, v112
	v_mov_b32_e32 v102, v122
	v_mov_b32_e32 v103, v120
.LBB0_459:
	v_cvt_pk_bf16_f32 v100, v100, v101
	v_cvt_pk_bf16_f32 v101, v102, v103
	v_cvt_pk_bf16_f32 v102, v96, v97
	v_lshl_add_u64 v[96:97], v[116:117], 1, v[108:109]
	v_cvt_pk_bf16_f32 v103, v98, v99
	global_store_dwordx4 v[96:97], v[100:103], off
	v_mul_f32_e32 v110, v94, v184
	v_mul_f32_e32 v111, v95, v184
	v_mul_f32_e32 v108, v92, v184
	v_mul_f32_e32 v109, v93, v184
	v_cvt_f32_f16_e32 v100, v148
	v_cvt_f32_f16_sdwa v102, v148 dst_sel:DWORD dst_unused:UNUSED_PAD src0_sel:WORD_1
	v_cvt_f32_f16_e32 v94, v150
	v_cvt_f32_f16_sdwa v96, v150 dst_sel:DWORD dst_unused:UNUSED_PAD src0_sel:WORD_1
	v_cvt_f32_f16_sdwa v99, v149 dst_sel:DWORD dst_unused:UNUSED_PAD src0_sel:WORD_1
	v_cvt_f32_f16_e32 v98, v149
	v_cvt_f32_f16_sdwa v93, v151 dst_sel:DWORD dst_unused:UNUSED_PAD src0_sel:WORD_1
	v_cvt_f32_f16_e32 v92, v151
	v_mul_f32_e32 v90, v90, v184
	v_mul_f32_e32 v91, v91, v184
	s_and_b64 vcc, exec, s[12:13]
	v_mul_f32_e32 v88, v88, v184
	v_mul_f32_e32 v89, v89, v184
	s_cbranch_vccnz .LBB0_461
	v_mul_f32_e32 v114, v109, v102
	v_mul_f32_e32 v115, v108, v102
	v_mul_f32_e32 v112, v108, v100
	v_mul_f32_e32 v113, v109, v100
	v_fma_f32 v108, v108, v100, v114
	v_fma_f32 v109, v109, v100, v115
	v_mul_f32_e32 v122, v89, v96
	v_mul_f32_e32 v123, v88, v96
	v_mul_f32_e32 v108, v111, v99
	v_fma_f32 v118, v110, v98, -v108
	v_fma_f32 v119, v111, v99, -v108
	v_mul_f32_e32 v108, v110, v99
	v_fma_f32 v120, v111, v98, v108
	v_fma_f32 v121, v110, v99, v108
	v_mul_f32_e32 v110, v88, v94
	v_mul_f32_e32 v111, v89, v94
	v_fma_f32 v88, v88, v94, v122
	v_fma_f32 v89, v89, v94, v123
	v_sub_f32_e32 v108, v112, v114
	v_mul_f32_e32 v88, v91, v93
	v_fma_f32 v130, v90, v92, -v88
	v_fma_f32 v131, v91, v93, -v88
	v_mul_f32_e32 v88, v90, v93
	v_fma_f32 v132, v91, v92, v88
	v_fma_f32 v133, v90, v93, v88
	v_sub_f32_e32 v88, v110, v122
	v_mov_b32_e32 v90, v130
	v_mov_b32_e32 v91, v132
	v_mov_b32_e32 v110, v118
	v_mov_b32_e32 v111, v120
.LBB0_461:
	v_or_b32_e32 v95, 32, v203
	v_cvt_pk_bf16_f32 v108, v108, v109
	v_cvt_pk_bf16_f32 v109, v110, v111
	v_cvt_pk_bf16_f32 v110, v88, v89
	v_mov_b64_e32 v[88:89], s[24:25]
	v_mad_i64_i32 v[88:89], s[42:43], v95, s76, v[88:89]
	v_cvt_pk_bf16_f32 v111, v90, v91
	v_lshl_add_u64 v[90:91], v[128:129], 1, v[88:89]
	v_mov_b32_e32 v185, v184
	global_store_dwordx4 v[90:91], v[108:111], off
	v_mov_b32_e32 v90, v184
	v_mov_b32_e32 v91, v184
	v_mul_f32_e32 v86, v86, v90
	v_mul_f32_e32 v87, v87, v91
	v_mul_f32_e32 v84, v84, v184
	v_mul_f32_e32 v85, v85, v185
	v_mul_f32_e32 v82, v82, v90
	v_mul_f32_e32 v83, v83, v91
	s_and_b64 vcc, exec, s[14:15]
	v_mul_f32_e32 v80, v80, v184
	v_mul_f32_e32 v81, v81, v185
	s_cbranch_vccnz .LBB0_463
	v_mul_f32_e32 v103, v84, v102
	v_mul_f32_e32 v102, v85, v102
	v_mul_f32_e32 v90, v84, v100
	v_mul_f32_e32 v91, v85, v100
	v_fma_f32 v84, v84, v100, v102
	v_fma_f32 v85, v85, v100, v103
	v_mul_f32_e32 v97, v80, v96
	v_mul_f32_e32 v96, v81, v96
	v_mul_f32_e32 v84, v87, v99
	v_fma_f32 v100, v86, v98, -v84
	v_fma_f32 v101, v87, v99, -v84
	v_mul_f32_e32 v84, v86, v99
	v_fma_f32 v98, v87, v98, v84
	v_fma_f32 v99, v86, v99, v84
	v_mul_f32_e32 v86, v80, v94
	v_mul_f32_e32 v87, v81, v94
	v_fma_f32 v80, v80, v94, v96
	v_fma_f32 v81, v81, v94, v97
	v_sub_f32_e32 v84, v90, v102
	v_mul_f32_e32 v80, v83, v93
	v_fma_f32 v94, v82, v92, -v80
	v_fma_f32 v95, v83, v93, -v80
	v_mul_f32_e32 v80, v82, v93
	v_fma_f32 v92, v83, v92, v80
	v_fma_f32 v93, v82, v93, v80
	v_sub_f32_e32 v80, v86, v96
	v_mov_b32_e32 v82, v94
	v_mov_b32_e32 v83, v92
	v_mov_b32_e32 v86, v100
	v_mov_b32_e32 v87, v98
; __device__ __forceinline__ u32x4 pack8(f32x4 v0, f32x4 v1) { u32x4 w; w.x = cvt_pk_bf16(v0[0], v0[1]); w.y = cvt_pk_bf16(v0[2], v0[3]); w.z = cvt_pk_bf16(v1[0], v1[1]); w.w = cvt_pk_bf16(v1[2], v1[3]); return w; }
; #define EPI_PIN8(a) asm volatile("" : "+v"(a[0][0]), "+v"(a[0][1]), "+v"(a[0][2]), "+v"(a[0][3]), "+v"(a[1][0]), "+v"(a[1][1]), "+v"(a[1][2]), "+v"(a[1][3]) :: "memory")
; __device__ __forceinline__ void rope8h(f32x4& v0, f32x4& v1, u32x4 t) {
;     float c[4], s[4];
; #pragma unroll
;     for (int k = 0; k < 4; ++k) { const h16x2 h = __builtin_bit_cast(h16x2, (unsigned)t[k]); c[k] = (float)h[0]; s[k] = (float)h[1]; }
;     f32x4 a, b;
;     a[0] = v0[0] * c[0] - v0[1] * s[0]; a[1] = v0[1] * c[0] + v0[0] * s[0]; a[2] = v0[2] * c[1] - v0[3] * s[1]; a[3] = v0[3] * c[1] + v0[2] * s[1];
;     b[0] = v1[0] * c[2] - v1[1] * s[2]; b[1] = v1[1] * c[2] + v1[0] * s[2]; b[2] = v1[2] * c[3] - v1[3] * s[3]; b[3] = v1[3] * c[3] + v1[2] * s[3];
;     v0 = a; v1 = b;
;     __device__ __forceinline__ int operator()(AccT acc, const Unit& u, int wr, int wc, int, int) const {
;     ...
;             for (int m = 0; m < 4; ++m) { const int r = row0 + ai * HALF + m * 16; const int pos = r & (SEQ - 1);
;                 rs[ai][m] = rtab[u.i * 256 + wr * 64 + fr + ai * HALF + m * 16];
;                 th[ai][m] = (u32x4){0u, 0u, 0u, 0u}; if (rb >= 0) th[ai][m] = *(const u32x4*)(rope + (size_t)pos * 32 + p0); }
;         EPI_PIN8(rs); EPI_PIN8(th);
; #pragma unroll
;         for (int ai = 0; ai < 2; ++ai)
; #pragma unroll
;             for (int m = 0; m < 4; ++m) { const int r = row0 + ai * HALF + m * 16;
; #pragma unroll
;                 for (int bj = 0; bj < 2; ++bj) { const int col = u.pn * BM + bj * HALF + wc * 32 + 8 * fq;
;                     f32x4 v0 = acc[ai][bj][m][0] * rs[ai][m], v1 = acc[ai][bj][m][1] * rs[ai][m];
;                     if (bj == rb) rope8h(v0, v1, th[ai][m]);
;                     *(u32x4*)(QA + (size_t)r * 768 + col) = pack8(v0, v1); } }
.LBB0_463:
	v_cvt_pk_bf16_f32 v84, v84, v85
	v_cvt_pk_bf16_f32 v85, v86, v87
	v_cvt_pk_bf16_f32 v86, v80, v81
	v_lshl_add_u64 v[80:81], v[116:117], 1, v[88:89]
	v_cvt_pk_bf16_f32 v87, v82, v83
	global_store_dwordx4 v[80:81], v[84:87], off
	v_mul_f32_e32 v90, v78, v182
	v_mul_f32_e32 v91, v79, v182
	v_mul_f32_e32 v88, v76, v182
	v_mul_f32_e32 v89, v77, v182
	v_cvt_f32_f16_e32 v84, v144
	v_cvt_f32_f16_sdwa v86, v144 dst_sel:DWORD dst_unused:UNUSED_PAD src0_sel:WORD_1
	v_cvt_f32_f16_e32 v78, v146
	v_cvt_f32_f16_sdwa v80, v146 dst_sel:DWORD dst_unused:UNUSED_PAD src0_sel:WORD_1
	v_cvt_f32_f16_sdwa v83, v145 dst_sel:DWORD dst_unused:UNUSED_PAD src0_sel:WORD_1
	v_cvt_f32_f16_e32 v82, v145
	v_cvt_f32_f16_sdwa v77, v147 dst_sel:DWORD dst_unused:UNUSED_PAD src0_sel:WORD_1
	v_cvt_f32_f16_e32 v76, v147
	v_mul_f32_e32 v74, v74, v182
	v_mul_f32_e32 v75, v75, v182
	s_and_b64 vcc, exec, s[12:13]
	v_mul_f32_e32 v72, v72, v182
	v_mul_f32_e32 v73, v73, v182
	s_cbranch_vccnz .LBB0_465
	v_mul_f32_e32 v94, v89, v86
	v_mul_f32_e32 v95, v88, v86
	v_mul_f32_e32 v92, v88, v84
	v_mul_f32_e32 v93, v89, v84
	v_fma_f32 v88, v88, v84, v94
	v_fma_f32 v89, v89, v84, v95
	v_mul_f32_e32 v100, v73, v80
	v_mul_f32_e32 v101, v72, v80
	v_mul_f32_e32 v88, v91, v83
	v_fma_f32 v96, v90, v82, -v88
	v_fma_f32 v97, v91, v83, -v88
	v_mul_f32_e32 v88, v90, v83
	v_fma_f32 v98, v91, v82, v88
	v_fma_f32 v99, v90, v83, v88
	v_mul_f32_e32 v90, v72, v78
	v_mul_f32_e32 v91, v73, v78
	v_fma_f32 v72, v72, v78, v100
	v_fma_f32 v73, v73, v78, v101
	v_sub_f32_e32 v88, v92, v94
	v_mul_f32_e32 v72, v75, v77
	v_fma_f32 v102, v74, v76, -v72
	v_fma_f32 v103, v75, v77, -v72
	v_mul_f32_e32 v72, v74, v77
	v_fma_f32 v108, v75, v76, v72
	v_fma_f32 v109, v74, v77, v72
	v_sub_f32_e32 v72, v90, v100
	v_mov_b32_e32 v74, v102
	v_mov_b32_e32 v75, v108
	v_mov_b32_e32 v90, v96
	v_mov_b32_e32 v91, v98
.LBB0_465:
	v_or_b32_e32 v79, 48, v203
	v_cvt_pk_bf16_f32 v88, v88, v89
	v_cvt_pk_bf16_f32 v89, v90, v91
	v_cvt_pk_bf16_f32 v90, v72, v73
	v_mov_b64_e32 v[72:73], s[24:25]
	v_mad_i64_i32 v[72:73], s[42:43], v79, s76, v[72:73]
	v_cvt_pk_bf16_f32 v91, v74, v75
	v_lshl_add_u64 v[74:75], v[128:129], 1, v[72:73]
	v_mov_b32_e32 v183, v182
	global_store_dwordx4 v[74:75], v[88:91], off
	v_mov_b32_e32 v74, v182
	v_mov_b32_e32 v75, v182
	v_mul_f32_e32 v70, v70, v74
	v_mul_f32_e32 v71, v71, v75
	v_mul_f32_e32 v68, v68, v182
	v_mul_f32_e32 v69, v69, v183
	v_mul_f32_e32 v66, v66, v74
	v_mul_f32_e32 v67, v67, v75
	s_and_b64 vcc, exec, s[14:15]
	v_mul_f32_e32 v64, v64, v182
	v_mul_f32_e32 v65, v65, v183
	s_cbranch_vccnz .LBB0_467
	v_mul_f32_e32 v87, v68, v86
	v_mul_f32_e32 v86, v69, v86
	v_mul_f32_e32 v74, v68, v84
	v_mul_f32_e32 v75, v69, v84
	v_fma_f32 v68, v68, v84, v86
	v_fma_f32 v69, v69, v84, v87
	v_mul_f32_e32 v81, v64, v80
	v_mul_f32_e32 v80, v65, v80
	v_mul_f32_e32 v68, v71, v83
	v_fma_f32 v84, v70, v82, -v68
	v_fma_f32 v85, v71, v83, -v68
	v_mul_f32_e32 v68, v70, v83
	v_fma_f32 v82, v71, v82, v68
	v_fma_f32 v83, v70, v83, v68
	v_mul_f32_e32 v70, v64, v78
	v_mul_f32_e32 v71, v65, v78
	v_fma_f32 v64, v64, v78, v80
	v_fma_f32 v65, v65, v78, v81
	v_sub_f32_e32 v68, v74, v86
	v_mul_f32_e32 v64, v67, v77
	v_fma_f32 v78, v66, v76, -v64
	v_fma_f32 v79, v67, v77, -v64
	v_mul_f32_e32 v64, v66, v77
	v_fma_f32 v76, v67, v76, v64
	v_fma_f32 v77, v66, v77, v64
	v_sub_f32_e32 v64, v70, v80
	v_mov_b32_e32 v66, v78
	v_mov_b32_e32 v67, v76
	v_mov_b32_e32 v70, v84
	v_mov_b32_e32 v71, v82
.LBB0_467:
	v_cvt_pk_bf16_f32 v68, v68, v69
	v_cvt_pk_bf16_f32 v69, v70, v71
	v_cvt_pk_bf16_f32 v70, v64, v65
	v_lshl_add_u64 v[64:65], v[116:117], 1, v[72:73]
	v_cvt_pk_bf16_f32 v71, v66, v67
	global_store_dwordx4 v[64:65], v[68:71], off
	v_mul_f32_e32 v74, v62, v180
	v_mul_f32_e32 v75, v63, v180
	v_mul_f32_e32 v72, v60, v180
	v_mul_f32_e32 v73, v61, v180
	v_cvt_f32_f16_e32 v68, v140
	v_cvt_f32_f16_sdwa v70, v140 dst_sel:DWORD dst_unused:UNUSED_PAD src0_sel:WORD_1
	v_cvt_f32_f16_e32 v62, v142
	v_cvt_f32_f16_sdwa v64, v142 dst_sel:DWORD dst_unused:UNUSED_PAD src0_sel:WORD_1
	v_cvt_f32_f16_sdwa v67, v141 dst_sel:DWORD dst_unused:UNUSED_PAD src0_sel:WORD_1
	v_cvt_f32_f16_e32 v66, v141
	v_cvt_f32_f16_sdwa v61, v143 dst_sel:DWORD dst_unused:UNUSED_PAD src0_sel:WORD_1
	v_cvt_f32_f16_e32 v60, v143
	v_mul_f32_e32 v58, v58, v180
	v_mul_f32_e32 v59, v59, v180
	s_and_b64 vcc, exec, s[12:13]
	v_mul_f32_e32 v56, v56, v180
	v_mul_f32_e32 v57, v57, v180
	s_cbranch_vccnz .LBB0_469
	v_mul_f32_e32 v78, v73, v70
	v_mul_f32_e32 v79, v72, v70
	v_mul_f32_e32 v76, v72, v68
	v_mul_f32_e32 v77, v73, v68
	v_fma_f32 v72, v72, v68, v78
	v_fma_f32 v73, v73, v68, v79
	v_mul_f32_e32 v84, v57, v64
	v_mul_f32_e32 v85, v56, v64
	v_mul_f32_e32 v72, v75, v67
	v_fma_f32 v80, v74, v66, -v72
	v_fma_f32 v81, v75, v67, -v72
	v_mul_f32_e32 v72, v74, v67
	v_fma_f32 v82, v75, v66, v72
	v_fma_f32 v83, v74, v67, v72
	v_mul_f32_e32 v74, v56, v62
	v_mul_f32_e32 v75, v57, v62
	v_fma_f32 v56, v56, v62, v84
	v_fma_f32 v57, v57, v62, v85
	v_sub_f32_e32 v72, v76, v78
	v_mul_f32_e32 v56, v59, v61
	v_fma_f32 v86, v58, v60, -v56
	v_fma_f32 v87, v59, v61, -v56
	v_mul_f32_e32 v56, v58, v61
	v_fma_f32 v88, v59, v60, v56
	v_fma_f32 v89, v58, v61, v56
	v_sub_f32_e32 v56, v74, v84
	v_mov_b32_e32 v58, v86
	v_mov_b32_e32 v59, v88
	v_mov_b32_e32 v74, v80
	v_mov_b32_e32 v75, v82
; __device__ __forceinline__ u32x4 pack8(f32x4 v0, f32x4 v1) { u32x4 w; w.x = cvt_pk_bf16(v0[0], v0[1]); w.y = cvt_pk_bf16(v0[2], v0[3]); w.z = cvt_pk_bf16(v1[0], v1[1]); w.w = cvt_pk_bf16(v1[2], v1[3]); return w; }
; #define EPI_PIN8(a) asm volatile("" : "+v"(a[0][0]), "+v"(a[0][1]), "+v"(a[0][2]), "+v"(a[0][3]), "+v"(a[1][0]), "+v"(a[1][1]), "+v"(a[1][2]), "+v"(a[1][3]) :: "memory")
; __device__ __forceinline__ void rope8h(f32x4& v0, f32x4& v1, u32x4 t) {
;     float c[4], s[4];
; #pragma unroll
;     for (int k = 0; k < 4; ++k) { const h16x2 h = __builtin_bit_cast(h16x2, (unsigned)t[k]); c[k] = (float)h[0]; s[k] = (float)h[1]; }
;     f32x4 a, b;
;     a[0] = v0[0] * c[0] - v0[1] * s[0]; a[1] = v0[1] * c[0] + v0[0] * s[0]; a[2] = v0[2] * c[1] - v0[3] * s[1]; a[3] = v0[3] * c[1] + v0[2] * s[1];
;     b[0] = v1[0] * c[2] - v1[1] * s[2]; b[1] = v1[1] * c[2] + v1[0] * s[2]; b[2] = v1[2] * c[3] - v1[3] * s[3]; b[3] = v1[3] * c[3] + v1[2] * s[3];
;     v0 = a; v1 = b;
;     __device__ __forceinline__ int operator()(AccT acc, const Unit& u, int wr, int wc, int, int) const {
;     ...
;             for (int m = 0; m < 4; ++m) { const int r = row0 + ai * HALF + m * 16; const int pos = r & (SEQ - 1);
;                 rs[ai][m] = rtab[u.i * 256 + wr * 64 + fr + ai * HALF + m * 16];
;                 th[ai][m] = (u32x4){0u, 0u, 0u, 0u}; if (rb >= 0) th[ai][m] = *(const u32x4*)(rope + (size_t)pos * 32 + p0); }
;         EPI_PIN8(rs); EPI_PIN8(th);
; #pragma unroll
;         for (int ai = 0; ai < 2; ++ai)
; #pragma unroll
;             for (int m = 0; m < 4; ++m) { const int r = row0 + ai * HALF + m * 16;
; #pragma unroll
;                 for (int bj = 0; bj < 2; ++bj) { const int col = u.pn * BM + bj * HALF + wc * 32 + 8 * fq;
;                     f32x4 v0 = acc[ai][bj][m][0] * rs[ai][m], v1 = acc[ai][bj][m][1] * rs[ai][m];
;                     if (bj == rb) rope8h(v0, v1, th[ai][m]);
;                     *(u32x4*)(QA + (size_t)r * 768 + col) = pack8(v0, v1); } }
.LBB0_469:
	v_cvt_pk_bf16_f32 v72, v72, v73
	v_cvt_pk_bf16_f32 v73, v74, v75
	v_cvt_pk_bf16_f32 v74, v56, v57
	v_mov_b64_e32 v[56:57], s[24:25]
	v_mad_i64_i32 v[56:57], s[42:43], v175, s76, v[56:57]
	v_cvt_pk_bf16_f32 v75, v58, v59
	v_lshl_add_u64 v[58:59], v[128:129], 1, v[56:57]
	v_mov_b32_e32 v181, v180
	global_store_dwordx4 v[58:59], v[72:75], off
	v_mov_b32_e32 v58, v180
	v_mov_b32_e32 v59, v180
	v_mul_f32_e32 v54, v54, v58
	v_mul_f32_e32 v55, v55, v59
	v_mul_f32_e32 v52, v52, v180
	v_mul_f32_e32 v53, v53, v181
	v_mul_f32_e32 v50, v50, v58
	v_mul_f32_e32 v51, v51, v59
	s_and_b64 vcc, exec, s[14:15]
	v_mul_f32_e32 v48, v48, v180
	v_mul_f32_e32 v49, v49, v181
	s_cbranch_vccnz .LBB0_471
	v_mul_f32_e32 v71, v52, v70
	v_mul_f32_e32 v70, v53, v70
	v_mul_f32_e32 v58, v52, v68
	v_mul_f32_e32 v59, v53, v68
	v_fma_f32 v52, v52, v68, v70
	v_fma_f32 v53, v53, v68, v71
	v_mul_f32_e32 v65, v48, v64
	v_mul_f32_e32 v64, v49, v64
	v_mul_f32_e32 v52, v55, v67
	v_fma_f32 v68, v54, v66, -v52
	v_fma_f32 v69, v55, v67, -v52
	v_mul_f32_e32 v52, v54, v67
	v_fma_f32 v66, v55, v66, v52
	v_fma_f32 v67, v54, v67, v52
	v_mul_f32_e32 v54, v48, v62
	v_mul_f32_e32 v55, v49, v62
	v_fma_f32 v48, v48, v62, v64
	v_fma_f32 v49, v49, v62, v65
	v_sub_f32_e32 v52, v58, v70
	v_mul_f32_e32 v48, v51, v61
	v_fma_f32 v62, v50, v60, -v48
	v_fma_f32 v63, v51, v61, -v48
	v_mul_f32_e32 v48, v50, v61
	v_fma_f32 v60, v51, v60, v48
	v_fma_f32 v61, v50, v61, v48
	v_sub_f32_e32 v48, v54, v64
	v_mov_b32_e32 v50, v62
	v_mov_b32_e32 v51, v60
	v_mov_b32_e32 v54, v68
	v_mov_b32_e32 v55, v66
.LBB0_471:
	v_cvt_pk_bf16_f32 v52, v52, v53
	v_cvt_pk_bf16_f32 v53, v54, v55
	v_cvt_pk_bf16_f32 v54, v48, v49
	v_lshl_add_u64 v[48:49], v[116:117], 1, v[56:57]
	v_cvt_pk_bf16_f32 v55, v50, v51
	global_store_dwordx4 v[48:49], v[52:55], off
	v_mul_f32_e32 v58, v46, v178
	v_mul_f32_e32 v59, v47, v178
	v_mul_f32_e32 v56, v44, v178
	v_mul_f32_e32 v57, v45, v178
	v_cvt_f32_f16_e32 v52, v136
	v_cvt_f32_f16_sdwa v54, v136 dst_sel:DWORD dst_unused:UNUSED_PAD src0_sel:WORD_1
	v_cvt_f32_f16_e32 v46, v138
	v_cvt_f32_f16_sdwa v48, v138 dst_sel:DWORD dst_unused:UNUSED_PAD src0_sel:WORD_1
	v_cvt_f32_f16_sdwa v51, v137 dst_sel:DWORD dst_unused:UNUSED_PAD src0_sel:WORD_1
	v_cvt_f32_f16_e32 v50, v137
	v_cvt_f32_f16_sdwa v45, v139 dst_sel:DWORD dst_unused:UNUSED_PAD src0_sel:WORD_1
	v_cvt_f32_f16_e32 v44, v139
	v_mul_f32_e32 v42, v42, v178
	v_mul_f32_e32 v43, v43, v178
	s_and_b64 vcc, exec, s[12:13]
	v_mul_f32_e32 v40, v40, v178
	v_mul_f32_e32 v41, v41, v178
	s_cbranch_vccnz .LBB0_473
	v_mul_f32_e32 v62, v57, v54
	v_mul_f32_e32 v63, v56, v54
	v_mul_f32_e32 v60, v56, v52
	v_mul_f32_e32 v61, v57, v52
	v_fma_f32 v56, v56, v52, v62
	v_fma_f32 v57, v57, v52, v63
	v_mul_f32_e32 v68, v41, v48
	v_mul_f32_e32 v69, v40, v48
	v_mul_f32_e32 v56, v59, v51
	v_fma_f32 v64, v58, v50, -v56
	v_fma_f32 v65, v59, v51, -v56
	v_mul_f32_e32 v56, v58, v51
	v_fma_f32 v66, v59, v50, v56
	v_fma_f32 v67, v58, v51, v56
	v_mul_f32_e32 v58, v40, v46
	v_mul_f32_e32 v59, v41, v46
	v_fma_f32 v40, v40, v46, v68
	v_fma_f32 v41, v41, v46, v69
	v_sub_f32_e32 v56, v60, v62
	v_mul_f32_e32 v40, v43, v45
	v_fma_f32 v70, v42, v44, -v40
	v_fma_f32 v71, v43, v45, -v40
	v_mul_f32_e32 v40, v42, v45
	v_fma_f32 v72, v43, v44, v40
	v_fma_f32 v73, v42, v45, v40
	v_sub_f32_e32 v40, v58, v68
	v_mov_b32_e32 v42, v70
	v_mov_b32_e32 v43, v72
	v_mov_b32_e32 v58, v64
	v_mov_b32_e32 v59, v66
.LBB0_473:
	v_add_u32_e32 v47, 0x90, v203
	v_cvt_pk_bf16_f32 v56, v56, v57
	v_cvt_pk_bf16_f32 v57, v58, v59
	v_cvt_pk_bf16_f32 v58, v40, v41
	v_mov_b64_e32 v[40:41], s[24:25]
	v_mad_i64_i32 v[40:41], s[42:43], v47, s76, v[40:41]
	v_cvt_pk_bf16_f32 v59, v42, v43
	v_lshl_add_u64 v[42:43], v[128:129], 1, v[40:41]
	v_mov_b32_e32 v179, v178
	global_store_dwordx4 v[42:43], v[56:59], off
	v_mov_b32_e32 v42, v178
	v_mov_b32_e32 v43, v178
	v_mul_f32_e32 v38, v38, v42
	v_mul_f32_e32 v39, v39, v43
	v_mul_f32_e32 v36, v36, v178
	v_mul_f32_e32 v37, v37, v179
	v_mul_f32_e32 v34, v34, v42
	v_mul_f32_e32 v35, v35, v43
	s_and_b64 vcc, exec, s[14:15]
	v_mul_f32_e32 v32, v32, v178
	v_mul_f32_e32 v33, v33, v179
	s_cbranch_vccnz .LBB0_475
	v_mul_f32_e32 v55, v36, v54
	v_mul_f32_e32 v54, v37, v54
	v_mul_f32_e32 v42, v36, v52
	v_mul_f32_e32 v43, v37, v52
	v_fma_f32 v36, v36, v52, v54
	v_fma_f32 v37, v37, v52, v55
	v_mul_f32_e32 v49, v32, v48
	v_mul_f32_e32 v48, v33, v48
	v_mul_f32_e32 v36, v39, v51
	v_fma_f32 v52, v38, v50, -v36
	v_fma_f32 v53, v39, v51, -v36
	v_mul_f32_e32 v36, v38, v51
	v_fma_f32 v50, v39, v50, v36
	v_fma_f32 v51, v38, v51, v36
	v_mul_f32_e32 v38, v32, v46
	v_mul_f32_e32 v39, v33, v46
	v_fma_f32 v32, v32, v46, v48
	v_fma_f32 v33, v33, v46, v49
	v_sub_f32_e32 v36, v42, v54
	v_mul_f32_e32 v32, v35, v45
	v_fma_f32 v46, v34, v44, -v32
	v_fma_f32 v47, v35, v45, -v32
	v_mul_f32_e32 v32, v34, v45
	v_fma_f32 v44, v35, v44, v32
	v_fma_f32 v45, v34, v45, v32
	v_sub_f32_e32 v32, v38, v48
	v_mov_b32_e32 v34, v46
	v_mov_b32_e32 v35, v44
	v_mov_b32_e32 v38, v52
	v_mov_b32_e32 v39, v50
; __device__ __forceinline__ u32x4 pack8(f32x4 v0, f32x4 v1) { u32x4 w; w.x = cvt_pk_bf16(v0[0], v0[1]); w.y = cvt_pk_bf16(v0[2], v0[3]); w.z = cvt_pk_bf16(v1[0], v1[1]); w.w = cvt_pk_bf16(v1[2], v1[3]); return w; }
; #define EPI_PIN8(a) asm volatile("" : "+v"(a[0][0]), "+v"(a[0][1]), "+v"(a[0][2]), "+v"(a[0][3]), "+v"(a[1][0]), "+v"(a[1][1]), "+v"(a[1][2]), "+v"(a[1][3]) :: "memory")
; __device__ __forceinline__ void rope8h(f32x4& v0, f32x4& v1, u32x4 t) {
;     float c[4], s[4];
; #pragma unroll
;     for (int k = 0; k < 4; ++k) { const h16x2 h = __builtin_bit_cast(h16x2, (unsigned)t[k]); c[k] = (float)h[0]; s[k] = (float)h[1]; }
;     f32x4 a, b;
;     a[0] = v0[0] * c[0] - v0[1] * s[0]; a[1] = v0[1] * c[0] + v0[0] * s[0]; a[2] = v0[2] * c[1] - v0[3] * s[1]; a[3] = v0[3] * c[1] + v0[2] * s[1];
;     b[0] = v1[0] * c[2] - v1[1] * s[2]; b[1] = v1[1] * c[2] + v1[0] * s[2]; b[2] = v1[2] * c[3] - v1[3] * s[3]; b[3] = v1[3] * c[3] + v1[2] * s[3];
;     v0 = a; v1 = b;
;     __device__ __forceinline__ int operator()(AccT acc, const Unit& u, int wr, int wc, int, int) const {
;     ...
;             for (int m = 0; m < 4; ++m) { const int r = row0 + ai * HALF + m * 16; const int pos = r & (SEQ - 1);
;                 rs[ai][m] = rtab[u.i * 256 + wr * 64 + fr + ai * HALF + m * 16];
;                 th[ai][m] = (u32x4){0u, 0u, 0u, 0u}; if (rb >= 0) th[ai][m] = *(const u32x4*)(rope + (size_t)pos * 32 + p0); }
;         EPI_PIN8(rs); EPI_PIN8(th);
; #pragma unroll
;         for (int ai = 0; ai < 2; ++ai)
; #pragma unroll
;             for (int m = 0; m < 4; ++m) { const int r = row0 + ai * HALF + m * 16;
; #pragma unroll
;                 for (int bj = 0; bj < 2; ++bj) { const int col = u.pn * BM + bj * HALF + wc * 32 + 8 * fq;
;                     f32x4 v0 = acc[ai][bj][m][0] * rs[ai][m], v1 = acc[ai][bj][m][1] * rs[ai][m];
;                     if (bj == rb) rope8h(v0, v1, th[ai][m]);
;                     *(u32x4*)(QA + (size_t)r * 768 + col) = pack8(v0, v1); } }
.LBB0_475:
	v_cvt_pk_bf16_f32 v36, v36, v37
	v_cvt_pk_bf16_f32 v37, v38, v39
	v_cvt_pk_bf16_f32 v38, v32, v33
	v_lshl_add_u64 v[32:33], v[116:117], 1, v[40:41]
	v_cvt_pk_bf16_f32 v39, v34, v35
	global_store_dwordx4 v[32:33], v[36:39], off
	v_mul_f32_e32 v42, v30, v176
	v_mul_f32_e32 v43, v31, v176
	v_mul_f32_e32 v40, v28, v176
	v_mul_f32_e32 v41, v29, v176
	v_cvt_f32_f16_e32 v36, v124
	v_cvt_f32_f16_sdwa v38, v124 dst_sel:DWORD dst_unused:UNUSED_PAD src0_sel:WORD_1
	v_cvt_f32_f16_e32 v30, v126
	v_cvt_f32_f16_sdwa v32, v126 dst_sel:DWORD dst_unused:UNUSED_PAD src0_sel:WORD_1
	v_cvt_f32_f16_sdwa v35, v125 dst_sel:DWORD dst_unused:UNUSED_PAD src0_sel:WORD_1
	v_cvt_f32_f16_e32 v34, v125
	v_cvt_f32_f16_sdwa v29, v127 dst_sel:DWORD dst_unused:UNUSED_PAD src0_sel:WORD_1
	v_cvt_f32_f16_e32 v28, v127
	v_mul_f32_e32 v26, v26, v176
	v_mul_f32_e32 v27, v27, v176
	s_and_b64 vcc, exec, s[12:13]
	v_mul_f32_e32 v24, v24, v176
	v_mul_f32_e32 v25, v25, v176
	s_cbranch_vccnz .LBB0_477
	v_mul_f32_e32 v46, v41, v38
	v_mul_f32_e32 v47, v40, v38
	v_mul_f32_e32 v44, v40, v36
	v_mul_f32_e32 v45, v41, v36
	v_fma_f32 v40, v40, v36, v46
	v_fma_f32 v41, v41, v36, v47
	v_mul_f32_e32 v52, v25, v32
	v_mul_f32_e32 v53, v24, v32
	v_mul_f32_e32 v40, v43, v35
	v_fma_f32 v48, v42, v34, -v40
	v_fma_f32 v49, v43, v35, -v40
	v_mul_f32_e32 v40, v42, v35
	v_fma_f32 v50, v43, v34, v40
	v_fma_f32 v51, v42, v35, v40
	v_mul_f32_e32 v42, v24, v30
	v_mul_f32_e32 v43, v25, v30
	v_fma_f32 v24, v24, v30, v52
	v_fma_f32 v25, v25, v30, v53
	v_sub_f32_e32 v40, v44, v46
	v_mul_f32_e32 v24, v27, v29
	v_fma_f32 v54, v26, v28, -v24
	v_fma_f32 v55, v27, v29, -v24
	v_mul_f32_e32 v24, v26, v29
	v_fma_f32 v56, v27, v28, v24
	v_fma_f32 v57, v26, v29, v24
	v_sub_f32_e32 v24, v42, v52
	v_mov_b32_e32 v26, v54
	v_mov_b32_e32 v27, v56
	v_mov_b32_e32 v42, v48
	v_mov_b32_e32 v43, v50
.LBB0_477:
	v_add_u32_e32 v31, 0xa0, v203
	v_cvt_pk_bf16_f32 v40, v40, v41
	v_cvt_pk_bf16_f32 v41, v42, v43
	v_cvt_pk_bf16_f32 v42, v24, v25
	v_mov_b64_e32 v[24:25], s[24:25]
	v_mad_i64_i32 v[24:25], s[42:43], v31, s76, v[24:25]
	v_cvt_pk_bf16_f32 v43, v26, v27
	v_lshl_add_u64 v[26:27], v[128:129], 1, v[24:25]
	v_mov_b32_e32 v177, v176
	global_store_dwordx4 v[26:27], v[40:43], off
	v_mov_b32_e32 v26, v176
	v_mov_b32_e32 v27, v176
	v_mul_f32_e32 v22, v22, v26
	v_mul_f32_e32 v23, v23, v27
	v_mul_f32_e32 v20, v20, v176
	v_mul_f32_e32 v21, v21, v177
	v_mul_f32_e32 v18, v18, v26
	v_mul_f32_e32 v19, v19, v27
	s_and_b64 vcc, exec, s[14:15]
	v_mul_f32_e32 v16, v16, v176
	v_mul_f32_e32 v17, v17, v177
	s_cbranch_vccnz .LBB0_479
	v_mul_f32_e32 v39, v20, v38
	v_mul_f32_e32 v38, v21, v38
	v_mul_f32_e32 v26, v20, v36
	v_mul_f32_e32 v27, v21, v36
	v_fma_f32 v20, v20, v36, v38
	v_fma_f32 v21, v21, v36, v39
	v_mul_f32_e32 v33, v16, v32
	v_mul_f32_e32 v32, v17, v32
	v_mul_f32_e32 v20, v23, v35
	v_fma_f32 v36, v22, v34, -v20
	v_fma_f32 v37, v23, v35, -v20
	v_mul_f32_e32 v20, v22, v35
	v_fma_f32 v34, v23, v34, v20
	v_fma_f32 v35, v22, v35, v20
	v_mul_f32_e32 v22, v16, v30
	v_mul_f32_e32 v23, v17, v30
	v_fma_f32 v16, v16, v30, v32
	v_fma_f32 v17, v17, v30, v33
	v_sub_f32_e32 v20, v26, v38
	v_mul_f32_e32 v16, v19, v29
	v_fma_f32 v30, v18, v28, -v16
	v_fma_f32 v31, v19, v29, -v16
	v_mul_f32_e32 v16, v18, v29
	v_fma_f32 v28, v19, v28, v16
	v_fma_f32 v29, v18, v29, v16
	v_sub_f32_e32 v16, v22, v32
	v_mov_b32_e32 v18, v30
	v_mov_b32_e32 v19, v28
	v_mov_b32_e32 v22, v36
	v_mov_b32_e32 v23, v34
.LBB0_479:
	v_cvt_pk_bf16_f32 v20, v20, v21
	v_cvt_pk_bf16_f32 v21, v22, v23
	v_cvt_pk_bf16_f32 v22, v16, v17
	v_lshl_add_u64 v[16:17], v[116:117], 1, v[24:25]
	v_cvt_pk_bf16_f32 v23, v18, v19
	global_store_dwordx4 v[16:17], v[20:23], off
	v_mul_f32_e32 v26, v14, v174
	v_mul_f32_e32 v27, v15, v174
	v_mul_f32_e32 v24, v12, v174
	v_mul_f32_e32 v25, v13, v174
	v_cvt_f32_f16_e32 v20, v104
	v_cvt_f32_f16_sdwa v22, v104 dst_sel:DWORD dst_unused:UNUSED_PAD src0_sel:WORD_1
	v_cvt_f32_f16_e32 v14, v106
	v_cvt_f32_f16_sdwa v16, v106 dst_sel:DWORD dst_unused:UNUSED_PAD src0_sel:WORD_1
	v_cvt_f32_f16_sdwa v19, v105 dst_sel:DWORD dst_unused:UNUSED_PAD src0_sel:WORD_1
	v_cvt_f32_f16_e32 v18, v105
	v_cvt_f32_f16_sdwa v13, v107 dst_sel:DWORD dst_unused:UNUSED_PAD src0_sel:WORD_1
	v_cvt_f32_f16_e32 v12, v107
	v_mul_f32_e32 v10, v10, v174
	v_mul_f32_e32 v11, v11, v174
	s_and_b64 vcc, exec, s[12:13]
	v_mul_f32_e32 v8, v8, v174
	v_mul_f32_e32 v9, v9, v174
	s_cbranch_vccnz .LBB0_481
	v_mul_f32_e32 v30, v25, v22
	v_mul_f32_e32 v31, v24, v22
	v_mul_f32_e32 v28, v24, v20
	v_mul_f32_e32 v29, v25, v20
	v_fma_f32 v24, v24, v20, v30
	v_fma_f32 v25, v25, v20, v31
	v_mul_f32_e32 v36, v9, v16
	v_mul_f32_e32 v37, v8, v16
	v_mul_f32_e32 v24, v27, v19
	v_fma_f32 v32, v26, v18, -v24
	v_fma_f32 v33, v27, v19, -v24
	v_mul_f32_e32 v24, v26, v19
	v_fma_f32 v34, v27, v18, v24
	v_fma_f32 v35, v26, v19, v24
	v_mul_f32_e32 v26, v8, v14
	v_mul_f32_e32 v27, v9, v14
	v_fma_f32 v8, v8, v14, v36
	v_fma_f32 v9, v9, v14, v37
	v_sub_f32_e32 v24, v28, v30
	v_mul_f32_e32 v8, v11, v13
	v_fma_f32 v38, v10, v12, -v8
	v_fma_f32 v39, v11, v13, -v8
	v_mul_f32_e32 v8, v10, v13
	v_fma_f32 v40, v11, v12, v8
	v_fma_f32 v41, v10, v13, v8
	v_sub_f32_e32 v8, v26, v36
	v_mov_b32_e32 v10, v38
	v_mov_b32_e32 v11, v40
	v_mov_b32_e32 v26, v32
	v_mov_b32_e32 v27, v34
.LBB0_481:
	v_add_u32_e32 v15, 0xb0, v203
	v_cvt_pk_bf16_f32 v24, v24, v25
	v_cvt_pk_bf16_f32 v25, v26, v27
	v_cvt_pk_bf16_f32 v26, v8, v9
	v_mov_b64_e32 v[8:9], s[24:25]
	v_mad_i64_i32 v[8:9], s[12:13], v15, s76, v[8:9]
	v_cvt_pk_bf16_f32 v27, v10, v11
	v_lshl_add_u64 v[10:11], v[128:129], 1, v[8:9]
	v_mov_b32_e32 v175, v174
	global_store_dwordx4 v[10:11], v[24:27], off
	v_mov_b32_e32 v10, v174
	v_mov_b32_e32 v11, v174
	v_mul_f32_e32 v6, v6, v10
	v_mul_f32_e32 v7, v7, v11
	v_mul_f32_e32 v4, v4, v174
	v_mul_f32_e32 v5, v5, v175
	v_mul_f32_e32 v2, v2, v10
	v_mul_f32_e32 v3, v3, v11
	s_and_b64 vcc, exec, s[14:15]
	v_mul_f32_e32 v0, v0, v174
	v_mul_f32_e32 v1, v1, v175
	s_cbranch_vccnz .LBB0_483
	v_mul_f32_e32 v23, v4, v22
	v_mul_f32_e32 v22, v5, v22
	v_mul_f32_e32 v10, v4, v20
	v_mul_f32_e32 v11, v5, v20
	v_fma_f32 v4, v4, v20, v22
	v_fma_f32 v5, v5, v20, v23
	v_mul_f32_e32 v17, v0, v16
	v_mul_f32_e32 v16, v1, v16
	v_mul_f32_e32 v4, v7, v19
	v_fma_f32 v20, v6, v18, -v4
	v_fma_f32 v21, v7, v19, -v4
	v_mul_f32_e32 v4, v6, v19
	v_fma_f32 v18, v7, v18, v4
	v_fma_f32 v19, v6, v19, v4
	v_mul_f32_e32 v6, v0, v14
	v_mul_f32_e32 v7, v1, v14
	v_fma_f32 v0, v0, v14, v16
	v_fma_f32 v1, v1, v14, v17
	v_sub_f32_e32 v4, v10, v22
	v_mul_f32_e32 v0, v3, v13
	v_fma_f32 v14, v2, v12, -v0
	v_fma_f32 v15, v3, v13, -v0
	v_mul_f32_e32 v0, v2, v13
	v_fma_f32 v12, v3, v12, v0
	v_fma_f32 v13, v2, v13, v0
	v_sub_f32_e32 v0, v6, v16
	v_mov_b32_e32 v2, v14
	v_mov_b32_e32 v3, v12
	v_mov_b32_e32 v6, v20
	v_mov_b32_e32 v7, v18

; #define LAS __attribute__((address_space(3)))
;     __device__ __forceinline__ bool next(int i, Unit& u) const {
;         const long L = (long)i * G + c; if (L >= nwg) return false;
;         int wgid = (int)L; { const int q = nwg / NXCD, r = nwg % NXCD, xcd = wgid % NXCD, off = wgid / NXCD; wgid = (xcd < r ? xcd * (q + 1) : r * (q + 1) + (xcd - r) * q) + off; }
;         const int nig = WGM * nN, gid = wgid / nig, fm = gid * WGM, gsz = (nM - fm) < WGM ? (nM - fm) : WGM;
;         u.pm = fm + ((wgid % nig) % gsz); u.pn = (wgid % nig) / gsz; u.e = 0; u.t = u.pm; u.cnt = 0x7fffffff; u.i = i; return true;
;     }
;     __device__ __forceinline__ void fill_rstd(LAS float* tab, const float* ssq, float inv_ncol, float scale, int tid) const {
;         Unit u; float v[8];
; #pragma unroll
;         for (int i = 0; i < 8; ++i) { v[i] = 0.f; if (next(i, u)) { const f32x4 ss = *(const f32x4*)(ssq + ((size_t)u.pm * BM + (tid & 255)) * 4); v[i] = __builtin_amdgcn_rsqf(((ss[0] + ss[1]) + (ss[2] + ss[3])) * inv_ncol + EPS) * scale; } }
; #pragma unroll
;         for (int i = 0; i < 8; ++i) if (tid < 256) tab[i * 256 + tid] = v[i];
.LBB0_487:
	s_lshl_b32 s4, s76, 7
	s_mulk_i32 s76, 0x81
	s_and_b64 s[12:13], s[60:61], exec
	s_cselect_b32 s4, s76, s4
	s_add_i32 s4, s4, s75
	s_ashr_i32 s12, s4, 31
	s_lshr_b32 s12, s12, 27
	s_add_i32 s12, s4, s12
	s_ashr_i32 s13, s12, 5
	s_lshl_b32 s13, s13, 3
	s_sub_i32 s14, 0x100, s13
	s_min_i32 s14, s14, 8
	s_abs_i32 s14, s14
	v_cvt_f32_u32_e32 v4, s14
	s_sub_i32 s15, 0, s14
	s_andn2_b32 s12, s12, 31
	s_sub_i32 s4, s4, s12
	v_rcp_iflag_f32_e32 v4, v4
	s_ashr_i32 s12, s4, 31
	s_abs_i32 s4, s4
	v_mul_f32_e32 v4, 0x4f7ffffe, v4
	v_cvt_u32_f32_e32 v4, v4
	s_nop 0
	v_readfirstlane_b32 s24, v4
	s_mul_i32 s15, s15, s24
	s_mul_hi_u32 s15, s24, s15
	s_add_i32 s24, s24, s15
	s_mul_hi_u32 s15, s4, s24
	s_mul_i32 s15, s15, s14
	s_sub_i32 s4, s4, s15
	s_sub_i32 s15, s4, s14
	s_cmp_ge_u32 s4, s14
	s_cselect_b32 s4, s15, s4
	s_sub_i32 s15, s4, s14
	s_cmp_ge_u32 s4, s14
	s_cselect_b32 s4, s15, s4
	s_xor_b32 s4, s4, s12
	s_sub_i32 s4, s4, s12
	s_add_i32 s12, s13, s4
	s_ashr_i32 s13, s12, 31
	s_lshl_b64 s[12:13], s[12:13], 12
	v_lshl_add_u64 v[2:3], v[2:3], 0, s[12:13]
	global_load_dwordx4 v[12:15], v[2:3], off
	s_waitcnt vmcnt(0)
	v_mov_b32_e32 v2, v13
	v_mov_b32_e32 v3, v14
	v_mov_b32_e32 v13, v15
	v_add_f32_e32 v2, v2, v12
	v_add_f32_e32 v3, v3, v13
	s_nop 0
	v_add_f32_e32 v2, v2, v3
	v_mov_b32_e32 v3, 0x358637bd
	v_fmac_f32_e32 v3, 0x3b800000, v2
	v_rsq_f32_e32 v4, v3
	s_and_saveexec_b64 s[12:13], s[8:9]
	s_cbranch_execnz .LBB0_419
	s_branch .LBB0_420

; __device__ __forceinline__ int lane_id_v() { int l; asm volatile("v_mbcnt_lo_u32_b32 %0, -1, 0\n\tv_mbcnt_hi_u32_b32 %0, -1, %0" : "=v"(l)); return l; }
; __device__ __forceinline__ u32x4 pack8(f32x4 v0, f32x4 v1) { u32x4 w; w.x = cvt_pk_bf16(v0[0], v0[1]); w.y = cvt_pk_bf16(v0[2], v0[3]); w.z = cvt_pk_bf16(v1[0], v1[1]); w.w = cvt_pk_bf16(v1[2], v1[3]); return w; }
; #define EPI_PIN8(a) asm volatile("" : "+v"(a[0][0]), "+v"(a[0][1]), "+v"(a[0][2]), "+v"(a[0][3]), "+v"(a[1][0]), "+v"(a[1][1]), "+v"(a[1][2]), "+v"(a[1][3]) :: "memory")
;     __device__ __forceinline__ int operator()(AccT acc, const Unit& u, int wr, int wc, int, int) const {
;         const int lane_ = lane_id_v(), fr = lane_ & 15, fq = lane_ >> 4;
;         const int row0 = u.pm * BM + wr * 64 + fr, cw = wc * 32 + 8 * fq, h = u.pn;
;         float rs[2][4];
; #pragma unroll
;         for (int ai = 0; ai < 2; ++ai)
; #pragma unroll
;             for (int m = 0; m < 4; ++m) { const int r = row0 + ai * HALF + m * 16;
;                 rs[ai][m] = rtab[u.i * 256 + wr * 64 + fr + ai * HALF + m * 16]; (void)r; }
;         EPI_PIN8(rs);
; #pragma unroll
;         for (int ai = 0; ai < 2; ++ai)
; #pragma unroll
;             for (int m = 0; m < 4; ++m) { const int r = row0 + ai * HALF + m * 16; const float rstd = rs[ai][m];
;                 *(u32x4*)(KA + (size_t)r * 768 + h * 192 + cw) = pack8(acc[ai][0][m][0] * rstd, acc[ai][0][m][1] * rstd);
;                 *(u32x4*)(VA + (size_t)r * 512 + h * 128 + cw) = pack8(acc[ai][1][m][0] * rstd, acc[ai][1][m][1] * rstd); }
;         return 16;
.LBB0_506:
	s_lshl_b32 s25, s35, 10
	v_mbcnt_lo_u32_b32 v140, -1, 0
	v_mbcnt_hi_u32_b32 v140, -1, v140
	s_add_i32 s25, s60, s25
	v_and_b32_e32 v142, 15, v140
	v_lshl_add_u32 v143, v142, 2, s25
	ds_read2_b32 v[148:149], v143 offset0:128 offset1:144
	ds_read2_b32 v[152:153], v143 offset1:16
	ds_read2_b32 v[144:145], v143 offset0:160 offset1:176
	ds_read2_b32 v[154:155], v143 offset0:32 offset1:48
	v_ashrrev_i32_e32 v140, 1, v140
	v_and_b32_e32 v140, -8, v140
	v_add_u32_e32 v156, s0, v140
	s_waitcnt lgkmcnt(0)
	v_mov_b32_e32 v146, v149
	v_mov_b32_e32 v140, v145
	v_or_b32_e32 v142, s1, v142
	v_lshl_add_u32 v142, s34, 8, v142
	s_mul_i32 s34, s74, 0xc0
	v_mul_f32_e32 v126, v126, v152
	v_mul_f32_e32 v127, v127, v152
	v_mul_f32_e32 v124, v124, v152
	v_mul_f32_e32 v125, v125, v152
	v_mul_f32_e32 v122, v122, v152
	v_mul_f32_e32 v123, v123, v152
	s_ashr_i32 s35, s34, 31
	v_mul_f32_e32 v120, v120, v152
	v_mul_f32_e32 v121, v121, v152
	v_cvt_pk_bf16_f32 v124, v124, v125
	v_cvt_pk_bf16_f32 v125, v126, v127
	v_ashrrev_i32_e32 v157, 31, v156
	v_cvt_pk_bf16_f32 v126, v120, v121
	v_cvt_pk_bf16_f32 v127, v122, v123
	v_mov_b64_e32 v[122:123], s[12:13]
	v_mad_i64_i32 v[120:121], s[38:39], v142, s68, v[122:123]
	s_lshl_b64 s[34:35], s[34:35], 1
	v_lshl_add_u64 v[158:159], v[120:121], 0, s[34:35]
	v_lshlrev_b64 v[120:121], 1, v[156:157]
	s_lshl_b32 s36, s74, 7
	v_ashrrev_i32_e32 v143, 31, v142
	v_lshl_add_u64 v[156:157], v[158:159], 0, v[120:121]
	v_mul_f32_e32 v116, v116, v152
	v_mul_f32_e32 v117, v117, v152
	s_ashr_i32 s37, s36, 31
	global_store_dwordx4 v[156:157], v[124:127], off
	s_lshl_b64 s[36:37], s[36:37], 1
	v_mul_f32_e32 v118, v118, v152
	v_mul_f32_e32 v119, v119, v152
	v_mul_f32_e32 v124, v114, v152
	v_mul_f32_e32 v125, v115, v152
	v_mul_f32_e32 v114, v112, v152
	v_mul_f32_e32 v115, v113, v152
	v_cvt_pk_bf16_f32 v112, v116, v117
	v_lshlrev_b64 v[116:117], 10, v[142:143]
	v_lshl_add_u64 v[116:117], s[14:15], 0, v[116:117]
	v_lshl_add_u64 v[116:117], v[116:117], 0, s[36:37]
	v_cvt_pk_bf16_f32 v113, v118, v119
	v_cvt_pk_bf16_f32 v114, v114, v115
	v_lshl_add_u64 v[116:117], v[116:117], 0, v[120:121]
	v_cvt_pk_bf16_f32 v115, v124, v125
	global_store_dwordx4 v[116:117], v[112:115], off
	v_mul_f32_e32 v92, v92, v154
	v_mul_f32_e32 v93, v93, v154
	v_mul_f32_e32 v94, v94, v154
	v_mul_f32_e32 v95, v95, v154
	v_mov_b32_e32 v114, v153
	v_or_b32_e32 v112, 16, v142
	v_mul_f32_e32 v108, v108, v114
	v_mul_f32_e32 v109, v109, v114
	v_mul_f32_e32 v116, v106, v114
	v_mul_f32_e32 v117, v107, v114
	v_mul_f32_e32 v106, v104, v114
	v_mul_f32_e32 v107, v105, v114
	v_cvt_pk_bf16_f32 v104, v108, v109
	v_mad_i64_i32 v[108:109], s[38:39], v112, s68, v[122:123]
	v_lshl_add_u64 v[108:109], v[108:109], 0, s[34:35]
	v_mul_f32_e32 v110, v110, v114
	v_mul_f32_e32 v111, v111, v114
	v_ashrrev_i32_e32 v113, 31, v112
	v_cvt_pk_bf16_f32 v105, v110, v111
	v_lshl_add_u64 v[108:109], v[108:109], 0, v[120:121]
	v_mul_f32_e32 v100, v100, v114
	v_mul_f32_e32 v101, v101, v114
	v_cvt_pk_bf16_f32 v106, v106, v107
	v_cvt_pk_bf16_f32 v107, v116, v117
	global_store_dwordx4 v[108:109], v[104:107], off
	v_mul_f32_e32 v102, v102, v114
	v_mul_f32_e32 v103, v103, v114
	v_mul_f32_e32 v84, v84, v154
	v_mul_f32_e32 v85, v85, v154
	v_mul_f32_e32 v104, v98, v114
	v_mul_f32_e32 v105, v99, v114
	v_mul_f32_e32 v98, v96, v114
	v_mul_f32_e32 v99, v97, v114
	v_cvt_pk_bf16_f32 v96, v100, v101
	v_lshlrev_b64 v[100:101], 10, v[112:113]
	v_lshl_add_u64 v[100:101], s[14:15], 0, v[100:101]
	v_lshl_add_u64 v[100:101], v[100:101], 0, s[36:37]
	v_lshl_add_u64 v[100:101], v[100:101], 0, v[120:121]
	v_cvt_pk_bf16_f32 v97, v102, v103
	v_cvt_pk_bf16_f32 v98, v98, v99
	v_cvt_pk_bf16_f32 v99, v104, v105
	global_store_dwordx4 v[100:101], v[96:99], off
	v_mul_f32_e32 v86, v86, v154
	v_mul_f32_e32 v87, v87, v154
	v_mul_f32_e32 v60, v60, v148
	v_mul_f32_e32 v61, v61, v148
	v_or_b32_e32 v96, 32, v142
	v_mul_f32_e32 v98, v90, v154
	v_mul_f32_e32 v99, v91, v154
	v_mul_f32_e32 v90, v88, v154
	v_mul_f32_e32 v91, v89, v154
	v_cvt_pk_bf16_f32 v88, v92, v93
	v_mad_i64_i32 v[92:93], s[38:39], v96, s68, v[122:123]
	v_lshl_add_u64 v[92:93], v[92:93], 0, s[34:35]
	v_cvt_pk_bf16_f32 v89, v94, v95
	v_ashrrev_i32_e32 v97, 31, v96
	v_lshl_add_u64 v[92:93], v[92:93], 0, v[120:121]
	v_cvt_pk_bf16_f32 v90, v90, v91
	v_cvt_pk_bf16_f32 v91, v98, v99
	global_store_dwordx4 v[92:93], v[88:91], off
	v_mul_f32_e32 v62, v62, v148
	v_mul_f32_e32 v63, v63, v148
	v_mul_f32_e32 v52, v52, v148
	v_mul_f32_e32 v53, v53, v148
	v_mul_f32_e32 v88, v82, v154
	v_mul_f32_e32 v89, v83, v154
	v_mul_f32_e32 v82, v80, v154
	v_mul_f32_e32 v83, v81, v154
	v_cvt_pk_bf16_f32 v80, v84, v85
	v_lshlrev_b64 v[84:85], 10, v[96:97]
	v_lshl_add_u64 v[84:85], s[14:15], 0, v[84:85]
	v_lshl_add_u64 v[84:85], v[84:85], 0, s[36:37]
	v_cvt_pk_bf16_f32 v81, v86, v87
	v_cvt_pk_bf16_f32 v82, v82, v83
	v_lshl_add_u64 v[84:85], v[84:85], 0, v[120:121]
	v_cvt_pk_bf16_f32 v83, v88, v89
	global_store_dwordx4 v[84:85], v[80:83], off
	v_mul_f32_e32 v54, v54, v148
	v_mul_f32_e32 v55, v55, v148
	v_mul_f32_e32 v44, v44, v146
	v_mul_f32_e32 v45, v45, v146
	v_mov_b32_e32 v82, v155
	v_or_b32_e32 v80, 48, v142
	v_mul_f32_e32 v76, v76, v82
	v_mul_f32_e32 v77, v77, v82
	v_mul_f32_e32 v84, v74, v82
	v_mul_f32_e32 v85, v75, v82
	v_mul_f32_e32 v74, v72, v82
	v_mul_f32_e32 v75, v73, v82
	v_cvt_pk_bf16_f32 v72, v76, v77
	v_mad_i64_i32 v[76:77], s[38:39], v80, s68, v[122:123]
	v_lshl_add_u64 v[76:77], v[76:77], 0, s[34:35]
	v_mul_f32_e32 v78, v78, v82
	v_mul_f32_e32 v79, v79, v82
	v_ashrrev_i32_e32 v81, 31, v80
	v_cvt_pk_bf16_f32 v73, v78, v79
; #define PG8_BAR __builtin_amdgcn_s_barrier()
; __device__ __forceinline__ u32x4 pack8(f32x4 v0, f32x4 v1) { u32x4 w; w.x = cvt_pk_bf16(v0[0], v0[1]); w.y = cvt_pk_bf16(v0[2], v0[3]); w.z = cvt_pk_bf16(v1[0], v1[1]); w.w = cvt_pk_bf16(v1[2], v1[3]); return w; }
; template <class Epi, class Sched, bool GATHER>
; __device__ __forceinline__ void gemm_phase(LAS unsigned char* lds, const int wid, const bf16_t* A, int lda, const bf16_t* Bt, int ldb, size_t b_estride, int K, const Sched& S, const Epi& E) {
;     ...
;         cur = nxt; cA = nA; cB = nB; ++ui;
;         if constexpr (GATHER) {
; #pragma unroll
;             for (int i = 0; i < 2; ++i) { gc0[i] = gn0[i]; gc1[i] = gn1[i]; }
;         }
;         if (wr == 1) PG8_BAR;
;     }
;     __device__ __forceinline__ int operator()(AccT acc, const Unit& u, int wr, int wc, int, int) const {
;     ...
;         for (int ai = 0; ai < 2; ++ai)
; #pragma unroll
;             for (int m = 0; m < 4; ++m) { const int r = row0 + ai * HALF + m * 16; const float rstd = rs[ai][m];
;                 *(u32x4*)(KA + (size_t)r * 768 + h * 192 + cw) = pack8(acc[ai][0][m][0] * rstd, acc[ai][0][m][1] * rstd);
;                 *(u32x4*)(VA + (size_t)r * 512 + h * 128 + cw) = pack8(acc[ai][1][m][0] * rstd, acc[ai][1][m][1] * rstd); }
;         return 16;
	v_lshl_add_u64 v[76:77], v[76:77], 0, v[120:121]
	v_mul_f32_e32 v68, v68, v82
	v_mul_f32_e32 v69, v69, v82
	v_cvt_pk_bf16_f32 v74, v74, v75
	v_cvt_pk_bf16_f32 v75, v84, v85
	global_store_dwordx4 v[76:77], v[72:75], off
	v_mul_f32_e32 v70, v70, v82
	v_mul_f32_e32 v71, v71, v82
	v_mul_f32_e32 v46, v46, v146
	v_mul_f32_e32 v47, v47, v146
	v_mul_f32_e32 v72, v66, v82
	v_mul_f32_e32 v73, v67, v82
	v_mul_f32_e32 v66, v64, v82
	v_mul_f32_e32 v67, v65, v82
	v_cvt_pk_bf16_f32 v64, v68, v69
	v_lshlrev_b64 v[68:69], 10, v[80:81]
	v_lshl_add_u64 v[68:69], s[14:15], 0, v[68:69]
	v_lshl_add_u64 v[68:69], v[68:69], 0, s[36:37]
	v_lshl_add_u64 v[68:69], v[68:69], 0, v[120:121]
	v_cvt_pk_bf16_f32 v65, v70, v71
	v_cvt_pk_bf16_f32 v66, v66, v67
	v_cvt_pk_bf16_f32 v67, v72, v73
	global_store_dwordx4 v[68:69], v[64:67], off
	v_mul_f32_e32 v36, v36, v146
	v_mul_f32_e32 v37, v37, v146
	v_mul_f32_e32 v38, v38, v146
	v_mul_f32_e32 v39, v39, v146
	v_add_u32_e32 v64, 0x80, v142
	v_mul_f32_e32 v66, v58, v148
	v_mul_f32_e32 v67, v59, v148
	v_mul_f32_e32 v58, v56, v148
	v_mul_f32_e32 v59, v57, v148
	v_cvt_pk_bf16_f32 v56, v60, v61
	v_mad_i64_i32 v[60:61], s[38:39], v64, s68, v[122:123]
	v_lshl_add_u64 v[60:61], v[60:61], 0, s[34:35]
	v_cvt_pk_bf16_f32 v57, v62, v63
	v_ashrrev_i32_e32 v65, 31, v64
	v_lshl_add_u64 v[60:61], v[60:61], 0, v[120:121]
	v_cvt_pk_bf16_f32 v58, v58, v59
	v_cvt_pk_bf16_f32 v59, v66, v67
	global_store_dwordx4 v[60:61], v[56:59], off
	v_mul_f32_e32 v28, v28, v144
	v_mul_f32_e32 v29, v29, v144
	v_mul_f32_e32 v30, v30, v144
	v_mul_f32_e32 v31, v31, v144
	v_mul_f32_e32 v56, v50, v148
	v_mul_f32_e32 v57, v51, v148
	v_mul_f32_e32 v50, v48, v148
	v_mul_f32_e32 v51, v49, v148
	v_cvt_pk_bf16_f32 v48, v52, v53
	v_lshlrev_b64 v[52:53], 10, v[64:65]
	v_lshl_add_u64 v[52:53], s[14:15], 0, v[52:53]
	v_lshl_add_u64 v[52:53], v[52:53], 0, s[36:37]
	v_lshl_add_u64 v[52:53], v[52:53], 0, v[120:121]
	v_cvt_pk_bf16_f32 v49, v54, v55
	v_cvt_pk_bf16_f32 v50, v50, v51
	v_cvt_pk_bf16_f32 v51, v56, v57
	global_store_dwordx4 v[52:53], v[48:51], off
	v_mul_f32_e32 v20, v20, v144
	v_mul_f32_e32 v21, v21, v144
	v_mul_f32_e32 v22, v22, v144
	v_mul_f32_e32 v23, v23, v144
	v_add_u32_e32 v48, 0x90, v142
	v_mul_f32_e32 v50, v42, v146
	v_mul_f32_e32 v51, v43, v146
	v_mul_f32_e32 v42, v40, v146
	v_mul_f32_e32 v43, v41, v146
	v_cvt_pk_bf16_f32 v40, v44, v45
	v_mad_i64_i32 v[44:45], s[38:39], v48, s68, v[122:123]
	v_lshl_add_u64 v[44:45], v[44:45], 0, s[34:35]
	v_cvt_pk_bf16_f32 v41, v46, v47
	v_ashrrev_i32_e32 v49, 31, v48
	v_lshl_add_u64 v[44:45], v[44:45], 0, v[120:121]
	v_cvt_pk_bf16_f32 v42, v42, v43
	v_cvt_pk_bf16_f32 v43, v50, v51
	global_store_dwordx4 v[44:45], v[40:43], off
	v_mul_f32_e32 v12, v12, v140
	v_mul_f32_e32 v13, v13, v140
	v_mul_f32_e32 v14, v14, v140
	v_mul_f32_e32 v15, v15, v140
	v_mul_f32_e32 v40, v34, v146
	v_mul_f32_e32 v41, v35, v146
	v_mul_f32_e32 v34, v32, v146
	v_mul_f32_e32 v35, v33, v146
	v_cvt_pk_bf16_f32 v32, v36, v37
	v_lshlrev_b64 v[36:37], 10, v[48:49]
	v_lshl_add_u64 v[36:37], s[14:15], 0, v[36:37]
	v_lshl_add_u64 v[36:37], v[36:37], 0, s[36:37]
	v_lshl_add_u64 v[36:37], v[36:37], 0, v[120:121]
	v_cvt_pk_bf16_f32 v33, v38, v39
	v_cvt_pk_bf16_f32 v34, v34, v35
	v_cvt_pk_bf16_f32 v35, v40, v41
	global_store_dwordx4 v[36:37], v[32:35], off
	v_mul_f32_e32 v4, v4, v140
	v_mul_f32_e32 v5, v5, v140
	s_andn2_b64 vcc, exec, s[10:11]
	v_add_u32_e32 v32, 0xa0, v142
	v_mul_f32_e32 v34, v26, v144
	v_mul_f32_e32 v35, v27, v144
	v_mul_f32_e32 v26, v24, v144
	v_mul_f32_e32 v27, v25, v144
	v_cvt_pk_bf16_f32 v24, v28, v29
	v_mad_i64_i32 v[28:29], s[38:39], v32, s68, v[122:123]
	v_lshl_add_u64 v[28:29], v[28:29], 0, s[34:35]
	v_cvt_pk_bf16_f32 v25, v30, v31
	v_ashrrev_i32_e32 v33, 31, v32
	v_lshl_add_u64 v[28:29], v[28:29], 0, v[120:121]
	v_cvt_pk_bf16_f32 v26, v26, v27
	v_cvt_pk_bf16_f32 v27, v34, v35
	global_store_dwordx4 v[28:29], v[24:27], off
	s_mov_b64 s[10:11], -1
	v_mul_f32_e32 v6, v6, v140
	v_mul_f32_e32 v7, v7, v140
	v_mul_f32_e32 v24, v18, v144
	v_mul_f32_e32 v25, v19, v144
	v_mul_f32_e32 v18, v16, v144
	v_mul_f32_e32 v19, v17, v144
	v_cvt_pk_bf16_f32 v16, v20, v21
	v_lshlrev_b64 v[20:21], 10, v[32:33]
	v_lshl_add_u64 v[20:21], s[14:15], 0, v[20:21]
	v_lshl_add_u64 v[20:21], v[20:21], 0, s[36:37]
	v_lshl_add_u64 v[20:21], v[20:21], 0, v[120:121]
	v_cvt_pk_bf16_f32 v17, v22, v23
	v_cvt_pk_bf16_f32 v18, v18, v19
	v_cvt_pk_bf16_f32 v19, v24, v25
	global_store_dwordx4 v[20:21], v[16:19], off
	s_nop 1
	v_add_u32_e32 v16, 0xb0, v142
	v_mul_f32_e32 v18, v10, v140
	v_mul_f32_e32 v19, v11, v140
	v_mul_f32_e32 v10, v8, v140
	v_mul_f32_e32 v11, v9, v140
	v_cvt_pk_bf16_f32 v8, v12, v13
	v_mad_i64_i32 v[12:13], s[38:39], v16, s68, v[122:123]
	v_lshl_add_u64 v[12:13], v[12:13], 0, s[34:35]
	v_cvt_pk_bf16_f32 v9, v14, v15
	v_ashrrev_i32_e32 v17, 31, v16
	v_lshl_add_u64 v[12:13], v[12:13], 0, v[120:121]
	v_cvt_pk_bf16_f32 v10, v10, v11
	v_cvt_pk_bf16_f32 v11, v18, v19
	global_store_dwordx4 v[12:13], v[8:11], off
	s_nop 1
	v_mul_f32_e32 v8, v2, v140
	v_mul_f32_e32 v9, v3, v140
	v_mul_f32_e32 v2, v0, v140
	v_mul_f32_e32 v3, v1, v140
	v_cvt_pk_bf16_f32 v0, v4, v5
	v_lshlrev_b64 v[4:5], 10, v[16:17]
	v_lshl_add_u64 v[4:5], s[14:15], 0, v[4:5]
	v_lshl_add_u64 v[4:5], v[4:5], 0, s[36:37]
	v_lshl_add_u64 v[4:5], v[4:5], 0, v[120:121]
	v_cvt_pk_bf16_f32 v1, v6, v7
	v_cvt_pk_bf16_f32 v2, v2, v3
	v_cvt_pk_bf16_f32 v3, v8, v9
	global_store_dwordx4 v[4:5], v[0:3], off
	s_cbranch_vccnz .LBB0_494
	s_and_b64 vcc, exec, s[6:7]
	s_cbranch_vccnz .LBB0_493
	s_barrier
	s_branch .LBB0_493

; __device__ __forceinline__ int lane_id_v() { int l; asm volatile("v_mbcnt_lo_u32_b32 %0, -1, 0\n\tv_mbcnt_hi_u32_b32 %0, -1, %0" : "=v"(l)); return l; }
; #define EPI_MEMBAR() asm volatile("" ::: "memory")
; #define X1_LD(k) do { const size_t off_ = X1_OFF(k); _Pragma("unroll") for (int bj = 0; bj < 2; ++bj) _Pragma("unroll") for (int n = 0; n < 2; ++n) xb[(k) % 3][bj][n] = *(const f32x4*)(x + off_ + bj * HALF + n * 16); } while (0)
; #define X1_ST(k) do { const size_t off_ = X1_OFF(k); _Pragma("unroll") for (int bj = 0; bj < 2; ++bj) _Pragma("unroll") for (int n = 0; n < 2; ++n) \
;             *(f32x4*)(x1 + off_ + bj * HALF + n * 16) = xb[(k) % 3][bj][n] + g[bj][n] * acc[(k) >> 2][bj][(k) & 3][n]; } while (0)
;     __device__ __forceinline__ int operator()(AccT acc, const Unit& u, int wr, int wc, int, int) const {
;         const int lane_ = lane_id_v(), fr = lane_ & 15, fq = lane_ >> 4;
;         const int row0 = u.pm * BM + wr * 64 + fr, col0 = u.pn * BM + wc * 32 + 4 * fq, b = u.pm >> 5;
;         f32x4 g[2][2];
; #pragma unroll
;         for (int bj = 0; bj < 2; ++bj)
; #pragma unroll
;             for (int n = 0; n < 2; ++n) g[bj][n] = *(const f32x4*)(mod + (size_t)(b * 6 + 2) * DM + col0 + bj * HALF + n * 16);
;         f32x4 xb[3][2][2];
;     ...
;         X1_LD(0); X1_LD(1); EPI_MEMBAR();
; #pragma unroll
;         for (int k = 0; k < 8; ++k) { if (k + 2 < 8) X1_LD(k + 2); EPI_MEMBAR(); X1_ST(k); EPI_MEMBAR(); }
.LBB0_778:
	v_mbcnt_lo_u32_b32 v154, -1, 0
	v_mbcnt_hi_u32_b32 v154, -1, v154
	s_lshl_b32 s25, s66, 8
	v_ashrrev_i32_e32 v128, 2, v154
	s_or_b32 s25, s25, s0
	v_and_b32_e32 v128, -4, v128
	v_add_u32_e32 v128, s25, v128
	s_ashr_i32 s25, s30, 5
	s_mul_i32 s34, s25, 6
	s_lshl_b32 s23, s30, 8
	s_ashr_i32 s35, s34, 31
	s_add_i32 s23, s23, s1
	s_lshl_b64 s[34:35], s[34:35], 12
	s_add_u32 s34, s51, s34
	v_ashrrev_i32_e32 v129, 31, v128
	v_and_or_b32 v154, v154, 15, s23
	s_addc_u32 s35, s52, s35
	v_lshlrev_b64 v[152:153], 2, v[128:129]
	v_ashrrev_i32_e32 v155, 31, v154
	v_lshl_add_u64 v[128:129], s[34:35], 0, v[152:153]
	v_lshlrev_b64 v[196:197], 12, v[154:155]
	v_lshl_add_u64 v[130:131], v[128:129], 0, s[18:19]
	v_add_co_u32_e32 v128, vcc, s47, v128
	v_lshl_add_u64 v[156:157], s[10:11], 0, v[196:197]
	s_nop 0
	v_addc_co_u32_e32 v129, vcc, 0, v129, vcc
	v_lshl_add_u64 v[156:157], v[156:157], 0, v[152:153]
	global_load_dwordx4 v[136:139], v[130:131], off offset:64
	global_load_dwordx4 v[132:135], v[130:131], off offset:512
	global_load_dwordx4 v[140:143], v[128:129], off
	s_nop 0
	global_load_dwordx4 v[128:131], v[130:131], off offset:576
	s_nop 0
	global_load_dwordx4 v[164:167], v[156:157], off
	global_load_dwordx4 v[168:171], v[156:157], off offset:64
	global_load_dwordx4 v[172:175], v[156:157], off offset:512
	global_load_dwordx4 v[176:179], v[156:157], off offset:576
	v_or_b32_e32 v156, 16, v154
	v_ashrrev_i32_e32 v157, 31, v156
	v_lshlrev_b64 v[200:201], 12, v[156:157]
	v_lshl_add_u64 v[156:157], s[10:11], 0, v[200:201]
	v_lshl_add_u64 v[156:157], v[156:157], 0, v[152:153]
	global_load_dwordx4 v[180:183], v[156:157], off
	global_load_dwordx4 v[184:187], v[156:157], off offset:64
	global_load_dwordx4 v[188:191], v[156:157], off offset:512
	global_load_dwordx4 v[192:195], v[156:157], off offset:576
	v_or_b32_e32 v156, 32, v154
	v_or_b32_e32 v158, 48, v154
	v_ashrrev_i32_e32 v157, 31, v156
	v_ashrrev_i32_e32 v159, 31, v158
	v_lshlrev_b64 v[156:157], 12, v[156:157]
	v_lshl_add_u64 v[202:203], s[12:13], 0, v[196:197]
	v_lshlrev_b64 v[158:159], 12, v[158:159]
	v_lshl_add_u64 v[196:197], v[196:197], 0, s[20:21]
	v_lshl_add_u64 v[204:205], s[10:11], 0, v[156:157]
	v_lshl_add_u64 v[216:217], v[202:203], 0, v[152:153]
	v_lshl_add_u64 v[202:203], s[10:11], 0, v[158:159]
	v_lshl_add_u64 v[200:201], s[12:13], 0, v[200:201]
	v_lshl_add_u64 v[206:207], s[10:11], 0, v[196:197]
	v_lshl_add_u64 v[212:213], v[204:205], 0, v[152:153]
	v_lshl_add_u64 v[218:219], v[202:203], 0, v[152:153]
	v_lshl_add_u64 v[220:221], v[200:201], 0, v[152:153]
	v_lshl_add_u64 v[222:223], v[206:207], 0, v[152:153]
	global_load_dwordx4 v[200:203], v[212:213], off
	global_load_dwordx4 v[204:207], v[212:213], off offset:64
	global_load_dwordx4 v[208:211], v[212:213], off offset:512
	s_nop 0
	global_load_dwordx4 v[212:215], v[212:213], off offset:576
	v_lshl_add_u64 v[156:157], s[12:13], 0, v[156:157]
	v_lshl_add_u64 v[156:157], v[156:157], 0, v[152:153]
	v_lshl_add_u64 v[158:159], s[12:13], 0, v[158:159]
	v_lshl_add_u64 v[158:159], v[158:159], 0, v[152:153]
	s_andn2_b64 vcc, exec, s[8:9]
	s_mov_b64 s[8:9], -1
	s_waitcnt vmcnt(0)
	v_fma_f32 v122, v122, v138, v170
	v_fma_f32 v123, v123, v139, v171
	v_fma_f32 v126, v126, v142, v166
	v_fma_f32 v127, v127, v143, v167
	v_fma_f32 v124, v124, v140, v164
	v_fma_f32 v125, v125, v141, v165
	v_fma_f32 v120, v120, v136, v168
	v_fma_f32 v121, v121, v137, v169
	v_fma_f32 v110, v110, v134, v174
	v_fma_f32 v111, v111, v135, v175
	v_fma_f32 v108, v108, v132, v172
	v_fma_f32 v109, v109, v133, v173
	v_fma_f32 v106, v106, v130, v178
	v_fma_f32 v107, v107, v131, v179
	v_fma_f32 v104, v104, v128, v176
	v_fma_f32 v105, v105, v129, v177
	global_store_dwordx4 v[216:217], v[124:127], off
	global_store_dwordx4 v[216:217], v[120:123], off offset:64
	global_store_dwordx4 v[216:217], v[108:111], off offset:512
	global_store_dwordx4 v[216:217], v[104:107], off offset:576
	global_load_dwordx4 v[104:107], v[218:219], off
	global_load_dwordx4 v[108:111], v[218:219], off offset:64
	v_fma_f32 v118, v118, v142, v182
	v_fma_f32 v119, v119, v143, v183
	v_fma_f32 v116, v116, v140, v180
	v_fma_f32 v117, v117, v141, v181
	global_load_dwordx4 v[120:123], v[218:219], off offset:512
	global_load_dwordx4 v[124:127], v[218:219], off offset:576
	v_fma_f32 v114, v114, v138, v186
	v_fma_f32 v115, v115, v139, v187
	v_fma_f32 v112, v112, v136, v184
	v_fma_f32 v113, v113, v137, v185
	v_fma_f32 v102, v102, v134, v190
	v_fma_f32 v103, v103, v135, v191
	v_fma_f32 v100, v100, v132, v188
	v_fma_f32 v101, v101, v133, v189
	v_fma_f32 v98, v98, v130, v194
	v_fma_f32 v99, v99, v131, v195
	v_fma_f32 v96, v96, v128, v192
	v_fma_f32 v97, v97, v129, v193
	global_store_dwordx4 v[220:221], v[116:119], off
	global_store_dwordx4 v[220:221], v[112:115], off offset:64
	global_store_dwordx4 v[220:221], v[100:103], off offset:512
	global_store_dwordx4 v[220:221], v[96:99], off offset:576
	global_load_dwordx4 v[96:99], v[222:223], off
	global_load_dwordx4 v[100:103], v[222:223], off offset:64
	global_load_dwordx4 v[112:115], v[222:223], off offset:512
	global_load_dwordx4 v[116:119], v[222:223], off offset:576
	v_add_u32_e32 v164, 0x90, v154
	v_ashrrev_i32_e32 v165, 31, v164
	v_add_u32_e32 v166, 0xa0, v154
	v_lshlrev_b64 v[164:165], 12, v[164:165]
	v_fma_f32 v94, v94, v142, v202
	v_fma_f32 v95, v95, v143, v203
	v_fma_f32 v92, v92, v140, v200
	v_fma_f32 v93, v93, v141, v201
	v_ashrrev_i32_e32 v167, 31, v166
	v_lshl_add_u64 v[168:169], s[10:11], 0, v[164:165]
	v_fma_f32 v90, v90, v138, v206
	v_fma_f32 v91, v91, v139, v207
	v_fma_f32 v88, v88, v136, v204
	v_fma_f32 v89, v89, v137, v205
	v_fma_f32 v78, v78, v134, v210
	v_fma_f32 v79, v79, v135, v211
	v_fma_f32 v76, v76, v132, v208
	v_fma_f32 v77, v77, v133, v209
	v_fma_f32 v74, v74, v130, v214
	v_fma_f32 v75, v75, v131, v215
	v_fma_f32 v72, v72, v128, v212
	v_fma_f32 v73, v73, v129, v213
	global_store_dwordx4 v[156:157], v[92:95], off
	global_store_dwordx4 v[156:157], v[88:91], off offset:64
	global_store_dwordx4 v[156:157], v[76:79], off offset:512
	global_store_dwordx4 v[156:157], v[72:75], off offset:576
	v_lshlrev_b64 v[166:167], 12, v[166:167]
	v_lshl_add_u64 v[168:169], v[168:169], 0, v[152:153]
	v_add_u32_e32 v154, 0xb0, v154
	v_lshl_add_u64 v[170:171], s[10:11], 0, v[166:167]
	global_load_dwordx4 v[72:75], v[168:169], off
	global_load_dwordx4 v[76:79], v[168:169], off offset:64
	global_load_dwordx4 v[88:91], v[168:169], off offset:512
	global_load_dwordx4 v[92:95], v[168:169], off offset:576
	v_ashrrev_i32_e32 v155, 31, v154
	v_lshl_add_u64 v[172:173], s[12:13], 0, v[196:197]
	v_lshl_add_u64 v[170:171], v[170:171], 0, v[152:153]
	v_lshlrev_b64 v[154:155], 12, v[154:155]
	v_lshl_add_u64 v[172:173], v[172:173], 0, v[152:153]
	v_lshl_add_u64 v[174:175], s[10:11], 0, v[154:155]
	v_lshl_add_u64 v[174:175], v[174:175], 0, v[152:153]
	s_waitcnt vmcnt(0)
; #define PG8_BAR __builtin_amdgcn_s_barrier()
; #define EPI_MEMBAR() asm volatile("" ::: "memory")
; #define X1_LD(k) do { const size_t off_ = X1_OFF(k); _Pragma("unroll") for (int bj = 0; bj < 2; ++bj) _Pragma("unroll") for (int n = 0; n < 2; ++n) xb[(k) % 3][bj][n] = *(const f32x4*)(x + off_ + bj * HALF + n * 16); } while (0)
; #define X1_ST(k) do { const size_t off_ = X1_OFF(k); _Pragma("unroll") for (int bj = 0; bj < 2; ++bj) _Pragma("unroll") for (int n = 0; n < 2; ++n) \
;             *(f32x4*)(x1 + off_ + bj * HALF + n * 16) = xb[(k) % 3][bj][n] + g[bj][n] * acc[(k) >> 2][bj][(k) & 3][n]; } while (0)
; template <class Epi, class Sched, bool GATHER>
; __device__ __forceinline__ void gemm_phase(LAS unsigned char* lds, const int wid, const bf16_t* A, int lda, const bf16_t* Bt, int ldb, size_t b_estride, int K, const Sched& S, const Epi& E) {
;     ...
;         cur = nxt; cA = nA; cB = nB; ++ui;
;         if constexpr (GATHER) {
; #pragma unroll
;             for (int i = 0; i < 2; ++i) { gc0[i] = gn0[i]; gc1[i] = gn1[i]; }
;         }
;         if (wr == 1) PG8_BAR;
;     }
;     __device__ __forceinline__ int operator()(AccT acc, const Unit& u, int wr, int wc, int, int) const {
;     ...
;         X1_LD(0); X1_LD(1); EPI_MEMBAR();
; #pragma unroll
;         for (int k = 0; k < 8; ++k) { if (k + 2 < 8) X1_LD(k + 2); EPI_MEMBAR(); X1_ST(k); EPI_MEMBAR(); }
	v_fma_f32 v86, v86, v142, v106
	v_fma_f32 v87, v87, v143, v107
	v_fma_f32 v84, v84, v140, v104
	v_fma_f32 v85, v85, v141, v105
	v_fma_f32 v82, v82, v138, v110
	v_fma_f32 v83, v83, v139, v111
	v_fma_f32 v80, v80, v136, v108
	v_fma_f32 v81, v81, v137, v109
	v_fma_f32 v70, v70, v134, v122
	v_fma_f32 v71, v71, v135, v123
	v_fma_f32 v68, v68, v132, v120
	v_fma_f32 v69, v69, v133, v121
	v_fma_f32 v66, v66, v130, v126
	v_fma_f32 v67, v67, v131, v127
	v_fma_f32 v64, v64, v128, v124
	v_fma_f32 v65, v65, v129, v125
	global_store_dwordx4 v[158:159], v[84:87], off
	global_store_dwordx4 v[158:159], v[80:83], off offset:64
	global_store_dwordx4 v[158:159], v[68:71], off offset:512
	global_store_dwordx4 v[158:159], v[64:67], off offset:576
	global_load_dwordx4 v[64:67], v[170:171], off
	global_load_dwordx4 v[68:71], v[170:171], off offset:64
	v_fma_f32 v62, v62, v142, v98
	v_fma_f32 v63, v63, v143, v99
	v_fma_f32 v60, v60, v140, v96
	v_fma_f32 v61, v61, v141, v97
	v_fma_f32 v58, v58, v138, v102
	v_fma_f32 v59, v59, v139, v103
	v_fma_f32 v56, v56, v136, v100
	v_fma_f32 v57, v57, v137, v101
	v_fma_f32 v54, v54, v134, v114
	v_fma_f32 v55, v55, v135, v115
	v_fma_f32 v52, v52, v132, v112
	v_fma_f32 v53, v53, v133, v113
	v_fma_f32 v50, v50, v130, v118
	v_fma_f32 v51, v51, v131, v119
	global_load_dwordx4 v[80:83], v[170:171], off offset:512
	global_load_dwordx4 v[84:87], v[170:171], off offset:576
	v_fma_f32 v48, v48, v128, v116
	v_fma_f32 v49, v49, v129, v117
	global_store_dwordx4 v[172:173], v[60:63], off
	global_store_dwordx4 v[172:173], v[56:59], off offset:64
	global_store_dwordx4 v[172:173], v[52:55], off offset:512
	global_store_dwordx4 v[172:173], v[48:51], off offset:576
	global_load_dwordx4 v[48:51], v[174:175], off
	global_load_dwordx4 v[52:55], v[174:175], off offset:64
	global_load_dwordx4 v[56:59], v[174:175], off offset:512
	global_load_dwordx4 v[60:63], v[174:175], off offset:576
	v_lshl_add_u64 v[96:97], s[12:13], 0, v[164:165]
	v_lshl_add_u64 v[96:97], v[96:97], 0, v[152:153]
	v_lshl_add_u64 v[98:99], s[12:13], 0, v[166:167]
	v_lshl_add_u64 v[98:99], v[98:99], 0, v[152:153]
	v_lshl_add_u64 v[100:101], s[12:13], 0, v[154:155]
	v_lshl_add_u64 v[100:101], v[100:101], 0, v[152:153]
	v_fma_f32 v46, v46, v142, v74
	v_fma_f32 v47, v47, v143, v75
	v_fma_f32 v44, v44, v140, v72
	v_fma_f32 v45, v45, v141, v73
	v_fma_f32 v42, v42, v138, v78
	v_fma_f32 v43, v43, v139, v79
	v_fma_f32 v40, v40, v136, v76
	v_fma_f32 v41, v41, v137, v77
	v_fma_f32 v30, v30, v134, v90
	v_fma_f32 v31, v31, v135, v91
	v_fma_f32 v28, v28, v132, v88
	v_fma_f32 v29, v29, v133, v89
	v_fma_f32 v26, v26, v130, v94
	v_fma_f32 v27, v27, v131, v95
	v_fma_f32 v24, v24, v128, v92
	v_fma_f32 v25, v25, v129, v93
	global_store_dwordx4 v[96:97], v[44:47], off
	global_store_dwordx4 v[96:97], v[40:43], off offset:64
	global_store_dwordx4 v[96:97], v[28:31], off offset:512
	global_store_dwordx4 v[96:97], v[24:27], off offset:576
	s_waitcnt vmcnt(0)
	v_fma_f32 v14, v14, v134, v82
	v_fma_f32 v15, v15, v135, v83
	v_fma_f32 v26, v38, v142, v66
	v_fma_f32 v27, v39, v143, v67
	v_fma_f32 v24, v36, v140, v64
	v_fma_f32 v25, v37, v141, v65
	v_fma_f32 v30, v34, v138, v70
	v_fma_f32 v31, v35, v139, v71
	v_fma_f32 v28, v32, v136, v68
	v_fma_f32 v29, v33, v137, v69
	v_fma_f32 v12, v12, v132, v80
	v_fma_f32 v13, v13, v133, v81
	v_fma_f32 v10, v10, v130, v86
	v_fma_f32 v11, v11, v131, v87
	v_fma_f32 v8, v8, v128, v84
	v_fma_f32 v9, v9, v129, v85
	global_store_dwordx4 v[98:99], v[24:27], off
	global_store_dwordx4 v[98:99], v[28:31], off offset:64
	global_store_dwordx4 v[98:99], v[12:15], off offset:512
	global_store_dwordx4 v[98:99], v[8:11], off offset:576
	v_fma_f32 v6, v6, v134, v58
	v_fma_f32 v7, v7, v135, v59
	v_fma_f32 v14, v18, v138, v54
	v_fma_f32 v15, v19, v139, v55
	v_fma_f32 v10, v22, v142, v50
	v_fma_f32 v11, v23, v143, v51
	v_fma_f32 v8, v20, v140, v48
	v_fma_f32 v9, v21, v141, v49
	v_fma_f32 v12, v16, v136, v52
	v_fma_f32 v13, v17, v137, v53
	v_fma_f32 v4, v4, v132, v56
	v_fma_f32 v5, v5, v133, v57
	v_fma_f32 v2, v2, v130, v62
	v_fma_f32 v3, v3, v131, v63
	v_fma_f32 v0, v0, v128, v60
	v_fma_f32 v1, v1, v129, v61
	global_store_dwordx4 v[100:101], v[8:11], off
	global_store_dwordx4 v[100:101], v[12:15], off offset:64
	global_store_dwordx4 v[100:101], v[4:7], off offset:512
	global_store_dwordx4 v[100:101], v[0:3], off offset:576
	s_cbranch_vccnz .LBB0_767
	s_and_b64 vcc, exec, s[6:7]
	s_cbranch_vccnz .LBB0_766
	s_barrier
	s_branch .LBB0_766

; #define P6_LDG(bi, grp) do { const int g_ = ((grp) < 32) ? (grp) : 31; _Pragma("unroll") for (int q = 0; q < 4; ++q) Xg[bi][q] = xp[2 * (4 * g_ + q)]; } while (0)
; #define P6_USE(bi, grp) do { _Pragma("unroll") for (int q = 0; q < 4; ++q) P6_STEP(Xg[bi][q], 4 * (grp) + q); } while (0)
; __global__ void __launch_bounds__(512, 2) hymba_fwd(Args args) {
;     ...
;             f32x4 Xg[3][4];
;     ...
;             P6_LDG(0, 0); P6_LDG(1, 1);
; #pragma nounroll
;             for (int gb = 0; gb < 30; gb += 3) {
;                 P6_LDG(2, gb + 2); P6_USE(0, gb);
;                 P6_LDG(0, gb + 3); P6_USE(1, gb + 1);
;                 P6_LDG(1, gb + 4); P6_USE(2, gb + 2);
;             }
;             P6_USE(0, 30); P6_USE(1, 31);
.LBB0_871:
	v_add_u32_e32 v221, 0, v215
	ds_read_b128 v[48:51], v221
	ds_read_b128 v[70:73], v221 offset:1024
	v_add_u32_e32 v212, 0, v220
	v_add_u32_e32 v64, 0x20000, v212
	v_add_u32_e32 v65, 0x20010, v212
	v_add_u32_e32 v66, 0x20020, v212
	v_add_u32_e32 v74, 0x20080, v212
	v_add_u32_e32 v75, 0x20090, v212
	global_load_dwordx4 v[56:59], v[176:177], off offset:-352
	s_waitcnt vmcnt(7) lgkmcnt(1)
	v_mfma_f32_32x32x2_f32 v[0:15], v48, v44, v[0:15]
	v_add_u32_e32 v88, 0x200a0, v212
	v_add_u32_e32 v89, 0x200b0, v212
	s_waitcnt vmcnt(5)
	v_mov_b64_e32 v[114:115], v[30:31]
	v_mov_b64_e32 v[112:113], v[28:29]
	v_add_u32_e32 v28, 0x20100, v212
	v_add_u32_e32 v31, 0x20130, v212
	v_add_u32_e32 v120, 0x201b0, v212
	v_add_u32_e32 v29, 0x20110, v212
	v_add_u32_e32 v30, 0x20120, v212
	v_mov_b32_e32 v185, v40
	v_mov_b32_e32 v183, v42
	v_mul_f32_e64 v232, v32, v32
	v_mul_f32_e64 v233, v33, v33
	v_add_u32_e32 v140, 0x20290, v212
	v_add_u32_e32 v141, 0x202a0, v212
	v_mov_b32_e32 v186, v47
	v_mfma_f32_32x32x2_f32 v[0:15], v49, v45, v[0:15]
	v_mov_b32_e32 v190, v43
	v_mov_b32_e32 v184, v44
	v_mov_b32_e32 v182, v46
	v_mov_b32_e32 v188, v35
	v_mul_f32_e64 v196, v34, v34
	v_mul_f32_e64 v197, v35, v35
	s_waitcnt vmcnt(3)
	v_mul_f32_e64 v236, v26, v26
	v_mul_f32_e64 v237, v27, v27
	v_pk_mov_b32 v[234:235], v[232:233], v[196:197] op_sel:[1,0]
	v_mov_b32_e32 v233, v197
	v_mul_f32_e32 v196, v113, v113
	v_mul_f32_e32 v175, v36, v36
	v_add_u32_e32 v240, 0x20400, v212
	v_add_u32_e32 v241, 0x20410, v212
	v_add_u32_e32 v242, 0x20420, v212
	v_add_u32_e32 v243, 0x20430, v212
	v_add_u32_e32 v244, 0x20480, v212
	v_mfma_f32_32x32x2_f32 v[0:15], v50, v46, v[0:15]
	v_add_u32_e32 v245, 0x20490, v212
	v_add_u32_e32 v246, 0x204a0, v212
	v_add_u32_e32 v247, 0x204b0, v212
	v_add_u32_e32 v222, 0x20500, v212
	v_add_u32_e32 v223, 0x20510, v212
	v_add_u32_e32 v224, 0x20520, v212
	v_add_u32_e32 v225, 0x20530, v212
	v_add_u32_e32 v226, 0x20580, v212
	v_add_u32_e32 v227, 0x20590, v212
	v_add_u32_e32 v228, 0x205a0, v212
	v_add_u32_e32 v229, 0x205b0, v212
	v_mov_b32_e32 v214, v27
	v_add_u32_e32 v215, 0x3000, v215
	s_add_i32 s8, s8, 3
	s_mov_b64 s[10:11], 0x180
	v_mfma_f32_32x32x2_f32 v[0:15], v51, v47, v[0:15]
	global_load_dwordx4 v[60:63], v[176:177], off offset:-320
	global_load_dwordx4 v[52:55], v[176:177], off offset:-288
	global_load_dwordx4 v[48:51], v[176:177], off offset:-256
	v_add_u32_e32 v220, 0x600, v220
	s_cmp_gt_u32 s8, 26
	s_waitcnt lgkmcnt(0)
	v_mfma_f32_32x32x2_f32 v[0:15], v70, v40, v[0:15]
	v_mfma_f32_32x32x2_f32 v[0:15], v71, v41, v[0:15]
	ds_read_b128 v[68:71], v64
	ds_read_b128 v[80:83], v65
	ds_read_b128 v[64:67], v66
	s_waitcnt lgkmcnt(1)
	v_mul_f32_e64 v80, v80, v45
	v_mul_f32_e64 v81, v81, v45
	v_mul_f32_e64 v82, v82, v45
	v_mul_f32_e64 v83, v83, v45
	v_fma_f32 v68, v68, v44, v80
	v_fma_f32 v69, v69, v44, v81
	v_fma_f32 v70, v70, v44, v82
	v_fma_f32 v71, v71, v44, v83
	s_waitcnt lgkmcnt(0)
	v_fma_f32 v204, v64, v46, v68
	v_fma_f32 v205, v65, v46, v69
	v_fma_f32 v206, v66, v46, v70
	v_fma_f32 v207, v67, v46, v71
	v_mfma_f32_32x32x2_f32 v[0:15], v72, v42, v[0:15]
	v_add_u32_e32 v72, 0x20030, v212
	v_mfma_f32_32x32x2_f32 v[0:15], v73, v43, v[0:15]
	ds_read_b128 v[104:107], v72
	ds_read_b128 v[76:79], v74
	ds_read_b128 v[84:87], v75
	ds_read_b128 v[72:75], v88
	ds_read_b128 v[108:111], v89
	ds_read_b128 v[88:91], v221 offset:2048
	s_waitcnt lgkmcnt(3)
	v_mul_f32_e64 v84, v84, v41
	v_mul_f32_e64 v85, v85, v41
	v_mul_f32_e64 v86, v86, v41
	v_mul_f32_e64 v87, v87, v41
	v_fma_f32 v76, v76, v40, v84
	v_fma_f32 v77, v77, v40, v85
	v_fma_f32 v78, v78, v40, v86
	v_fma_f32 v79, v79, v40, v87
	s_waitcnt lgkmcnt(2)
	v_fma_f32 v208, v72, v42, v76
	v_fma_f32 v209, v73, v42, v77
	v_fma_f32 v210, v74, v42, v78
	v_fma_f32 v211, v75, v42, v79
	v_mov_b32_e32 v40, v45
	v_mov_b32_e32 v42, v47
	v_mul_f32_e32 v194, v40, v40
	v_mul_f32_e32 v195, v41, v41
	v_mul_f32_e32 v192, v42, v42
	v_mul_f32_e32 v193, v43, v43
	v_add_u32_e32 v76, 0x203b0, v212
	v_fma_f32 v104, v104, v186, v204
	v_fma_f32 v105, v105, v186, v205
	s_waitcnt lgkmcnt(0)
	v_mfma_f32_32x32x2_f32 v[0:15], v88, v32, v[0:15]
	v_fma_f32 v106, v106, v186, v206
	v_fma_f32 v107, v107, v186, v207
	v_fma_f32 v108, v108, v190, v208
	v_fma_f32 v109, v109, v190, v209
	v_add_f32_e64 v104, v178, v104
	v_add_f32_e64 v105, v179, v105
	v_mfma_f32_32x32x2_f32 v[0:15], v89, v33, v[0:15]
	v_mfma_f32_32x32x2_f32 v[0:15], v90, v34, v[0:15]
	v_mfma_f32_32x32x2_f32 v[0:15], v91, v35, v[0:15]
	ds_read_b128 v[88:91], v221 offset:3072
	ds_read_b128 v[92:95], v28
	ds_read_b128 v[96:99], v29
	ds_read_b128 v[100:103], v30
	s_waitcnt lgkmcnt(1)
	v_mul_f32_e64 v80, v96, v33
	v_mul_f32_e64 v81, v97, v33
	v_mul_f32_e64 v82, v98, v33
	v_mul_f32_e64 v83, v99, v33
	v_fma_f32 v64, v92, v32, v80
	v_fma_f32 v65, v93, v32, v81
	v_fma_f32 v33, v95, v32, v83
	v_fma_f32 v32, v94, v32, v82
	s_waitcnt lgkmcnt(0)
	v_fma_f32 v202, v100, v34, v64
	v_fma_f32 v203, v101, v34, v65
	v_fma_f32 v200, v102, v34, v32
	v_fma_f32 v201, v103, v34, v33
	s_waitcnt vmcnt(5)
	v_mov_b64_e32 v[66:67], v[18:19]
	v_mov_b64_e32 v[64:65], v[16:17]
	v_mul_f32_e32 v198, v65, v65
	v_mfma_f32_32x32x2_f32 v[0:15], v88, v112, v[0:15]
	v_add_u32_e32 v88, 0x20180, v212
	v_mfma_f32_32x32x2_f32 v[0:15], v89, v113, v[0:15]
	v_add_u32_e32 v89, 0x20190, v212
	v_mfma_f32_32x32x2_f32 v[0:15], v90, v114, v[0:15]
	v_add_u32_e32 v90, 0x201a0, v212
	ds_read_b128 v[116:119], v31
	ds_read_b128 v[128:131], v88
	ds_read_b128 v[132:135], v89
	ds_read_b128 v[124:127], v90
	ds_read_b128 v[120:123], v120
	ds_read_b128 v[28:31], v221 offset:4096
	v_mfma_f32_32x32x2_f32 v[0:15], v91, v115, v[0:15]
	ds_read_b128 v[88:91], v221 offset:5120
	s_waitcnt lgkmcnt(1)
; #define P6_LDG(bi, grp) do { const int g_ = ((grp) < 32) ? (grp) : 31; _Pragma("unroll") for (int q = 0; q < 4; ++q) Xg[bi][q] = xp[2 * (4 * g_ + q)]; } while (0)
; #define P6_USE(bi, grp) do { _Pragma("unroll") for (int q = 0; q < 4; ++q) P6_STEP(Xg[bi][q], 4 * (grp) + q); } while (0)
; __global__ void __launch_bounds__(512, 2) hymba_fwd(Args args) {
;     ...
;             f32x4 Xg[3][4];
;     ...
;             P6_LDG(0, 0); P6_LDG(1, 1);
; #pragma nounroll
;             for (int gb = 0; gb < 30; gb += 3) {
;                 P6_LDG(2, gb + 2); P6_USE(0, gb);
;                 P6_LDG(0, gb + 3); P6_USE(1, gb + 1);
;                 P6_LDG(1, gb + 4); P6_USE(2, gb + 2);
;             }
;             P6_USE(0, 30); P6_USE(1, 31);
	v_mfma_f32_32x32x2_f32 v[0:15], v28, v36, v[0:15]
	v_add_u32_e32 v28, 0x20200, v212
	v_mfma_f32_32x32x2_f32 v[0:15], v29, v37, v[0:15]
	v_add_u32_e32 v29, 0x20210, v212
	v_mfma_f32_32x32x2_f32 v[0:15], v30, v38, v[0:15]
	v_add_u32_e32 v30, 0x20220, v212
	v_mfma_f32_32x32x2_f32 v[0:15], v31, v39, v[0:15]
	v_add_u32_e32 v31, 0x20230, v212
	s_waitcnt lgkmcnt(0)
	v_mfma_f32_32x32x2_f32 v[0:15], v88, v24, v[0:15]
	v_add_u32_e32 v88, 0x20280, v212
	v_mfma_f32_32x32x2_f32 v[0:15], v89, v25, v[0:15]
	v_add_u32_e32 v89, 0x202b0, v212
	ds_read_b128 v[152:155], v28
	ds_read_b128 v[160:163], v29
	ds_read_b128 v[144:147], v30
	ds_read_b128 v[136:139], v31
	ds_read_b128 v[156:159], v88
	ds_read_b128 v[164:167], v140
	ds_read_b128 v[148:151], v141
	ds_read_b128 v[140:143], v89
	global_load_dwordx4 v[28:31], v[176:177], off offset:-128
	global_load_dwordx4 v[44:47], v[176:177], off offset:-224
	global_load_dwordx4 v[40:43], v[176:177], off offset:-192
	global_load_dwordx4 v[32:35], v[176:177], off offset:-160
	ds_read_b128 v[68:71], v221 offset:6144
	ds_read_b128 v[16:19], v221 offset:7168
	v_mfma_f32_32x32x2_f32 v[0:15], v90, v26, v[0:15]
	v_mfma_f32_32x32x2_f32 v[0:15], v91, v27, v[0:15]
	s_waitcnt lgkmcnt(1)
	v_mfma_f32_32x32x2_f32 v[0:15], v68, v64, v[0:15]
	v_mfma_f32_32x32x2_f32 v[0:15], v69, v65, v[0:15]
	v_mfma_f32_32x32x2_f32 v[0:15], v70, v66, v[0:15]
	v_mfma_f32_32x32x2_f32 v[0:15], v71, v67, v[0:15]
	s_waitcnt vmcnt(8)
	v_mov_b64_e32 v[70:71], v[22:23]
	v_mov_b64_e32 v[68:69], v[20:21]
	v_add_u32_e32 v20, 0x20330, v212
	v_add_u32_e32 v21, 0x20380, v212
	v_add_u32_e32 v22, 0x20390, v212
	v_add_u32_e32 v23, 0x203a0, v212
	v_mul_f32_e32 v238, v70, v70
	v_mul_f32_e32 v239, v71, v71
	v_mul_f32_e32 v230, v68, v68
	v_mul_f32_e32 v231, v69, v69
	s_waitcnt lgkmcnt(0)
	v_mfma_f32_32x32x2_f32 v[0:15], v16, v68, v[0:15]
	v_add_u32_e32 v16, 0x20300, v212
	v_mfma_f32_32x32x2_f32 v[0:15], v17, v69, v[0:15]
	v_add_u32_e32 v17, 0x20310, v212
	v_mfma_f32_32x32x2_f32 v[0:15], v18, v70, v[0:15]
	v_add_u32_e32 v18, 0x20320, v212
	ds_read_b128 v[88:91], v16
	ds_read_b128 v[96:99], v17
	ds_read_b128 v[80:83], v18
	ds_read_b128 v[72:75], v20
	ds_read_b128 v[92:95], v21
	ds_read_b128 v[100:103], v22
	ds_read_b128 v[84:87], v23
	ds_read_b128 v[76:79], v76
	ds_read_b128 v[216:219], v221 offset:8192
	v_mul_f32_e32 v18, v115, v115
	v_mul_f32_e32 v21, v39, v39
	v_mul_f32_e64 v22, v24, v24
	v_mul_f32_e64 v23, v25, v25
	v_mul_f32_e32 v20, v67, v67
	v_mul_f32_e32 v17, v37, v37
	v_mov_b32_e32 v16, v115
	v_mov_b32_e32 v212, v39
	s_waitcnt lgkmcnt(7)
	v_mul_f32_e32 v96, v96, v65
	v_mul_f32_e32 v97, v97, v65
	v_mul_f32_e32 v98, v98, v65
	v_mul_f32_e32 v99, v99, v65
	s_waitcnt lgkmcnt(3)
	v_mul_f32_e32 v100, v100, v69
	v_mul_f32_e32 v101, v101, v69
	v_mfma_f32_32x32x2_f32 v[0:15], v19, v71, v[0:15]
	v_mul_f32_e32 v19, v38, v38
	v_mul_f32_e64 v102, v102, v69
	v_mul_f32_e64 v103, v103, v69
	v_fma_f32 v88, v88, v64, v96
	v_fma_f32 v89, v89, v64, v97
	v_fma_f32 v92, v92, v68, v100
	v_fma_f32 v93, v93, v68, v101
	v_fma_f32 v69, v95, v68, v103
	v_fma_f32 v68, v94, v68, v102
	v_fma_f32 v80, v80, v66, v88
	v_fma_f32 v81, v81, v66, v89
	s_waitcnt lgkmcnt(2)
	v_fma_f32 v84, v84, v70, v92
	v_fma_f32 v85, v85, v70, v93
	s_waitcnt vmcnt(7) lgkmcnt(0)
	v_mfma_f32_32x32x2_f32 v[0:15], v216, v56, v[0:15]
	v_mfma_f32_32x32x2_f32 v[0:15], v217, v57, v[0:15]
	v_fma_f32 v216, v112, v112, v196
	v_fma_f32 v217, v113, v113, v196
	v_pk_mov_b32 v[196:197], v[22:23], v[236:237] op_sel:[1,0]
	v_mov_b32_e32 v217, v19
	v_fma_f32 v19, v115, v115, v18
	v_fma_f32 v18, v114, v114, v18
	v_mov_b32_e32 v23, v237
	v_fma_f32 v236, v64, v64, v198
	v_fma_f32 v237, v65, v65, v198
	v_mov_b32_e32 v19, v21
	v_fma_f32 v21, v67, v67, v20
	v_fma_f32 v20, v66, v66, v20
	v_add_f32_e32 v22, v196, v22
	v_add_f32_e32 v23, v197, v23
	v_mov_b32_e32 v237, v238
	v_mov_b32_e32 v21, v239
	v_add_f32_e32 v216, v216, v18
	v_add_f32_e32 v217, v217, v19
	v_mul_f32_e32 v18, v132, v113
	v_mul_f32_e32 v19, v133, v113
	v_add_f32_e32 v238, v22, v23
	v_add_f32_e32 v239, v23, v22
	v_add_f32_e32 v236, v236, v20
	v_add_f32_e32 v237, v237, v21
	v_mfma_f32_32x32x2_f32 v[0:15], v218, v58, v[0:15]
	v_mul_f32_e64 v20, v134, v113
	v_mul_f32_e64 v21, v135, v113
	v_fma_f32 v18, v128, v112, v18
	v_fma_f32 v19, v129, v112, v19
	v_mul_f32_e64 v22, v160, v37
	v_mul_f32_e64 v23, v161, v37
	v_fma_f32 v20, v130, v112, v20
	v_fma_f32 v21, v131, v112, v21
	v_mul_f32_e64 v112, v162, v37
	v_mul_f32_e64 v113, v163, v37
	v_mul_f32_e64 v128, v164, v25
	v_mul_f32_e64 v129, v165, v25
	v_mul_f32_e64 v130, v166, v25
	v_mul_f32_e64 v131, v167, v25
	v_fma_f32 v18, v124, v114, v18
	v_fma_f32 v19, v125, v114, v19
	v_fma_f32 v22, v152, v36, v22
	v_fma_f32 v23, v153, v36, v23
	v_fma_f32 v160, v110, v190, v210
	v_fma_f32 v161, v111, v190, v211
	v_fma_f32 v110, v156, v24, v128
	v_fma_f32 v111, v157, v24, v129
	v_fma_f32 v20, v126, v114, v20
	v_fma_f32 v21, v127, v114, v21
	v_fma_f32 v37, v155, v36, v113
	v_fma_f32 v36, v154, v36, v112
	v_fma_f32 v25, v159, v24, v131
	v_fma_f32 v24, v158, v24, v130
	v_fma_f32 v156, v120, v16, v18
	v_fma_f32 v157, v121, v16, v19
	v_mfma_f32_32x32x2_f32 v[0:15], v219, v59, v[0:15]
	v_add_f32_e64 v218, v234, v232
	v_add_f32_e64 v219, v235, v233
	ds_read_b128 v[232:235], v221 offset:9216
	v_pk_add_f32 v[218:219], v[218:219], v[218:219] op_sel:[0,1] op_sel_hi:[1,0]
	v_fma_f32 v18, v144, v38, v22
	v_fma_f32 v19, v145, v38, v23
	v_mov_b32_e32 v219, v17
	v_add_f32_e32 v152, v180, v106
	v_add_f32_e32 v153, v181, v107
	v_fma_f32 v154, v116, v188, v202
	v_fma_f32 v155, v117, v188, v203
	v_fma_f32 v144, v148, v26, v110
	v_fma_f32 v145, v149, v26, v111
	v_fma_f32 v158, v118, v188, v200
	v_fma_f32 v159, v119, v188, v201
	v_fma_f32 v162, v122, v16, v20
	v_fma_f32 v163, v123, v16, v21
	v_fma_f32 v164, v146, v38, v36
	v_fma_f32 v165, v147, v38, v37
	v_fma_f32 v150, v150, v26, v24
	v_fma_f32 v151, v151, v26, v25
	v_add_f32_e32 v166, v104, v108
	v_add_f32_e32 v167, v105, v109
	v_fma_f32 v136, v136, v212, v18
	v_fma_f32 v137, v137, v212, v19
	global_load_dwordx4 v[36:39], v[176:177], off offset:-96
	global_load_dwordx4 v[24:27], v[176:177], off offset:-64
	global_load_dwordx4 v[16:19], v[176:177], off offset:-32
	global_load_dwordx4 v[20:23], v[176:177], off
	s_waitcnt vmcnt(10) lgkmcnt(0)
; #define P6_LDG(bi, grp) do { const int g_ = ((grp) < 32) ? (grp) : 31; _Pragma("unroll") for (int q = 0; q < 4; ++q) Xg[bi][q] = xp[2 * (4 * g_ + q)]; } while (0)
; #define P6_USE(bi, grp) do { _Pragma("unroll") for (int q = 0; q < 4; ++q) P6_STEP(Xg[bi][q], 4 * (grp) + q); } while (0)
; __global__ void __launch_bounds__(512, 2) hymba_fwd(Args args) {
;     ...
;             f32x4 Xg[3][4];
;     ...
;             P6_LDG(0, 0); P6_LDG(1, 1);
; #pragma nounroll
;             for (int gb = 0; gb < 30; gb += 3) {
;                 P6_LDG(2, gb + 2); P6_USE(0, gb);
;                 P6_LDG(0, gb + 3); P6_USE(1, gb + 1);
;                 P6_LDG(1, gb + 4); P6_USE(2, gb + 2);
;             }
	v_mfma_f32_32x32x2_f32 v[0:15], v232, v60, v[0:15]
	ds_read_b128 v[120:123], v240
	ds_read_b128 v[128:131], v241
	ds_read_b128 v[112:115], v242
	ds_read_b128 v[104:107], v243
	ds_read_b128 v[124:127], v244
	ds_read_b128 v[132:135], v245
	ds_read_b128 v[116:119], v246
	ds_read_b128 v[108:111], v247
	ds_read_b128 v[146:149], v221 offset:10240
	v_fma_f32 v140, v140, v214, v144
	v_fma_f32 v141, v141, v214, v145
	v_add_f32_e64 v144, v152, v160
	v_add_f32_e64 v145, v153, v161
	v_fma_f32 v150, v142, v214, v150
	v_fma_f32 v151, v143, v214, v151
	v_add_f32_e32 v142, v166, v154
	v_add_f32_e32 v143, v167, v155
	v_add_f32_e32 v144, v144, v158
	v_add_f32_e32 v145, v145, v159
	v_fma_f32 v138, v138, v212, v164
	v_fma_f32 v139, v139, v212, v165
	v_add_f32_e32 v142, v142, v156
	v_add_f32_e32 v143, v143, v157
	v_add_f32_e32 v144, v144, v162
	v_add_f32_e32 v145, v145, v163
	v_mul_f32_e32 v152, v58, v58
	v_mul_f32_e32 v153, v59, v59
	v_mul_f32_e32 v154, v56, v56
	v_mul_f32_e32 v155, v57, v57
	v_mul_f32_e32 v156, v61, v61
	v_mfma_f32_32x32x2_f32 v[0:15], v233, v61, v[0:15]
	v_mul_f32_e32 v158, v63, v63
	s_waitcnt vmcnt(8)
	v_mul_f32_e64 v160, v50, v50
	v_mul_f32_e64 v161, v51, v51
	v_mul_f32_e64 v162, v48, v48
	v_mul_f32_e64 v163, v49, v49
	v_add_f32_e64 v138, v144, v138
	v_add_f32_e64 v139, v145, v139
	v_mul_f32_e32 v145, v54, v54
	v_mul_f32_e32 v166, v55, v55
	v_pk_mov_b32 v[164:165], v[154:155], v[152:153] op_sel:[1,0]
	v_mov_b32_e32 v155, v153
	v_fma_f32 v152, v60, v60, v156
	v_fma_f32 v153, v61, v61, v156
	v_fma_f32 v156, v62, v62, v158
	v_fma_f32 v157, v63, v63, v158
	v_pk_mov_b32 v[158:159], v[162:163], v[160:161] op_sel:[1,0]
	v_mov_b32_e32 v163, v161
	v_add_f32_e32 v136, v142, v136
	v_add_f32_e32 v137, v143, v137
	v_mov_b32_e32 v153, v145
	v_mov_b32_e32 v157, v166
	v_mfma_f32_32x32x2_f32 v[0:15], v234, v62, v[0:15]
	v_add_f32_e64 v158, v158, v162
	v_add_f32_e64 v159, v159, v163
	v_add_f32_e64 v142, v136, v140
	v_add_f32_e64 v143, v137, v141
	v_add_f32_e64 v136, v138, v150
	v_add_f32_e64 v137, v139, v151
	v_fma_f32 v150, v184, v184, v194
	v_fma_f32 v151, v185, v185, v195
	v_add_f32_e64 v154, v164, v154
	v_add_f32_e64 v155, v165, v155
	v_add_f32_e64 v152, v152, v156
	v_add_f32_e64 v153, v153, v157
	v_add_f32_e64 v156, v158, v159
	v_add_f32_e64 v157, v159, v158
	v_fma_f32 v158, v182, v182, v192
	v_fma_f32 v159, v183, v183, v193
	v_mul_f32_e32 v141, v53, v53
	v_pk_add_f32 v[154:155], v[154:155], v[154:155] op_sel:[0,1] op_sel_hi:[1,0]
	v_add_f32_e32 v150, v150, v158
	v_add_f32_e32 v151, v151, v159
	v_mov_b32_e32 v155, v141
	v_add_f32_e32 v141, v174, v150
	v_add_f32_e32 v174, v141, v151
	v_add_f32_e32 v150, v174, v218
	v_add_f32_e32 v151, v175, v219
	v_mfma_f32_32x32x2_f32 v[0:15], v235, v63, v[0:15]
	v_add_f32_e64 v150, v150, v216
	v_add_f32_e64 v151, v151, v217
	v_mov_b32_e32 v239, v231
	v_pk_add_f32 v[150:151], v[150:151], v[150:151] op_sel:[0,1] op_sel_hi:[1,0]
	v_mul_f32_e32 v139, v52, v52
	v_mov_b32_e32 v151, v230
	v_add_f32_e32 v150, v150, v238
	v_add_f32_e32 v151, v151, v239
	v_fma_f32 v65, v91, v64, v99
	v_fma_f32 v64, v90, v64, v98
	v_add_f32_e32 v150, v150, v236
	v_add_f32_e32 v151, v151, v237
	v_mov_b32_e32 v196, v67
	v_pk_add_f32 v[150:151], v[150:151], v[150:151] op_sel:[0,1] op_sel_hi:[1,0]
	s_waitcnt lgkmcnt(7)
	v_mul_f32_e32 v96, v128, v57
	v_mul_f32_e32 v97, v129, v57
	v_mov_b32_e32 v151, v139
	s_waitcnt lgkmcnt(3)
	v_mul_f32_e32 v100, v132, v61
	v_mul_f32_e32 v101, v133, v61
	v_mul_f32_e32 v90, v130, v57
	v_mul_f32_e32 v91, v131, v57
	v_mul_f32_e32 v94, v134, v61
	v_mul_f32_e32 v95, v135, v61
	s_waitcnt lgkmcnt(0)
	v_mfma_f32_32x32x2_f32 v[0:15], v146, v52, v[0:15]
	v_fma_f32 v64, v82, v66, v64
	v_fma_f32 v65, v83, v66, v65
	v_mov_b32_e32 v198, v71
	v_fma_f32 v88, v120, v56, v96
	v_fma_f32 v89, v121, v56, v97
	v_fma_f32 v92, v124, v60, v100
	v_fma_f32 v93, v125, v60, v101
	v_fma_f32 v66, v86, v70, v68
	v_fma_f32 v67, v87, v70, v69
	v_fma_f32 v57, v123, v56, v91
	v_fma_f32 v56, v122, v56, v90
	v_fma_f32 v61, v127, v60, v95
	v_fma_f32 v60, v126, v60, v94
	v_fma_f32 v72, v72, v196, v80
	v_fma_f32 v73, v73, v196, v81
	v_fma_f32 v64, v74, v196, v64
	v_fma_f32 v65, v75, v196, v65
	v_mov_b32_e32 v144, v59
	v_fma_f32 v76, v76, v198, v84
	v_fma_f32 v77, v77, v198, v85
	v_fma_f32 v80, v112, v58, v88
	v_fma_f32 v81, v113, v58, v89
	v_fma_f32 v66, v78, v198, v66
	v_fma_f32 v67, v79, v198, v67
	v_fma_f32 v56, v114, v58, v56
	v_fma_f32 v57, v115, v58, v57
	v_fma_f32 v58, v118, v62, v60
	v_fma_f32 v59, v119, v62, v61
	v_mfma_f32_32x32x2_f32 v[0:15], v147, v53, v[0:15]
	v_add_f32_e64 v60, v142, v72
	v_add_f32_e64 v61, v143, v73
	v_add_f32_e64 v64, v136, v64
	v_add_f32_e64 v65, v137, v65
	v_mov_b32_e32 v146, v63
	v_mov_b32_e32 v140, v51
	v_fma_f32 v82, v116, v62, v92
	v_fma_f32 v83, v117, v62, v93
	v_fma_f32 v62, v104, v144, v80
	v_fma_f32 v63, v105, v144, v81
	v_fma_f32 v56, v106, v144, v56
	v_fma_f32 v57, v107, v144, v57
	v_add_f32_e64 v64, v64, v66
	v_add_f32_e64 v65, v65, v67
	v_mov_b32_e32 v138, v55
	v_fma_f32 v58, v110, v146, v58
	v_fma_f32 v59, v111, v146, v59
	v_add_f32_e32 v56, v64, v56
	v_add_f32_e32 v57, v65, v57
	v_lshl_add_u64 v[176:177], v[176:177], 0, s[10:11]
	v_add_f32_e32 v56, v56, v58
	v_add_f32_e32 v57, v57, v59
	v_mfma_f32_32x32x2_f32 v[0:15], v148, v54, v[0:15]
	v_mfma_f32_32x32x2_f32 v[0:15], v149, v55, v[0:15]
	v_add_f32_e64 v148, v150, v154
	v_add_f32_e64 v149, v151, v155
	v_add_f32_e64 v148, v148, v152
	v_add_f32_e64 v149, v149, v153
	v_pk_add_f32 v[148:149], v[148:149], v[148:149] op_sel:[0,1] op_sel_hi:[1,0]
	s_nop 0
	v_add_f32_e32 v174, v148, v156
	v_add_f32_e32 v175, v149, v157
	ds_read_b128 v[148:151], v221 offset:11264
	ds_read_b128 v[152:155], v222
	ds_read_b128 v[156:159], v223
	ds_read_b128 v[160:163], v224
	ds_read_b128 v[164:167], v225
	ds_read_b128 v[178:181], v226
	ds_read_b128 v[182:185], v227
	ds_read_b128 v[192:195], v228
	ds_read_b128 v[200:203], v229
	s_waitcnt lgkmcnt(6)
; #define P6_LDG(bi, grp) do { const int g_ = ((grp) < 32) ? (grp) : 31; _Pragma("unroll") for (int q = 0; q < 4; ++q) Xg[bi][q] = xp[2 * (4 * g_ + q)]; } while (0)
; #define P6_USE(bi, grp) do { _Pragma("unroll") for (int q = 0; q < 4; ++q) P6_STEP(Xg[bi][q], 4 * (grp) + q); } while (0)
; __global__ void __launch_bounds__(512, 2) hymba_fwd(Args args) {
;     ...
;             f32x4 Xg[3][4];
;     ...
;             P6_LDG(0, 0); P6_LDG(1, 1);
; #pragma nounroll
;             for (int gb = 0; gb < 30; gb += 3) {
;                 P6_LDG(2, gb + 2); P6_USE(0, gb);
;                 P6_LDG(0, gb + 3); P6_USE(1, gb + 1);
;                 P6_LDG(1, gb + 4); P6_USE(2, gb + 2);
;             }
;             P6_USE(0, 30); P6_USE(1, 31);
	v_mul_f32_e32 v96, v156, v53
	v_mul_f32_e32 v97, v157, v53
	v_mul_f32_e32 v68, v158, v53
	v_mul_f32_e32 v69, v159, v53
	s_waitcnt lgkmcnt(2)
	v_mul_f32_e32 v98, v182, v49
	v_mul_f32_e32 v99, v183, v49
	v_mul_f32_e32 v70, v184, v49
	v_mul_f32_e32 v71, v185, v49
	v_fma_f32 v86, v178, v48, v98
	v_fma_f32 v87, v179, v48, v99
	v_fma_f32 v84, v152, v52, v96
	v_fma_f32 v85, v153, v52, v97
	v_fma_f32 v53, v155, v52, v69
	v_fma_f32 v52, v154, v52, v68
	v_mfma_f32_32x32x2_f32 v[0:15], v148, v48, v[0:15]
	s_waitcnt lgkmcnt(1)
	v_fma_f32 v72, v192, v50, v86
	v_fma_f32 v73, v193, v50, v87
	v_fma_f32 v68, v108, v146, v82
	v_fma_f32 v69, v109, v146, v83
	v_fma_f32 v52, v162, v54, v52
	v_fma_f32 v53, v163, v54, v53
	v_fma_f32 v52, v166, v138, v52
	v_fma_f32 v53, v167, v138, v53
	v_add_f32_e64 v52, v56, v52
	v_add_f32_e64 v53, v57, v53
	v_mfma_f32_32x32x2_f32 v[0:15], v149, v49, v[0:15]
	v_fma_f32 v49, v181, v48, v71
	v_fma_f32 v48, v180, v48, v70
	v_fma_f32 v70, v160, v54, v84
	v_fma_f32 v71, v161, v54, v85
	v_fma_f32 v48, v194, v50, v48
	v_fma_f32 v49, v195, v50, v49
	v_fma_f32 v54, v164, v138, v70
	v_fma_f32 v55, v165, v138, v71
	s_waitcnt lgkmcnt(0)
	v_fma_f32 v48, v202, v140, v48
	v_fma_f32 v49, v203, v140, v49
	s_nop 0
	v_add_f32_e32 v180, v52, v48
	v_add_f32_e32 v181, v53, v49
	v_mfma_f32_32x32x2_f32 v[0:15], v150, v50, v[0:15]
	v_mfma_f32_32x32x2_f32 v[0:15], v151, v51, v[0:15]
	v_add_f32_e64 v50, v60, v76
	v_add_f32_e64 v51, v61, v77
	v_fma_f32 v60, v200, v140, v72
	v_fma_f32 v61, v201, v140, v73
	v_add_f32_e64 v50, v50, v62
	v_add_f32_e64 v51, v51, v63
	v_add_f32_e64 v50, v50, v68
	v_add_f32_e64 v51, v51, v69
	v_add_f32_e64 v50, v50, v54
	v_add_f32_e64 v51, v51, v55
	v_add_f32_e64 v178, v50, v60
	v_add_f32_e64 v179, v51, v61
	s_cbranch_scc0 .LBB0_871
	v_lshl_add_u32 v70, v171, 4, 0
	v_add_u32_e32 v48, 0x1e000, v70
	ds_read_b128 v[48:51], v48
	s_add_i32 s8, 0, 0x20000
	v_add_u32_e32 v71, s8, v173
	ds_read_b128 v[52:55], v71 offset:15360
	ds_read_b128 v[56:59], v71 offset:15376
	ds_read_b128 v[60:63], v71 offset:15392
	ds_read_b128 v[64:67], v71 offset:15408
	s_waitcnt vmcnt(4)
	v_mov_b32_e32 v88, v32
	v_mov_b32_e32 v89, v28
	v_mov_b32_e32 v90, v34
	v_mov_b32_e32 v91, v30
	s_mov_b32 s8, 0xf800000
	s_waitcnt lgkmcnt(4)
	v_mfma_f32_32x32x2_f32 v[0:15], v48, v44, v[0:15]
	s_waitcnt lgkmcnt(2)
	v_mul_f32_e32 v48, v58, v45
	v_fmac_f32_e32 v48, v54, v44
	s_waitcnt lgkmcnt(1)
	v_fmac_f32_e32 v48, v62, v46
	s_waitcnt lgkmcnt(0)
	v_fmac_f32_e32 v48, v66, v47
	v_add_f32_e32 v84, v180, v48
	v_mul_f32_e32 v48, v59, v45
	v_fmac_f32_e32 v48, v55, v44
	v_fmac_f32_e32 v48, v63, v46
	v_fmac_f32_e32 v48, v67, v47
	v_add_u32_e32 v54, 0x1e400, v70
	v_add_f32_e32 v85, v181, v48
	v_mov_b32_e32 v58, v44
	v_mov_b32_e32 v62, v56
	v_mov_b32_e32 v44, v45
	v_mov_b32_e32 v59, v40
	v_mfma_f32_32x32x2_f32 v[0:15], v49, v45, v[0:15]
	v_mov_b32_e32 v45, v41
	v_mfma_f32_32x32x2_f32 v[0:15], v50, v46, v[0:15]
	v_mfma_f32_32x32x2_f32 v[0:15], v51, v47, v[0:15]
	ds_read_b128 v[48:51], v71 offset:15536
	ds_read_b128 v[66:69], v71 offset:15520
	ds_read_b128 v[72:75], v71 offset:15504
	ds_read_b128 v[76:79], v71 offset:15488
	ds_read_b128 v[80:83], v54
	v_mov_b32_e32 v54, v52
	s_waitcnt lgkmcnt(2)
	v_mov_b32_e32 v63, v72
	v_mov_b32_e32 v72, v57
	s_waitcnt lgkmcnt(1)
	v_mov_b32_e32 v55, v76
	v_mul_f32_e64 v62, v62, v44
	v_mul_f32_e64 v63, v63, v45
	v_mov_b32_e32 v76, v53
	v_mul_f32_e32 v52, v72, v44
	v_mul_f32_e32 v53, v73, v45
	v_fma_f32 v54, v54, v58, v62
	v_fma_f32 v55, v55, v59, v63
	v_mov_b32_e32 v62, v60
	v_mov_b32_e32 v63, v66
	v_fma_f32 v52, v76, v58, v52
	v_fma_f32 v53, v77, v59, v53
	v_mov_b32_e32 v66, v61
	s_waitcnt lgkmcnt(0)
	v_mfma_f32_32x32x2_f32 v[0:15], v80, v40, v[0:15]
	v_mov_b32_e32 v80, v46
	v_mov_b32_e32 v46, v47
	v_mov_b32_e32 v47, v43
	v_mul_f32_e64 v60, v34, v34
	v_mul_f32_e64 v61, v35, v35
	v_mfma_f32_32x32x2_f32 v[0:15], v81, v41, v[0:15]
	v_mov_b32_e32 v81, v42
	v_fma_f32 v54, v62, v80, v54
	v_fma_f32 v55, v63, v81, v55
	v_mov_b32_e32 v63, v48
	v_fma_f32 v52, v66, v80, v52
	v_fma_f32 v53, v67, v81, v53
	v_mov_b32_e32 v48, v65
	v_fma_f32 v48, v48, v46, v52
	v_fma_f32 v49, v49, v47, v53
	v_mov_b32_e32 v62, v64
	v_add_f32_e64 v52, v179, v48
	v_add_f32_e64 v53, v178, v49
	v_add_f32_e64 v64, v52, v49
	v_add_f32_e64 v65, v53, v48
	v_mul_f32_e32 v48, v74, v41
	v_mul_f32_e32 v41, v75, v41
	v_fmac_f32_e32 v41, v79, v40
	v_fmac_f32_e32 v48, v78, v40
	v_fmac_f32_e32 v41, v69, v42
	v_fmac_f32_e32 v48, v68, v42
	v_mfma_f32_32x32x2_f32 v[0:15], v82, v42, v[0:15]
	v_fmac_f32_e32 v41, v51, v43
	v_fmac_f32_e32 v48, v50, v43
	v_add_f32_e32 v93, v85, v41
	v_mul_f32_e64 v40, v44, v44
	v_mul_f32_e64 v41, v45, v45
	v_fma_f32 v54, v62, v46, v54
	v_fma_f32 v55, v63, v47, v55
	v_fma_f32 v40, v58, v58, v40
	v_fma_f32 v41, v59, v59, v41
	v_add_f32_e64 v62, v178, v54
	v_add_f32_e64 v63, v179, v55
	v_add_f32_e32 v92, v84, v48
	v_add_f32_e64 v62, v62, v55
	v_add_f32_e64 v63, v63, v54
	v_mfma_f32_32x32x2_f32 v[0:15], v83, v43, v[0:15]
	v_mul_f32_e64 v42, v46, v46
	v_mul_f32_e64 v43, v47, v47
	v_fma_f32 v42, v80, v80, v42
	v_fma_f32 v43, v81, v81, v43
	v_add_f32_e64 v56, v40, v42
	v_add_f32_e64 v57, v41, v43
	v_add_u32_e32 v40, 0x1e800, v70
	ds_read_b128 v[66:69], v40
	ds_read_b128 v[48:51], v71 offset:15616
	ds_read_b128 v[52:55], v71 offset:15632
	ds_read_b128 v[44:47], v71 offset:15648
	ds_read_b128 v[40:43], v71 offset:15664
	ds_read_b128 v[72:75], v71 offset:15792
	ds_read_b128 v[76:79], v71 offset:15776
	ds_read_b128 v[80:83], v71 offset:15760
	ds_read_b128 v[84:87], v71 offset:15744
	v_add_f32_e32 v58, v174, v56
	v_add_f32_e32 v59, v175, v57
	s_waitcnt lgkmcnt(8)
; #define P6_LDG(bi, grp) do { const int g_ = ((grp) < 32) ? (grp) : 31; _Pragma("unroll") for (int q = 0; q < 4; ++q) Xg[bi][q] = xp[2 * (4 * g_ + q)]; } while (0)
; #define P6_USE(bi, grp) do { _Pragma("unroll") for (int q = 0; q < 4; ++q) P6_STEP(Xg[bi][q], 4 * (grp) + q); } while (0)
; __global__ void __launch_bounds__(512, 2) hymba_fwd(Args args) {
;     ...
;             f32x4 Xg[3][4];
;     ...
;             P6_LDG(0, 0); P6_LDG(1, 1);
; #pragma nounroll
;             for (int gb = 0; gb < 30; gb += 3) {
;                 P6_LDG(2, gb + 2); P6_USE(0, gb);
;                 P6_LDG(0, gb + 3); P6_USE(1, gb + 1);
;                 P6_LDG(1, gb + 4); P6_USE(2, gb + 2);
;             }
;             P6_USE(0, 30); P6_USE(1, 31);
	v_mfma_f32_32x32x2_f32 v[0:15], v66, v32, v[0:15]
	v_mfma_f32_32x32x2_f32 v[0:15], v67, v33, v[0:15]
	v_mul_f32_e64 v66, v32, v32
	v_mul_f32_e64 v67, v33, v33
	v_mov_b32_e32 v32, v33
	v_mov_b32_e32 v33, v29
	v_mfma_f32_32x32x2_f32 v[0:15], v68, v34, v[0:15]
	v_mov_b32_e32 v34, v35
	v_mfma_f32_32x32x2_f32 v[0:15], v69, v35, v[0:15]
	v_pk_mov_b32 v[68:69], v[66:67], v[60:61] op_sel:[1,0]
	v_mov_b32_e32 v67, v61
	v_add_f32_e32 v60, v68, v66
	v_add_f32_e32 v61, v69, v67
	v_add_u32_e32 v66, 0x1ec00, v70
	ds_read_b128 v[66:69], v66
	v_mov_b32_e32 v35, v31
	s_waitcnt lgkmcnt(0)
	v_mfma_f32_32x32x2_f32 v[0:15], v66, v28, v[0:15]
	v_mov_b32_e32 v66, v48
	v_mfma_f32_32x32x2_f32 v[0:15], v67, v29, v[0:15]
	v_mov_b32_e32 v67, v84
	v_mov_b32_e32 v84, v49
	v_mfma_f32_32x32x2_f32 v[0:15], v68, v30, v[0:15]
	v_mov_b32_e32 v68, v52
	v_mfma_f32_32x32x2_f32 v[0:15], v69, v31, v[0:15]
	v_mov_b32_e32 v69, v80
	v_mov_b32_e32 v80, v53
	v_mul_f32_e64 v68, v68, v32
	v_mul_f32_e64 v69, v69, v33
	v_mul_f32_e64 v48, v80, v32
	v_mul_f32_e64 v49, v81, v33
	v_fma_f32 v66, v66, v88, v68
	v_fma_f32 v67, v67, v89, v69
	v_mov_b32_e32 v68, v44
	v_mov_b32_e32 v69, v76
	v_fma_f32 v48, v84, v88, v48
	v_fma_f32 v49, v85, v89, v49
	v_mov_b32_e32 v76, v45
	v_fma_f32 v66, v68, v90, v66
	v_fma_f32 v67, v69, v91, v67
	v_mov_b32_e32 v69, v72
	v_fma_f32 v44, v76, v90, v48
	v_fma_f32 v45, v77, v91, v49
	v_mov_b32_e32 v72, v41
	v_mov_b32_e32 v68, v40
	v_fma_f32 v40, v72, v34, v44
	v_fma_f32 v41, v73, v35, v45
	v_fma_f32 v66, v68, v34, v66
	v_fma_f32 v67, v69, v35, v67
	v_add_f32_e32 v44, v64, v40
	v_add_f32_e32 v45, v65, v41
	v_add_f32_e32 v62, v62, v66
	v_add_f32_e32 v63, v63, v67
	v_add_f32_e32 v68, v44, v41
	v_add_f32_e32 v69, v45, v40
	v_mov_b32_e32 v44, v54
	v_mov_b32_e32 v45, v82
	v_mov_b32_e32 v82, v55
	v_mov_b32_e32 v40, v50
	v_mov_b32_e32 v41, v86
	v_mul_f32_e32 v44, v44, v32
	v_mul_f32_e32 v45, v45, v33
	v_mov_b32_e32 v86, v51
	v_mul_f32_e32 v32, v82, v32
	v_mul_f32_e32 v33, v83, v33
	v_fma_f32 v40, v40, v88, v44
	v_fma_f32 v41, v41, v89, v45
	v_mov_b32_e32 v44, v46
	v_mov_b32_e32 v45, v78
	v_fma_f32 v32, v86, v88, v32
	v_fma_f32 v33, v87, v89, v33
	v_mov_b32_e32 v78, v47
	v_fma_f32 v40, v44, v90, v40
	v_fma_f32 v41, v45, v91, v41
	v_mov_b32_e32 v45, v74
	v_fma_f32 v32, v78, v90, v32
	v_fma_f32 v33, v79, v91, v33
	v_mov_b32_e32 v74, v43
	v_mov_b32_e32 v44, v42
	v_fma_f32 v32, v74, v34, v32
	v_fma_f32 v33, v75, v35, v33
	v_fma_f32 v40, v44, v34, v40
	v_fma_f32 v41, v45, v35, v41
	v_add_f32_e32 v32, v93, v32
	v_add_f32_e32 v40, v92, v40
	v_add_f32_e32 v73, v32, v33
	v_add_u32_e32 v32, 0x1f000, v70
	v_add_f32_e32 v72, v40, v41
	ds_read_b128 v[52:55], v32
	ds_read_b128 v[44:47], v71 offset:15872
	ds_read_b128 v[48:51], v71 offset:15888
	ds_read_b128 v[40:43], v71 offset:15904
	ds_read_b128 v[32:35], v71 offset:15920
	s_waitcnt vmcnt(3) lgkmcnt(4)
	v_mfma_f32_32x32x2_f32 v[0:15], v52, v36, v[0:15]
	v_pk_add_f32 v[66:67], v[62:63], v[66:67] op_sel:[0,1] op_sel_hi:[1,0]
	v_mul_f32_e32 v62, v37, v37
	v_mul_f32_e32 v63, v38, v38
	v_mul_f32_e32 v64, v39, v39
	v_add_u32_e32 v74, 0x1f400, v70
	s_waitcnt lgkmcnt(2)
	v_mov_b32_e32 v78, v48
	v_mov_b32_e32 v80, v38
	s_waitcnt vmcnt(2)
	v_mov_b32_e32 v81, v26
	v_mfma_f32_32x32x2_f32 v[0:15], v53, v37, v[0:15]
	v_add_f32_e64 v52, v58, v57
	v_add_f32_e64 v53, v59, v56
	v_mfma_f32_32x32x2_f32 v[0:15], v54, v38, v[0:15]
	v_mul_f32_e32 v54, v36, v36
	v_mov_b32_e32 v53, v54
	v_mov_b32_e32 v38, v39
	v_mfma_f32_32x32x2_f32 v[0:15], v55, v39, v[0:15]
	v_add_f32_e64 v54, v60, v61
	v_add_f32_e64 v55, v61, v60
	v_mov_b32_e32 v39, v27
	v_mov_b32_e32 v55, v62
	v_add_f32_e64 v52, v52, v54
	v_add_f32_e64 v53, v53, v55
	v_mul_f32_e32 v54, v29, v29
	v_fma_f32 v28, v28, v28, v54
	v_fma_f32 v29, v29, v29, v54
	v_mul_f32_e32 v54, v31, v31
	v_fma_f32 v30, v30, v30, v54
	v_fma_f32 v31, v31, v31, v54
	v_mov_b32_e32 v29, v63
	v_mov_b32_e32 v31, v64
	v_add_f32_e32 v28, v28, v30
	v_add_f32_e32 v29, v29, v31
	s_nop 0
	v_add_f32_e32 v64, v52, v28
	v_add_f32_e32 v65, v53, v29
	ds_read_b128 v[28:31], v71 offset:16048
	ds_read_b128 v[52:55], v71 offset:16032
	ds_read_b128 v[56:59], v71 offset:16016
	ds_read_b128 v[60:63], v71 offset:16000
	ds_read_b128 v[74:77], v74
	s_waitcnt lgkmcnt(0)
	v_mfma_f32_32x32x2_f32 v[0:15], v74, v24, v[0:15]
	v_mov_b32_e32 v79, v56
	v_mov_b32_e32 v56, v49
	v_mov_b32_e32 v74, v44
	v_mfma_f32_32x32x2_f32 v[0:15], v75, v25, v[0:15]
	v_mov_b32_e32 v75, v60
	v_mov_b32_e32 v60, v45
	v_mfma_f32_32x32x2_f32 v[0:15], v76, v26, v[0:15]
	v_mov_b32_e32 v76, v36
	v_mov_b32_e32 v36, v37
	v_mov_b32_e32 v37, v25
	v_mul_f32_e64 v78, v78, v36
	v_mul_f32_e64 v79, v79, v37
	v_mul_f32_e64 v44, v56, v36
	v_mul_f32_e64 v45, v57, v37
	v_add_u32_e32 v56, 0x1fc00, v70
	v_mfma_f32_32x32x2_f32 v[0:15], v77, v27, v[0:15]
	v_mov_b32_e32 v77, v24
	v_fma_f32 v74, v74, v76, v78
	v_fma_f32 v75, v75, v77, v79
	v_mov_b32_e32 v78, v40
	v_mov_b32_e32 v79, v52
	v_fma_f32 v44, v60, v76, v44
	v_fma_f32 v45, v61, v77, v45
	v_mov_b32_e32 v52, v41
	v_fma_f32 v74, v78, v80, v74
	v_fma_f32 v75, v79, v81, v75
	v_mov_b32_e32 v79, v28
	v_fma_f32 v40, v52, v80, v44
	v_fma_f32 v41, v53, v81, v45
	v_mov_b32_e32 v28, v33
	v_fma_f32 v28, v28, v38, v40
	v_fma_f32 v29, v29, v39, v41
	v_mov_b32_e32 v78, v32
	v_add_f32_e32 v32, v68, v28
	v_add_f32_e32 v33, v69, v29
	v_mul_f32_e32 v26, v26, v26
	v_mul_f32_e32 v27, v27, v27
	v_add_f32_e32 v60, v32, v29
	v_add_f32_e32 v61, v33, v28
	v_mov_b32_e32 v32, v50
	v_mov_b32_e32 v33, v58
	v_mov_b32_e32 v28, v46
	v_mov_b32_e32 v29, v62
	v_mul_f32_e32 v32, v32, v36
	v_mul_f32_e32 v33, v33, v37
	v_mov_b32_e32 v58, v51
	v_fma_f32 v28, v28, v76, v32
	v_fma_f32 v29, v29, v77, v33
	v_mov_b32_e32 v32, v42
	v_mov_b32_e32 v33, v54
	v_fma_f32 v28, v32, v80, v28
	v_fma_f32 v29, v33, v81, v29
	v_mov_b32_e32 v32, v34
	v_mov_b32_e32 v33, v30
	v_fma_f32 v28, v32, v38, v28
	v_fma_f32 v29, v33, v39, v29
	v_mov_b32_e32 v62, v47
	v_add_f32_e32 v28, v72, v28
	v_add_f32_e32 v68, v28, v29
	v_mul_f32_e32 v28, v58, v36
	v_mul_f32_e32 v29, v59, v37
	v_mov_b32_e32 v54, v43
	v_fma_f32 v28, v62, v76, v28
	v_fma_f32 v29, v63, v77, v29
	v_mov_b32_e32 v30, v35
	v_fma_f32 v28, v54, v80, v28
	v_fma_f32 v29, v55, v81, v29
	v_mul_f32_e32 v24, v24, v24
	v_mul_f32_e32 v25, v25, v25
	v_fma_f32 v28, v30, v38, v28
	v_fma_f32 v29, v31, v39, v29
	v_fma_f32 v74, v78, v38, v74
	v_fma_f32 v75, v79, v39, v75
	v_add_f32_e32 v28, v73, v28
	v_add_f32_e32 v62, v28, v29
	v_pk_mov_b32 v[28:29], v[24:25], v[26:27] op_sel:[1,0]
	v_mov_b32_e32 v25, v27
	v_add_f32_e32 v58, v28, v24
	v_add_f32_e32 v59, v29, v25
	v_add_u32_e32 v24, 0x1f800, v70
	ds_read_b128 v[40:43], v24
	ds_read_b128 v[24:27], v71 offset:16128
	ds_read_b128 v[28:31], v71 offset:16144
	ds_read_b128 v[36:39], v71 offset:16160
	ds_read_b128 v[32:35], v71 offset:16176
	s_waitcnt vmcnt(1) lgkmcnt(4)
; #define P6_USE(bi, grp) do { _Pragma("unroll") for (int q = 0; q < 4; ++q) P6_STEP(Xg[bi][q], 4 * (grp) + q); } while (0)
; #define XSUM(v) do { auto rr_ = __builtin_amdgcn_permlane32_swap(__float_as_uint(v), __float_as_uint(v), false, false); v = __uint_as_float(rr_[0]) + __uint_as_float(rr_[1]); } while (0)
; __global__ void __launch_bounds__(512, 2) hymba_fwd(Args args) {
;     ...
;             P6_USE(0, 30); P6_USE(1, 31);
;     ...
;             XSUM(ssq); XSUM(gl0); XSUM(gl1); XSUM(gl2); XSUM(gl3);
;     ...
;             const float rstd = 1.0f / sqrtf(ssq * (1.0f / DM) + EPS);
;             { float lg0 = rstd * gl0 + biasL[0], lg1 = rstd * gl1 + biasL[1], lg2 = rstd * gl2 + biasL[2], lg3 = rstd * gl3 + biasL[3];
	v_mfma_f32_32x32x2_f32 v[0:15], v40, v16, v[0:15]
	v_add_f32_e64 v66, v66, v74
	v_add_f32_e64 v67, v67, v75
	v_mov_b32_e32 v76, v18
	v_add_f32_e64 v66, v66, v75
	v_add_f32_e64 v67, v67, v74
	v_mov_b32_e32 v74, v17
	s_waitcnt vmcnt(0)
	v_mov_b32_e32 v75, v21
	v_mov_b32_e32 v77, v22
	v_mov_b32_e32 v78, v19
	v_mov_b32_e32 v79, v23
	v_mfma_f32_32x32x2_f32 v[0:15], v41, v17, v[0:15]
	v_mfma_f32_32x32x2_f32 v[0:15], v42, v18, v[0:15]
	v_mfma_f32_32x32x2_f32 v[0:15], v43, v19, v[0:15]
	ds_read_b128 v[40:43], v71 offset:16304
	ds_read_b128 v[44:47], v71 offset:16288
	ds_read_b128 v[48:51], v71 offset:16272
	ds_read_b128 v[52:55], v71 offset:16256
	ds_read_b128 v[70:73], v56
	s_waitcnt lgkmcnt(8)
	v_mov_b32_e32 v56, v24
	s_waitcnt lgkmcnt(1)
	v_mov_b32_e32 v57, v52
	v_mov_b32_e32 v52, v25
	s_waitcnt lgkmcnt(0)
	v_mfma_f32_32x32x2_f32 v[0:15], v70, v20, v[0:15]
	v_mov_b32_e32 v70, v16
	v_mfma_f32_32x32x2_f32 v[0:15], v71, v21, v[0:15]
	v_mov_b32_e32 v71, v20
	v_mfma_f32_32x32x2_f32 v[0:15], v72, v22, v[0:15]
	v_mov_b32_e32 v72, v28
	v_mfma_f32_32x32x2_f32 v[0:15], v73, v23, v[0:15]
	v_mov_b32_e32 v73, v48
	v_mov_b32_e32 v48, v29
	v_mul_f32_e64 v72, v72, v74
	v_mul_f32_e64 v73, v73, v75
	v_mul_f32_e64 v24, v48, v74
	v_mul_f32_e64 v25, v49, v75
	v_fma_f32 v56, v56, v70, v72
	v_fma_f32 v57, v57, v71, v73
	v_mov_b32_e32 v72, v36
	v_mov_b32_e32 v73, v44
	v_fma_f32 v24, v52, v70, v24
	v_fma_f32 v25, v53, v71, v25
	v_mov_b32_e32 v44, v37
	v_fma_f32 v56, v72, v76, v56
	v_fma_f32 v57, v73, v77, v57
	v_mov_b32_e32 v73, v40
	v_fma_f32 v24, v44, v76, v24
	v_fma_f32 v25, v45, v77, v25
	v_mov_b32_e32 v40, v33
	v_fma_f32 v24, v40, v78, v24
	v_fma_f32 v25, v41, v79, v25
	v_mov_b32_e32 v72, v32
	v_add_f32_e32 v28, v60, v24
	v_add_f32_e32 v29, v61, v25
	v_mov_b32_e32 v32, v30
	v_mov_b32_e32 v33, v50
	v_mov_b32_e32 v50, v31
	v_pk_add_f32 v[24:25], v[28:29], v[24:25] op_sel:[0,1] op_sel_hi:[1,0]
	v_mov_b32_e32 v28, v26
	v_mov_b32_e32 v29, v54
	v_mul_f32_e32 v32, v32, v74
	v_mul_f32_e32 v33, v33, v75
	v_mov_b32_e32 v54, v27
	v_mul_f32_e32 v26, v50, v74
	v_mul_f32_e32 v27, v51, v75
	v_fma_f32 v28, v28, v70, v32
	v_fma_f32 v29, v29, v71, v33
	v_mov_b32_e32 v32, v38
	v_mov_b32_e32 v33, v46
	v_fma_f32 v26, v54, v70, v26
	v_fma_f32 v27, v55, v71, v27
	v_mov_b32_e32 v46, v39
	v_fma_f32 v28, v32, v76, v28
	v_fma_f32 v29, v33, v77, v29
	v_mov_b32_e32 v32, v34
	v_mov_b32_e32 v33, v42
	v_fma_f32 v26, v46, v76, v26
	v_fma_f32 v27, v47, v77, v27
	v_mov_b32_e32 v42, v35
	v_fma_f32 v28, v32, v78, v28
	v_fma_f32 v29, v33, v79, v29
	v_fma_f32 v26, v42, v78, v26
	v_fma_f32 v27, v43, v79, v27
	v_add_f32_e32 v25, v68, v28
	v_add_f32_e32 v26, v62, v26
	v_add_f32_e32 v25, v25, v29
	v_add_f32_e32 v26, v26, v27
	v_mul_f32_e32 v27, v20, v20
	v_mul_f32_e32 v28, v21, v21
	v_mul_f32_e32 v29, v22, v22
	v_mul_f32_e32 v30, v23, v23
	v_add_f32_e32 v20, v64, v65
	v_add_f32_e32 v21, v65, v64
	v_add_f32_e32 v22, v58, v59
	v_add_f32_e32 v23, v59, v58
	v_mov_b32_e32 v21, v27
	v_mov_b32_e32 v23, v28
	v_add_f32_e32 v20, v20, v22
	v_add_f32_e32 v21, v21, v23
	v_mul_f32_e32 v22, v17, v17
	v_fma_f32 v16, v16, v16, v22
	v_fma_f32 v17, v17, v17, v22
	v_mul_f32_e32 v22, v19, v19
	v_fma_f32 v18, v18, v18, v22
	v_fma_f32 v19, v19, v19, v22
	v_mov_b32_e32 v17, v29
	v_mov_b32_e32 v19, v30
	v_add_f32_e32 v16, v16, v18
	v_add_f32_e32 v17, v17, v19
	v_mov_b32_e32 v19, v25
	v_add_f32_e32 v16, v20, v16
	v_add_f32_e32 v17, v21, v17
	s_nop 0
	v_permlane32_swap_b32_e32 v25, v19
	v_pk_add_f32 v[16:17], v[16:17], v[16:17] op_sel:[0,1] op_sel_hi:[1,0]
	v_add_f32_e32 v22, v25, v19
	v_mov_b32_e32 v17, v16
	s_nop 1
	v_permlane32_swap_b32_e32 v16, v17
	v_add_f32_e32 v18, v16, v17
	v_mov_b32_e32 v19, v26
	s_nop 1
	v_permlane32_swap_b32_e32 v26, v19
	v_fmamk_f32 v18, v18, 0x3a800000, v187
	v_add_f32_e32 v23, v26, v19
	v_cmp_gt_f32_e32 vcc, s8, v18
	v_mul_f32_e32 v19, 0x4f800000, v18
	v_fma_f32 v56, v72, v78, v56
	v_fma_f32 v57, v73, v79, v57
	v_cndmask_b32_e32 v18, v18, v19, vcc
	v_sqrt_f32_e32 v19, v18
	v_add_f32_e32 v66, v66, v56
	v_add_f32_e32 v67, v67, v57
	v_mov_b32_e32 v17, v24
	v_pk_add_f32 v[56:57], v[66:67], v[56:57] op_sel:[0,1] op_sel_hi:[1,0]
	v_add_u32_e32 v20, -1, v19
	v_fma_f32 v21, -v20, v19, v18
	v_cmp_ge_f32_e64 s[8:9], 0, v21
	v_add_u32_e32 v21, 1, v19
	v_mov_b32_e32 v16, v56
	v_cndmask_b32_e64 v20, v19, v20, s[8:9]
	v_fma_f32 v19, -v21, v19, v18
	v_cmp_lt_f32_e64 s[8:9], 0, v19
	v_permlane32_swap_b32_e32 v24, v17
	s_nop 0
	v_cndmask_b32_e64 v19, v20, v21, s[8:9]
	v_mul_f32_e32 v20, 0x37800000, v19
	v_cndmask_b32_e32 v19, v19, v20, vcc
	v_cmp_class_f32_e32 vcc, v18, v189
	v_permlane32_swap_b32_e32 v56, v16
	s_nop 0
	v_cndmask_b32_e32 v18, v19, v18, vcc
	v_div_scale_f32 v19, s[8:9], v18, v18, 1.0
	v_rcp_f32_e32 v20, v19
	v_mov_b32_e32 v57, v24
	s_add_i32 s8, 0, 0x25900
	v_fma_f32 v21, -v19, v20, 1.0
	v_fmac_f32_e32 v20, v21, v20
	v_div_scale_f32 v21, vcc, 1.0, v18, 1.0
	v_mul_f32_e32 v25, v21, v20
	v_fma_f32 v26, -v19, v25, v21
	v_fmac_f32_e32 v25, v26, v20
	v_fma_f32 v19, -v19, v25, v21
	v_div_fmas_f32 v19, v19, v20, v25
	v_add_f32_e32 v20, v56, v16
	v_add_f32_e32 v21, v57, v17
	v_mov_b32_e32 v16, s8
	v_div_fixup_f32 v80, v19, v18, 1.0
	ds_read_b128 v[16:19], v16
	s_waitcnt lgkmcnt(0)
; __global__ void __launch_bounds__(512, 2) hymba_fwd(Args args) {
;     ...
;             { float lg0 = rstd * gl0 + biasL[0], lg1 = rstd * gl1 + biasL[1], lg2 = rstd * gl2 + biasL[2], lg3 = rstd * gl3 + biasL[3];
;               int gi = 0; float gm = lg0; if (lg1 > gm) { gm = lg1; gi = 1; } if (lg2 > gm) { gm = lg2; gi = 2; } if (lg3 > gm) { gm = lg3; gi = 3; }
;               const float gprob = 1.0f / (expf(lg0 - gm) + expf(lg1 - gm) + expf(lg2 - gm) + expf(lg3 - gm));
;               float mine[4], oth[4];
; #pragma unroll
;               for (int q = 0; q < 4; ++q) { const float c = (gi == 0) ? acc[q] : (gi == 1) ? acc[4 + q] : (gi == 2) ? acc[8 + q] : acc[12 + q];
;                   mine[q] = rstd * c + biasL[4 + gi * 8 + khalf * 4 + q];
;                   auto rr_ = __builtin_amdgcn_permlane32_swap(__float_as_uint(mine[q]), __float_as_uint(mine[q]), false, false);
;                   oth[q] = khalf ? __uint_as_float(rr_[0]) : __uint_as_float(rr_[1]); }
;               float es[8];
; #pragma unroll
;               for (int j = 0; j < 8; ++j) es[j] = ((j >> 2) == khalf) ? mine[j & 3] : oth[j & 3];
	v_fma_f32 v16, v20, v80, v16
	v_fma_f32 v17, v21, v80, v17
	s_nop 0
	v_cmp_gt_f32_e32 vcc, v17, v16
	v_fma_f32 v24, v22, v80, v18
	v_fmac_f32_e32 v19, v80, v23
	v_cndmask_b32_e32 v18, v16, v17, vcc
	v_cndmask_b32_e64 v20, 0, 1, vcc
	v_cmp_gt_f32_e32 vcc, v24, v18
	v_lshlrev_b32_e32 v21, 4, v172
	s_nop 0
	v_cndmask_b32_e32 v25, v18, v24, vcc
	v_cndmask_b32_e64 v18, v20, 2, vcc
	v_cmp_gt_f32_e32 vcc, v19, v25
	s_nop 1
	v_cndmask_b32_e64 v18, v18, 3, vcc
	v_lshlrev_b32_e32 v29, 2, v18
	v_lshlrev_b32_e32 v20, 5, v18
	v_cmp_eq_u32_e64 s[10:11], 1, v29
	v_add3_u32 v20, s8, v20, v21
	v_cmp_gt_u32_e64 s[8:9], 32, v171
	v_cndmask_b32_e64 v21, v0, v1, s[10:11]
	v_cmp_eq_u32_e64 s[10:11], 2, v29
	s_nop 1
	v_cndmask_b32_e64 v21, v21, v2, s[10:11]
	v_cmp_eq_u32_e64 s[10:11], 3, v29
	s_nop 1
	v_cndmask_b32_e64 v21, v21, v3, s[10:11]
	v_cmp_eq_u32_e64 s[10:11], 4, v29
	s_nop 1
	v_cndmask_b32_e64 v21, v21, v4, s[10:11]
	v_cmp_eq_u32_e64 s[10:11], 5, v29
	s_nop 1
	v_cndmask_b32_e64 v21, v21, v5, s[10:11]
	v_cmp_eq_u32_e64 s[10:11], 6, v29
	s_nop 1
	v_cndmask_b32_e64 v21, v21, v6, s[10:11]
	v_cmp_eq_u32_e64 s[10:11], 7, v29
	s_nop 1
	v_cndmask_b32_e64 v21, v21, v7, s[10:11]
	v_cmp_eq_u32_e64 s[10:11], 8, v29
	s_nop 1
	v_cndmask_b32_e64 v21, v21, v8, s[10:11]
	v_cmp_eq_u32_e64 s[10:11], 9, v29
	s_nop 1
	v_cndmask_b32_e64 v21, v21, v9, s[10:11]
	v_cmp_eq_u32_e64 s[10:11], 10, v29
	s_nop 1
	v_cndmask_b32_e64 v21, v21, v10, s[10:11]
	v_cmp_eq_u32_e64 s[10:11], 11, v29
	s_nop 1
	v_cndmask_b32_e64 v21, v21, v11, s[10:11]
	v_cmp_eq_u32_e64 s[10:11], 12, v29
	s_nop 1
	v_cndmask_b32_e64 v21, v21, v12, s[10:11]
	v_cmp_eq_u32_e64 s[10:11], 13, v29
	s_nop 1
	v_cndmask_b32_e64 v21, v21, v13, s[10:11]
	v_cmp_eq_u32_e64 s[10:11], 14, v29
	s_nop 1
	v_cndmask_b32_e64 v21, v21, v14, s[10:11]
	v_cmp_eq_u32_e64 s[10:11], 15, v29
	s_nop 1
	v_cndmask_b32_e64 v26, v21, v15, s[10:11]
	ds_read_b128 v[20:23], v20 offset:16
	s_waitcnt lgkmcnt(0)
	v_fma_f32 v20, v80, v26, v20
	v_mov_b32_e32 v26, v20
	v_mov_b32_e32 v27, v20
	s_nop 1
	v_permlane32_swap_b32_e32 v26, v27
	v_cndmask_b32_e64 v26, v26, v27, s[8:9]
	v_or_b32_e32 v27, 1, v29
	v_cmp_eq_u32_e64 s[10:11], 1, v27
	s_nop 1
	v_cndmask_b32_e64 v28, v0, v1, s[10:11]
	v_cmp_eq_u32_e64 s[10:11], 2, v27
	s_nop 1
	v_cndmask_b32_e64 v28, v28, v2, s[10:11]
	v_cmp_eq_u32_e64 s[10:11], 3, v27
	s_nop 1
	v_cndmask_b32_e64 v28, v28, v3, s[10:11]
	v_cmp_eq_u32_e64 s[10:11], 4, v27
	s_nop 1
	v_cndmask_b32_e64 v28, v28, v4, s[10:11]
	v_cmp_eq_u32_e64 s[10:11], 5, v27
	s_nop 1
	v_cndmask_b32_e64 v28, v28, v5, s[10:11]
	v_cmp_eq_u32_e64 s[10:11], 6, v27
	s_nop 1
	v_cndmask_b32_e64 v28, v28, v6, s[10:11]
	v_cmp_eq_u32_e64 s[10:11], 7, v27
	s_nop 1
	v_cndmask_b32_e64 v28, v28, v7, s[10:11]
	v_cmp_eq_u32_e64 s[10:11], 8, v27
	s_nop 1
	v_cndmask_b32_e64 v28, v28, v8, s[10:11]
	v_cmp_eq_u32_e64 s[10:11], 9, v27
	s_nop 1
	v_cndmask_b32_e64 v28, v28, v9, s[10:11]
	v_cmp_eq_u32_e64 s[10:11], 10, v27
	s_nop 1
	v_cndmask_b32_e64 v28, v28, v10, s[10:11]
	v_cmp_eq_u32_e64 s[10:11], 11, v27
	s_nop 1
	v_cndmask_b32_e64 v28, v28, v11, s[10:11]
	v_cmp_eq_u32_e64 s[10:11], 12, v27
	s_nop 1
	v_cndmask_b32_e64 v28, v28, v12, s[10:11]
	v_cmp_eq_u32_e64 s[10:11], 13, v27
	s_nop 1
	v_cndmask_b32_e64 v28, v28, v13, s[10:11]
	v_cmp_eq_u32_e64 s[10:11], 14, v27
	s_nop 1
	v_cndmask_b32_e64 v28, v28, v14, s[10:11]
	v_cmp_eq_u32_e64 s[10:11], 15, v27
	s_nop 1
	v_cndmask_b32_e64 v27, v28, v15, s[10:11]
	v_fma_f32 v21, v80, v27, v21
	v_mov_b32_e32 v27, v21
	v_mov_b32_e32 v28, v21
	s_nop 1
	v_permlane32_swap_b32_e32 v27, v28
	v_cndmask_b32_e64 v27, v27, v28, s[8:9]
	v_or_b32_e32 v28, 2, v29
	v_cmp_eq_u32_e64 s[10:11], 1, v28
	v_or_b32_e32 v29, 3, v29
	s_nop 0
	v_cndmask_b32_e64 v30, v0, v1, s[10:11]
	v_cmp_eq_u32_e64 s[10:11], 2, v28
	s_nop 1
	v_cndmask_b32_e64 v30, v30, v2, s[10:11]
	v_cmp_eq_u32_e64 s[10:11], 3, v28
	s_nop 1
	v_cndmask_b32_e64 v30, v30, v3, s[10:11]
	v_cmp_eq_u32_e64 s[10:11], 4, v28
	s_nop 1
	v_cndmask_b32_e64 v30, v30, v4, s[10:11]
	v_cmp_eq_u32_e64 s[10:11], 5, v28
	s_nop 1
	v_cndmask_b32_e64 v30, v30, v5, s[10:11]
	v_cmp_eq_u32_e64 s[10:11], 6, v28
	s_nop 1
	v_cndmask_b32_e64 v30, v30, v6, s[10:11]
	v_cmp_eq_u32_e64 s[10:11], 7, v28
	s_nop 1
	v_cndmask_b32_e64 v30, v30, v7, s[10:11]
	v_cmp_eq_u32_e64 s[10:11], 8, v28
	s_nop 1
	v_cndmask_b32_e64 v30, v30, v8, s[10:11]
	v_cmp_eq_u32_e64 s[10:11], 9, v28
	s_nop 1
	v_cndmask_b32_e64 v30, v30, v9, s[10:11]
	v_cmp_eq_u32_e64 s[10:11], 10, v28
	s_nop 1
	v_cndmask_b32_e64 v30, v30, v10, s[10:11]
	v_cmp_eq_u32_e64 s[10:11], 11, v28
	s_nop 1
	v_cndmask_b32_e64 v30, v30, v11, s[10:11]
	v_cmp_eq_u32_e64 s[10:11], 12, v28
	s_nop 1
	v_cndmask_b32_e64 v30, v30, v12, s[10:11]
	v_cmp_eq_u32_e64 s[10:11], 13, v28
	s_nop 1
	v_cndmask_b32_e64 v30, v30, v13, s[10:11]
	v_cmp_eq_u32_e64 s[10:11], 14, v28
	s_nop 1
	v_cndmask_b32_e64 v30, v30, v14, s[10:11]
	v_cmp_eq_u32_e64 s[10:11], 15, v28
	s_nop 1
	v_cndmask_b32_e64 v28, v30, v15, s[10:11]
	v_cmp_eq_u32_e64 s[10:11], 1, v29
	v_fma_f32 v22, v80, v28, v22
	v_mov_b32_e32 v28, v22
	v_cndmask_b32_e64 v0, v0, v1, s[10:11]
	v_cmp_eq_u32_e64 s[10:11], 2, v29
	v_mov_b32_e32 v30, v22
	s_nop 1
	v_permlane32_swap_b32_e32 v28, v30
	v_cndmask_b32_e64 v0, v0, v2, s[10:11]
	v_cmp_eq_u32_e64 s[10:11], 3, v29
	v_cndmask_b32_e64 v28, v28, v30, s[8:9]
	s_nop 0
	v_cndmask_b32_e64 v0, v0, v3, s[10:11]
	v_cmp_eq_u32_e64 s[10:11], 4, v29
	v_cndmask_b32_e64 v3, v26, v20, s[8:9]
	s_nop 0
	v_cndmask_b32_e64 v0, v0, v4, s[10:11]
	v_cmp_eq_u32_e64 s[10:11], 5, v29
	v_cndmask_b32_e64 v4, v27, v21, s[8:9]
	v_cmp_gt_f32_e64 s[12:13], v4, v3
	v_cndmask_b32_e64 v0, v0, v5, s[10:11]
	v_cmp_eq_u32_e64 s[10:11], 6, v29
; __global__ void __launch_bounds__(512, 2) hymba_fwd(Args args) {
;     ...
;               for (int j = 0; j < 8; ++j) es[j] = ((j >> 2) == khalf) ? mine[j & 3] : oth[j & 3];
;               int i0 = 0; float l0 = es[0];
; #pragma unroll
;               for (int j = 1; j < 8; ++j) if (es[j] > l0) { l0 = es[j]; i0 = j; }
;               int i1 = -1; float l1 = -3.0e38f;
; #pragma unroll
;               for (int j = 0; j < 8; ++j) if (j != i0 && (i1 < 0 || es[j] > l1)) { l1 = es[j]; i1 = j; }
;               const float ex = expf(l1 - l0); const float w0 = gprob / (1.0f + ex), w1 = gprob * ex / (1.0f + ex);
	v_cndmask_b32_e64 v5, v28, v22, s[8:9]
	v_cndmask_b32_e64 v2, 0, 1, s[12:13]
	v_cndmask_b32_e64 v0, v0, v6, s[10:11]
	v_cmp_eq_u32_e64 s[10:11], 7, v29
	s_nop 1
	v_cndmask_b32_e64 v0, v0, v7, s[10:11]
	v_cmp_eq_u32_e64 s[10:11], 8, v29
	s_nop 1
	v_cndmask_b32_e64 v0, v0, v8, s[10:11]
	v_cmp_eq_u32_e64 s[10:11], 9, v29
	s_nop 1
	v_cndmask_b32_e64 v0, v0, v9, s[10:11]
	v_cmp_eq_u32_e64 s[10:11], 10, v29
	s_nop 1
	v_cndmask_b32_e64 v0, v0, v10, s[10:11]
	v_cmp_eq_u32_e64 s[10:11], 11, v29
	s_nop 1
	v_cndmask_b32_e64 v0, v0, v11, s[10:11]
	v_cmp_eq_u32_e64 s[10:11], 12, v29
	s_nop 1
	v_cndmask_b32_e64 v0, v0, v12, s[10:11]
	v_cmp_eq_u32_e64 s[10:11], 13, v29
	s_nop 1
	v_cndmask_b32_e64 v0, v0, v13, s[10:11]
	v_cmp_eq_u32_e64 s[10:11], 14, v29
	s_nop 1
	v_cndmask_b32_e64 v0, v0, v14, s[10:11]
	v_cmp_eq_u32_e64 s[10:11], 15, v29
	s_nop 1
	v_cndmask_b32_e64 v0, v0, v15, s[10:11]
	v_fmac_f32_e32 v23, v80, v0
	v_mov_b32_e32 v0, v23
	v_mov_b32_e32 v1, v23
	s_nop 1
	v_permlane32_swap_b32_e32 v0, v1
	v_cndmask_b32_e64 v0, v0, v1, s[8:9]
	v_cmp_eq_u32_e64 s[10:11], 1, v172
	v_cndmask_b32_e64 v6, v0, v23, s[8:9]
	s_nop 0
	v_cndmask_b32_e64 v1, v0, v23, s[10:11]
	v_cndmask_b32_e64 v0, v3, v4, s[12:13]
	v_cndmask_b32_e64 v7, v26, v20, s[10:11]
	v_cndmask_b32_e64 v8, v27, v21, s[10:11]
	v_cndmask_b32_e64 v9, v28, v22, s[10:11]
	v_cmp_gt_f32_e64 s[10:11], v5, v0
	s_nop 1
	v_cndmask_b32_e64 v0, v0, v5, s[10:11]
	v_cndmask_b32_e64 v2, v2, 2, s[10:11]
	v_cmp_gt_f32_e64 s[10:11], v6, v0
	s_nop 1
	v_cndmask_b32_e64 v0, v0, v6, s[10:11]
	v_cndmask_b32_e64 v2, v2, 3, s[10:11]
	v_cmp_gt_f32_e64 s[10:11], v7, v0
	s_nop 1
	v_cndmask_b32_e64 v0, v0, v7, s[10:11]
	v_cndmask_b32_e64 v2, v2, 4, s[10:11]
	v_cmp_gt_f32_e64 s[10:11], v8, v0
	s_nop 1
	v_cndmask_b32_e64 v0, v0, v8, s[10:11]
	v_cmp_gt_f32_e64 s[14:15], v9, v0
	v_cndmask_b32_e64 v10, v2, 5, s[10:11]
	s_nop 0
	v_cndmask_b32_e64 v2, v0, v9, s[14:15]
	v_cndmask_b32_e64 v0, v10, 6, s[14:15]
	v_cmp_ngt_f32_e64 s[10:11], v1, v2
	s_nop 1
	v_cndmask_b32_e64 v0, 7, v0, s[10:11]
	v_cmp_eq_u32_e64 s[16:17], 0, v0
	v_cmp_ne_u32_e64 s[18:19], 1, v0
	s_or_b64 s[12:13], s[16:17], s[12:13]
	s_and_b64 s[12:13], s[18:19], s[12:13]
	v_cndmask_b32_e64 v3, v3, v4, s[12:13]
	v_cmp_gt_f32_e64 s[16:17], v5, v3
	v_cndmask_b32_e64 v4, 0, 1, s[12:13]
	v_cmp_eq_u32_e64 s[12:13], 2, v0
	v_cndmask_b32_e64 v5, v3, v5, s[16:17]
	v_cndmask_b32_e64 v10, v4, 2, s[16:17]
	v_cndmask_b32_e64 v3, v5, v3, s[12:13]
	v_cmp_gt_f32_e64 s[16:17], v6, v3
	v_cndmask_b32_e64 v4, v10, v4, s[12:13]
	v_cmp_eq_u32_e64 s[12:13], 3, v0
	v_cndmask_b32_e64 v3, v3, v6, s[16:17]
	v_cndmask_b32_e64 v4, v4, 3, s[16:17]
	v_cndmask_b32_e64 v5, v3, v5, s[12:13]
	v_cmp_gt_f32_e64 s[16:17], v7, v5
	v_cndmask_b32_e64 v6, v4, v10, s[12:13]
	v_cmp_eq_u32_e64 s[12:13], 4, v0
	v_cndmask_b32_e64 v5, v5, v7, s[16:17]
	v_cndmask_b32_e64 v6, v6, 4, s[16:17]
	v_cndmask_b32_e64 v3, v5, v3, s[12:13]
	v_cmp_gt_f32_e64 s[16:17], v8, v3
	v_cndmask_b32_e64 v4, v6, v4, s[12:13]
	v_cmp_eq_u32_e64 s[12:13], 5, v0
	v_cndmask_b32_e64 v5, v3, v8, s[16:17]
	v_cndmask_b32_e64 v6, v4, 5, s[16:17]
	v_cndmask_b32_e64 v3, v5, v3, s[12:13]
	v_cndmask_b32_e64 v5, v6, v4, s[12:13]
	s_and_b64 s[12:13], s[10:11], s[14:15]
	v_cmp_gt_f32_e64 s[14:15], v9, v3
	s_nop 1
	v_cndmask_b32_e64 v4, v3, v9, s[14:15]
	v_cndmask_b32_e64 v6, v5, 6, s[14:15]
	v_cndmask_b32_e64 v4, v4, v3, s[12:13]
	v_cndmask_b32_e64 v3, v6, v5, s[12:13]
	s_and_saveexec_b64 s[16:17], s[10:11]
	v_cmp_gt_i32_e64 s[12:13], 0, v3
	v_cmp_gt_f32_e64 s[14:15], v1, v4
	s_or_b64 s[12:13], s[12:13], s[14:15]
	v_cndmask_b32_e64 v4, v4, v1, s[12:13]
	v_cndmask_b32_e64 v3, v3, 7, s[12:13]
	s_or_b64 exec, exec, s[16:17]
	s_and_saveexec_b64 s[12:13], s[8:9]
	s_cbranch_execz .LBB0_876
	v_cndmask_b32_e32 v5, v25, v19, vcc
	v_sub_f32_e32 v6, v16, v5
	v_mul_f32_e32 v7, 0x3fb8aa3b, v6
	v_fma_f32 v8, v6, s4, -v7
	v_rndne_f32_e32 v9, v7
	v_fmac_f32_e32 v8, 0x32a5705f, v6
	v_sub_f32_e32 v7, v7, v9
	v_add_f32_e32 v7, v7, v8
	v_exp_f32_e32 v7, v7
	v_cvt_i32_f32_e32 v8, v9
	v_cmp_ngt_f32_e32 vcc, s5, v6
	v_cndmask_b32_e64 v1, v1, v2, s[10:11]
	v_sub_f32_e32 v1, v4, v1
	v_ldexp_f32 v7, v7, v8
	v_cndmask_b32_e32 v7, 0, v7, vcc
	v_cmp_nlt_f32_e32 vcc, s22, v6
	v_mul_f32_e32 v2, 0x3fb8aa3b, v1
	v_fma_f32 v4, v1, s4, -v2
	v_cndmask_b32_e32 v6, v213, v7, vcc
	v_sub_f32_e32 v7, v17, v5
	v_mul_f32_e32 v8, 0x3fb8aa3b, v7
	v_fma_f32 v9, v7, s4, -v8
	v_rndne_f32_e32 v10, v8
	v_fmac_f32_e32 v9, 0x32a5705f, v7
	v_sub_f32_e32 v8, v8, v10
	v_add_f32_e32 v8, v8, v9
	v_exp_f32_e32 v8, v8
	v_cvt_i32_f32_e32 v9, v10
	v_cmp_ngt_f32_e32 vcc, s5, v7
	v_fmac_f32_e32 v4, 0x32a5705f, v1
	v_ldexp_f32 v8, v8, v9
	v_cndmask_b32_e32 v8, 0, v8, vcc
	v_cmp_nlt_f32_e32 vcc, s22, v7
	s_nop 1
	v_cndmask_b32_e32 v7, v213, v8, vcc
	v_add_f32_e32 v6, v6, v7
	v_sub_f32_e32 v7, v24, v5
	v_mul_f32_e32 v8, 0x3fb8aa3b, v7
	v_fma_f32 v9, v7, s4, -v8
	v_rndne_f32_e32 v10, v8
	v_fmac_f32_e32 v9, 0x32a5705f, v7
	v_sub_f32_e32 v8, v8, v10
	v_add_f32_e32 v8, v8, v9
	v_exp_f32_e32 v8, v8
	v_cvt_i32_f32_e32 v9, v10
	v_cmp_ngt_f32_e32 vcc, s5, v7
	v_sub_f32_e32 v5, v19, v5
	v_ldexp_f32 v8, v8, v9
	v_cndmask_b32_e32 v8, 0, v8, vcc
	v_cmp_nlt_f32_e32 vcc, s22, v7
	s_nop 1
	v_cndmask_b32_e32 v7, v213, v8, vcc
	v_add_f32_e32 v6, v7, v6
	v_mul_f32_e32 v7, 0x3fb8aa3b, v5
	v_fma_f32 v8, v5, s4, -v7
	v_rndne_f32_e32 v9, v7
	v_fmac_f32_e32 v8, 0x32a5705f, v5
	v_sub_f32_e32 v7, v7, v9
	v_add_f32_e32 v7, v7, v8
	v_exp_f32_e32 v7, v7
	v_cvt_i32_f32_e32 v8, v9
	v_cmp_ngt_f32_e32 vcc, s5, v5
	v_ldexp_f32 v7, v7, v8
	s_nop 0
	v_cndmask_b32_e32 v7, 0, v7, vcc
	v_cmp_nlt_f32_e32 vcc, s22, v5
	s_nop 1
	v_cndmask_b32_e32 v5, v213, v7, vcc
; #define P6_LD(bi, r) do { const GAS f32x4* xr_ = (const GAS f32x4*)(XOUT + ((size_t)p * 256 + wave * 32 + (r)) * DM) + lane2; _Pragma("unroll") for (int j = 0; j < 4; ++j) xq[bi][j] = xr_[64 * j]; } while (0)
; __global__ void __launch_bounds__(512, 2) hymba_fwd(Args args) {
;     ...
;               const float ex = expf(l1 - l0); const float w0 = gprob / (1.0f + ex), w1 = gprob * ex / (1.0f + ex);
;               if (khalf == 0) { const int e0 = gi * 8 + i0, e1 = gi * 8 + i1;
;                   selE[rl * 2] = e0; selE[rl * 2 + 1] = e1; selW[rl * 2] = w0; selW[rl * 2 + 1] = w1;
;                   selP[rl * 2] = __hip_atomic_fetch_add(lcnt + e0, 1, __ATOMIC_RELAXED, __HIP_MEMORY_SCOPE_WORKGROUP);
;                   selP[rl * 2 + 1] = __hip_atomic_fetch_add(lcnt + e1, 1, __ATOMIC_RELAXED, __HIP_MEMORY_SCOPE_WORKGROUP); } }
;             { f32x4 av[4], sv[4]; int lane2 = lane; asm volatile("" : "+v"(lane2));
; #pragma unroll
;               for (int j = 0; j < 4; ++j) { const int c0 = 4 * lane2 + 256 * j; sv[j] = *(const f32x4*)(sh2 + c0); av[j] = *(const f32x4*)(g2p + c0) * (1.0f + *(const f32x4*)(scl2 + c0)); }
;               f32x4 xq[4][4];
;     ...
;               P6_LD(0, 0); P6_LD(1, 1); P6_LD(2, 2); asm volatile("" ::: "memory");
	v_add_f32_e32 v5, v5, v6
	v_div_scale_f32 v6, s[8:9], v5, v5, 1.0
	v_rcp_f32_e32 v7, v6
	s_nop 0
	v_fma_f32 v8, -v6, v7, 1.0
	v_fmac_f32_e32 v7, v8, v7
	v_div_scale_f32 v8, vcc, 1.0, v5, 1.0
	v_mul_f32_e32 v9, v8, v7
	v_fma_f32 v10, -v6, v9, v8
	v_fmac_f32_e32 v9, v10, v7
	v_fma_f32 v6, -v6, v9, v8
	v_div_fmas_f32 v6, v6, v7, v9
	v_div_fixup_f32 v5, v6, v5, 1.0
	v_rndne_f32_e32 v6, v2
	v_sub_f32_e32 v2, v2, v6
	v_add_f32_e32 v2, v2, v4
	v_exp_f32_e32 v2, v2
	v_cvt_i32_f32_e32 v4, v6
	v_cmp_ngt_f32_e32 vcc, s5, v1
	v_lshl_add_u32 v7, v168, 3, 0
	v_add_u32_e32 v8, 0x24800, v7
	v_ldexp_f32 v2, v2, v4
	v_cndmask_b32_e32 v2, 0, v2, vcc
	v_cmp_nlt_f32_e32 vcc, s22, v1
	s_nop 1
	v_cndmask_b32_e32 v1, v213, v2, vcc
	v_mul_f32_e32 v4, v5, v1
	v_add_f32_e32 v6, 1.0, v1
	v_lshlrev_b32_e32 v1, 3, v18
	v_or_b32_e32 v0, v0, v1
	v_add_u32_e32 v1, v3, v1
	v_add_u32_e32 v2, 0x24000, v7
	ds_write_b64 v2, v[0:1]
	v_div_scale_f32 v2, s[8:9], v6, v6, v5
	v_rcp_f32_e32 v3, v2
	s_nop 0
	v_fma_f32 v9, -v2, v3, 1.0
	v_fmac_f32_e32 v3, v9, v3
	v_div_scale_f32 v9, vcc, v5, v6, v5
	v_mul_f32_e32 v10, v9, v3
	v_fma_f32 v11, -v2, v10, v9
	v_fmac_f32_e32 v10, v11, v3
	v_fma_f32 v2, -v2, v10, v9
	v_div_fmas_f32 v2, v2, v3, v10
	v_div_scale_f32 v3, s[8:9], v6, v6, v4
	v_div_fixup_f32 v2, v2, v6, v5
	v_rcp_f32_e32 v5, v3
	s_add_i32 s8, 0, 0x25800
	v_lshl_add_u32 v0, v0, 2, s8
	v_fma_f32 v9, -v3, v5, 1.0
	v_fmac_f32_e32 v5, v9, v5
	v_div_scale_f32 v9, vcc, v4, v6, v4
	v_mul_f32_e32 v10, v9, v5
	v_fma_f32 v11, -v3, v10, v9
	v_fmac_f32_e32 v10, v11, v5
	v_fma_f32 v3, -v3, v10, v9
	v_div_fmas_f32 v3, v3, v5, v10
	v_div_fixup_f32 v3, v3, v6, v4
	ds_write_b64 v8, v[2:3]
	ds_add_rtn_u32 v0, v0, v191
	v_add_u32_e32 v2, 0x25000, v7
	s_waitcnt lgkmcnt(0)
	ds_write_b32 v2, v0
	v_lshl_add_u32 v0, v1, 2, s8
	ds_add_rtn_u32 v0, v0, v191
	s_waitcnt lgkmcnt(0)
	ds_write_b32 v2, v0 offset:4
.LBB0_876:
	s_or_b64 exec, exec, s[12:13]
	s_mul_i32 s8, s43, 6
	s_ashr_i32 s9, s8, 31
	s_lshl_b64 s[8:9], s[8:9], 12
	s_add_u32 s8, s52, s8
	v_lshlrev_b32_e32 v0, 2, v170
	v_ashrrev_i32_e32 v1, 31, v0
	s_addc_u32 s9, s53, s9
	v_lshlrev_b64 v[4:5], 2, v[0:1]
	v_lshl_add_u64 v[8:9], s[8:9], 0, v[4:5]
	s_mov_b64 s[8:9], 0x3000
	v_lshl_add_u64 v[20:21], v[8:9], 0, s[8:9]
	s_movk_i32 s8, 0x4000
	v_add_co_u32_e32 v10, vcc, s8, v8
	s_load_dwordx2 s[8:9], s[20:21], 0x80
	s_nop 0
	v_addc_co_u32_e32 v11, vcc, 0, v9, vcc
	global_load_dwordx4 v[0:3], v[10:11], off offset:-4096
	v_lshl_add_u64 v[24:25], v[8:9], 0, s[94:95]
	s_waitcnt lgkmcnt(0)
	v_lshl_add_u64 v[22:23], s[8:9], 0, v[4:5]
	global_load_dwordx4 v[8:11], v[10:11], off
	s_add_u32 s2, s2, s57
	global_load_dwordx4 v[4:7], v[22:23], off
	s_addc_u32 s3, s3, 0
	s_lshl_b64 s[8:9], s[2:3], 12
	v_ashrrev_i32_e32 v171, 31, v170
	s_add_u32 s8, s58, s8
	s_addc_u32 s9, s59, s9
	v_lshlrev_b64 v[64:65], 4, v[170:171]
	v_lshl_add_u64 v[44:45], s[8:9], 0, v[64:65]
	s_mov_b64 s[8:9], 0x1000
	s_mov_b32 s16, 0
	v_lshl_add_u64 v[98:99], s[58:59], 0, v[64:65]
	v_lshlrev_b64 v[100:101], 3, v[170:171]
	s_mov_b64 s[18:19], s[88:89]
	s_waitcnt vmcnt(1)
	v_add_f32_e32 v10, 1.0, v10
	v_add_f32_e32 v11, 1.0, v11
	v_add_f32_e32 v8, 1.0, v8
	v_add_f32_e32 v9, 1.0, v9
	s_waitcnt vmcnt(0)
	v_mul_f32_e32 v82, v6, v10
	v_mul_f32_e32 v83, v7, v11
	v_mul_f32_e32 v84, v4, v8
	v_mul_f32_e32 v85, v5, v9
	global_load_dwordx4 v[4:7], v[20:21], off offset:1024
	global_load_dwordx4 v[8:11], v[22:23], off offset:1024
	global_load_dwordx4 v[12:15], v[24:25], off offset:1024
	s_waitcnt vmcnt(0)
	v_add_f32_e32 v14, 1.0, v14
	v_add_f32_e32 v15, 1.0, v15
	v_add_f32_e32 v12, 1.0, v12
	v_add_f32_e32 v13, 1.0, v13
	v_mul_f32_e32 v86, v10, v14
	v_mul_f32_e32 v87, v11, v15
	v_mul_f32_e32 v88, v8, v12
	v_mul_f32_e32 v89, v9, v13
	global_load_dwordx4 v[8:11], v[20:21], off offset:2048
	global_load_dwordx4 v[12:15], v[22:23], off offset:2048
	global_load_dwordx4 v[16:19], v[24:25], off offset:2048
	s_waitcnt vmcnt(0)
	v_add_f32_e32 v18, 1.0, v18
	v_add_f32_e32 v19, 1.0, v19
	v_add_f32_e32 v16, 1.0, v16
	v_add_f32_e32 v17, 1.0, v17
	v_mul_f32_e32 v90, v14, v18
	v_mul_f32_e32 v91, v15, v19
	v_mul_f32_e32 v92, v12, v16
	v_mul_f32_e32 v93, v13, v17
	global_load_dwordx4 v[12:15], v[20:21], off offset:3072
	global_load_dwordx4 v[16:19], v[22:23], off offset:3072
	s_nop 0
	global_load_dwordx4 v[20:23], v[24:25], off offset:3072
	s_waitcnt vmcnt(0)
	v_add_f32_e32 v20, 1.0, v20
	v_add_f32_e32 v21, 1.0, v21
	s_nop 0
	v_mul_f32_e32 v96, v16, v20
	v_mul_f32_e32 v97, v17, v21
	v_lshl_add_u64 v[16:17], v[44:45], 0, s[8:9]
	s_movk_i32 s8, 0x2000
	v_add_f32_e32 v22, 1.0, v22
	v_add_f32_e32 v23, 1.0, v23
	v_add_co_u32_e32 v46, vcc, s8, v44
	s_mov_b64 s[8:9], 0x2000
	v_mul_f32_e32 v94, v18, v22
	v_mul_f32_e32 v95, v19, v23
	global_load_dwordx4 v[48:51], v[44:45], off
	global_load_dwordx4 v[36:39], v[44:45], off offset:1024
	global_load_dwordx4 v[28:31], v[44:45], off offset:2048
	global_load_dwordx4 v[20:23], v[44:45], off offset:3072
	v_addc_co_u32_e32 v47, vcc, 0, v45, vcc
	v_lshl_add_u64 v[44:45], v[44:45], 0, s[8:9]
	global_load_dwordx4 v[40:43], v[46:47], off offset:-4096
	global_load_dwordx4 v[32:35], v[16:17], off offset:1024
	global_load_dwordx4 v[24:27], v[16:17], off offset:2048
	s_nop 0
	global_load_dwordx4 v[16:19], v[16:17], off offset:3072
	s_nop 0
	global_load_dwordx4 v[60:63], v[46:47], off
	global_load_dwordx4 v[56:59], v[44:45], off offset:1024
	global_load_dwordx4 v[52:55], v[44:45], off offset:2048
	s_nop 0
	global_load_dwordx4 v[44:47], v[44:45], off offset:3072
	s_add_u32 s8, s58, s51
	s_addc_u32 s9, s59, s63
	v_lshl_add_u64 v[102:103], s[8:9], 0, v[64:65]
; #define P6_LD(bi, r) do { const GAS f32x4* xr_ = (const GAS f32x4*)(XOUT + ((size_t)p * 256 + wave * 32 + (r)) * DM) + lane2; _Pragma("unroll") for (int j = 0; j < 4; ++j) xq[bi][j] = xr_[64 * j]; } while (0)
; __global__ void __launch_bounds__(512, 2) hymba_fwd(Args args) {
;     ...
;               P6_LD(0, 0); P6_LD(1, 1); P6_LD(2, 2); asm volatile("" ::: "memory");
; #pragma nounroll
;               for (int rr = 0; rr < 32; rr += 4) { const int r4 = (rr + 4 < 32) ? rr + 4 : 28;
;                   P6_LD(3, rr + 3); asm volatile("" ::: "memory"); P6_ST(0, rr); asm volatile("" ::: "memory");
;                   P6_LD(0, r4); asm volatile("" ::: "memory"); P6_ST(1, rr + 1); asm volatile("" ::: "memory");
;                   P6_LD(1, r4 + 1); asm volatile("" ::: "memory"); P6_ST(2, rr + 2); asm volatile("" ::: "memory");
;                   P6_LD(2, r4 + 2); asm volatile("" ::: "memory"); P6_ST(3, rr + 3); asm volatile("" ::: "memory"); }
.LBB0_877:
	s_add_i32 s43, s16, 3
	s_add_i32 s17, s16, 4
	s_cmp_lt_u32 s16, 28
	s_cselect_b32 s10, s17, 28
	s_add_u32 s8, s2, s10
	s_addc_u32 s9, s3, 0
	s_lshl_b64 s[14:15], s[8:9], 12
	s_add_i32 s59, s16, 1
	s_or_b32 s8, s10, 1
	s_add_u32 s8, s2, s8
	s_addc_u32 s9, s3, 0
	s_lshl_b64 s[12:13], s[8:9], 12
	s_add_i32 s58, s16, 2
	s_or_b32 s8, s10, 2
	s_add_u32 s8, s2, s8
	s_addc_u32 s9, s3, 0
	s_lshl_b64 s[10:11], s[8:9], 12
	s_add_u32 s8, s18, 0x2000
	s_addc_u32 s9, s19, 0
	s_cmp_gt_u32 s16, 27
	v_readlane_b32 s16, v80, s16
	v_lshl_add_u64 v[104:105], s[18:19], 0, v[100:101]
	s_movk_i32 s18, 0xf000
	s_waitcnt vmcnt(11)
	v_mul_f32_e32 v48, s16, v48
	v_mul_f32_e32 v49, s16, v49
	v_fma_f32 v48, v48, v84, v0
	v_fma_f32 v49, v49, v85, v1
	v_mul_f32_e32 v50, s16, v50
	v_mul_f32_e32 v51, s16, v51
	v_bfe_u32 v81, v48, 16, 1
	v_add3_u32 v48, v48, v81, s23
	v_bfe_u32 v81, v49, 16, 1
	v_fma_f32 v50, v50, v82, v2
	v_fma_f32 v51, v51, v83, v3
	v_lshrrev_b32_e32 v48, 16, v48
	v_add3_u32 v49, v49, v81, s23
	v_and_or_b32 v48, v49, s42, v48
	v_bfe_u32 v49, v50, 16, 1
	v_add3_u32 v49, v50, v49, s23
	v_bfe_u32 v50, v51, 16, 1
	v_lshrrev_b32_e32 v49, 16, v49
	v_add3_u32 v50, v51, v50, s23
	v_add_co_u32_e32 v106, vcc, s18, v104
	s_waitcnt vmcnt(10)
	v_mul_f32_e32 v36, s16, v36
	v_mul_f32_e32 v37, s16, v37
	v_and_or_b32 v49, v50, s42, v49
	v_addc_co_u32_e32 v107, vcc, -1, v105, vcc
	v_fma_f32 v36, v36, v88, v4
	v_fma_f32 v37, v37, v89, v5
	global_load_dwordx4 v[76:79], v[102:103], off
	global_load_dwordx4 v[72:75], v[102:103], off offset:1024
	global_load_dwordx4 v[68:71], v[102:103], off offset:2048
	global_load_dwordx4 v[64:67], v[102:103], off offset:3072
	global_store_dwordx2 v[106:107], v[48:49], off offset:-3584
	v_bfe_u32 v48, v36, 16, 1
	v_mul_f32_e32 v38, s16, v38
	v_mul_f32_e32 v39, s16, v39
	v_add3_u32 v36, v36, v48, s23
	v_bfe_u32 v48, v37, 16, 1
	v_fma_f32 v38, v38, v86, v6
	v_fma_f32 v39, v39, v87, v7
	v_lshrrev_b32_e32 v36, 16, v36
	v_add3_u32 v37, v37, v48, s23
	v_and_or_b32 v36, v37, s42, v36
	v_bfe_u32 v37, v38, 16, 1
	v_add3_u32 v37, v38, v37, s23
	v_bfe_u32 v38, v39, 16, 1
	v_lshrrev_b32_e32 v37, 16, v37
	v_add3_u32 v38, v39, v38, s23
	s_waitcnt vmcnt(14)
	v_mul_f32_e32 v28, s16, v28
	v_mul_f32_e32 v29, s16, v29
	v_and_or_b32 v37, v38, s42, v37
	v_fma_f32 v28, v28, v92, v8
	v_fma_f32 v29, v29, v93, v9
	global_store_dwordx2 v[106:107], v[36:37], off offset:-3072
	v_bfe_u32 v36, v28, 16, 1
	v_mul_f32_e32 v30, s16, v30
	v_mul_f32_e32 v31, s16, v31
	v_add3_u32 v28, v28, v36, s23
	v_bfe_u32 v36, v29, 16, 1
	v_fma_f32 v30, v30, v90, v10
	v_fma_f32 v31, v31, v91, v11
	v_lshrrev_b32_e32 v28, 16, v28
	v_add3_u32 v29, v29, v36, s23
	v_and_or_b32 v28, v29, s42, v28
	v_bfe_u32 v29, v30, 16, 1
	v_add3_u32 v29, v30, v29, s23
	v_bfe_u32 v30, v31, 16, 1
	v_lshrrev_b32_e32 v29, 16, v29
	v_add3_u32 v30, v31, v30, s23
	s_waitcnt vmcnt(14)
	v_mul_f32_e32 v20, s16, v20
	v_mul_f32_e32 v21, s16, v21
	v_and_or_b32 v29, v30, s42, v29
	v_fma_f32 v20, v20, v96, v12
	v_fma_f32 v21, v21, v97, v13
	global_store_dwordx2 v[106:107], v[28:29], off offset:-2560
	v_bfe_u32 v28, v20, 16, 1
	v_mul_f32_e32 v22, s16, v22
	v_mul_f32_e32 v23, s16, v23
	v_add3_u32 v20, v20, v28, s23
	v_bfe_u32 v28, v21, 16, 1
	v_fma_f32 v22, v22, v94, v14
	v_fma_f32 v23, v23, v95, v15
	v_lshrrev_b32_e32 v20, 16, v20
	v_add3_u32 v21, v21, v28, s23
	v_and_or_b32 v20, v21, s42, v20
	v_bfe_u32 v21, v22, 16, 1
	v_add3_u32 v21, v22, v21, s23
	v_bfe_u32 v22, v23, 16, 1
	v_lshrrev_b32_e32 v21, 16, v21
	v_add3_u32 v22, v23, v22, s23
	v_and_or_b32 v21, v22, s42, v21
	global_store_dwordx2 v[106:107], v[20:21], off offset:-2048
	v_lshl_add_u64 v[20:21], v[98:99], 0, s[14:15]
	v_readlane_b32 s14, v80, s59
	global_load_dwordx4 v[48:51], v[20:21], off
	global_load_dwordx4 v[36:39], v[20:21], off offset:1024
	global_load_dwordx4 v[28:31], v[20:21], off offset:2048
	s_nop 0
	global_load_dwordx4 v[20:23], v[20:21], off offset:3072
	s_waitcnt vmcnt(19)
	v_mul_f32_e32 v40, s14, v40
	v_mul_f32_e32 v41, s14, v41
	v_fma_f32 v40, v40, v84, v0
	v_fma_f32 v41, v41, v85, v1
	v_mul_f32_e32 v42, s14, v42
	v_mul_f32_e32 v43, s14, v43
	v_bfe_u32 v81, v40, 16, 1
	v_add3_u32 v40, v40, v81, s23
	v_bfe_u32 v81, v41, 16, 1
	v_fma_f32 v42, v42, v82, v2
	v_fma_f32 v43, v43, v83, v3
	v_lshrrev_b32_e32 v40, 16, v40
	v_add3_u32 v41, v41, v81, s23
	v_and_or_b32 v40, v41, s42, v40
	v_bfe_u32 v41, v42, 16, 1
	v_add3_u32 v41, v42, v41, s23
	v_bfe_u32 v42, v43, 16, 1
	v_lshrrev_b32_e32 v41, 16, v41
	v_add3_u32 v42, v43, v42, s23
	s_waitcnt vmcnt(18)
	v_mul_f32_e32 v32, s14, v32
	v_mul_f32_e32 v33, s14, v33
	v_and_or_b32 v41, v42, s42, v41
	v_fma_f32 v32, v32, v88, v4
	v_fma_f32 v33, v33, v89, v5
	global_store_dwordx2 v[106:107], v[40:41], off offset:-1536
	v_bfe_u32 v40, v32, 16, 1
	v_mul_f32_e32 v34, s14, v34
	v_mul_f32_e32 v35, s14, v35
	v_add3_u32 v32, v32, v40, s23
	v_bfe_u32 v40, v33, 16, 1
	v_fma_f32 v34, v34, v86, v6
	v_fma_f32 v35, v35, v87, v7
	v_lshrrev_b32_e32 v32, 16, v32
	v_add3_u32 v33, v33, v40, s23
	v_and_or_b32 v32, v33, s42, v32
	v_bfe_u32 v33, v34, 16, 1
	v_add3_u32 v33, v34, v33, s23
	v_bfe_u32 v34, v35, 16, 1
	v_lshrrev_b32_e32 v33, 16, v33
	v_add3_u32 v34, v35, v34, s23
	s_waitcnt vmcnt(18)
	v_mul_f32_e32 v24, s14, v24
	v_mul_f32_e32 v25, s14, v25
	v_and_or_b32 v33, v34, s42, v33
	v_fma_f32 v24, v24, v92, v8
	v_fma_f32 v25, v25, v93, v9
	global_store_dwordx2 v[106:107], v[32:33], off offset:-1024
	v_bfe_u32 v32, v24, 16, 1
	v_mul_f32_e32 v26, s14, v26
	v_mul_f32_e32 v27, s14, v27
	v_add3_u32 v24, v24, v32, s23
	v_bfe_u32 v32, v25, 16, 1
	v_fma_f32 v26, v26, v90, v10
	v_fma_f32 v27, v27, v91, v11
	v_lshrrev_b32_e32 v24, 16, v24
	v_add3_u32 v25, v25, v32, s23
	v_and_or_b32 v24, v25, s42, v24
	v_bfe_u32 v25, v26, 16, 1
	v_add3_u32 v25, v26, v25, s23
	v_bfe_u32 v26, v27, 16, 1
	v_lshrrev_b32_e32 v25, 16, v25
	v_add3_u32 v26, v27, v26, s23
	s_waitcnt vmcnt(18)
; #define P6_LD(bi, r) do { const GAS f32x4* xr_ = (const GAS f32x4*)(XOUT + ((size_t)p * 256 + wave * 32 + (r)) * DM) + lane2; _Pragma("unroll") for (int j = 0; j < 4; ++j) xq[bi][j] = xr_[64 * j]; } while (0)
; __global__ void __launch_bounds__(512, 2) hymba_fwd(Args args) {
;     ...
;               P6_LD(0, 0); P6_LD(1, 1); P6_LD(2, 2); asm volatile("" ::: "memory");
; #pragma nounroll
;               for (int rr = 0; rr < 32; rr += 4) { const int r4 = (rr + 4 < 32) ? rr + 4 : 28;
;                   P6_LD(3, rr + 3); asm volatile("" ::: "memory"); P6_ST(0, rr); asm volatile("" ::: "memory");
;                   P6_LD(0, r4); asm volatile("" ::: "memory"); P6_ST(1, rr + 1); asm volatile("" ::: "memory");
;                   P6_LD(1, r4 + 1); asm volatile("" ::: "memory"); P6_ST(2, rr + 2); asm volatile("" ::: "memory");
;                   P6_LD(2, r4 + 2); asm volatile("" ::: "memory"); P6_ST(3, rr + 3); asm volatile("" ::: "memory"); }
	v_mul_f32_e32 v16, s14, v16
	v_mul_f32_e32 v17, s14, v17
	v_and_or_b32 v25, v26, s42, v25
	v_fma_f32 v16, v16, v96, v12
	v_fma_f32 v17, v17, v97, v13
	global_store_dwordx2 v[106:107], v[24:25], off offset:-512
	v_bfe_u32 v24, v16, 16, 1
	v_mul_f32_e32 v18, s14, v18
	v_mul_f32_e32 v19, s14, v19
	v_add3_u32 v16, v16, v24, s23
	v_bfe_u32 v24, v17, 16, 1
	v_fma_f32 v18, v18, v94, v14
	v_fma_f32 v19, v19, v95, v15
	v_lshrrev_b32_e32 v16, 16, v16
	v_add3_u32 v17, v17, v24, s23
	v_and_or_b32 v16, v17, s42, v16
	v_bfe_u32 v17, v18, 16, 1
	v_add3_u32 v17, v18, v17, s23
	v_bfe_u32 v18, v19, 16, 1
	v_lshrrev_b32_e32 v17, 16, v17
	v_add3_u32 v18, v19, v18, s23
	v_and_or_b32 v17, v18, s42, v17
	global_store_dwordx2 v[104:105], v[16:17], off offset:-4096
	v_lshl_add_u64 v[16:17], v[98:99], 0, s[12:13]
	v_readlane_b32 s12, v80, s58
	global_load_dwordx4 v[40:43], v[16:17], off
	global_load_dwordx4 v[32:35], v[16:17], off offset:1024
	global_load_dwordx4 v[24:27], v[16:17], off offset:2048
	s_nop 0
	global_load_dwordx4 v[16:19], v[16:17], off offset:3072
	s_waitcnt vmcnt(23)
	v_mul_f32_e32 v60, s12, v60
	v_mul_f32_e32 v61, s12, v61
	v_fma_f32 v60, v60, v84, v0
	v_fma_f32 v61, v61, v85, v1
	v_mul_f32_e32 v62, s12, v62
	v_mul_f32_e32 v63, s12, v63
	v_bfe_u32 v81, v60, 16, 1
	v_add3_u32 v60, v60, v81, s23
	v_bfe_u32 v81, v61, 16, 1
	v_fma_f32 v62, v62, v82, v2
	v_fma_f32 v63, v63, v83, v3
	v_lshrrev_b32_e32 v60, 16, v60
	v_add3_u32 v61, v61, v81, s23
	v_and_or_b32 v60, v61, s42, v60
	v_bfe_u32 v61, v62, 16, 1
	v_add3_u32 v61, v62, v61, s23
	v_bfe_u32 v62, v63, 16, 1
	v_lshrrev_b32_e32 v61, 16, v61
	v_add3_u32 v62, v63, v62, s23
	s_waitcnt vmcnt(22)
	v_mul_f32_e32 v56, s12, v56
	v_mul_f32_e32 v57, s12, v57
	v_and_or_b32 v61, v62, s42, v61
	v_fma_f32 v56, v56, v88, v4
	v_fma_f32 v57, v57, v89, v5
	global_store_dwordx2 v[104:105], v[60:61], off offset:-3584
	v_bfe_u32 v60, v56, 16, 1
	v_mul_f32_e32 v58, s12, v58
	v_mul_f32_e32 v59, s12, v59
	v_add3_u32 v56, v56, v60, s23
	v_bfe_u32 v60, v57, 16, 1
	v_fma_f32 v58, v58, v86, v6
	v_fma_f32 v59, v59, v87, v7
	v_lshrrev_b32_e32 v56, 16, v56
	v_add3_u32 v57, v57, v60, s23
	v_and_or_b32 v56, v57, s42, v56
	v_bfe_u32 v57, v58, 16, 1
	v_add3_u32 v57, v58, v57, s23
	v_bfe_u32 v58, v59, 16, 1
	v_lshrrev_b32_e32 v57, 16, v57
	v_add3_u32 v58, v59, v58, s23
	s_waitcnt vmcnt(22)
	v_mul_f32_e32 v52, s12, v52
	v_mul_f32_e32 v53, s12, v53
	v_and_or_b32 v57, v58, s42, v57
	v_fma_f32 v52, v52, v92, v8
	v_fma_f32 v53, v53, v93, v9
	global_store_dwordx2 v[104:105], v[56:57], off offset:-3072
	v_bfe_u32 v56, v52, 16, 1
	v_mul_f32_e32 v54, s12, v54
	v_mul_f32_e32 v55, s12, v55
	v_add3_u32 v52, v52, v56, s23
	v_bfe_u32 v56, v53, 16, 1
	v_fma_f32 v54, v54, v90, v10
	v_fma_f32 v55, v55, v91, v11
	v_lshrrev_b32_e32 v52, 16, v52
	v_add3_u32 v53, v53, v56, s23
	v_and_or_b32 v52, v53, s42, v52
	v_bfe_u32 v53, v54, 16, 1
	v_add3_u32 v53, v54, v53, s23
	v_bfe_u32 v54, v55, 16, 1
	v_lshrrev_b32_e32 v53, 16, v53
	v_add3_u32 v54, v55, v54, s23
	s_waitcnt vmcnt(22)
	v_mul_f32_e32 v44, s12, v44
	v_mul_f32_e32 v45, s12, v45
	v_and_or_b32 v53, v54, s42, v53
	v_fma_f32 v44, v44, v96, v12
	v_fma_f32 v45, v45, v97, v13
	global_store_dwordx2 v[104:105], v[52:53], off offset:-2560
	v_bfe_u32 v52, v44, 16, 1
	v_mul_f32_e32 v46, s12, v46
	v_mul_f32_e32 v47, s12, v47
	v_add3_u32 v44, v44, v52, s23
	v_bfe_u32 v52, v45, 16, 1
	v_fma_f32 v46, v46, v94, v14
	v_fma_f32 v47, v47, v95, v15
	v_lshrrev_b32_e32 v44, 16, v44
	v_add3_u32 v45, v45, v52, s23
	v_and_or_b32 v44, v45, s42, v44
	v_bfe_u32 v45, v46, 16, 1
	v_add3_u32 v45, v46, v45, s23
	v_bfe_u32 v46, v47, 16, 1
	v_lshrrev_b32_e32 v45, 16, v45
	v_add3_u32 v46, v47, v46, s23
	v_and_or_b32 v45, v46, s42, v45
	global_store_dwordx2 v[104:105], v[44:45], off offset:-2048
	v_lshl_add_u64 v[44:45], v[98:99], 0, s[10:11]
	global_load_dwordx4 v[60:63], v[44:45], off
	global_load_dwordx4 v[56:59], v[44:45], off offset:1024
	global_load_dwordx4 v[52:55], v[44:45], off offset:2048
	s_nop 0
	global_load_dwordx4 v[44:47], v[44:45], off offset:3072
	v_readlane_b32 s10, v80, s43
	v_lshl_add_u64 v[102:103], v[102:103], 0, s[94:95]
	s_mov_b64 s[18:19], s[8:9]
	s_waitcnt vmcnt(27)
	v_mul_f32_e32 v76, s10, v76
	v_mul_f32_e32 v77, s10, v77
	v_fma_f32 v76, v76, v84, v0
	v_fma_f32 v77, v77, v85, v1
	v_mul_f32_e32 v78, s10, v78
	v_mul_f32_e32 v79, s10, v79
	v_bfe_u32 v81, v76, 16, 1
	v_add3_u32 v76, v76, v81, s23
	v_bfe_u32 v81, v77, 16, 1
	v_fma_f32 v78, v78, v82, v2
	v_fma_f32 v79, v79, v83, v3
	v_lshrrev_b32_e32 v76, 16, v76
	v_add3_u32 v77, v77, v81, s23
	v_and_or_b32 v76, v77, s42, v76
	v_bfe_u32 v77, v78, 16, 1
	v_add3_u32 v77, v78, v77, s23
	v_bfe_u32 v78, v79, 16, 1
	v_lshrrev_b32_e32 v77, 16, v77
	v_add3_u32 v78, v79, v78, s23
	s_waitcnt vmcnt(26)
	v_mul_f32_e32 v72, s10, v72
	v_mul_f32_e32 v73, s10, v73
	v_and_or_b32 v77, v78, s42, v77
	v_fma_f32 v72, v72, v88, v4
	v_fma_f32 v73, v73, v89, v5
	global_store_dwordx2 v[104:105], v[76:77], off offset:-1536
	v_bfe_u32 v76, v72, 16, 1
	v_mul_f32_e32 v74, s10, v74
	v_mul_f32_e32 v75, s10, v75
	v_add3_u32 v72, v72, v76, s23
	v_bfe_u32 v76, v73, 16, 1
	v_fma_f32 v74, v74, v86, v6
	v_fma_f32 v75, v75, v87, v7
	v_lshrrev_b32_e32 v72, 16, v72
	v_add3_u32 v73, v73, v76, s23
	v_and_or_b32 v72, v73, s42, v72
	v_bfe_u32 v73, v74, 16, 1
	v_add3_u32 v73, v74, v73, s23
	v_bfe_u32 v74, v75, 16, 1
	v_lshrrev_b32_e32 v73, 16, v73
	v_add3_u32 v74, v75, v74, s23
	s_waitcnt vmcnt(26)
	v_mul_f32_e32 v68, s10, v68
	v_mul_f32_e32 v69, s10, v69
	v_and_or_b32 v73, v74, s42, v73
	v_fma_f32 v68, v68, v92, v8
	v_fma_f32 v69, v69, v93, v9
	global_store_dwordx2 v[104:105], v[72:73], off offset:-1024
	v_bfe_u32 v72, v68, 16, 1
	v_mul_f32_e32 v70, s10, v70
	v_mul_f32_e32 v71, s10, v71
	v_add3_u32 v68, v68, v72, s23
	v_bfe_u32 v72, v69, 16, 1
	v_fma_f32 v70, v70, v90, v10
	v_fma_f32 v71, v71, v91, v11
	v_lshrrev_b32_e32 v68, 16, v68
	v_add3_u32 v69, v69, v72, s23
	v_and_or_b32 v68, v69, s42, v68
	v_bfe_u32 v69, v70, 16, 1
	v_add3_u32 v69, v70, v69, s23
	v_bfe_u32 v70, v71, 16, 1
	v_lshrrev_b32_e32 v69, 16, v69
	v_add3_u32 v70, v71, v70, s23
	s_waitcnt vmcnt(26)
	v_mul_f32_e32 v64, s10, v64
	v_mul_f32_e32 v65, s10, v65
	v_and_or_b32 v69, v70, s42, v69
	v_fma_f32 v64, v64, v96, v12
	v_fma_f32 v65, v65, v97, v13
	global_store_dwordx2 v[104:105], v[68:69], off offset:-512
	v_bfe_u32 v68, v64, 16, 1
	v_mul_f32_e32 v66, s10, v66
	v_mul_f32_e32 v67, s10, v67
	v_add3_u32 v64, v64, v68, s23
	v_bfe_u32 v68, v65, 16, 1
	v_fma_f32 v66, v66, v94, v14
	v_fma_f32 v67, v67, v95, v15
	v_lshrrev_b32_e32 v64, 16, v64
	v_add3_u32 v65, v65, v68, s23
	v_and_or_b32 v64, v65, s42, v64
	v_bfe_u32 v65, v66, 16, 1
	v_add3_u32 v65, v66, v65, s23
	v_bfe_u32 v66, v67, 16, 1
	v_lshrrev_b32_e32 v65, 16, v65
	v_add3_u32 v66, v67, v66, s23
	v_and_or_b32 v65, v66, s42, v65
	global_store_dwordx2 v[104:105], v[64:65], off
	s_mov_b32 s16, s17
	s_cbranch_scc0 .LBB0_877
; __device__ __forceinline__ int lane_id_v() { int l; asm volatile("v_mbcnt_lo_u32_b32 %0, -1, 0\n\tv_mbcnt_hi_u32_b32 %0, -1, %0" : "=v"(l)); return l; }
; __global__ void __launch_bounds__(512, 2) hymba_fwd(Args args) {
;     ...
;             __syncthreads();
;             const int tidB = wave * 64 + lane_id_v();
;             if (tidB < 32) lbase[tidB] = (int)__hip_atomic_fetch_add(ECNT + tidB, (unsigned)lcnt[tidB], RLX_AGENT);
;             __syncthreads();
	s_barrier
	v_mbcnt_lo_u32_b32 v3, -1, 0
	v_mbcnt_hi_u32_b32 v3, -1, v3
	s_nop 0
	v_add_u32_e32 v0, s56, v3
	v_cmp_gt_i32_e32 vcc, 32, v0
	v_lshl_add_u32 v2, v0, 2, 0
	s_and_saveexec_b64 s[2:3], vcc
	s_cbranch_execz .LBB0_865
	v_readlane_b32 s8, v248, 16
	v_add_u32_e32 v7, 0x25800, v2
	v_ashrrev_i32_e32 v1, 31, v0
	v_readlane_b32 s9, v248, 17
	v_add_u32_e32 v6, 0x25880, v2
	s_nop 0
	v_lshl_add_u64 v[4:5], v[0:1], 2, s[8:9]
	ds_read_b32 v1, v7
	s_waitcnt lgkmcnt(0)
	global_atomic_add v1, v[4:5], v1, off sc0
	s_waitcnt vmcnt(0)
	ds_write_b32 v6, v1
	s_branch .LBB0_865

; __device__ __forceinline__ u32x4 pack8(f32x4 v0, f32x4 v1) { u32x4 w; w.x = cvt_pk_bf16(v0[0], v0[1]); w.y = cvt_pk_bf16(v0[2], v0[3]); w.z = cvt_pk_bf16(v1[0], v1[1]); w.w = cvt_pk_bf16(v1[2], v1[3]); return w; }
; #define EPI_PIN8(a) asm volatile("" : "+v"(a[0][0]), "+v"(a[0][1]), "+v"(a[0][2]), "+v"(a[0][3]), "+v"(a[1][0]), "+v"(a[1][1]), "+v"(a[1][2]), "+v"(a[1][3]) :: "memory")
;     __device__ __forceinline__ int operator()(AccT acc, const Unit& u, int wr, int wc, int, int) const {
;     ...
;             for (int m = 0; m < 4; ++m) { const int li = u.i * 256 + ai * HALF + wr * 64 + m * 16 + fr; ent[ai][m] = etab[li]; wv[ai][m] = wtab[li]; }
;         EPI_PIN8(ent); EPI_PIN8(wv);
; #pragma unroll
;         for (int ai = 0; ai < 2; ++ai)
; #pragma unroll
;             for (int m = 0; m < 4; ++m) { const int idx = u.t * 256 + ai * HALF + wr * 64 + m * 16 + fr;
;                 if (idx < u.cnt) { const float w = wv[ai][m];
; #pragma unroll
;                     for (int bj = 0; bj < 2; ++bj) *(u32x4*)(Y + (size_t)ent[ai][m] * DM + cw + bj * HALF) = pack8(acc[ai][bj][m][0] * w, acc[ai][bj][m][1] * w); } }
.LBB0_1205:
	v_mbcnt_lo_u32_b32 v136, -1, 0
	v_mbcnt_hi_u32_b32 v136, -1, v136
	s_lshl_b32 s5, s21, 8
	v_and_or_b32 v141, v136, 15, s1
	v_ashrrev_i32_e32 v137, 1, v136
	v_add_lshl_u32 v136, v141, s5, 2
	v_or_b32_e32 v140, 64, v136
	v_add_u32_e32 v138, s56, v136
	v_add_u32_e32 v142, s58, v136
	v_add_u32_e32 v144, s56, v140
	v_add_u32_e32 v145, s58, v140
	v_or_b32_e32 v140, 0x80, v136
	v_or_b32_e32 v136, 0xc0, v136
	ds_read2st64_b32 v[166:167], v138 offset1:2
	v_add_u32_e32 v148, s56, v140
	v_add_u32_e32 v149, s58, v140
	v_add_u32_e32 v140, s56, v136
	ds_read2_b32 v[146:147], v138 offset0:144 offset1:160
	v_add_u32_e32 v150, s58, v136
	ds_read_b32 v162, v144
	ds_read_b32 v160, v148
	ds_read_b32 v156, v140
	ds_read_b32 v140, v138 offset:704
	ds_read_b32 v154, v150
	ds_read_b32 v158, v149
	ds_read_b32 v164, v145
	ds_read_b32 v138, v142 offset:704
	ds_read2st64_b32 v[168:169], v142 offset1:2
	ds_read2_b32 v[148:149], v142 offset0:144 offset1:160
	s_lshl_b32 s5, s20, 8
	s_waitcnt lgkmcnt(0)
	v_mov_b32_e32 v152, v167
	v_mov_b32_e32 v144, v147
	v_and_b32_e32 v137, -8, v137
	s_or_b32 s5, s5, s0
	v_mov_b32_e32 v150, v169
	v_mov_b32_e32 v142, v149
	v_add_u32_e32 v136, s5, v137
	s_lshl_b32 s5, s63, 8
	v_add_u32_e32 v141, s5, v141
	v_ashrrev_i32_e32 v137, 31, v136
	v_cmp_gt_i32_e32 vcc, s42, v141
	s_and_saveexec_b64 s[20:21], vcc
	s_cbranch_execz .LBB0_1207
	v_mul_f32_e32 v124, v124, v168
	v_mul_f32_e32 v125, v125, v168
	v_ashrrev_i32_e32 v167, 31, v166
	v_mul_f32_e32 v172, v122, v168
	v_mul_f32_e32 v173, v123, v168
	v_mul_f32_e32 v122, v120, v168
	v_mul_f32_e32 v123, v121, v168
	v_cvt_pk_bf16_f32 v120, v124, v125
	v_lshlrev_b64 v[124:125], 11, v[166:167]
	v_lshl_add_u64 v[124:125], s[2:3], 0, v[124:125]
	v_mul_f32_e32 v126, v126, v168
	v_mul_f32_e32 v127, v127, v168
	v_lshl_add_u64 v[124:125], v[136:137], 1, v[124:125]
	v_cvt_pk_bf16_f32 v121, v126, v127
	v_cvt_pk_bf16_f32 v122, v122, v123
	v_cvt_pk_bf16_f32 v123, v172, v173
	global_store_dwordx4 v[124:125], v[120:123], off
	v_mul_f32_e32 v118, v118, v168
	v_mul_f32_e32 v119, v119, v168
	v_mul_f32_e32 v116, v116, v168
	v_mul_f32_e32 v117, v117, v168
	v_mul_f32_e32 v120, v114, v168
	v_mul_f32_e32 v121, v115, v168
	v_mul_f32_e32 v114, v112, v168
	v_mul_f32_e32 v115, v113, v168
	v_cvt_pk_bf16_f32 v112, v116, v117
	v_cvt_pk_bf16_f32 v113, v118, v119
	s_nop 0
	v_cvt_pk_bf16_f32 v114, v114, v115
	v_cvt_pk_bf16_f32 v115, v120, v121
	global_store_dwordx4 v[124:125], v[112:115], off offset:256
.LBB0_1207:
	s_or_b64 exec, exec, s[20:21]
	s_nop 0
	v_or_b32_e32 v112, 16, v141
	v_cmp_gt_i32_e32 vcc, s42, v112
	s_and_saveexec_b64 s[20:21], vcc
	s_cbranch_execz .LBB0_1209
	v_mul_f32_e32 v108, v108, v164
	v_mul_f32_e32 v109, v109, v164
	v_ashrrev_i32_e32 v163, 31, v162
	v_mul_f32_e32 v112, v106, v164
	v_mul_f32_e32 v113, v107, v164
	v_mul_f32_e32 v106, v104, v164
	v_mul_f32_e32 v107, v105, v164
	v_cvt_pk_bf16_f32 v104, v108, v109
	v_lshlrev_b64 v[108:109], 11, v[162:163]
	v_lshl_add_u64 v[108:109], s[2:3], 0, v[108:109]
	v_mul_f32_e32 v110, v110, v164
	v_mul_f32_e32 v111, v111, v164
	v_lshl_add_u64 v[108:109], v[136:137], 1, v[108:109]
	v_cvt_pk_bf16_f32 v105, v110, v111
	v_cvt_pk_bf16_f32 v106, v106, v107
	v_cvt_pk_bf16_f32 v107, v112, v113
	global_store_dwordx4 v[108:109], v[104:107], off
	v_mul_f32_e32 v102, v102, v164
	v_mul_f32_e32 v103, v103, v164
	v_mul_f32_e32 v100, v100, v164
	v_mul_f32_e32 v101, v101, v164
	v_mul_f32_e32 v104, v98, v164
	v_mul_f32_e32 v105, v99, v164
	v_mul_f32_e32 v98, v96, v164
	v_mul_f32_e32 v99, v97, v164
	v_cvt_pk_bf16_f32 v96, v100, v101
	v_cvt_pk_bf16_f32 v97, v102, v103
	s_nop 0
	v_cvt_pk_bf16_f32 v98, v98, v99
	v_cvt_pk_bf16_f32 v99, v104, v105
	global_store_dwordx4 v[108:109], v[96:99], off offset:256
.LBB0_1209:
	s_or_b64 exec, exec, s[20:21]
	s_nop 0
	v_or_b32_e32 v96, 32, v141
	v_cmp_gt_i32_e32 vcc, s42, v96
	s_and_saveexec_b64 s[20:21], vcc
	s_cbranch_execz .LBB0_1211
	v_mul_f32_e32 v92, v92, v158
	v_mul_f32_e32 v93, v93, v158
	v_ashrrev_i32_e32 v161, 31, v160
	v_mul_f32_e32 v96, v90, v158
	v_mul_f32_e32 v97, v91, v158
	v_mul_f32_e32 v90, v88, v158
	v_mul_f32_e32 v91, v89, v158
	v_cvt_pk_bf16_f32 v88, v92, v93
	v_lshlrev_b64 v[92:93], 11, v[160:161]
	v_lshl_add_u64 v[92:93], s[2:3], 0, v[92:93]
	v_mul_f32_e32 v94, v94, v158
	v_mul_f32_e32 v95, v95, v158
	v_lshl_add_u64 v[92:93], v[136:137], 1, v[92:93]
	v_cvt_pk_bf16_f32 v89, v94, v95
	v_cvt_pk_bf16_f32 v90, v90, v91
	v_cvt_pk_bf16_f32 v91, v96, v97
	global_store_dwordx4 v[92:93], v[88:91], off
	v_mul_f32_e32 v86, v86, v158
	v_mul_f32_e32 v87, v87, v158
	v_mul_f32_e32 v84, v84, v158
	v_mul_f32_e32 v85, v85, v158
	v_mul_f32_e32 v88, v82, v158
	v_mul_f32_e32 v89, v83, v158
	v_mul_f32_e32 v82, v80, v158
	v_mul_f32_e32 v83, v81, v158
	v_cvt_pk_bf16_f32 v80, v84, v85
	v_cvt_pk_bf16_f32 v81, v86, v87
	s_nop 0
	v_cvt_pk_bf16_f32 v82, v82, v83
	v_cvt_pk_bf16_f32 v83, v88, v89
	global_store_dwordx4 v[92:93], v[80:83], off offset:256
; __device__ __forceinline__ u32x4 pack8(f32x4 v0, f32x4 v1) { u32x4 w; w.x = cvt_pk_bf16(v0[0], v0[1]); w.y = cvt_pk_bf16(v0[2], v0[3]); w.z = cvt_pk_bf16(v1[0], v1[1]); w.w = cvt_pk_bf16(v1[2], v1[3]); return w; }
;     __device__ __forceinline__ int operator()(AccT acc, const Unit& u, int wr, int wc, int, int) const {
;     ...
;         for (int ai = 0; ai < 2; ++ai)
; #pragma unroll
;             for (int m = 0; m < 4; ++m) { const int idx = u.t * 256 + ai * HALF + wr * 64 + m * 16 + fr;
;                 if (idx < u.cnt) { const float w = wv[ai][m];
; #pragma unroll
;                     for (int bj = 0; bj < 2; ++bj) *(u32x4*)(Y + (size_t)ent[ai][m] * DM + cw + bj * HALF) = pack8(acc[ai][bj][m][0] * w, acc[ai][bj][m][1] * w); } }
.LBB0_1211:
	s_or_b64 exec, exec, s[20:21]
	s_nop 0
	v_or_b32_e32 v80, 48, v141
	v_cmp_gt_i32_e32 vcc, s42, v80
	s_and_saveexec_b64 s[20:21], vcc
	s_cbranch_execz .LBB0_1213
	v_mul_f32_e32 v76, v76, v154
	v_mul_f32_e32 v77, v77, v154
	v_ashrrev_i32_e32 v157, 31, v156
	v_mul_f32_e32 v80, v74, v154
	v_mul_f32_e32 v81, v75, v154
	v_mul_f32_e32 v74, v72, v154
	v_mul_f32_e32 v75, v73, v154
	v_cvt_pk_bf16_f32 v72, v76, v77
	v_lshlrev_b64 v[76:77], 11, v[156:157]
	v_lshl_add_u64 v[76:77], s[2:3], 0, v[76:77]
	v_mul_f32_e32 v78, v78, v154
	v_mul_f32_e32 v79, v79, v154
	v_lshl_add_u64 v[76:77], v[136:137], 1, v[76:77]
	v_cvt_pk_bf16_f32 v73, v78, v79
	v_cvt_pk_bf16_f32 v74, v74, v75
	v_cvt_pk_bf16_f32 v75, v80, v81
	global_store_dwordx4 v[76:77], v[72:75], off
	v_mul_f32_e32 v70, v70, v154
	v_mul_f32_e32 v71, v71, v154
	v_mul_f32_e32 v68, v68, v154
	v_mul_f32_e32 v69, v69, v154
	v_mul_f32_e32 v72, v66, v154
	v_mul_f32_e32 v73, v67, v154
	v_mul_f32_e32 v66, v64, v154
	v_mul_f32_e32 v67, v65, v154
	v_cvt_pk_bf16_f32 v64, v68, v69
	v_cvt_pk_bf16_f32 v65, v70, v71
	s_nop 0
	v_cvt_pk_bf16_f32 v66, v66, v67
	v_cvt_pk_bf16_f32 v67, v72, v73
	global_store_dwordx4 v[76:77], v[64:67], off offset:256
.LBB0_1213:
	s_or_b64 exec, exec, s[20:21]
	s_nop 0
	v_add_u32_e32 v64, 0x80, v141
	v_cmp_gt_i32_e32 vcc, s42, v64
	s_and_saveexec_b64 s[20:21], vcc
	s_cbranch_execz .LBB0_1215
	v_mul_f32_e32 v60, v60, v150
	v_mul_f32_e32 v61, v61, v150
	v_ashrrev_i32_e32 v153, 31, v152
	v_mul_f32_e32 v64, v58, v150
	v_mul_f32_e32 v65, v59, v150
	v_mul_f32_e32 v58, v56, v150
	v_mul_f32_e32 v59, v57, v150
	v_cvt_pk_bf16_f32 v56, v60, v61
	v_lshlrev_b64 v[60:61], 11, v[152:153]
	v_lshl_add_u64 v[60:61], s[2:3], 0, v[60:61]
	v_mul_f32_e32 v62, v62, v150
	v_mul_f32_e32 v63, v63, v150
	v_lshl_add_u64 v[60:61], v[136:137], 1, v[60:61]
	v_cvt_pk_bf16_f32 v57, v62, v63
	v_cvt_pk_bf16_f32 v58, v58, v59
	v_cvt_pk_bf16_f32 v59, v64, v65
	global_store_dwordx4 v[60:61], v[56:59], off
	v_mul_f32_e32 v54, v54, v150
	v_mul_f32_e32 v55, v55, v150
	v_mul_f32_e32 v52, v52, v150
	v_mul_f32_e32 v53, v53, v150
	v_mul_f32_e32 v56, v50, v150
	v_mul_f32_e32 v57, v51, v150
	v_mul_f32_e32 v50, v48, v150
	v_mul_f32_e32 v51, v49, v150
	v_cvt_pk_bf16_f32 v48, v52, v53
	v_cvt_pk_bf16_f32 v49, v54, v55
	s_nop 0
	v_cvt_pk_bf16_f32 v50, v50, v51
	v_cvt_pk_bf16_f32 v51, v56, v57
	global_store_dwordx4 v[60:61], v[48:51], off offset:256
.LBB0_1215:
	s_or_b64 exec, exec, s[20:21]
	s_nop 0
	v_add_u32_e32 v48, 0x90, v141
	v_cmp_gt_i32_e32 vcc, s42, v48
	s_and_saveexec_b64 s[20:21], vcc
	s_cbranch_execz .LBB0_1217
	v_mul_f32_e32 v44, v44, v148
	v_mul_f32_e32 v45, v45, v148
	v_ashrrev_i32_e32 v147, 31, v146
	v_mul_f32_e32 v48, v42, v148
	v_mul_f32_e32 v49, v43, v148
	v_mul_f32_e32 v42, v40, v148
	v_mul_f32_e32 v43, v41, v148
	v_cvt_pk_bf16_f32 v40, v44, v45
	v_lshlrev_b64 v[44:45], 11, v[146:147]
	v_lshl_add_u64 v[44:45], s[2:3], 0, v[44:45]
	v_mul_f32_e32 v46, v46, v148
	v_mul_f32_e32 v47, v47, v148
	v_lshl_add_u64 v[44:45], v[136:137], 1, v[44:45]
	v_cvt_pk_bf16_f32 v41, v46, v47
	v_cvt_pk_bf16_f32 v42, v42, v43
	v_cvt_pk_bf16_f32 v43, v48, v49
	global_store_dwordx4 v[44:45], v[40:43], off
	v_mul_f32_e32 v38, v38, v148
	v_mul_f32_e32 v39, v39, v148
	v_mul_f32_e32 v36, v36, v148
	v_mul_f32_e32 v37, v37, v148
	v_mul_f32_e32 v40, v34, v148
	v_mul_f32_e32 v41, v35, v148
	v_mul_f32_e32 v34, v32, v148
	v_mul_f32_e32 v35, v33, v148
	v_cvt_pk_bf16_f32 v32, v36, v37
	v_cvt_pk_bf16_f32 v33, v38, v39
	s_nop 0
	v_cvt_pk_bf16_f32 v34, v34, v35
	v_cvt_pk_bf16_f32 v35, v40, v41
	global_store_dwordx4 v[44:45], v[32:35], off offset:256
.LBB0_1217:
	s_or_b64 exec, exec, s[20:21]
	s_nop 0
	v_add_u32_e32 v32, 0xa0, v141
	v_cmp_gt_i32_e32 vcc, s42, v32
	s_and_saveexec_b64 s[20:21], vcc
	s_cbranch_execz .LBB0_1219
	v_mul_f32_e32 v28, v28, v142
	v_mul_f32_e32 v29, v29, v142
	v_ashrrev_i32_e32 v145, 31, v144
	v_mul_f32_e32 v32, v26, v142
	v_mul_f32_e32 v33, v27, v142
	v_mul_f32_e32 v26, v24, v142
	v_mul_f32_e32 v27, v25, v142
	v_cvt_pk_bf16_f32 v24, v28, v29
	v_lshlrev_b64 v[28:29], 11, v[144:145]
	v_lshl_add_u64 v[28:29], s[2:3], 0, v[28:29]
	v_mul_f32_e32 v30, v30, v142
	v_mul_f32_e32 v31, v31, v142
	v_lshl_add_u64 v[28:29], v[136:137], 1, v[28:29]
	v_cvt_pk_bf16_f32 v25, v30, v31
	v_cvt_pk_bf16_f32 v26, v26, v27
	v_cvt_pk_bf16_f32 v27, v32, v33
	global_store_dwordx4 v[28:29], v[24:27], off
	v_mul_f32_e32 v22, v22, v142
	v_mul_f32_e32 v23, v23, v142
	v_mul_f32_e32 v20, v20, v142
	v_mul_f32_e32 v21, v21, v142
	v_mul_f32_e32 v24, v18, v142
	v_mul_f32_e32 v25, v19, v142
	v_mul_f32_e32 v18, v16, v142
	v_mul_f32_e32 v19, v17, v142
	v_cvt_pk_bf16_f32 v16, v20, v21
	v_cvt_pk_bf16_f32 v17, v22, v23
	s_nop 0
	v_cvt_pk_bf16_f32 v18, v18, v19
	v_cvt_pk_bf16_f32 v19, v24, v25
	global_store_dwordx4 v[28:29], v[16:19], off offset:256
.LBB0_1219:
	s_or_b64 exec, exec, s[20:21]
	s_nop 0
	v_add_u32_e32 v16, 0xb0, v141
	v_cmp_gt_i32_e32 vcc, s42, v16
	s_and_saveexec_b64 s[20:21], vcc
	s_cbranch_execz .LBB0_1221
	v_mul_f32_e32 v12, v12, v138
	v_mul_f32_e32 v13, v13, v138
	v_ashrrev_i32_e32 v141, 31, v140
	v_mul_f32_e32 v16, v10, v138
	v_mul_f32_e32 v17, v11, v138
	v_mul_f32_e32 v10, v8, v138
	v_mul_f32_e32 v11, v9, v138
	v_cvt_pk_bf16_f32 v8, v12, v13
	v_lshlrev_b64 v[12:13], 11, v[140:141]
	v_lshl_add_u64 v[12:13], s[2:3], 0, v[12:13]
	v_mul_f32_e32 v14, v14, v138
	v_mul_f32_e32 v15, v15, v138
	v_lshl_add_u64 v[12:13], v[136:137], 1, v[12:13]
	v_cvt_pk_bf16_f32 v9, v14, v15
	v_cvt_pk_bf16_f32 v10, v10, v11
	v_cvt_pk_bf16_f32 v11, v16, v17
	global_store_dwordx4 v[12:13], v[8:11], off
	v_mul_f32_e32 v6, v6, v138
	v_mul_f32_e32 v7, v7, v138
	v_mul_f32_e32 v4, v4, v138
	v_mul_f32_e32 v5, v5, v138
	v_mul_f32_e32 v8, v2, v138
	v_mul_f32_e32 v9, v3, v138
	v_mul_f32_e32 v2, v0, v138
	v_mul_f32_e32 v3, v1, v138
	v_cvt_pk_bf16_f32 v0, v4, v5
	v_cvt_pk_bf16_f32 v1, v6, v7
	s_nop 0
	v_cvt_pk_bf16_f32 v2, v2, v3
	v_cvt_pk_bf16_f32 v3, v8, v9
	global_store_dwordx4 v[12:13], v[0:3], off offset:256

.LBB0_1282:
	s_waitcnt vmcnt(31)
	v_lshlrev_b32_e32 v82, 16, v118
	v_and_b32_e32 v83, 0xffff0000, v118
	s_waitcnt vmcnt(27)
	v_lshlrev_b32_e32 v84, 16, v124
	v_and_b32_e32 v85, 0xffff0000, v124
	v_lshlrev_b32_e32 v86, 16, v119
	v_and_b32_e32 v87, 0xffff0000, v119
	v_lshlrev_b32_e32 v88, 16, v125
	v_and_b32_e32 v89, 0xffff0000, v125
	v_lshlrev_b32_e32 v90, 16, v114
	v_and_b32_e32 v91, 0xffff0000, v114
	s_waitcnt vmcnt(26)
	v_lshlrev_b32_e32 v92, 16, v116
	v_and_b32_e32 v93, 0xffff0000, v116
	v_lshlrev_b32_e32 v94, 16, v115
	v_and_b32_e32 v95, 0xffff0000, v115
	v_lshlrev_b32_e32 v114, 16, v117
	v_and_b32_e32 v115, 0xffff0000, v117
	v_lshlrev_b32_e32 v116, 16, v120
	v_and_b32_e32 v117, 0xffff0000, v120
	s_waitcnt vmcnt(25)
	v_lshlrev_b32_e32 v118, 16, v122
	v_and_b32_e32 v119, 0xffff0000, v122
	v_lshlrev_b32_e32 v120, 16, v121
	v_and_b32_e32 v121, 0xffff0000, v121
	v_lshlrev_b32_e32 v122, 16, v123
	v_and_b32_e32 v123, 0xffff0000, v123
	v_lshlrev_b32_e32 v124, 16, v128
	v_and_b32_e32 v125, 0xffff0000, v128
	s_waitcnt vmcnt(24)
	v_lshlrev_b32_e32 v126, 16, v130
	v_and_b32_e32 v127, 0xffff0000, v130
	v_lshlrev_b32_e32 v128, 16, v129
	v_and_b32_e32 v129, 0xffff0000, v129
	v_lshlrev_b32_e32 v130, 16, v131
	v_and_b32_e32 v131, 0xffff0000, v131
	s_waitcnt vmcnt(19)
	v_lshlrev_b32_e32 v148, 16, v152
	v_and_b32_e32 v149, 0xffff0000, v152
	s_waitcnt vmcnt(15)
	v_lshlrev_b32_e32 v150, 16, v154
	v_and_b32_e32 v151, 0xffff0000, v154
	v_lshlrev_b32_e32 v152, 16, v153
	v_and_b32_e32 v153, 0xffff0000, v153
	v_lshlrev_b32_e32 v154, 16, v155
	v_and_b32_e32 v155, 0xffff0000, v155
	v_lshlrev_b32_e32 v156, 16, v162
	v_and_b32_e32 v157, 0xffff0000, v162
	s_waitcnt vmcnt(14)
	v_lshlrev_b32_e32 v158, 16, v166
	v_and_b32_e32 v159, 0xffff0000, v166
	v_lshlrev_b32_e32 v162, 16, v163
	v_and_b32_e32 v163, 0xffff0000, v163
	v_lshlrev_b32_e32 v166, 16, v167
	v_and_b32_e32 v167, 0xffff0000, v167
	v_lshlrev_b32_e32 v168, 16, v170
	v_and_b32_e32 v169, 0xffff0000, v170
	s_waitcnt vmcnt(13)
	v_lshlrev_b32_e32 v172, 16, v174
	v_and_b32_e32 v173, 0xffff0000, v174
	v_lshlrev_b32_e32 v170, 16, v171
	v_and_b32_e32 v171, 0xffff0000, v171
	v_lshlrev_b32_e32 v174, 16, v175
	v_and_b32_e32 v175, 0xffff0000, v175
	v_lshlrev_b32_e32 v176, 16, v160
	v_and_b32_e32 v177, 0xffff0000, v160
	s_waitcnt vmcnt(12)
	v_lshlrev_b32_e32 v178, 16, v164
	v_and_b32_e32 v179, 0xffff0000, v164
	v_lshlrev_b32_e32 v160, 16, v161
	v_and_b32_e32 v161, 0xffff0000, v161
	v_lshlrev_b32_e32 v164, 16, v165
	v_and_b32_e32 v165, 0xffff0000, v165
	s_waitcnt vmcnt(7)
	v_lshlrev_b32_e32 v182, 16, v144
	v_and_b32_e32 v183, 0xffff0000, v144
	s_waitcnt vmcnt(3)
	v_lshlrev_b32_e32 v184, 16, v146
	v_and_b32_e32 v185, 0xffff0000, v146
	v_lshlrev_b32_e32 v144, 16, v145
	v_and_b32_e32 v145, 0xffff0000, v145
	v_lshlrev_b32_e32 v146, 16, v147
	v_and_b32_e32 v147, 0xffff0000, v147
	v_lshlrev_b32_e32 v186, 16, v140
	v_and_b32_e32 v187, 0xffff0000, v140
	s_waitcnt vmcnt(2)
	v_lshlrev_b32_e32 v188, 16, v142
	v_and_b32_e32 v189, 0xffff0000, v142
	v_lshlrev_b32_e32 v140, 16, v141
	v_and_b32_e32 v141, 0xffff0000, v141
	v_lshlrev_b32_e32 v142, 16, v143
	v_and_b32_e32 v143, 0xffff0000, v143
	v_add_f32_e32 v224, v82, v84
	v_add_f32_e32 v225, v83, v85
	v_add_f32_e32 v226, v86, v88
	v_add_f32_e32 v227, v87, v89
	v_add_f32_e32 v228, v90, v92
	v_add_f32_e32 v229, v91, v93
	v_add_f32_e32 v114, v94, v114
	v_add_f32_e32 v115, v95, v115
	v_lshl_add_u64 v[80:81], v[108:109], 0, s[12:13]
	v_lshlrev_b32_e32 v190, 16, v136
	v_and_b32_e32 v191, 0xffff0000, v136
	s_waitcnt vmcnt(1)
	v_lshlrev_b32_e32 v192, 16, v138
	v_and_b32_e32 v193, 0xffff0000, v138
	v_lshlrev_b32_e32 v198, 16, v137
	v_and_b32_e32 v199, 0xffff0000, v137
	v_lshlrev_b32_e32 v200, 16, v139
	v_and_b32_e32 v201, 0xffff0000, v139
	v_lshlrev_b32_e32 v206, 16, v132
	v_and_b32_e32 v207, 0xffff0000, v132
	s_waitcnt vmcnt(0)
	v_lshlrev_b32_e32 v208, 16, v134
	v_and_b32_e32 v209, 0xffff0000, v134
	v_lshlrev_b32_e32 v210, 16, v133
	v_and_b32_e32 v211, 0xffff0000, v133
	v_lshlrev_b32_e32 v212, 16, v135
	v_and_b32_e32 v213, 0xffff0000, v135
	v_add_f32_e32 v116, v116, v118
	v_add_f32_e32 v117, v117, v119
	v_add_f32_e32 v118, v120, v122
	v_add_f32_e32 v119, v121, v123
	v_add_f32_e32 v120, v124, v126
	v_add_f32_e32 v121, v125, v127
	v_add_f32_e32 v122, v128, v130
	v_add_f32_e32 v123, v129, v131
	v_add_f32_e32 v124, v148, v150
	v_add_f32_e32 v125, v149, v151
	v_add_f32_e32 v128, v152, v154
	v_add_f32_e32 v129, v153, v155
	v_add_f32_e32 v130, v156, v158
	v_add_f32_e32 v131, v157, v159
	v_add_f32_e32 v150, v162, v166
	v_add_f32_e32 v151, v163, v167
	v_add_f32_e32 v152, v168, v172
	v_add_f32_e32 v153, v169, v173
	v_add_f32_e32 v154, v170, v174
	v_add_f32_e32 v155, v171, v175
	v_add_f32_e32 v156, v176, v178
	v_add_f32_e32 v157, v177, v179
	v_add_f32_e32 v158, v160, v164
	v_add_f32_e32 v159, v161, v165
	v_add_f32_e32 v160, v182, v184
	v_add_f32_e32 v161, v183, v185
	v_add_f32_e32 v144, v144, v146
	v_add_f32_e32 v145, v145, v147
	v_add_f32_e32 v146, v186, v188
	v_add_f32_e32 v147, v187, v189
	v_add_f32_e32 v140, v140, v142
	v_add_f32_e32 v141, v141, v143
	v_fma_f32 v168, v16, v224, v32
	v_fma_f32 v169, v17, v225, v33
	v_fma_f32 v170, v18, v226, v34
	v_fma_f32 v171, v19, v227, v35
	v_fma_f32 v172, v8, v228, v36
	v_fma_f32 v173, v9, v229, v37
	v_fma_f32 v174, v10, v114, v38
	v_fma_f32 v175, v11, v115, v39
	global_load_dwordx2 v[202:203], v[80:81], off offset:-2048
	global_load_dwordx2 v[194:195], v[80:81], off offset:-1536
	global_load_dwordx2 v[136:137], v[80:81], off offset:-1024
	global_load_dwordx2 v[132:133], v[80:81], off offset:-512
	global_load_dwordx2 v[204:205], v[80:81], off
	global_load_dwordx2 v[196:197], v[80:81], off offset:512
	global_load_dwordx2 v[138:139], v[80:81], off offset:1024
	global_load_dwordx2 v[134:135], v[80:81], off offset:1536
	v_add_f32_e32 v142, v190, v192
	v_add_f32_e32 v143, v191, v193
	v_add_f32_e32 v162, v198, v200
	v_add_f32_e32 v163, v199, v201
	v_add_f32_e32 v164, v206, v208
	v_add_f32_e32 v165, v207, v209
	v_add_f32_e32 v166, v210, v212
	v_add_f32_e32 v167, v211, v213
	v_fma_f32 v118, v14, v118, v42
	v_fma_f32 v119, v15, v119, v43
	v_fma_f32 v116, v12, v116, v40
	v_fma_f32 v117, v13, v117, v41
	v_fma_f32 v122, v22, v122, v46
	v_fma_f32 v123, v23, v123, v47
	v_fma_f32 v120, v20, v120, v44
	v_fma_f32 v121, v21, v121, v45
	v_fma_f32 v114, v16, v124, v48
	v_fma_f32 v115, v17, v125, v49
	v_fma_f32 v124, v18, v128, v50
	v_fma_f32 v125, v19, v129, v51
	v_fma_f32 v52, v8, v130, v52
	v_fma_f32 v53, v9, v131, v53
	v_fma_f32 v128, v10, v150, v54
	v_fma_f32 v129, v11, v151, v55
	v_fma_f32 v54, v14, v154, v58
	v_fma_f32 v55, v15, v155, v59
	v_fma_f32 v56, v12, v152, v56
	v_fma_f32 v57, v13, v153, v57
	v_fma_f32 v58, v22, v158, v62
	v_fma_f32 v59, v23, v159, v63
	v_fma_f32 v62, v20, v156, v60
	v_fma_f32 v63, v21, v157, v61
	v_fma_f32 v32, v16, v160, v64
	v_fma_f32 v33, v17, v161, v65
	v_fma_f32 v44, v18, v144, v66
	v_fma_f32 v45, v19, v145, v67
	v_fma_f32 v34, v8, v146, v68
	v_fma_f32 v35, v9, v147, v69
	v_fma_f32 v46, v10, v140, v70
	v_fma_f32 v47, v11, v141, v71
	v_mul_f32_e32 v48, v170, v170
	v_mul_f32_e32 v49, v171, v171
	v_mul_f32_e32 v50, v168, v168
	v_mul_f32_e32 v51, v169, v169
	v_mul_f32_e32 v60, v174, v174
	v_mul_f32_e32 v61, v175, v175
	v_mul_f32_e32 v64, v172, v172
	v_mul_f32_e32 v65, v173, v173
	v_fma_f32 v36, v14, v162, v74
	v_fma_f32 v37, v15, v163, v75
	v_fma_f32 v38, v12, v142, v72
	v_fma_f32 v39, v13, v143, v73
	v_fma_f32 v40, v22, v166, v78
	v_fma_f32 v41, v23, v167, v79
	v_fma_f32 v42, v20, v164, v76
	v_fma_f32 v43, v21, v165, v77
	v_mul_f32_e32 v66, v117, v117
	v_mul_f32_e32 v68, v119, v119
	v_mul_f32_e32 v70, v124, v124
	v_mul_f32_e32 v71, v125, v125
	v_mul_f32_e32 v72, v114, v114
	v_mul_f32_e32 v73, v115, v115
	v_mul_f32_e32 v74, v128, v128
	v_mul_f32_e32 v75, v129, v129
	v_mul_f32_e32 v76, v52, v52
	v_mul_f32_e32 v77, v53, v53
	v_mul_f32_e32 v78, v57, v57
	v_mul_f32_e32 v130, v55, v55
	v_mul_f32_e32 v140, v44, v44
	v_mul_f32_e32 v141, v45, v45
	v_mul_f32_e32 v142, v32, v32
	v_mul_f32_e32 v143, v33, v33
	v_mul_f32_e32 v144, v46, v46
	v_mul_f32_e32 v145, v47, v47
	v_mul_f32_e32 v146, v34, v34
	v_mul_f32_e32 v147, v35, v35
	v_pk_mov_b32 v[154:155], v[50:51], v[48:49] op_sel:[1,0]
	v_mov_b32_e32 v51, v49
	v_pk_mov_b32 v[48:49], v[64:65], v[60:61] op_sel:[1,0]
	v_mov_b32_e32 v65, v61
	v_mul_f32_e32 v157, v122, v122
	v_mul_f32_e32 v158, v123, v123
	v_fma_f32 v60, v116, v116, v66
	v_fma_f32 v61, v117, v117, v66
	v_fma_f32 v66, v118, v118, v68
	v_fma_f32 v67, v119, v119, v68
	v_pk_mov_b32 v[68:69], v[72:73], v[70:71] op_sel:[1,0]
	v_mov_b32_e32 v73, v71
	v_pk_mov_b32 v[70:71], v[76:77], v[74:75] op_sel:[1,0]
	v_mov_b32_e32 v77, v75
	v_fma_f32 v74, v56, v56, v78
	v_fma_f32 v75, v57, v57, v78
	v_fma_f32 v78, v54, v54, v130
	v_fma_f32 v79, v55, v55, v130
	v_pk_mov_b32 v[130:131], v[142:143], v[140:141] op_sel:[1,0]
	v_mov_b32_e32 v143, v141
	v_pk_mov_b32 v[140:141], v[146:147], v[144:145] op_sel:[1,0]
	v_mov_b32_e32 v147, v145
	v_add_f32_e32 v50, v154, v50
	v_add_f32_e32 v51, v155, v51
	v_add_f32_e32 v48, v48, v64
	v_add_f32_e32 v49, v49, v65
	v_mul_f32_e32 v153, v120, v120
	v_mul_f32_e32 v156, v121, v121
	v_mul_f32_e32 v150, v39, v39
	v_mul_f32_e32 v152, v37, v37
	v_mov_b32_e32 v61, v157
	v_mov_b32_e32 v67, v158
	v_add_f32_e32 v64, v68, v72
	v_add_f32_e32 v65, v69, v73
	v_add_f32_e32 v68, v70, v76
	v_add_f32_e32 v69, v71, v77
	v_add_f32_e32 v70, v130, v142
	v_add_f32_e32 v71, v131, v143
	v_add_f32_e32 v72, v140, v146
	v_add_f32_e32 v73, v141, v147
	v_add_f32_e32 v76, v50, v51
	v_add_f32_e32 v77, v51, v50
	v_add_f32_e32 v130, v48, v49
	v_add_f32_e32 v131, v49, v48
	v_mul_f32_e32 v159, v62, v62
	v_mul_f32_e32 v160, v63, v63
	v_mul_f32_e32 v161, v58, v58
	v_mul_f32_e32 v162, v59, v59
	v_mul_f32_e32 v163, v42, v42
	v_mul_f32_e32 v164, v43, v43
	v_mul_f32_e32 v165, v40, v40
	v_mul_f32_e32 v166, v41, v41
	v_fma_f32 v144, v38, v38, v150
	v_fma_f32 v145, v39, v39, v150
	v_fma_f32 v150, v36, v36, v152
	v_fma_f32 v151, v37, v37, v152
	v_add_f32_e32 v60, v60, v66
	v_add_f32_e32 v61, v61, v67
	v_pk_add_f32 v[64:65], v[64:65], v[64:65] op_sel:[0,1] op_sel_hi:[1,0]
	v_add_f32_e32 v66, v68, v69
	v_add_f32_e32 v67, v69, v68
	v_pk_add_f32 v[70:71], v[70:71], v[70:71] op_sel:[0,1] op_sel_hi:[1,0]
	v_pk_add_f32 v[72:73], v[72:73], v[72:73] op_sel:[0,1] op_sel_hi:[1,0]
	v_mov_b32_e32 v77, v153
	v_mov_b32_e32 v131, v156
	v_mov_b32_e32 v75, v161
	v_mov_b32_e32 v79, v162
	v_mov_b32_e32 v145, v165
	v_mov_b32_e32 v151, v166
	v_mov_b32_e32 v65, v159
	v_mov_b32_e32 v67, v160
	v_mov_b32_e32 v71, v163
	v_mov_b32_e32 v73, v164
	v_add_f32_e32 v76, v76, v130
	v_add_f32_e32 v77, v77, v131
	v_add_f32_e32 v68, v74, v78
	v_add_f32_e32 v69, v75, v79
	v_add_f32_e32 v74, v144, v150
	v_add_f32_e32 v75, v145, v151
	v_add_f32_e32 v64, v64, v66
	v_add_f32_e32 v65, v65, v67
	v_add_f32_e32 v66, v70, v72
	v_add_f32_e32 v67, v71, v73
	v_add_f32_e32 v70, v76, v60
	v_add_f32_e32 v71, v77, v61
	v_add_f32_e32 v68, v64, v68
	v_add_f32_e32 v69, v65, v69
	v_add_f32_e32 v66, v66, v74
	v_add_f32_e32 v67, v67, v75
	v_add_f32_e32 v70, v70, v71
	v_add_f32_e32 v68, v68, v69
	v_add_f32_e32 v66, v66, v67
	ds_bpermute_b32 v67, v214, v70
	ds_bpermute_b32 v69, v214, v68
	ds_bpermute_b32 v71, v214, v66
	v_lshl_add_u64 v[112:113], v[110:111], 0, s[12:13]
	v_add_co_u32_e32 v180, vcc, s24, v112
	s_waitcnt lgkmcnt(2)
	v_add_f32_e32 v67, v70, v67
	v_addc_co_u32_e32 v181, vcc, 0, v113, vcc
	global_load_dwordx4 v[92:95], v[180:181], off
	global_load_dwordx4 v[88:91], v[180:181], off offset:1024
	global_load_dwordx4 v[84:87], v[180:181], off offset:2048
	global_load_dwordx4 v[80:83], v[180:181], off offset:3072
	s_waitcnt lgkmcnt(1)
	v_add_f32_e32 v68, v68, v69
	s_waitcnt lgkmcnt(0)
	v_add_f32_e32 v66, v66, v71
	ds_bpermute_b32 v69, v215, v67
	ds_bpermute_b32 v71, v215, v66
	ds_bpermute_b32 v70, v215, v68
	s_add_i32 s27, s26, -4
	s_cmp_lt_u32 s27, 28
	s_waitcnt lgkmcnt(2)
	v_add_f32_e32 v67, v67, v69
	s_waitcnt lgkmcnt(1)
	v_add_f32_e32 v66, v66, v71
	ds_bpermute_b32 v69, v216, v67
	s_waitcnt lgkmcnt(1)
	v_add_f32_e32 v68, v68, v70
	ds_bpermute_b32 v71, v216, v66
	ds_bpermute_b32 v70, v216, v68
	s_cselect_b32 s4, s26, 28
	s_waitcnt lgkmcnt(2)
	v_add_f32_e32 v67, v67, v69
	ds_bpermute_b32 v69, v217, v67
	s_waitcnt lgkmcnt(2)
	v_add_f32_e32 v66, v66, v71
	s_waitcnt lgkmcnt(1)
	v_add_f32_e32 v68, v68, v70
	ds_bpermute_b32 v71, v217, v66
	ds_bpermute_b32 v70, v217, v68
	s_waitcnt lgkmcnt(2)
	v_add_f32_e32 v67, v67, v69
	ds_bpermute_b32 v69, v218, v67
	s_add_u32 s2, s20, s4
	s_waitcnt lgkmcnt(2)
	v_add_f32_e32 v66, v66, v71
	s_waitcnt lgkmcnt(1)
	v_add_f32_e32 v68, v68, v70
	ds_bpermute_b32 v71, v218, v66
	ds_bpermute_b32 v70, v218, v68
	s_waitcnt lgkmcnt(2)
	v_add_f32_e32 v67, v67, v69
	s_addc_u32 s3, s21, 0
	ds_bpermute_b32 v69, v219, v67
	s_waitcnt lgkmcnt(2)
	v_add_f32_e32 v66, v66, v71
	s_or_b32 s5, s4, 1
	s_lshl_b64 s[2:3], s[2:3], 12
	s_waitcnt lgkmcnt(1)
	v_add_f32_e32 v68, v68, v70
	ds_bpermute_b32 v71, v219, v66
	v_lshl_add_u64 v[50:51], v[96:97], 0, s[2:3]
	v_lshl_add_u64 v[48:49], v[102:103], 0, s[2:3]
	s_add_u32 s2, s20, s5
	ds_bpermute_b32 v70, v219, v68
	s_addc_u32 s3, s21, 0
	s_or_b32 s4, s4, 2
	s_lshl_b64 s[2:3], s[2:3], 12
	v_add_co_u32_e32 v148, vcc, s22, v112
	v_lshl_add_u64 v[60:61], v[96:97], 0, s[2:3]
	v_lshl_add_u64 v[64:65], v[102:103], 0, s[2:3]
	s_add_u32 s2, s20, s4
	s_waitcnt lgkmcnt(2)
	v_add_f32_e32 v67, v67, v69
	v_addc_co_u32_e32 v149, vcc, 0, v113, vcc
	s_addc_u32 s3, s21, 0
	s_waitcnt lgkmcnt(1)
	v_add_f32_e32 v66, v66, v71
	v_fmamk_f32 v67, v67, 0x3a800000, v220
	v_add_co_u32_e32 v126, vcc, s23, v112
	s_lshl_b64 s[2:3], s[2:3], 12
	s_waitcnt lgkmcnt(0)
	v_add_f32_e32 v68, v68, v70
	v_fmamk_f32 v66, v66, 0x3a800000, v220
	v_mul_f32_e32 v69, 0x4f800000, v67
	v_cmp_gt_f32_e64 s[4:5], s25, v67
	v_addc_co_u32_e32 v127, vcc, 0, v113, vcc
	v_lshl_add_u64 v[76:77], v[96:97], 0, s[2:3]
	v_lshl_add_u64 v[150:151], v[102:103], 0, s[2:3]
	v_fmamk_f32 v68, v68, 0x3a800000, v220
	v_mul_f32_e32 v71, 0x4f800000, v66
	v_cmp_gt_f32_e64 s[2:3], s25, v66
	v_cndmask_b32_e64 v67, v67, v69, s[4:5]
	v_mul_f32_e32 v70, 0x4f800000, v68
	v_cmp_gt_f32_e32 vcc, s25, v68
	v_cndmask_b32_e64 v66, v66, v71, s[2:3]
	v_sqrt_f32_e32 v69, v67
	v_cndmask_b32_e32 v68, v68, v70, vcc
	v_sqrt_f32_e32 v71, v66
	v_sqrt_f32_e32 v70, v68
	v_add_u32_e32 v72, -1, v69
	v_add_u32_e32 v73, 1, v69
	v_add_u32_e32 v78, -1, v71
	v_fma_f32 v130, -v72, v69, v67
	v_add_u32_e32 v74, -1, v70
	v_add_u32_e32 v79, 1, v71
	v_fma_f32 v131, -v73, v69, v67
	v_fma_f32 v142, -v78, v71, v66
	v_cmp_ge_f32_e64 s[6:7], 0, v130
	v_add_u32_e32 v75, 1, v70
	v_fma_f32 v140, -v74, v70, v68
	v_fma_f32 v143, -v79, v71, v66
	v_cndmask_b32_e64 v69, v69, v72, s[6:7]
	v_cmp_ge_f32_e64 s[8:9], 0, v142
	v_cmp_lt_f32_e64 s[10:11], 0, v131
	v_fma_f32 v141, -v75, v70, v68
	v_cmp_ge_f32_e64 s[6:7], 0, v140
	v_cndmask_b32_e64 v71, v71, v78, s[8:9]
	v_cmp_lt_f32_e64 s[8:9], 0, v143
	v_cndmask_b32_e64 v69, v69, v73, s[10:11]
	v_cndmask_b32_e64 v70, v70, v74, s[6:7]
	v_cmp_lt_f32_e64 s[6:7], 0, v141
	v_cndmask_b32_e64 v71, v71, v79, s[8:9]
	v_mul_f32_e32 v72, 0x37800000, v69
	v_cndmask_b32_e64 v70, v70, v75, s[6:7]
	v_mul_f32_e32 v74, 0x37800000, v71
	v_cndmask_b32_e64 v69, v69, v72, s[4:5]
	v_cmp_class_f32_e64 s[4:5], v67, v221
	v_mul_f32_e32 v73, 0x37800000, v70
	v_cndmask_b32_e64 v71, v71, v74, s[2:3]
	v_cmp_class_f32_e64 s[2:3], v66, v221
	v_cndmask_b32_e64 v67, v69, v67, s[4:5]
	v_cndmask_b32_e32 v70, v70, v73, vcc
	v_cmp_class_f32_e32 vcc, v68, v221
	v_cndmask_b32_e64 v146, v71, v66, s[2:3]
	v_div_scale_f32 v66, s[2:3], v67, v67, 1.0
	v_cndmask_b32_e32 v130, v70, v68, vcc
	v_rcp_f32_e32 v73, v66
	v_div_scale_f32 v69, s[2:3], v130, v130, 1.0
	v_div_scale_f32 v71, s[4:5], v146, v146, 1.0
	v_rcp_f32_e32 v74, v69
	v_rcp_f32_e32 v131, v71
	v_fma_f32 v75, -v66, v73, 1.0
	v_div_scale_f32 v68, vcc, 1.0, v67, 1.0
	v_fmac_f32_e32 v73, v75, v73
	v_fma_f32 v78, -v69, v74, 1.0
	v_fma_f32 v79, -v71, v131, 1.0
	v_mul_f32_e32 v75, v68, v73
	v_div_scale_f32 v70, s[2:3], 1.0, v130, 1.0
	v_fmac_f32_e32 v74, v78, v74
	v_fmac_f32_e32 v131, v79, v131
	v_fma_f32 v79, -v66, v75, v68
	v_div_scale_f32 v72, s[4:5], 1.0, v146, 1.0
	v_mul_f32_e32 v78, v70, v74
	v_fmac_f32_e32 v75, v79, v73
	v_mul_f32_e32 v140, v72, v131
	v_fma_f32 v141, -v69, v78, v70
	v_fma_f32 v66, -v66, v75, v68
	v_fma_f32 v142, -v71, v140, v72
	v_fmac_f32_e32 v78, v141, v74
	v_div_fmas_f32 v66, v66, v73, v75
	v_fmac_f32_e32 v140, v142, v131
	v_fma_f32 v68, -v69, v78, v70
	v_div_fixup_f32 v66, v66, v67, 1.0
	s_mov_b64 vcc, s[2:3]
	v_fma_f32 v141, -v71, v140, v72
	v_div_fmas_f32 v142, v68, v74, v78
	v_mul_f32_e32 v68, v66, v170
	v_mul_f32_e32 v69, v66, v171
	v_mul_f32_e32 v70, v66, v168
	v_mul_f32_e32 v71, v66, v169
	s_mov_b64 vcc, s[4:5]
	v_mul_f32_e32 v72, v66, v174
	v_mul_f32_e32 v73, v66, v175
	v_mul_f32_e32 v74, v66, v172
	v_mul_f32_e32 v75, v66, v173
	v_mul_f32_e32 v78, v66, v118
	v_mul_f32_e32 v79, v66, v119
	v_mul_f32_e32 v116, v66, v116
	v_mul_f32_e32 v117, v66, v117
; __global__ void __launch_bounds__(512, 2) hymba_fwd(Args args) {
;     ...
;             P9_LD(0, 0); P9_LD(1, 1); P9_LD(2, 2); asm volatile("" ::: "memory");
; #pragma nounroll
;             for (int rr = 0; rr < 32; rr += 4) { const int r4 = (rr + 4 < 32) ? rr + 4 : 28;
;                 P9_LD(3, rr + 3); asm volatile("" ::: "memory"); P9_ST(0, rr); asm volatile("" ::: "memory");
;                 P9_LD(0, r4); asm volatile("" ::: "memory"); P9_ST(1, rr + 1); asm volatile("" ::: "memory");
;                 P9_LD(1, r4 + 1); asm volatile("" ::: "memory"); P9_ST(2, rr + 2); asm volatile("" ::: "memory");
;                 P9_LD(2, r4 + 2); asm volatile("" ::: "memory"); P9_ST(3, rr + 3); asm volatile("" ::: "memory"); }
	v_mul_f32_e32 v118, v66, v122
	v_mul_f32_e32 v119, v66, v123
	v_mul_f32_e32 v67, v66, v121
	v_mul_f32_e32 v66, v66, v120
	v_div_fixup_f32 v120, v142, v130, 1.0
	v_div_fmas_f32 v121, v141, v131, v140
	v_mul_f32_e32 v70, v70, v0
	v_mul_f32_e32 v71, v71, v1
	v_mul_f32_e32 v68, v68, v2
	v_mul_f32_e32 v69, v69, v3
	v_mul_f32_e32 v74, v74, v4
	v_mul_f32_e32 v75, v75, v5
	v_mul_f32_e32 v72, v72, v6
	v_mul_f32_e32 v73, v73, v7
	v_mul_f32_e32 v116, v116, v24
	v_mul_f32_e32 v117, v117, v25
	v_mul_f32_e32 v78, v78, v26
	v_mul_f32_e32 v79, v79, v27
	v_mul_f32_e32 v122, v66, v28
	v_mul_f32_e32 v123, v67, v29
	v_mul_f32_e32 v118, v118, v30
	v_mul_f32_e32 v119, v119, v31
	v_mul_f32_e32 v124, v120, v124
	v_mul_f32_e32 v125, v120, v125
	v_mul_f32_e32 v114, v120, v114
	v_mul_f32_e32 v115, v120, v115
	v_mul_f32_e32 v128, v120, v128
	v_mul_f32_e32 v129, v120, v129
	v_mul_f32_e32 v130, v120, v52
	v_mul_f32_e32 v131, v120, v53
	v_mul_f32_e32 v140, v120, v54
	v_mul_f32_e32 v141, v120, v55
	v_mul_f32_e32 v142, v120, v56
	v_mul_f32_e32 v143, v120, v57
	v_mul_f32_e32 v144, v120, v58
	v_mul_f32_e32 v145, v120, v59
	v_mul_f32_e32 v62, v120, v62
	v_mul_f32_e32 v63, v120, v63
	v_div_fixup_f32 v120, v121, v146, 1.0
	v_cndmask_b32_e64 v55, v222, v69, s[0:1]
	v_cndmask_b32_e64 v54, v222, v68, s[0:1]
	v_cndmask_b32_e64 v53, v222, v71, s[0:1]
	v_cndmask_b32_e64 v52, v222, v70, s[0:1]
	v_cndmask_b32_e64 v59, v222, v73, s[0:1]
	v_cndmask_b32_e64 v58, v222, v72, s[0:1]
	v_cndmask_b32_e64 v57, v222, v75, s[0:1]
	v_cndmask_b32_e64 v56, v222, v74, s[0:1]
	v_cndmask_b32_e64 v69, v222, v79, s[0:1]
	v_cndmask_b32_e64 v68, v222, v78, s[0:1]
	v_cndmask_b32_e64 v67, v222, v117, s[0:1]
	v_cndmask_b32_e64 v66, v222, v116, s[0:1]
	v_cndmask_b32_e64 v73, v222, v119, s[0:1]
	v_cndmask_b32_e64 v72, v222, v118, s[0:1]
	v_cndmask_b32_e64 v71, v222, v123, s[0:1]
	v_cndmask_b32_e64 v70, v222, v122, s[0:1]
	v_mul_f32_e32 v74, v114, v0
	v_mul_f32_e32 v75, v115, v1
	v_mul_f32_e32 v78, v124, v2
	v_mul_f32_e32 v79, v125, v3
	v_mul_f32_e32 v44, v120, v44
	v_mul_f32_e32 v45, v120, v45
	v_mul_f32_e32 v32, v120, v32
	v_mul_f32_e32 v33, v120, v33
	v_mul_f32_e32 v46, v120, v46
	v_mul_f32_e32 v47, v120, v47
	v_mul_f32_e32 v34, v120, v34
	v_mul_f32_e32 v35, v120, v35
	v_mul_f32_e32 v36, v120, v36
	v_mul_f32_e32 v37, v120, v37
	v_mul_f32_e32 v38, v120, v38
	v_mul_f32_e32 v39, v120, v39
	v_mul_f32_e32 v40, v120, v40
	v_mul_f32_e32 v41, v120, v41
	v_mul_f32_e32 v42, v120, v42
	v_mul_f32_e32 v43, v120, v43
	global_store_dwordx4 v[112:113], v[52:55], off
	global_store_dwordx4 v[112:113], v[56:59], off offset:1024
	global_store_dwordx4 v[112:113], v[66:69], off offset:2048
	global_store_dwordx4 v[112:113], v[70:73], off offset:3072
	v_mul_f32_e32 v114, v130, v4
	v_mul_f32_e32 v115, v131, v5
	v_mul_f32_e32 v116, v128, v6
	v_mul_f32_e32 v117, v129, v7
	v_mul_f32_e32 v118, v142, v24
	v_mul_f32_e32 v119, v143, v25
	v_mul_f32_e32 v122, v140, v26
	v_mul_f32_e32 v123, v141, v27
	v_mul_f32_e32 v62, v62, v28
	v_mul_f32_e32 v63, v63, v29
	v_mul_f32_e32 v124, v144, v30
	v_mul_f32_e32 v125, v145, v31
	v_cndmask_b32_e64 v55, v222, v79, s[0:1]
	v_cndmask_b32_e64 v54, v222, v78, s[0:1]
	v_cndmask_b32_e64 v53, v222, v75, s[0:1]
	v_cndmask_b32_e64 v52, v222, v74, s[0:1]
	v_mul_f32_e32 v32, v32, v0
	v_mul_f32_e32 v33, v33, v1
	v_mul_f32_e32 v44, v44, v2
	v_mul_f32_e32 v45, v45, v3
	v_mul_f32_e32 v34, v34, v4
	v_mul_f32_e32 v35, v35, v5
	v_mul_f32_e32 v46, v46, v6
	v_mul_f32_e32 v47, v47, v7
	v_mul_f32_e32 v38, v38, v24
	v_mul_f32_e32 v39, v39, v25
	v_mul_f32_e32 v36, v36, v26
	v_mul_f32_e32 v37, v37, v27
	v_mul_f32_e32 v42, v42, v28
	v_mul_f32_e32 v43, v43, v29
	v_mul_f32_e32 v40, v40, v30
	v_mul_f32_e32 v41, v41, v31
	v_cndmask_b32_e64 v59, v222, v117, s[0:1]
	v_cndmask_b32_e64 v58, v222, v116, s[0:1]
	v_cndmask_b32_e64 v57, v222, v115, s[0:1]
	v_cndmask_b32_e64 v56, v222, v114, s[0:1]
	v_cndmask_b32_e64 v69, v222, v123, s[0:1]
	v_cndmask_b32_e64 v68, v222, v122, s[0:1]
	v_cndmask_b32_e64 v67, v222, v119, s[0:1]
	v_cndmask_b32_e64 v66, v222, v118, s[0:1]
	v_cndmask_b32_e64 v73, v222, v125, s[0:1]
	v_cndmask_b32_e64 v72, v222, v124, s[0:1]
	v_cndmask_b32_e64 v71, v222, v63, s[0:1]
	v_cndmask_b32_e64 v70, v222, v62, s[0:1]
	v_cndmask_b32_e64 v143, v222, v45, s[0:1]
	v_cndmask_b32_e64 v142, v222, v44, s[0:1]
	v_cndmask_b32_e64 v141, v222, v33, s[0:1]
	v_cndmask_b32_e64 v140, v222, v32, s[0:1]
	v_cndmask_b32_e64 v147, v222, v47, s[0:1]
	v_cndmask_b32_e64 v146, v222, v46, s[0:1]
	v_cndmask_b32_e64 v145, v222, v35, s[0:1]
	v_cndmask_b32_e64 v144, v222, v34, s[0:1]
	v_cndmask_b32_e64 v159, v222, v37, s[0:1]
	v_cndmask_b32_e64 v158, v222, v36, s[0:1]
	v_cndmask_b32_e64 v157, v222, v39, s[0:1]
	v_cndmask_b32_e64 v156, v222, v38, s[0:1]
	v_cndmask_b32_e64 v179, v222, v41, s[0:1]
	v_cndmask_b32_e64 v178, v222, v40, s[0:1]
	v_cndmask_b32_e64 v177, v222, v43, s[0:1]
	v_cndmask_b32_e64 v176, v222, v42, s[0:1]
	global_load_dwordx4 v[32:35], v[50:51], off
	global_load_dwordx4 v[36:39], v[50:51], off offset:1024
	global_load_dwordx4 v[40:43], v[50:51], off offset:2048
	global_load_dwordx4 v[44:47], v[50:51], off offset:3072
	global_load_dwordx2 v[118:119], v[48:49], off
	global_load_dwordx2 v[114:115], v[48:49], off offset:512
	global_load_dwordx2 v[120:121], v[48:49], off offset:1024
	global_load_dwordx2 v[128:129], v[48:49], off offset:1536
	global_load_dwordx2 v[124:125], v[48:49], off offset:2048
	global_load_dwordx2 v[116:117], v[48:49], off offset:2560
	global_load_dwordx2 v[122:123], v[48:49], off offset:3072
	global_load_dwordx2 v[130:131], v[48:49], off offset:3584
	global_store_dwordx4 v[126:127], v[52:55], off offset:-4096
	global_store_dwordx4 v[148:149], v[56:59], off offset:1024
	global_store_dwordx4 v[148:149], v[66:69], off offset:2048
	global_store_dwordx4 v[148:149], v[70:73], off offset:3072
	global_load_dwordx4 v[48:51], v[60:61], off
	global_load_dwordx4 v[52:55], v[60:61], off offset:1024
	global_load_dwordx4 v[56:59], v[60:61], off offset:2048
	s_nop 0
	global_load_dwordx4 v[60:63], v[60:61], off offset:3072
	s_nop 0
	global_load_dwordx2 v[152:153], v[64:65], off
	global_load_dwordx2 v[162:163], v[64:65], off offset:512
	global_load_dwordx2 v[170:171], v[64:65], off offset:1024
	global_load_dwordx2 v[160:161], v[64:65], off offset:1536
	global_load_dwordx2 v[154:155], v[64:65], off offset:2048
	global_load_dwordx2 v[166:167], v[64:65], off offset:2560
	global_load_dwordx2 v[174:175], v[64:65], off offset:3072
	global_load_dwordx2 v[164:165], v[64:65], off offset:3584
	global_store_dwordx4 v[126:127], v[140:143], off
	global_store_dwordx4 v[126:127], v[144:147], off offset:1024
	global_store_dwordx4 v[126:127], v[156:159], off offset:2048
	global_store_dwordx4 v[126:127], v[176:179], off offset:3072
	s_waitcnt vmcnt(47)
	v_lshlrev_b32_e32 v64, 16, v202
	v_and_b32_e32 v65, 0xffff0000, v202
	s_waitcnt vmcnt(43)
	v_lshlrev_b32_e32 v66, 16, v204
	v_and_b32_e32 v67, 0xffff0000, v204
	v_lshlrev_b32_e32 v68, 16, v203
	v_and_b32_e32 v69, 0xffff0000, v203
	v_lshlrev_b32_e32 v70, 16, v205
	v_and_b32_e32 v71, 0xffff0000, v205
	v_lshlrev_b32_e32 v72, 16, v194
	v_and_b32_e32 v73, 0xffff0000, v194
	s_waitcnt vmcnt(42)
	v_lshlrev_b32_e32 v74, 16, v196
	v_and_b32_e32 v75, 0xffff0000, v196
	v_lshlrev_b32_e32 v78, 16, v195
	v_and_b32_e32 v79, 0xffff0000, v195
	v_lshlrev_b32_e32 v112, 16, v197
	v_and_b32_e32 v113, 0xffff0000, v197
	v_lshlrev_b32_e32 v126, 16, v136
	v_and_b32_e32 v127, 0xffff0000, v136
	s_waitcnt vmcnt(41)
	v_lshlrev_b32_e32 v140, 16, v138
	v_and_b32_e32 v141, 0xffff0000, v138
	v_lshlrev_b32_e32 v136, 16, v137
	v_and_b32_e32 v137, 0xffff0000, v137
	v_lshlrev_b32_e32 v138, 16, v139
	v_and_b32_e32 v139, 0xffff0000, v139
	v_lshlrev_b32_e32 v142, 16, v132
	v_and_b32_e32 v143, 0xffff0000, v132
	s_waitcnt vmcnt(40)
	v_lshlrev_b32_e32 v144, 16, v134
	v_and_b32_e32 v145, 0xffff0000, v134
	v_lshlrev_b32_e32 v132, 16, v133
	v_and_b32_e32 v133, 0xffff0000, v133
	v_lshlrev_b32_e32 v134, 16, v135
	v_and_b32_e32 v135, 0xffff0000, v135
	v_add_f32_e32 v148, v64, v66
	v_add_f32_e32 v149, v65, v67
	v_add_f32_e32 v156, v68, v70
	v_add_f32_e32 v157, v69, v71
	v_add_f32_e32 v158, v72, v74
	v_add_f32_e32 v159, v73, v75
	v_add_f32_e32 v112, v78, v112
	v_add_f32_e32 v113, v79, v113
	v_add_f32_e32 v126, v126, v140
	v_add_f32_e32 v127, v127, v141
	v_add_f32_e32 v168, v136, v138
	v_add_f32_e32 v169, v137, v139
	v_add_f32_e32 v172, v142, v144
	v_add_f32_e32 v173, v143, v145
	v_add_f32_e32 v176, v132, v134
	v_add_f32_e32 v177, v133, v135
	global_load_dwordx4 v[64:67], v[76:77], off
	global_load_dwordx4 v[68:71], v[76:77], off offset:1024
	global_load_dwordx4 v[72:75], v[76:77], off offset:2048
	s_nop 0
	global_load_dwordx4 v[76:79], v[76:77], off offset:3072
	s_nop 0
	global_load_dwordx2 v[144:145], v[150:151], off
	global_load_dwordx2 v[140:141], v[150:151], off offset:512
	global_load_dwordx2 v[136:137], v[150:151], off offset:1024
	global_load_dwordx2 v[132:133], v[150:151], off offset:1536
	global_load_dwordx2 v[146:147], v[150:151], off offset:2048
	global_load_dwordx2 v[142:143], v[150:151], off offset:2560
	global_load_dwordx2 v[138:139], v[150:151], off offset:3072
	global_load_dwordx2 v[134:135], v[150:151], off offset:3584
	s_waitcnt vmcnt(51)
	v_fma_f32 v92, v16, v148, v92
	v_fma_f32 v93, v17, v149, v93
	v_fma_f32 v94, v18, v156, v94
	v_fma_f32 v95, v19, v157, v95
	s_waitcnt vmcnt(50)
	v_fma_f32 v88, v8, v158, v88
	v_fma_f32 v89, v9, v159, v89
	v_fma_f32 v90, v10, v112, v90
	v_fma_f32 v91, v11, v113, v91
	s_waitcnt vmcnt(49)
	v_fma_f32 v84, v12, v126, v84
	v_fma_f32 v85, v13, v127, v85
	v_mul_f32_e32 v112, v94, v94
	v_mul_f32_e32 v113, v95, v95
	v_mul_f32_e32 v126, v92, v92
	v_mul_f32_e32 v127, v93, v93
	v_mul_f32_e32 v148, v90, v90
	v_mul_f32_e32 v149, v91, v91
	v_mul_f32_e32 v150, v88, v88
	v_mul_f32_e32 v151, v89, v89
	v_fma_f32 v86, v14, v168, v86
	v_fma_f32 v87, v15, v169, v87
	s_waitcnt vmcnt(48)
	v_fma_f32 v80, v20, v172, v80
	v_fma_f32 v81, v21, v173, v81
	v_pk_mov_b32 v[168:169], v[126:127], v[112:113] op_sel:[1,0]
	v_mov_b32_e32 v127, v113
	v_pk_mov_b32 v[112:113], v[150:151], v[148:149] op_sel:[1,0]
	v_mov_b32_e32 v151, v149
	v_fma_f32 v82, v22, v176, v82
	v_fma_f32 v83, v23, v177, v83
	v_mul_f32_e32 v159, v80, v80
	v_mul_f32_e32 v156, v85, v85
	v_mul_f32_e32 v158, v87, v87
	v_add_f32_e32 v126, v168, v126
	v_add_f32_e32 v127, v169, v127
	v_add_f32_e32 v112, v112, v150
	v_add_f32_e32 v113, v113, v151
	v_mul_f32_e32 v172, v81, v81
	v_mul_f32_e32 v173, v82, v82
	v_mul_f32_e32 v176, v83, v83
	v_fma_f32 v148, v84, v84, v156
	v_fma_f32 v149, v85, v85, v156
	v_fma_f32 v156, v86, v86, v158
	v_fma_f32 v157, v87, v87, v158
	v_pk_add_f32 v[126:127], v[126:127], v[126:127] op_sel:[0,1] op_sel_hi:[1,0]
	v_pk_add_f32 v[112:113], v[112:113], v[112:113] op_sel:[0,1] op_sel_hi:[1,0]
	v_mov_b32_e32 v149, v173
	v_mov_b32_e32 v157, v176
	v_mov_b32_e32 v127, v159
	v_mov_b32_e32 v113, v172
	v_add_f32_e32 v148, v148, v156
	v_add_f32_e32 v149, v149, v157
	v_add_f32_e32 v112, v126, v112
	v_add_f32_e32 v113, v127, v113
	s_add_i32 s26, s26, 4
	v_add_f32_e32 v112, v112, v148
	v_add_f32_e32 v113, v113, v149
	v_lshl_add_u64 v[110:111], v[110:111], 0, s[18:19]
	v_add_f32_e32 v112, v112, v113
	ds_bpermute_b32 v113, v214, v112
	s_cmp_gt_u32 s27, 27
	v_lshl_add_u64 v[108:109], v[108:109], 0, s[18:19]
	s_waitcnt lgkmcnt(0)
; __global__ void __launch_bounds__(512, 2) hymba_fwd(Args args) {
;     ...
;             P9_LD(0, 0); P9_LD(1, 1); P9_LD(2, 2); asm volatile("" ::: "memory");
; #pragma nounroll
;             for (int rr = 0; rr < 32; rr += 4) { const int r4 = (rr + 4 < 32) ? rr + 4 : 28;
;                 P9_LD(3, rr + 3); asm volatile("" ::: "memory"); P9_ST(0, rr); asm volatile("" ::: "memory");
;                 P9_LD(0, r4); asm volatile("" ::: "memory"); P9_ST(1, rr + 1); asm volatile("" ::: "memory");
;                 P9_LD(1, r4 + 1); asm volatile("" ::: "memory"); P9_ST(2, rr + 2); asm volatile("" ::: "memory");
;                 P9_LD(2, r4 + 2); asm volatile("" ::: "memory"); P9_ST(3, rr + 3); asm volatile("" ::: "memory"); }
	v_add_f32_e32 v112, v112, v113
	ds_bpermute_b32 v113, v215, v112
	s_waitcnt lgkmcnt(0)
	v_add_f32_e32 v112, v112, v113
	ds_bpermute_b32 v113, v216, v112
	s_waitcnt lgkmcnt(0)
	v_add_f32_e32 v112, v112, v113
	ds_bpermute_b32 v113, v217, v112
	s_waitcnt lgkmcnt(0)
	v_add_f32_e32 v112, v112, v113
	ds_bpermute_b32 v113, v218, v112
	s_waitcnt lgkmcnt(0)
	v_add_f32_e32 v112, v112, v113
	ds_bpermute_b32 v113, v219, v112
	s_waitcnt lgkmcnt(0)
	v_add_f32_e32 v112, v112, v113
	v_fmamk_f32 v112, v112, 0x3a800000, v220
	v_mul_f32_e32 v113, 0x4f800000, v112
	v_cmp_gt_f32_e32 vcc, s25, v112
	s_nop 1
	v_cndmask_b32_e32 v112, v112, v113, vcc
	v_sqrt_f32_e32 v113, v112
	s_nop 0
	v_add_u32_e32 v126, -1, v113
	v_add_u32_e32 v127, 1, v113
	v_fma_f32 v148, -v126, v113, v112
	v_fma_f32 v149, -v127, v113, v112
	v_cmp_ge_f32_e64 s[2:3], 0, v148
	s_nop 1
	v_cndmask_b32_e64 v113, v113, v126, s[2:3]
	v_cmp_lt_f32_e64 s[2:3], 0, v149
	s_nop 1
	v_cndmask_b32_e64 v113, v113, v127, s[2:3]
	v_mul_f32_e32 v126, 0x37800000, v113
	v_cndmask_b32_e32 v113, v113, v126, vcc
	v_cmp_class_f32_e32 vcc, v112, v221
	s_nop 1
	v_cndmask_b32_e32 v112, v113, v112, vcc
	v_div_scale_f32 v113, s[2:3], v112, v112, 1.0
	v_rcp_f32_e32 v127, v113
	v_div_scale_f32 v126, vcc, 1.0, v112, 1.0
	v_fma_f32 v148, -v113, v127, 1.0
	v_fmac_f32_e32 v127, v148, v127
	v_mul_f32_e32 v148, v126, v127
	v_fma_f32 v149, -v113, v148, v126
	v_fmac_f32_e32 v148, v149, v127
	v_fma_f32 v113, -v113, v148, v126
	v_div_fmas_f32 v113, v113, v127, v148
	v_div_fixup_f32 v112, v113, v112, 1.0
	v_mul_f32_e32 v94, v112, v94
	v_mul_f32_e32 v95, v112, v95
	v_mul_f32_e32 v92, v112, v92
	v_mul_f32_e32 v93, v112, v93
	v_mul_f32_e32 v90, v112, v90
	v_mul_f32_e32 v91, v112, v91
	v_mul_f32_e32 v88, v112, v88
	v_mul_f32_e32 v89, v112, v89
	v_mul_f32_e32 v86, v112, v86
	v_mul_f32_e32 v87, v112, v87
	v_mul_f32_e32 v84, v112, v84
	v_mul_f32_e32 v85, v112, v85
	v_mul_f32_e32 v82, v112, v82
	v_mul_f32_e32 v83, v112, v83
	v_mul_f32_e32 v80, v112, v80
	v_mul_f32_e32 v81, v112, v81
	v_mul_f32_e32 v92, v92, v0
	v_mul_f32_e32 v93, v93, v1
	v_mul_f32_e32 v94, v94, v2
	v_mul_f32_e32 v95, v95, v3
	v_mul_f32_e32 v88, v88, v4
	v_mul_f32_e32 v89, v89, v5
	v_mul_f32_e32 v90, v90, v6
	v_mul_f32_e32 v91, v91, v7
	v_mul_f32_e32 v112, v84, v24
	v_mul_f32_e32 v113, v85, v25
	v_mul_f32_e32 v126, v86, v26
	v_mul_f32_e32 v127, v87, v27
	v_mul_f32_e32 v148, v80, v28
	v_mul_f32_e32 v149, v81, v29
	v_mul_f32_e32 v150, v82, v30
	v_mul_f32_e32 v151, v83, v31
	v_cndmask_b32_e64 v83, v222, v95, s[0:1]
	v_cndmask_b32_e64 v82, v222, v94, s[0:1]
	v_cndmask_b32_e64 v81, v222, v93, s[0:1]
	v_cndmask_b32_e64 v80, v222, v92, s[0:1]
	v_cndmask_b32_e64 v87, v222, v91, s[0:1]
	v_cndmask_b32_e64 v86, v222, v90, s[0:1]
	v_cndmask_b32_e64 v85, v222, v89, s[0:1]
	v_cndmask_b32_e64 v84, v222, v88, s[0:1]
	v_cndmask_b32_e64 v91, v222, v127, s[0:1]
	v_cndmask_b32_e64 v90, v222, v126, s[0:1]
	v_cndmask_b32_e64 v89, v222, v113, s[0:1]
	v_cndmask_b32_e64 v88, v222, v112, s[0:1]
	v_cndmask_b32_e64 v95, v222, v151, s[0:1]
	v_cndmask_b32_e64 v94, v222, v150, s[0:1]
	v_cndmask_b32_e64 v93, v222, v149, s[0:1]
	v_cndmask_b32_e64 v92, v222, v148, s[0:1]
	global_store_dwordx4 v[180:181], v[80:83], off
	global_store_dwordx4 v[180:181], v[84:87], off offset:1024
	global_store_dwordx4 v[180:181], v[88:91], off offset:2048
	global_store_dwordx4 v[180:181], v[92:95], off offset:3072
	s_cbranch_scc0 .LBB0_1282
	s_add_i32 s50, s50, s48
	v_lshl_add_u64 v[104:105], v[104:105], 0, s[14:15]
	s_cmpk_gt_i32 s50, 0xff
	v_lshl_add_u64 v[106:107], v[106:107], 0, s[14:15]
	s_cbranch_scc0 .LBB0_1281
